# bf16 packing: bit-trick RNE sequences (bfe/add3/lshr/and_or) replaced by v_cvt_pk_bf16_f32 where dataflow proves equivalence (547 pairs), in GEMM epilogues, LN, chunk phases
# speedup vs baseline: 1.0069x; 1.0069x over previous
.LBB0_55:
	v_lshl_add_u64 v[68:69], v[44:45], 0, s[6:7]
	v_lshl_add_u64 v[70:71], v[42:43], 0, s[6:7]
	v_lshl_add_u64 v[72:73], v[40:41], 0, s[6:7]
	v_lshl_add_u64 v[74:75], v[38:39], 0, s[6:7]
	v_lshl_add_u64 v[76:77], v[36:37], 0, s[6:7]
	v_lshl_add_u64 v[78:79], v[34:35], 0, s[6:7]
	v_lshl_add_u64 v[80:81], v[32:33], 0, s[6:7]
	v_lshl_add_u64 v[82:83], v[30:31], 0, s[6:7]
	global_load_dword v67, v[68:69], off nt
	s_nop 0
	global_load_dword v68, v[70:71], off nt
	global_load_dword v69, v[72:73], off nt
	s_nop 0
	global_load_dword v70, v[74:75], off nt
	global_load_dword v71, v[76:77], off nt
	global_load_dword v72, v[78:79], off nt
	global_load_dword v73, v[80:81], off nt
	s_nop 0
	global_load_dword v74, v[82:83], off nt
	s_add_u32 s6, s6, 0x2c000
	s_addc_u32 s7, s7, 0
	v_add_u32_e32 v75, 0x400, v8
	s_cmp_lg_u32 s6, 0xb0000
	s_waitcnt vmcnt(6)
	ds_write2_b32 v8, v67, v68 offset1:66
	s_waitcnt vmcnt(4)
	ds_write2_b32 v8, v69, v70 offset0:132 offset1:198
	s_waitcnt vmcnt(2)
	ds_write2_b32 v75, v71, v72 offset0:8 offset1:74
	s_waitcnt vmcnt(0)
	ds_write2_b32 v75, v73, v74 offset0:140 offset1:206
	v_add_u32_e32 v8, 0x840, v8
	s_cbranch_scc1 .LBB0_55
	s_waitcnt lgkmcnt(0)
	ds_read2_b32 v[34:35], v47 offset1:8
	ds_read2_b32 v[38:39], v47 offset0:33 offset1:41
	ds_read2_b32 v[40:41], v47 offset0:66 offset1:74
	ds_read2_b32 v[42:43], v47 offset0:99 offset1:107
	ds_read2_b32 v[44:45], v47 offset0:132 offset1:140
	s_waitcnt lgkmcnt(4)
	s_waitcnt lgkmcnt(3)
	ds_read2_b32 v[68:69], v47 offset0:165 offset1:173
	v_cvt_pk_bf16_f32 v30, v34, v38
	s_waitcnt lgkmcnt(3)
	s_waitcnt lgkmcnt(2)
	ds_read2_b32 v[70:71], v47 offset0:198 offset1:206
	ds_read2_b32 v[72:73], v47 offset0:231 offset1:239
	s_lshl_b32 s0, s46, 1
	v_cvt_pk_bf16_f32 v31, v40, v42
	s_waitcnt lgkmcnt(3)
	s_and_b32 s0, s0, 0x3fe0
	s_waitcnt lgkmcnt(2)
	s_add_i32 s6, s0, 0xffffe600
	s_lshl_b32 s0, s46, 7
	v_cvt_pk_bf16_f32 v32, v44, v68
	s_waitcnt lgkmcnt(1)
	v_add_u32_e32 v74, s6, v46
	s_and_b32 s0, s0, 0x780
	s_waitcnt lgkmcnt(0)
	v_ashrrev_i32_e32 v75, 31, v74
	v_lshl_add_u64 v[36:37], v[14:15], 0, s[0:1]
	v_lshlrev_b64 v[74:75], 11, v[74:75]
	v_cvt_pk_bf16_f32 v33, v70, v72
	v_lshl_add_u64 v[74:75], v[36:37], 0, v[74:75]
	v_bfe_u32 v8, v35, 16, 1
	global_store_dwordx4 v[74:75], v[30:33], off
	v_add3_u32 v8, v35, v8, s42
	v_lshrrev_b32_e32 v8, 16, v8
	v_bfe_u32 v30, v39, 16, 1
	v_add3_u32 v30, v39, v30, s42
	v_and_or_b32 v30, v30, s43, v8
	v_cvt_pk_bf16_f32 v31, v41, v43
	v_cvt_pk_bf16_f32 v32, v45, v69
	v_add_u32_e32 v34, s6, v48
	v_ashrrev_i32_e32 v35, 31, v34
	v_lshlrev_b64 v[34:35], 11, v[34:35]
	v_cvt_pk_bf16_f32 v33, v71, v73
	ds_read2_b32 v[38:39], v47 offset0:16 offset1:24
	v_lshl_add_u64 v[34:35], v[36:37], 0, v[34:35]
	global_store_dwordx4 v[34:35], v[30:33], off
	ds_read2_b32 v[34:35], v47 offset0:49 offset1:57
	ds_read2_b32 v[40:41], v47 offset0:82 offset1:90
	ds_read2_b32 v[42:43], v47 offset0:115 offset1:123
	s_waitcnt lgkmcnt(3)
	s_waitcnt lgkmcnt(2)
	ds_read2_b32 v[44:45], v47 offset0:148 offset1:156
	ds_read2_b32 v[68:69], v47 offset0:181 offset1:189
	v_cvt_pk_bf16_f32 v30, v38, v34
	s_waitcnt lgkmcnt(3)
	s_waitcnt lgkmcnt(2)
	ds_read2_b32 v[70:71], v47 offset0:214 offset1:222
	ds_read2_b32 v[72:73], v47 offset0:247 offset1:255
	v_cvt_pk_bf16_f32 v31, v40, v42
	s_waitcnt lgkmcnt(3)
	s_waitcnt lgkmcnt(2)
	v_cvt_pk_bf16_f32 v32, v44, v68
	s_waitcnt lgkmcnt(1)
	v_add_u32_e32 v74, s6, v49
	s_waitcnt lgkmcnt(0)
	v_ashrrev_i32_e32 v75, 31, v74
	v_lshlrev_b64 v[74:75], 11, v[74:75]
	v_cvt_pk_bf16_f32 v33, v70, v72
	v_lshl_add_u64 v[74:75], v[36:37], 0, v[74:75]
	v_bfe_u32 v8, v39, 16, 1
	global_store_dwordx4 v[74:75], v[30:33], off
	v_add3_u32 v8, v39, v8, s42
	v_lshrrev_b32_e32 v8, 16, v8
	v_bfe_u32 v30, v35, 16, 1
	v_add3_u32 v30, v35, v30, s42
	v_and_or_b32 v30, v30, s43, v8
	v_cvt_pk_bf16_f32 v31, v41, v43
	v_cvt_pk_bf16_f32 v32, v45, v69
	v_add_u32_e32 v34, s6, v50
	v_ashrrev_i32_e32 v35, 31, v34
	v_lshlrev_b64 v[34:35], 11, v[34:35]
	v_cvt_pk_bf16_f32 v33, v71, v73
	v_lshl_add_u64 v[34:35], v[36:37], 0, v[34:35]
	global_store_dwordx4 v[34:35], v[30:33], off
	s_waitcnt lgkmcnt(0)

.LBB0_60:
	v_lshl_add_u64 v[68:69], v[44:45], 0, s[6:7]
	v_lshl_add_u64 v[70:71], v[42:43], 0, s[6:7]
	v_lshl_add_u64 v[72:73], v[40:41], 0, s[6:7]
	v_lshl_add_u64 v[74:75], v[38:39], 0, s[6:7]
	v_lshl_add_u64 v[76:77], v[36:37], 0, s[6:7]
	v_lshl_add_u64 v[78:79], v[34:35], 0, s[6:7]
	v_lshl_add_u64 v[80:81], v[32:33], 0, s[6:7]
	v_lshl_add_u64 v[82:83], v[30:31], 0, s[6:7]
	global_load_dword v67, v[68:69], off nt
	s_nop 0
	global_load_dword v68, v[70:71], off nt
	global_load_dword v69, v[72:73], off nt
	s_nop 0
	global_load_dword v70, v[74:75], off nt
	global_load_dword v71, v[76:77], off nt
	global_load_dword v72, v[78:79], off nt
	global_load_dword v73, v[80:81], off nt
	s_nop 0
	global_load_dword v74, v[82:83], off nt
	s_add_u32 s6, s6, 0x10000
	s_addc_u32 s7, s7, 0
	v_add_u32_e32 v75, 0x400, v8
	s_cmp_lg_u32 s6, 0x40000
	s_waitcnt vmcnt(6)
	ds_write2_b32 v8, v67, v68 offset1:66
	s_waitcnt vmcnt(4)
	ds_write2_b32 v8, v69, v70 offset0:132 offset1:198
	s_waitcnt vmcnt(2)
	ds_write2_b32 v75, v71, v72 offset0:8 offset1:74
	s_waitcnt vmcnt(0)
	ds_write2_b32 v75, v73, v74 offset0:140 offset1:206
	v_add_u32_e32 v8, 0x840, v8
	s_cbranch_scc1 .LBB0_60
	s_lshr_b32 s0, s0, 9
	s_lshl_b32 s6, s46, 5
	s_waitcnt lgkmcnt(0)
	s_and_b32 s8, s6, 0x3e0
	s_lshl_b64 s[6:7], s[0:1], 21
	ds_read2_b32 v[34:35], v47 offset1:8
	s_add_u32 s0, s24, s6
	ds_read2_b32 v[38:39], v47 offset0:33 offset1:41
	s_addc_u32 s7, s25, s7
	s_lshl_b32 s6, s9, 1
	s_add_u32 s6, s0, s6
	ds_read2_b32 v[40:41], v47 offset0:66 offset1:74
	s_addc_u32 s7, s7, 0
	v_lshlrev_b32_e32 v8, 1, v12
	ds_read2_b32 v[42:43], v47 offset0:99 offset1:107
	v_lshl_add_u64 v[36:37], s[6:7], 0, v[8:9]
	s_waitcnt lgkmcnt(3)
	s_waitcnt lgkmcnt(2)
	ds_read2_b32 v[44:45], v47 offset0:132 offset1:140
	ds_read2_b32 v[68:69], v47 offset0:165 offset1:173
	v_cvt_pk_bf16_f32 v30, v34, v38
	s_waitcnt lgkmcnt(3)
	s_waitcnt lgkmcnt(2)
	ds_read2_b32 v[70:71], v47 offset0:198 offset1:206
	ds_read2_b32 v[72:73], v47 offset0:231 offset1:239
	v_cvt_pk_bf16_f32 v31, v40, v42
	s_waitcnt lgkmcnt(3)
	s_waitcnt lgkmcnt(2)
	v_cvt_pk_bf16_f32 v32, v44, v68
	s_waitcnt lgkmcnt(1)
	v_add_u32_e32 v74, s8, v46
	s_waitcnt lgkmcnt(0)
	v_ashrrev_i32_e32 v75, 31, v74
	v_lshlrev_b64 v[74:75], 11, v[74:75]
	v_cvt_pk_bf16_f32 v33, v70, v72
	v_lshl_add_u64 v[74:75], v[36:37], 0, v[74:75]
	v_bfe_u32 v8, v35, 16, 1
	global_store_dwordx4 v[74:75], v[30:33], off
	v_add3_u32 v8, v35, v8, s42
	v_lshrrev_b32_e32 v8, 16, v8
	v_bfe_u32 v30, v39, 16, 1
	v_add3_u32 v30, v39, v30, s42
	v_and_or_b32 v30, v30, s43, v8
	v_cvt_pk_bf16_f32 v31, v41, v43
	v_cvt_pk_bf16_f32 v32, v45, v69
	v_add_u32_e32 v34, s8, v48
	v_ashrrev_i32_e32 v35, 31, v34
	v_lshlrev_b64 v[34:35], 11, v[34:35]
	v_cvt_pk_bf16_f32 v33, v71, v73
	ds_read2_b32 v[38:39], v47 offset0:16 offset1:24
	v_lshl_add_u64 v[34:35], v[36:37], 0, v[34:35]
	global_store_dwordx4 v[34:35], v[30:33], off
	ds_read2_b32 v[34:35], v47 offset0:49 offset1:57
	ds_read2_b32 v[40:41], v47 offset0:82 offset1:90
	ds_read2_b32 v[42:43], v47 offset0:115 offset1:123
	s_waitcnt lgkmcnt(3)
	s_waitcnt lgkmcnt(2)
	ds_read2_b32 v[44:45], v47 offset0:148 offset1:156
	ds_read2_b32 v[68:69], v47 offset0:181 offset1:189
	v_cvt_pk_bf16_f32 v30, v38, v34
	s_waitcnt lgkmcnt(3)
	s_waitcnt lgkmcnt(2)
	ds_read2_b32 v[70:71], v47 offset0:214 offset1:222
	ds_read2_b32 v[72:73], v47 offset0:247 offset1:255
	v_cvt_pk_bf16_f32 v31, v40, v42
	s_waitcnt lgkmcnt(3)
	s_waitcnt lgkmcnt(2)
	v_cvt_pk_bf16_f32 v32, v44, v68
	s_waitcnt lgkmcnt(1)
	v_add_u32_e32 v74, s8, v49
	s_waitcnt lgkmcnt(0)
	v_ashrrev_i32_e32 v75, 31, v74
	v_lshlrev_b64 v[74:75], 11, v[74:75]
	v_cvt_pk_bf16_f32 v33, v70, v72
	v_lshl_add_u64 v[74:75], v[36:37], 0, v[74:75]
	v_bfe_u32 v8, v39, 16, 1
	global_store_dwordx4 v[74:75], v[30:33], off
	v_add3_u32 v8, v39, v8, s42
	v_lshrrev_b32_e32 v8, 16, v8
	v_bfe_u32 v30, v35, 16, 1
	v_add3_u32 v30, v35, v30, s42
	v_and_or_b32 v30, v30, s43, v8
	v_cvt_pk_bf16_f32 v31, v41, v43
	v_cvt_pk_bf16_f32 v32, v45, v69
	v_add_u32_e32 v34, s8, v50
	v_ashrrev_i32_e32 v35, 31, v34
	v_lshlrev_b64 v[34:35], 11, v[34:35]
	v_cvt_pk_bf16_f32 v33, v71, v73
	v_lshl_add_u64 v[34:35], v[36:37], 0, v[34:35]
	global_store_dwordx4 v[34:35], v[30:33], off
	s_waitcnt lgkmcnt(0)

.LBB0_65:
	v_lshl_add_u64 v[68:69], v[44:45], 0, s[10:11]
	v_lshl_add_u64 v[70:71], v[42:43], 0, s[10:11]
	v_lshl_add_u64 v[72:73], v[40:41], 0, s[10:11]
	v_lshl_add_u64 v[74:75], v[38:39], 0, s[10:11]
	v_lshl_add_u64 v[76:77], v[36:37], 0, s[10:11]
	v_lshl_add_u64 v[78:79], v[34:35], 0, s[10:11]
	v_lshl_add_u64 v[80:81], v[32:33], 0, s[10:11]
	v_lshl_add_u64 v[82:83], v[30:31], 0, s[10:11]
	global_load_dword v67, v[68:69], off nt
	s_nop 0
	global_load_dword v68, v[70:71], off nt
	global_load_dword v69, v[72:73], off nt
	s_nop 0
	global_load_dword v70, v[74:75], off nt
	global_load_dword v71, v[76:77], off nt
	global_load_dword v72, v[78:79], off nt
	global_load_dword v73, v[80:81], off nt
	s_nop 0
	global_load_dword v74, v[82:83], off nt
	s_add_u32 s10, s10, 0x24000
	s_addc_u32 s11, s11, 0
	v_add_u32_e32 v75, 0x400, v8
	s_cmp_lg_u32 s10, 0x90000
	s_waitcnt vmcnt(6)
	ds_write2_b32 v8, v67, v68 offset1:66
	s_waitcnt vmcnt(4)
	ds_write2_b32 v8, v69, v70 offset0:132 offset1:198
	s_waitcnt vmcnt(2)
	ds_write2_b32 v75, v71, v72 offset0:8 offset1:74
	s_waitcnt vmcnt(0)
	ds_write2_b32 v75, v73, v74 offset0:140 offset1:206
	v_add_u32_e32 v8, 0x840, v8
	s_cbranch_scc1 .LBB0_65
	s_waitcnt lgkmcnt(0)
	s_mul_hi_i32 s7, s0, 0x480000
	s_mul_i32 s0, s0, 0x480000
	ds_read2_b32 v[34:35], v47 offset1:8
	s_add_u32 s0, s26, s0
	ds_read2_b32 v[38:39], v47 offset0:33 offset1:41
	s_addc_u32 s7, s27, s7
	s_lshl_b64 s[8:9], s[8:9], 1
	s_add_u32 s8, s0, s8
	ds_read2_b32 v[40:41], v47 offset0:66 offset1:74
	s_addc_u32 s9, s7, s9
	v_lshlrev_b32_e32 v8, 1, v12
	ds_read2_b32 v[42:43], v47 offset0:99 offset1:107
	v_lshl_add_u64 v[36:37], s[8:9], 0, v[8:9]
	s_waitcnt lgkmcnt(3)
	s_waitcnt lgkmcnt(2)
	ds_read2_b32 v[44:45], v47 offset0:132 offset1:140
	ds_read2_b32 v[68:69], v47 offset0:165 offset1:173
	v_cvt_pk_bf16_f32 v30, v34, v38
	s_waitcnt lgkmcnt(3)
	s_waitcnt lgkmcnt(2)
	ds_read2_b32 v[70:71], v47 offset0:198 offset1:206
	ds_read2_b32 v[72:73], v47 offset0:231 offset1:239
	v_cvt_pk_bf16_f32 v31, v40, v42
	s_waitcnt lgkmcnt(3)
	s_waitcnt lgkmcnt(2)
	v_cvt_pk_bf16_f32 v32, v44, v68
	s_waitcnt lgkmcnt(1)
	v_add_u32_e32 v74, s6, v46
	s_waitcnt lgkmcnt(0)
	v_ashrrev_i32_e32 v75, 31, v74
	v_lshlrev_b64 v[74:75], 11, v[74:75]
	v_cvt_pk_bf16_f32 v33, v70, v72
	v_lshl_add_u64 v[74:75], v[36:37], 0, v[74:75]
	v_bfe_u32 v8, v35, 16, 1
	global_store_dwordx4 v[74:75], v[30:33], off
	v_add3_u32 v8, v35, v8, s42
	v_lshrrev_b32_e32 v8, 16, v8
	v_bfe_u32 v30, v39, 16, 1
	v_add3_u32 v30, v39, v30, s42
	v_and_or_b32 v30, v30, s43, v8
	v_cvt_pk_bf16_f32 v31, v41, v43
	v_cvt_pk_bf16_f32 v32, v45, v69
	v_add_u32_e32 v34, s6, v48
	v_ashrrev_i32_e32 v35, 31, v34
	v_lshlrev_b64 v[34:35], 11, v[34:35]
	v_cvt_pk_bf16_f32 v33, v71, v73
	ds_read2_b32 v[38:39], v47 offset0:16 offset1:24
	v_lshl_add_u64 v[34:35], v[36:37], 0, v[34:35]
	global_store_dwordx4 v[34:35], v[30:33], off
	ds_read2_b32 v[34:35], v47 offset0:49 offset1:57
	ds_read2_b32 v[40:41], v47 offset0:82 offset1:90
	ds_read2_b32 v[42:43], v47 offset0:115 offset1:123
	s_waitcnt lgkmcnt(3)
	s_waitcnt lgkmcnt(2)
	ds_read2_b32 v[44:45], v47 offset0:148 offset1:156
	ds_read2_b32 v[68:69], v47 offset0:181 offset1:189
	v_cvt_pk_bf16_f32 v30, v38, v34
	s_waitcnt lgkmcnt(3)
	s_waitcnt lgkmcnt(2)
	ds_read2_b32 v[70:71], v47 offset0:214 offset1:222
	ds_read2_b32 v[72:73], v47 offset0:247 offset1:255
	v_cvt_pk_bf16_f32 v31, v40, v42
	s_waitcnt lgkmcnt(3)
	s_waitcnt lgkmcnt(2)
	v_cvt_pk_bf16_f32 v32, v44, v68
	s_waitcnt lgkmcnt(1)
	v_add_u32_e32 v74, s6, v49
	s_waitcnt lgkmcnt(0)
	v_ashrrev_i32_e32 v75, 31, v74
	v_lshlrev_b64 v[74:75], 11, v[74:75]
	v_cvt_pk_bf16_f32 v33, v70, v72
	v_lshl_add_u64 v[74:75], v[36:37], 0, v[74:75]
	v_bfe_u32 v8, v39, 16, 1
	global_store_dwordx4 v[74:75], v[30:33], off
	v_add3_u32 v8, v39, v8, s42
	v_lshrrev_b32_e32 v8, 16, v8
	v_bfe_u32 v30, v35, 16, 1
	v_add3_u32 v30, v35, v30, s42
	v_and_or_b32 v30, v30, s43, v8
	v_cvt_pk_bf16_f32 v31, v41, v43
	v_cvt_pk_bf16_f32 v32, v45, v69
	v_add_u32_e32 v34, s6, v50
	v_ashrrev_i32_e32 v35, 31, v34
	v_lshlrev_b64 v[34:35], 11, v[34:35]
	v_cvt_pk_bf16_f32 v33, v71, v73
	v_lshl_add_u64 v[34:35], v[36:37], 0, v[34:35]
	global_store_dwordx4 v[34:35], v[30:33], off
	s_waitcnt lgkmcnt(0)
	s_branch .LBB0_34

.LBB0_153:
	v_cvt_pk_bf16_f32 v114, v130, v131
	v_cvt_pk_bf16_f32 v115, v132, v133
	s_lshl_b32 s4, s4, 8
	v_cvt_pk_bf16_f32 v116, v134, v135
	s_ashr_i32 s5, s4, 31
	v_lshl_add_u32 v168, s54, 8, v164
	v_lshl_add_u64 v[162:163], s[4:5], 1, v[154:155]
	v_mad_i64_i32 v[118:119], s[4:5], v168, s86, v[162:163]
	v_cvt_pk_bf16_f32 v117, v136, v137
	global_store_dwordx4 v[118:119], v[114:117], off
	v_bfe_u32 v120, v145, 16, 1
	v_add3_u32 v120, v145, v120, s87
	v_cvt_pk_bf16_f32 v114, v138, v139
	v_cvt_pk_bf16_f32 v115, v140, v141
	v_cvt_pk_bf16_f32 v116, v142, v143
	v_bfe_u32 v117, v144, 16, 1
	v_add3_u32 v117, v144, v117, s87
	v_lshrrev_b32_e32 v117, 16, v117
	v_and_or_b32 v117, v120, s88, v117
	global_store_dwordx4 v[118:119], v[114:117], off offset:256
	s_andn2_b64 vcc, exec, s[62:63]
	s_mov_b64 s[38:39], -1
	v_cndmask_b32_e64 v114, 0, 1, s[62:63]
	v_cmp_ne_u32_e64 s[4:5], 1, v114
	s_cbranch_vccnz .LBB0_157
	v_mov_b64_e32 v[116:117], v[112:113]
	v_mov_b64_e32 v[128:129], v[100:101]
	v_mov_b64_e32 v[124:125], v[104:105]
	v_mov_b64_e32 v[120:121], v[108:109]
	s_and_b64 vcc, exec, s[2:3]
	v_mov_b64_e32 v[114:115], v[110:111]
	v_mov_b64_e32 v[126:127], v[98:99]
	v_mov_b64_e32 v[122:123], v[102:103]
	v_mov_b64_e32 v[118:119], v[106:107]
	s_cbranch_vccnz .LBB0_156
	v_pk_mul_f32 v[116:117], v[112:113], s[24:25] op_sel_hi:[1,0]
	v_pk_mul_f32 v[114:115], v[110:111], s[24:25] op_sel_hi:[1,0]
	v_pk_mul_f32 v[120:121], v[108:109], s[24:25] op_sel_hi:[1,0]
	v_pk_mul_f32 v[118:119], v[106:107], s[24:25] op_sel_hi:[1,0]
	v_pk_mul_f32 v[124:125], v[104:105], s[24:25] op_sel_hi:[1,0]
	v_pk_mul_f32 v[122:123], v[102:103], s[24:25] op_sel_hi:[1,0]
	v_pk_mul_f32 v[128:129], v[100:101], s[24:25] op_sel_hi:[1,0]
	v_pk_mul_f32 v[126:127], v[98:99], s[24:25] op_sel_hi:[1,0]

.LBB0_159:
	v_or_b32_e32 v98, 16, v168
	v_mad_i64_i32 v[102:103], s[38:39], v98, s86, v[162:163]
	v_cvt_pk_bf16_f32 v98, v114, v115
	v_cvt_pk_bf16_f32 v99, v116, v117
	v_cvt_pk_bf16_f32 v100, v118, v119
	v_cvt_pk_bf16_f32 v101, v120, v121
	global_store_dwordx4 v[102:103], v[98:101], off
	v_bfe_u32 v104, v129, 16, 1
	v_add3_u32 v104, v129, v104, s87
	v_cvt_pk_bf16_f32 v98, v122, v123
	v_cvt_pk_bf16_f32 v99, v124, v125
	v_cvt_pk_bf16_f32 v100, v126, v127
	v_bfe_u32 v101, v128, 16, 1
	v_add3_u32 v101, v128, v101, s87
	v_lshrrev_b32_e32 v101, 16, v101
	v_and_or_b32 v101, v104, s88, v101
	s_and_b64 vcc, exec, s[4:5]
	s_mov_b64 s[38:39], -1
	global_store_dwordx4 v[102:103], v[98:101], off offset:256
	s_cbranch_vccnz .LBB0_163
	s_nop 0
	v_mov_b64_e32 v[100:101], v[96:97]
	v_mov_b64_e32 v[112:113], v[84:85]
	v_mov_b64_e32 v[108:109], v[88:89]
	v_mov_b64_e32 v[104:105], v[92:93]
	s_and_b64 vcc, exec, s[2:3]
	v_mov_b64_e32 v[98:99], v[94:95]
	v_mov_b64_e32 v[110:111], v[82:83]
	v_mov_b64_e32 v[106:107], v[86:87]
	v_mov_b64_e32 v[102:103], v[90:91]
	s_cbranch_vccnz .LBB0_162
	v_pk_mul_f32 v[100:101], v[96:97], s[24:25] op_sel_hi:[1,0]
	v_pk_mul_f32 v[98:99], v[94:95], s[24:25] op_sel_hi:[1,0]
	v_pk_mul_f32 v[104:105], v[92:93], s[24:25] op_sel_hi:[1,0]
	v_pk_mul_f32 v[102:103], v[90:91], s[24:25] op_sel_hi:[1,0]
	v_pk_mul_f32 v[108:109], v[88:89], s[24:25] op_sel_hi:[1,0]
	v_pk_mul_f32 v[106:107], v[86:87], s[24:25] op_sel_hi:[1,0]
	v_pk_mul_f32 v[112:113], v[84:85], s[24:25] op_sel_hi:[1,0]
	v_pk_mul_f32 v[110:111], v[82:83], s[24:25] op_sel_hi:[1,0]

.LBB0_165:
	v_or_b32_e32 v82, 32, v168
	v_mad_i64_i32 v[86:87], s[38:39], v82, s86, v[162:163]
	v_cvt_pk_bf16_f32 v82, v98, v99
	v_cvt_pk_bf16_f32 v83, v100, v101
	v_cvt_pk_bf16_f32 v84, v102, v103
	v_cvt_pk_bf16_f32 v85, v104, v105
	global_store_dwordx4 v[86:87], v[82:85], off
	v_bfe_u32 v88, v113, 16, 1
	v_add3_u32 v88, v113, v88, s87
	v_cvt_pk_bf16_f32 v82, v106, v107
	v_cvt_pk_bf16_f32 v83, v108, v109
	v_cvt_pk_bf16_f32 v84, v110, v111
	v_bfe_u32 v85, v112, 16, 1
	v_add3_u32 v85, v112, v85, s87
	v_lshrrev_b32_e32 v85, 16, v85
	v_and_or_b32 v85, v88, s88, v85
	s_and_b64 vcc, exec, s[4:5]
	s_mov_b64 s[38:39], -1
	global_store_dwordx4 v[86:87], v[82:85], off offset:256
	s_cbranch_vccnz .LBB0_169
	s_nop 0
	v_mov_b64_e32 v[84:85], v[80:81]
	v_mov_b64_e32 v[96:97], v[68:69]
	v_mov_b64_e32 v[92:93], v[72:73]
	v_mov_b64_e32 v[88:89], v[76:77]
	s_and_b64 vcc, exec, s[2:3]
	v_mov_b64_e32 v[82:83], v[78:79]
	v_mov_b64_e32 v[94:95], v[66:67]
	v_mov_b64_e32 v[90:91], v[70:71]
	v_mov_b64_e32 v[86:87], v[74:75]
	s_cbranch_vccnz .LBB0_168
	v_pk_mul_f32 v[84:85], v[80:81], s[24:25] op_sel_hi:[1,0]
	v_pk_mul_f32 v[82:83], v[78:79], s[24:25] op_sel_hi:[1,0]
	v_pk_mul_f32 v[88:89], v[76:77], s[24:25] op_sel_hi:[1,0]
	v_pk_mul_f32 v[86:87], v[74:75], s[24:25] op_sel_hi:[1,0]
	v_pk_mul_f32 v[92:93], v[72:73], s[24:25] op_sel_hi:[1,0]
	v_pk_mul_f32 v[90:91], v[70:71], s[24:25] op_sel_hi:[1,0]
	v_pk_mul_f32 v[96:97], v[68:69], s[24:25] op_sel_hi:[1,0]
	v_pk_mul_f32 v[94:95], v[66:67], s[24:25] op_sel_hi:[1,0]

.LBB0_171:
	v_or_b32_e32 v66, 48, v168
	v_mad_i64_i32 v[70:71], s[38:39], v66, s86, v[162:163]
	v_cvt_pk_bf16_f32 v66, v82, v83
	v_cvt_pk_bf16_f32 v67, v84, v85
	v_cvt_pk_bf16_f32 v68, v86, v87
	v_cvt_pk_bf16_f32 v69, v88, v89
	global_store_dwordx4 v[70:71], v[66:69], off
	v_bfe_u32 v72, v97, 16, 1
	v_add3_u32 v72, v97, v72, s87
	v_cvt_pk_bf16_f32 v66, v90, v91
	v_cvt_pk_bf16_f32 v67, v92, v93
	v_cvt_pk_bf16_f32 v68, v94, v95
	v_bfe_u32 v69, v96, 16, 1
	v_add3_u32 v69, v96, v69, s87
	v_lshrrev_b32_e32 v69, 16, v69
	v_and_or_b32 v69, v72, s88, v69
	s_and_b64 vcc, exec, s[4:5]
	s_mov_b64 s[38:39], -1
	global_store_dwordx4 v[70:71], v[66:69], off offset:256
	s_cbranch_vccnz .LBB0_175
	s_nop 0
	v_mov_b64_e32 v[68:69], v[64:65]
	v_mov_b64_e32 v[80:81], v[52:53]
	v_mov_b64_e32 v[76:77], v[56:57]
	v_mov_b64_e32 v[72:73], v[60:61]
	s_and_b64 vcc, exec, s[2:3]
	v_mov_b64_e32 v[66:67], v[62:63]
	v_mov_b64_e32 v[78:79], v[50:51]
	v_mov_b64_e32 v[74:75], v[54:55]
	v_mov_b64_e32 v[70:71], v[58:59]
	s_cbranch_vccnz .LBB0_174
	v_pk_mul_f32 v[68:69], v[64:65], s[24:25] op_sel_hi:[1,0]
	v_pk_mul_f32 v[66:67], v[62:63], s[24:25] op_sel_hi:[1,0]
	v_pk_mul_f32 v[72:73], v[60:61], s[24:25] op_sel_hi:[1,0]
	v_pk_mul_f32 v[70:71], v[58:59], s[24:25] op_sel_hi:[1,0]
	v_pk_mul_f32 v[76:77], v[56:57], s[24:25] op_sel_hi:[1,0]
	v_pk_mul_f32 v[74:75], v[54:55], s[24:25] op_sel_hi:[1,0]
	v_pk_mul_f32 v[80:81], v[52:53], s[24:25] op_sel_hi:[1,0]
	v_pk_mul_f32 v[78:79], v[50:51], s[24:25] op_sel_hi:[1,0]

.LBB0_177:
	v_add_u32_e32 v50, 0x80, v168
	v_mad_i64_i32 v[54:55], s[38:39], v50, s86, v[162:163]
	v_cvt_pk_bf16_f32 v50, v66, v67
	v_cvt_pk_bf16_f32 v51, v68, v69
	v_cvt_pk_bf16_f32 v52, v70, v71
	v_cvt_pk_bf16_f32 v53, v72, v73
	global_store_dwordx4 v[54:55], v[50:53], off
	v_bfe_u32 v56, v81, 16, 1
	v_add3_u32 v56, v81, v56, s87
	v_cvt_pk_bf16_f32 v50, v74, v75
	v_cvt_pk_bf16_f32 v51, v76, v77
	v_cvt_pk_bf16_f32 v52, v78, v79
	v_bfe_u32 v53, v80, 16, 1
	v_add3_u32 v53, v80, v53, s87
	v_lshrrev_b32_e32 v53, 16, v53
	v_and_or_b32 v53, v56, s88, v53
	s_and_b64 vcc, exec, s[4:5]
	s_mov_b64 s[38:39], -1
	global_store_dwordx4 v[54:55], v[50:53], off offset:256
	s_cbranch_vccnz .LBB0_181
	s_nop 0
	v_mov_b64_e32 v[52:53], v[48:49]
	v_mov_b64_e32 v[64:65], v[36:37]
	v_mov_b64_e32 v[60:61], v[40:41]
	v_mov_b64_e32 v[56:57], v[44:45]
	s_and_b64 vcc, exec, s[2:3]
	v_mov_b64_e32 v[50:51], v[46:47]
	v_mov_b64_e32 v[62:63], v[34:35]
	v_mov_b64_e32 v[58:59], v[38:39]
	v_mov_b64_e32 v[54:55], v[42:43]
	s_cbranch_vccnz .LBB0_180
	v_pk_mul_f32 v[52:53], v[48:49], s[24:25] op_sel_hi:[1,0]
	v_pk_mul_f32 v[50:51], v[46:47], s[24:25] op_sel_hi:[1,0]
	v_pk_mul_f32 v[56:57], v[44:45], s[24:25] op_sel_hi:[1,0]
	v_pk_mul_f32 v[54:55], v[42:43], s[24:25] op_sel_hi:[1,0]
	v_pk_mul_f32 v[60:61], v[40:41], s[24:25] op_sel_hi:[1,0]
	v_pk_mul_f32 v[58:59], v[38:39], s[24:25] op_sel_hi:[1,0]
	v_pk_mul_f32 v[64:65], v[36:37], s[24:25] op_sel_hi:[1,0]
	v_pk_mul_f32 v[62:63], v[34:35], s[24:25] op_sel_hi:[1,0]

.LBB0_183:
	v_add_u32_e32 v34, 0x90, v168
	v_mad_i64_i32 v[38:39], s[38:39], v34, s86, v[162:163]
	v_cvt_pk_bf16_f32 v34, v50, v51
	v_cvt_pk_bf16_f32 v35, v52, v53
	v_cvt_pk_bf16_f32 v36, v54, v55
	v_cvt_pk_bf16_f32 v37, v56, v57
	global_store_dwordx4 v[38:39], v[34:37], off
	v_bfe_u32 v40, v65, 16, 1
	v_add3_u32 v40, v65, v40, s87
	v_cvt_pk_bf16_f32 v34, v58, v59
	v_cvt_pk_bf16_f32 v35, v60, v61
	v_cvt_pk_bf16_f32 v36, v62, v63
	v_bfe_u32 v37, v64, 16, 1
	v_add3_u32 v37, v64, v37, s87
	v_lshrrev_b32_e32 v37, 16, v37
	v_and_or_b32 v37, v40, s88, v37
	s_and_b64 vcc, exec, s[4:5]
	s_mov_b64 s[38:39], -1
	global_store_dwordx4 v[38:39], v[34:37], off offset:256
	s_cbranch_vccnz .LBB0_187
	s_nop 0
	v_mov_b64_e32 v[36:37], v[32:33]
	v_mov_b64_e32 v[48:49], v[20:21]
	v_mov_b64_e32 v[44:45], v[24:25]
	v_mov_b64_e32 v[40:41], v[28:29]
	s_and_b64 vcc, exec, s[2:3]
	v_mov_b64_e32 v[34:35], v[30:31]
	v_mov_b64_e32 v[46:47], v[18:19]
	v_mov_b64_e32 v[42:43], v[22:23]
	v_mov_b64_e32 v[38:39], v[26:27]
	s_cbranch_vccnz .LBB0_186
	v_pk_mul_f32 v[36:37], v[32:33], s[24:25] op_sel_hi:[1,0]
	v_pk_mul_f32 v[34:35], v[30:31], s[24:25] op_sel_hi:[1,0]
	v_pk_mul_f32 v[40:41], v[28:29], s[24:25] op_sel_hi:[1,0]
	v_pk_mul_f32 v[38:39], v[26:27], s[24:25] op_sel_hi:[1,0]
	v_pk_mul_f32 v[44:45], v[24:25], s[24:25] op_sel_hi:[1,0]
	v_pk_mul_f32 v[42:43], v[22:23], s[24:25] op_sel_hi:[1,0]
	v_pk_mul_f32 v[48:49], v[20:21], s[24:25] op_sel_hi:[1,0]
	v_pk_mul_f32 v[46:47], v[18:19], s[24:25] op_sel_hi:[1,0]

.LBB0_189:
	v_add_u32_e32 v18, 0xa0, v168
	v_mad_i64_i32 v[22:23], s[38:39], v18, s86, v[162:163]
	v_cvt_pk_bf16_f32 v18, v34, v35
	v_cvt_pk_bf16_f32 v19, v36, v37
	v_cvt_pk_bf16_f32 v20, v38, v39
	v_cvt_pk_bf16_f32 v21, v40, v41
	global_store_dwordx4 v[22:23], v[18:21], off
	v_bfe_u32 v24, v49, 16, 1
	v_add3_u32 v24, v49, v24, s87
	v_cvt_pk_bf16_f32 v18, v42, v43
	v_cvt_pk_bf16_f32 v19, v44, v45
	v_cvt_pk_bf16_f32 v20, v46, v47
	v_bfe_u32 v21, v48, 16, 1
	v_add3_u32 v21, v48, v21, s87
	v_lshrrev_b32_e32 v21, 16, v21
	v_and_or_b32 v21, v24, s88, v21
	s_and_b64 vcc, exec, s[4:5]
	s_mov_b64 s[4:5], -1
	global_store_dwordx4 v[22:23], v[18:21], off offset:256
	s_cbranch_vccnz .LBB0_193
	s_nop 0
	v_mov_b64_e32 v[20:21], v[16:17]
	v_mov_b64_e32 v[32:33], v[4:5]
	v_mov_b64_e32 v[28:29], v[8:9]
	v_mov_b64_e32 v[24:25], v[12:13]
	s_and_b64 vcc, exec, s[2:3]
	v_mov_b64_e32 v[18:19], v[14:15]
	v_mov_b64_e32 v[30:31], v[2:3]
	v_mov_b64_e32 v[26:27], v[6:7]
	v_mov_b64_e32 v[22:23], v[10:11]
	s_cbranch_vccnz .LBB0_192
	v_pk_mul_f32 v[20:21], v[16:17], s[24:25] op_sel_hi:[1,0]
	v_pk_mul_f32 v[18:19], v[14:15], s[24:25] op_sel_hi:[1,0]
	v_pk_mul_f32 v[24:25], v[12:13], s[24:25] op_sel_hi:[1,0]
	v_pk_mul_f32 v[22:23], v[10:11], s[24:25] op_sel_hi:[1,0]
	v_pk_mul_f32 v[28:29], v[8:9], s[24:25] op_sel_hi:[1,0]
	v_pk_mul_f32 v[26:27], v[6:7], s[24:25] op_sel_hi:[1,0]
	v_pk_mul_f32 v[32:33], v[4:5], s[24:25] op_sel_hi:[1,0]
	v_pk_mul_f32 v[30:31], v[2:3], s[24:25] op_sel_hi:[1,0]

.LBB0_195:
	v_add_u32_e32 v2, 0xb0, v168
	v_mad_i64_i32 v[6:7], s[2:3], v2, s86, v[162:163]
	v_cvt_pk_bf16_f32 v2, v18, v19
	v_cvt_pk_bf16_f32 v3, v20, v21
	v_cvt_pk_bf16_f32 v4, v22, v23
	v_cvt_pk_bf16_f32 v5, v24, v25
	global_store_dwordx4 v[6:7], v[2:5], off
	v_bfe_u32 v8, v33, 16, 1
	v_add3_u32 v8, v33, v8, s87
	v_cvt_pk_bf16_f32 v2, v26, v27
	v_cvt_pk_bf16_f32 v3, v28, v29
	v_cvt_pk_bf16_f32 v4, v30, v31
	v_bfe_u32 v5, v32, 16, 1
	v_add3_u32 v5, v32, v5, s87
	v_lshrrev_b32_e32 v5, 16, v5
	v_and_or_b32 v5, v8, s88, v5
	s_mov_b64 s[2:3], -1
	s_and_b64 vcc, exec, s[46:47]
	global_store_dwordx4 v[6:7], v[2:5], off offset:256
	s_cbranch_vccz .LBB0_139
	s_and_b64 vcc, exec, s[6:7]
	s_cbranch_vccz .LBB0_138
	s_barrier
	s_branch .LBB0_138

.LBB0_342:
	s_cmp_lg_u32 0, -1
	s_cselect_b32 s0, 0, 0
	s_addk_i32 s0, 0x6000
	v_add3_u32 v8, v237, s0, v233
	s_add_i32 s0, s33, 0x4000
	v_add_f32_e32 v2, v243, v2
	s_and_b32 s0, s0, 0xffff
	v_add3_u32 v16, v8, v236, s0
	ds_read_b64_tr_b16 v[8:9],v16 offset:0
	ds_read_b64_tr_b16 v[10:11],v16 offset:512
	ds_read_b64_tr_b16 v[12:13],v16 offset:1024
	ds_read_b64_tr_b16 v[14:15],v16 offset:1536
	ds_read_b64_tr_b16 v[82:83],v16 offset:2048
	ds_read_b64_tr_b16 v[84:85],v16 offset:2560
	ds_read_b64_tr_b16 v[86:87],v16 offset:3072
	ds_read_b64_tr_b16 v[88:89],v16 offset:3584
	s_waitcnt lgkmcnt(0)
	s_nop 0
	v_mfma_f32_32x32x16_bf16 v[66:81], v[138:141], v[8:11], v[66:81]
	ds_read_b64_tr_b16 v[8:9],v16 offset:4096
	ds_read_b64_tr_b16 v[10:11],v16 offset:4608
	v_mfma_f32_32x32x16_bf16 v[66:81], v[134:137], v[12:15], v[66:81]
	ds_read_b64_tr_b16 v[12:13],v16 offset:5120
	ds_read_b64_tr_b16 v[14:15],v16 offset:5632
	v_mfma_f32_32x32x16_bf16 v[66:81], v[130:133], v[82:85], v[66:81]
	ds_read_b64_tr_b16 v[82:83],v16 offset:6144
	ds_read_b64_tr_b16 v[84:85],v16 offset:6656
	ds_read_b64_tr_b16 v[90:91],v16 offset:7168
	ds_read_b64_tr_b16 v[92:93],v16 offset:7680
	s_waitcnt lgkmcnt(0)
	v_mfma_f32_32x32x16_bf16 v[66:81], v[4:7], v[86:89], v[66:81]
	v_mfma_f32_32x32x16_bf16 v[50:65], v[138:141], v[8:11], v[50:65]
	v_add_u32_e32 v16, 0x2000, v16
	ds_read_b64_tr_b16 v[8:9],v16 offset:0
	ds_read_b64_tr_b16 v[10:11],v16 offset:512
	v_mfma_f32_32x32x16_bf16 v[50:65], v[134:137], v[12:15], v[50:65]
	ds_read_b64_tr_b16 v[12:13],v16 offset:1024
	ds_read_b64_tr_b16 v[14:15],v16 offset:1536
	v_mfma_f32_32x32x16_bf16 v[50:65], v[130:133], v[82:85], v[50:65]
	ds_read_b64_tr_b16 v[82:83],v16 offset:2048
	ds_read_b64_tr_b16 v[84:85],v16 offset:2560
	ds_read_b64_tr_b16 v[86:87],v16 offset:3072
	ds_read_b64_tr_b16 v[88:89],v16 offset:3584
	s_waitcnt lgkmcnt(0)
	v_mfma_f32_32x32x16_bf16 v[50:65], v[4:7], v[90:93], v[50:65]
	v_mfma_f32_32x32x16_bf16 v[34:49], v[138:141], v[8:11], v[34:49]
	ds_read_b64_tr_b16 v[8:9],v16 offset:4096
	ds_read_b64_tr_b16 v[10:11],v16 offset:4608
	v_mfma_f32_32x32x16_bf16 v[34:49], v[134:137], v[12:15], v[34:49]
	ds_read_b64_tr_b16 v[12:13],v16 offset:5120
	ds_read_b64_tr_b16 v[14:15],v16 offset:5632
	v_mfma_f32_32x32x16_bf16 v[34:49], v[130:133], v[82:85], v[34:49]
	ds_read_b64_tr_b16 v[82:83],v16 offset:6144
	ds_read_b64_tr_b16 v[84:85],v16 offset:6656
	ds_read_b64_tr_b16 v[90:91],v16 offset:7168
	ds_read_b64_tr_b16 v[92:93],v16 offset:7680
	s_waitcnt lgkmcnt(0)
	v_mfma_f32_32x32x16_bf16 v[34:49], v[4:7], v[86:89], v[34:49]
	v_mfma_f32_32x32x16_bf16 v[18:33], v[138:141], v[8:11], v[18:33]
	v_mov_b32_e32 v8, v2
	s_nop 1
	v_permlane32_swap_b32_e32 v2, v8
	v_cmp_gt_u32_e32 vcc, 32, v230
	v_mfma_f32_32x32x16_bf16 v[18:33], v[134:137], v[12:15], v[18:33]
	v_mfma_f32_32x32x16_bf16 v[18:33], v[130:133], v[82:85], v[18:33]
	v_mfma_f32_32x32x16_bf16 v[18:33], v[4:7], v[90:93], v[18:33]
	s_and_saveexec_b64 s[0:1], vcc
	v_add_f32_e32 v2, v2, v8
	ds_write_b32 v235, v2 offset:128
	s_or_b64 exec, exec, s[0:1]
	s_waitcnt lgkmcnt(0)
	ds_read_b128 v[4:7], v234 offset:128
	ds_read_b128 v[8:11], v234 offset:160
	s_lshl_b32 s0, s84, 8
	s_add_u32 s2, s6, s0
	s_addc_u32 s3, s7, 0
	s_waitcnt lgkmcnt(1)
	v_rcp_f32_e32 v14, v4
	v_rcp_f32_e32 v15, v5
	v_rcp_f32_e32 v16, v6
	v_rcp_f32_e32 v17, v7
	ds_read_b128 v[4:7], v234 offset:192
	s_lshl_b64 s[0:1], s[34:35], 11
	s_add_u32 s0, s2, s0
	s_addc_u32 s1, s3, s1
	s_lshl_b32 s2, s83, 12
	s_add_i32 s2, s2, 0
	v_lshlrev_b32_e32 v2, 1, v232
	s_add_i32 s2, s2, 0x16800
	v_and_b32_e32 v2, 0x70, v2
	s_waitcnt lgkmcnt(1)
	v_rcp_f32_e32 v82, v8
	v_rcp_f32_e32 v83, v9
	v_rcp_f32_e32 v84, v10
	v_rcp_f32_e32 v85, v11
	ds_read_b128 v[8:11], v234 offset:224
	s_waitcnt lgkmcnt(1)
	v_rcp_f32_e32 v86, v4
	v_lshlrev_b32_e32 v4, 1, v231
	v_add_u32_e32 v95, s2, v2
	v_lshl_add_u64 v[12:13], s[0:1], 0, v[2:3]
	v_lshlrev_b32_e32 v2, 9, v229
	v_add3_u32 v97, s2, v4, v2
	v_mul_f32_e32 v2, v66, v14
	v_cvt_pk_bf16_f32 v2, v2, s0
	ds_write_b16 v97, v2
	v_mul_f32_e32 v2, v50, v14
	v_cvt_pk_bf16_f32 v2, v2, s0
	ds_write_b16 v97, v2 offset:64
	v_mul_f32_e32 v2, v67, v15
	v_cvt_pk_bf16_f32 v2, v2, s0
	ds_write_b16 v97, v2 offset:128
	v_mul_f32_e32 v2, v51, v15
	v_cvt_pk_bf16_f32 v2, v2, s0
	ds_write_b16 v97, v2 offset:192
	v_mul_f32_e32 v2, v68, v16
	v_cvt_pk_bf16_f32 v2, v2, s0
	ds_write_b16 v97, v2 offset:256
	v_mul_f32_e32 v2, v52, v16
	v_cvt_pk_bf16_f32 v2, v2, s0
	ds_write_b16 v97, v2 offset:320
	v_mul_f32_e32 v2, v69, v17
	v_cvt_pk_bf16_f32 v2, v2, s0
	ds_write_b16 v97, v2 offset:384
	v_mul_f32_e32 v2, v53, v17
	v_cvt_pk_bf16_f32 v2, v2, s0
	ds_write_b16 v97, v2 offset:448
	v_mul_f32_e32 v2, v70, v82
	v_cvt_pk_bf16_f32 v2, v2, s0
	ds_write_b16 v97, v2 offset:1024
	v_mul_f32_e32 v2, v54, v82
	v_cvt_pk_bf16_f32 v2, v2, s0
	ds_write_b16 v97, v2 offset:1088
	v_mul_f32_e32 v2, v71, v83
	v_cvt_pk_bf16_f32 v2, v2, s0
	ds_write_b16 v97, v2 offset:1152
	v_mul_f32_e32 v2, v55, v83
	v_cvt_pk_bf16_f32 v2, v2, s0
	ds_write_b16 v97, v2 offset:1216
	v_mul_f32_e32 v2, v72, v84
	v_cvt_pk_bf16_f32 v2, v2, s0
	ds_write_b16 v97, v2 offset:1280
	v_mul_f32_e32 v2, v56, v84
	v_cvt_pk_bf16_f32 v2, v2, s0
	ds_write_b16 v97, v2 offset:1344
	v_mul_f32_e32 v2, v73, v85
	v_cvt_pk_bf16_f32 v2, v2, s0
	ds_write_b16 v97, v2 offset:1408
	v_mul_f32_e32 v2, v57, v85
	v_cvt_pk_bf16_f32 v2, v2, s0
	v_rcp_f32_e32 v87, v5
	ds_write_b16 v97, v2 offset:1472
	v_mul_f32_e32 v2, v74, v86
	v_cvt_pk_bf16_f32 v2, v2, s0
	ds_write_b16 v97, v2 offset:2048
	v_mul_f32_e32 v2, v58, v86
	v_cvt_pk_bf16_f32 v2, v2, s0
	v_rcp_f32_e32 v88, v6
	ds_write_b16 v97, v2 offset:2112
	v_mul_f32_e32 v2, v75, v87
	v_cvt_pk_bf16_f32 v2, v2, s0
	ds_write_b16 v97, v2 offset:2176
	v_mul_f32_e32 v2, v59, v87
	v_cvt_pk_bf16_f32 v2, v2, s0
	v_rcp_f32_e32 v89, v7
	ds_write_b16 v97, v2 offset:2240
	v_mul_f32_e32 v2, v76, v88
	v_cvt_pk_bf16_f32 v2, v2, s0
	ds_write_b16 v97, v2 offset:2304
	v_mul_f32_e32 v2, v60, v88
	v_cvt_pk_bf16_f32 v2, v2, s0
	s_waitcnt lgkmcnt(14)
	v_rcp_f32_e32 v90, v8
	ds_write_b16 v97, v2 offset:2368
	v_mul_f32_e32 v2, v77, v89
	v_cvt_pk_bf16_f32 v2, v2, s0
	ds_write_b16 v97, v2 offset:2432
	v_mul_f32_e32 v2, v61, v89
	v_cvt_pk_bf16_f32 v2, v2, s0
	v_rcp_f32_e32 v91, v9
	ds_write_b16 v97, v2 offset:2496
	v_mul_f32_e32 v2, v78, v90
	v_cvt_pk_bf16_f32 v2, v2, s0
	ds_write_b16 v97, v2 offset:3072
	v_mul_f32_e32 v2, v62, v90
	v_cvt_pk_bf16_f32 v2, v2, s0
	v_rcp_f32_e32 v92, v10
	ds_write_b16 v97, v2 offset:3136
	v_mul_f32_e32 v2, v79, v91
	v_cvt_pk_bf16_f32 v2, v2, s0
	ds_write_b16 v97, v2 offset:3200
	v_mul_f32_e32 v2, v63, v91
	v_cvt_pk_bf16_f32 v2, v2, s0
	v_rcp_f32_e32 v93, v11
	ds_write_b16 v97, v2 offset:3264
	v_mul_f32_e32 v2, v80, v92
	v_cvt_pk_bf16_f32 v2, v2, s0
	ds_write_b16 v97, v2 offset:3328
	v_mul_f32_e32 v2, v64, v92
	v_cvt_pk_bf16_f32 v2, v2, s0
	ds_write_b16 v97, v2 offset:3392
	v_mul_f32_e32 v2, v81, v93
	v_cvt_pk_bf16_f32 v2, v2, s0
	ds_write_b16 v97, v2 offset:3456
	v_mul_f32_e32 v2, v65, v93
	v_lshrrev_b32_e32 v94, 3, v230
	v_cvt_pk_bf16_f32 v2, v2, s0
	ds_write_b16 v97, v2 offset:3520
	v_or_b32_e32 v52, 8, v94
	v_lshl_add_u32 v96, v94, 7, v95
	s_waitcnt lgkmcnt(0)
	v_lshl_add_u32 v58, v52, 7, v95
	ds_read_b128 v[4:7], v96
	ds_read_b128 v[8:11], v58
	v_lshlrev_b32_e32 v2, 11, v94
	v_lshl_add_u64 v[50:51], v[12:13], 0, v[2:3]
	v_lshlrev_b32_e32 v2, 11, v52
	v_lshl_add_u64 v[52:53], v[12:13], 0, v[2:3]
	v_or_b32_e32 v2, 16, v94
	v_or_b32_e32 v56, 24, v94
	v_lshl_add_u32 v59, v2, 7, v95
	v_lshl_add_u32 v60, v56, 7, v95
	s_waitcnt lgkmcnt(1)
	global_store_dwordx4 v[50:51], v[4:7], off
	ds_read_b128 v[4:7], v59
	s_waitcnt lgkmcnt(1)
	global_store_dwordx4 v[52:53], v[8:11], off
	ds_read_b128 v[8:11], v60
	v_lshlrev_b32_e32 v2, 11, v2
	v_lshl_add_u64 v[54:55], v[12:13], 0, v[2:3]
	v_lshlrev_b32_e32 v2, 11, v56
	v_lshl_add_u64 v[56:57], v[12:13], 0, v[2:3]
	v_mul_f32_e32 v2, v34, v14
	s_waitcnt lgkmcnt(1)
	global_store_dwordx4 v[54:55], v[4:7], off
	s_waitcnt lgkmcnt(0)
	global_store_dwordx4 v[56:57], v[8:11], off
	v_cvt_pk_bf16_f32 v2, v2, s0
	s_waitcnt lgkmcnt(0)
	ds_write_b16 v97, v2
	v_mul_f32_e32 v2, v18, v14
	v_cvt_pk_bf16_f32 v2, v2, s0
	ds_write_b16 v97, v2 offset:64
	v_mul_f32_e32 v2, v35, v15
	v_cvt_pk_bf16_f32 v2, v2, s0
	ds_write_b16 v97, v2 offset:128
	v_mul_f32_e32 v2, v19, v15
	v_cvt_pk_bf16_f32 v2, v2, s0
	ds_write_b16 v97, v2 offset:192
	v_mul_f32_e32 v2, v36, v16
	v_cvt_pk_bf16_f32 v2, v2, s0
	ds_write_b16 v97, v2 offset:256
	v_mul_f32_e32 v2, v20, v16
	v_cvt_pk_bf16_f32 v2, v2, s0
	ds_write_b16 v97, v2 offset:320
	v_mul_f32_e32 v2, v37, v17
	v_cvt_pk_bf16_f32 v2, v2, s0
	ds_write_b16 v97, v2 offset:384
	v_mul_f32_e32 v2, v21, v17
	v_cvt_pk_bf16_f32 v2, v2, s0
	ds_write_b16 v97, v2 offset:448
	v_mul_f32_e32 v2, v38, v82
	v_cvt_pk_bf16_f32 v2, v2, s0
	ds_write_b16 v97, v2 offset:1024
	v_mul_f32_e32 v2, v22, v82
	v_cvt_pk_bf16_f32 v2, v2, s0
	ds_write_b16 v97, v2 offset:1088
	v_mul_f32_e32 v2, v39, v83
	v_cvt_pk_bf16_f32 v2, v2, s0
	ds_write_b16 v97, v2 offset:1152
	v_mul_f32_e32 v2, v23, v83
	v_cvt_pk_bf16_f32 v2, v2, s0
	ds_write_b16 v97, v2 offset:1216
	v_mul_f32_e32 v2, v40, v84
	v_cvt_pk_bf16_f32 v2, v2, s0
	ds_write_b16 v97, v2 offset:1280
	v_mul_f32_e32 v2, v24, v84
	v_cvt_pk_bf16_f32 v2, v2, s0
	ds_write_b16 v97, v2 offset:1344
	v_mul_f32_e32 v2, v41, v85
	v_cvt_pk_bf16_f32 v2, v2, s0
	ds_write_b16 v97, v2 offset:1408
	v_mul_f32_e32 v2, v25, v85
	v_cvt_pk_bf16_f32 v2, v2, s0
	ds_write_b16 v97, v2 offset:1472
	v_mul_f32_e32 v2, v42, v86
	v_cvt_pk_bf16_f32 v2, v2, s0
	ds_write_b16 v97, v2 offset:2048
	v_mul_f32_e32 v2, v26, v86
	v_cvt_pk_bf16_f32 v2, v2, s0
	ds_write_b16 v97, v2 offset:2112
	v_mul_f32_e32 v2, v43, v87
	v_cvt_pk_bf16_f32 v2, v2, s0
	ds_write_b16 v97, v2 offset:2176
	v_mul_f32_e32 v2, v27, v87
	v_cvt_pk_bf16_f32 v2, v2, s0
	ds_write_b16 v97, v2 offset:2240
	v_mul_f32_e32 v2, v44, v88
	v_cvt_pk_bf16_f32 v2, v2, s0
	ds_write_b16 v97, v2 offset:2304
	v_mul_f32_e32 v2, v28, v88
	v_cvt_pk_bf16_f32 v2, v2, s0
	ds_write_b16 v97, v2 offset:2368
	v_mul_f32_e32 v2, v45, v89
	v_cvt_pk_bf16_f32 v2, v2, s0
	ds_write_b16 v97, v2 offset:2432
	v_mul_f32_e32 v2, v29, v89
	v_cvt_pk_bf16_f32 v2, v2, s0
	ds_write_b16 v97, v2 offset:2496
	v_mul_f32_e32 v2, v46, v90
	v_cvt_pk_bf16_f32 v2, v2, s0
	ds_write_b16 v97, v2 offset:3072
	v_mul_f32_e32 v2, v30, v90
	v_cvt_pk_bf16_f32 v2, v2, s0
	ds_write_b16 v97, v2 offset:3136
	v_mul_f32_e32 v2, v47, v91
	v_cvt_pk_bf16_f32 v2, v2, s0
	ds_write_b16 v97, v2 offset:3200
	v_mul_f32_e32 v2, v31, v91
	v_cvt_pk_bf16_f32 v2, v2, s0
	ds_write_b16 v97, v2 offset:3264
	v_mul_f32_e32 v2, v48, v92
	v_cvt_pk_bf16_f32 v2, v2, s0
	ds_write_b16 v97, v2 offset:3328
	v_mul_f32_e32 v2, v32, v92
	v_cvt_pk_bf16_f32 v2, v2, s0
	ds_write_b16 v97, v2 offset:3392
	v_mul_f32_e32 v2, v49, v93
	v_cvt_pk_bf16_f32 v2, v2, s0
	ds_write_b16 v97, v2 offset:3456
	v_mul_f32_e32 v2, v33, v93
	v_cvt_pk_bf16_f32 v2, v2, s0
	ds_write_b16 v97, v2 offset:3520
	s_waitcnt lgkmcnt(0)
	ds_read_b128 v[4:7], v96
	ds_read_b128 v[8:11], v58
	ds_read_b128 v[12:15], v59
	ds_read_b128 v[16:19], v60
	s_waitcnt lgkmcnt(3)
	global_store_dwordx4 v[50:51], v[4:7], off offset:128
	s_waitcnt lgkmcnt(2)
	global_store_dwordx4 v[52:53], v[8:11], off offset:128
	s_waitcnt lgkmcnt(1)
	global_store_dwordx4 v[54:55], v[12:15], off offset:128
	s_waitcnt lgkmcnt(0)
	global_store_dwordx4 v[56:57], v[16:19], off offset:128
	s_waitcnt lgkmcnt(0)
	s_waitcnt lgkmcnt(0)
	s_barrier
	s_cmp_lt_u32 s21, 2
	s_cbranch_scc1 .LBB0_259
	v_mov_b32_e32 v6, v0
	s_lshl_b32 s0, s82, 8
	v_ashrrev_i32_e32 v4, 1, v6
	s_or_b32 s0, s8, s0
	s_mov_b32 s1, s9
	v_ashrrev_i32_e32 v5, 31, v4
	v_lshl_add_u64 v[12:13], s[0:1], 0, v[4:5]
	v_lshlrev_b32_e32 v2, 6, v6
	v_lshlrev_b64 v[4:5], 11, v[12:13]
	v_and_b32_e32 v7, 64, v2
	v_lshl_add_u64 v[4:5], s[6:7], 0, v[4:5]
	v_lshlrev_b32_e32 v2, 1, v7
	v_lshl_add_u64 v[4:5], v[4:5], 0, v[2:3]
	s_waitcnt vmcnt(0)
	s_barrier
	global_load_dwordx2 v[16:17], v[4:5], off sc1
	global_load_dwordx2 v[18:19], v[4:5], off offset:256 sc1
	global_load_dwordx2 v[24:25], v[4:5], off offset:8 sc1
	global_load_dwordx2 v[26:27], v[4:5], off offset:264 sc1
	global_load_dwordx2 v[30:31], v[4:5], off offset:16 sc1
	global_load_dwordx2 v[34:35], v[4:5], off offset:272 sc1
	global_load_dwordx2 v[42:43], v[4:5], off offset:24 sc1
	global_load_dwordx2 v[50:51], v[4:5], off offset:280 sc1
	v_lshlrev_b32_e32 v6, 2, v6
	v_bitop3_b32 v83, v6, 4, v228 bitop3:0x6c
	v_lshlrev_b32_e32 v82, 2, v7
	global_load_dwordx2 v[54:55], v[4:5], off offset:32 sc1
	global_load_dwordx2 v[60:61], v[4:5], off offset:288 sc1
	global_load_dwordx2 v[74:75], v[4:5], off offset:40 sc1
	global_load_dwordx2 v[84:85], v[4:5], off offset:296 sc1
	global_load_dwordx2 v[86:87], v[4:5], off offset:48 sc1
	global_load_dwordx2 v[88:89], v[4:5], off offset:304 sc1
	global_load_dwordx2 v[90:91], v[4:5], off offset:56 sc1
	global_load_dwordx2 v[28:29], v[4:5], off offset:312 sc1
	global_load_dwordx2 v[58:59], v[4:5], off offset:64 sc1
	global_load_dwordx2 v[36:37], v[4:5], off offset:320 sc1
	global_load_dwordx2 v[66:67], v[4:5], off offset:72 sc1
	global_load_dwordx2 v[44:45], v[4:5], off offset:328 sc1
	global_load_dwordx2 v[62:63], v[4:5], off offset:80 sc1
	global_load_dwordx2 v[52:53], v[4:5], off offset:336 sc1
	global_load_dwordx2 v[76:77], v[4:5], off offset:88 sc1
	global_load_dwordx2 v[32:33], v[4:5], off offset:344 sc1
	global_load_dwordx2 v[68:69], v[4:5], off offset:96 sc1
	global_load_dwordx2 v[38:39], v[4:5], off offset:352 sc1
	global_load_dwordx2 v[80:81], v[4:5], off offset:104 sc1
	global_load_dwordx2 v[20:21], v[4:5], off offset:360 sc1
	global_load_dwordx2 v[46:47], v[4:5], off offset:112 sc1
	global_load_dwordx2 v[22:23], v[4:5], off offset:368 sc1
	global_load_dwordx2 v[56:57], v[4:5], off offset:120 sc1
	global_load_dwordx2 v[48:49], v[4:5], off offset:376 sc1
	s_nop 0
	global_load_dwordx4 v[4:7], v82, s[58:59] offset:16
	global_load_dwordx4 v[8:11], v82, s[58:59]
	v_mov_b64_e32 v[14:15], s[24:25]
	v_mad_u64_u32 v[14:15], s[0:1], v12, s5, v[14:15]
	v_mad_i32_i24 v15, v13, s5, v15
	v_lshl_add_u64 v[12:13], v[14:15], 0, v[2:3]
	s_mov_b32 s0, 0xf800000
	s_waitcnt vmcnt(33)
	v_lshlrev_b32_e32 v41, 16, v17
	v_lshlrev_b32_e32 v40, 16, v16
	s_waitcnt vmcnt(32)
	v_lshlrev_b32_e32 v65, 16, v19
	v_lshlrev_b32_e32 v64, 16, v18
	v_and_b32_e32 v17, 0xffff0000, v17
	v_and_b32_e32 v16, 0xffff0000, v16
	v_and_b32_e32 v19, 0xffff0000, v19
	v_and_b32_e32 v18, 0xffff0000, v18
	s_waitcnt vmcnt(29)
	v_lshlrev_b32_e32 v95, 16, v31
	v_lshlrev_b32_e32 v94, 16, v30
	s_waitcnt vmcnt(28)
	v_lshlrev_b32_e32 v97, 16, v35
	v_lshlrev_b32_e32 v96, 16, v34
	v_and_b32_e32 v31, 0xffff0000, v31
	v_and_b32_e32 v30, 0xffff0000, v30
	v_and_b32_e32 v35, 0xffff0000, v35
	v_and_b32_e32 v34, 0xffff0000, v34
	v_pk_fma_f32 v[72:73], v[214:215], v[18:19], v[16:17] neg_lo:[1,0,0] neg_hi:[1,0,0]
	v_pk_fma_f32 v[18:19], v[214:215], v[96:97], v[94:95] neg_lo:[1,0,0] neg_hi:[1,0,0]
	v_pk_fma_f32 v[16:17], v[214:215], v[34:35], v[30:31] neg_lo:[1,0,0] neg_hi:[1,0,0]
	v_lshlrev_b32_e32 v71, 16, v25
	v_lshlrev_b32_e32 v70, 16, v24
	v_lshlrev_b32_e32 v93, 16, v27
	v_lshlrev_b32_e32 v92, 16, v26
	v_and_b32_e32 v25, 0xffff0000, v25
	v_and_b32_e32 v24, 0xffff0000, v24
	v_and_b32_e32 v27, 0xffff0000, v27
	v_and_b32_e32 v26, 0xffff0000, v26
	v_mov_b32_e32 v30, v18
	v_mov_b32_e32 v31, v16
	v_mul_f32_e32 v34, v16, v16
	v_pk_fma_f32 v[78:79], v[214:215], v[64:65], v[40:41] neg_lo:[1,0,0] neg_hi:[1,0,0]
	v_pk_fma_f32 v[64:65], v[214:215], v[26:27], v[24:25] neg_lo:[1,0,0] neg_hi:[1,0,0]
	v_pk_fma_f32 v[30:31], v[30:31], v[30:31], v[34:35] op_sel_hi:[1,1,0]
	v_mov_b32_e32 v34, v19
	v_mov_b32_e32 v35, v17
	v_mul_f32_e32 v40, v17, v17
	v_pk_fma_f32 v[70:71], v[214:215], v[92:93], v[70:71] neg_lo:[1,0,0] neg_hi:[1,0,0]
	v_pk_mul_f32 v[24:25], v[72:73], v[72:73]
	v_pk_mul_f32 v[26:27], v[64:65], v[64:65]
	v_pk_fma_f32 v[34:35], v[34:35], v[34:35], v[40:41] op_sel_hi:[1,1,0]
	s_waitcnt vmcnt(27)
	v_lshlrev_b32_e32 v41, 16, v43
	v_lshlrev_b32_e32 v40, 16, v42
	s_waitcnt vmcnt(26)
	v_lshlrev_b32_e32 v93, 16, v51
	v_lshlrev_b32_e32 v92, 16, v50
	v_and_b32_e32 v43, 0xffff0000, v43
	v_and_b32_e32 v42, 0xffff0000, v42
	v_and_b32_e32 v51, 0xffff0000, v51
	v_and_b32_e32 v50, 0xffff0000, v50
	v_pk_fma_f32 v[24:25], v[78:79], v[78:79], v[24:25]
	v_pk_fma_f32 v[26:27], v[70:71], v[70:71], v[26:27]
	v_pk_fma_f32 v[40:41], v[214:215], v[92:93], v[40:41] neg_lo:[1,0,0] neg_hi:[1,0,0]
	v_pk_fma_f32 v[50:51], v[214:215], v[50:51], v[42:43] neg_lo:[1,0,0] neg_hi:[1,0,0]
	v_pk_add_f32 v[24:25], v[24:25], v[24:25] op_sel:[0,1] op_sel_hi:[1,0]
	v_pk_add_f32 v[26:27], v[26:27], v[26:27] op_sel:[0,1] op_sel_hi:[1,0]
	v_pk_mul_f32 v[42:43], v[40:41], v[40:41]
	v_pk_mul_f32 v[92:93], v[50:51], v[50:51]
	v_mov_b32_e32 v25, v42
	v_mov_b32_e32 v27, v92
	v_mov_b32_e32 v31, v43
	v_mov_b32_e32 v35, v93
	v_pk_add_f32 v[24:25], v[24:25], v[26:27]
	v_pk_add_f32 v[26:27], v[30:31], v[34:35]
	s_waitcnt vmcnt(24)
	v_and_b32_e32 v31, 0xffff0000, v61
	v_pk_add_f32 v[24:25], v[24:25], v[26:27]
	v_lshlrev_b32_e32 v27, 16, v61
	v_pk_add_f32 v[92:93], v[24:25], v[24:25] op_sel:[0,1] op_sel_hi:[1,0]
	v_lshlrev_b32_e32 v25, 16, v55
	v_lshlrev_b32_e32 v24, 16, v54
	v_lshlrev_b32_e32 v26, 16, v60
	v_pk_fma_f32 v[26:27], v[214:215], v[26:27], v[24:25] neg_lo:[1,0,0] neg_hi:[1,0,0]
	v_and_b32_e32 v25, 0xffff0000, v55
	v_and_b32_e32 v24, 0xffff0000, v54
	v_and_b32_e32 v30, 0xffff0000, v60
	v_pk_fma_f32 v[34:35], v[214:215], v[30:31], v[24:25] neg_lo:[1,0,0] neg_hi:[1,0,0]
	s_waitcnt vmcnt(22)
	v_lshlrev_b32_e32 v31, 16, v85
	v_pk_mul_f32 v[24:25], v[34:35], v[34:35]
	v_lshlrev_b32_e32 v30, 16, v84
	v_pk_fma_f32 v[24:25], v[26:27], v[26:27], v[24:25]
	s_waitcnt vmcnt(0)
	v_mov_b32_e32 v15, v10
	v_pk_add_f32 v[60:61], v[24:25], v[24:25] op_sel:[0,1] op_sel_hi:[1,0]
	v_lshlrev_b32_e32 v25, 16, v75
	v_lshlrev_b32_e32 v24, 16, v74
	v_pk_fma_f32 v[42:43], v[214:215], v[30:31], v[24:25] neg_lo:[1,0,0] neg_hi:[1,0,0]
	v_and_b32_e32 v25, 0xffff0000, v75
	v_and_b32_e32 v24, 0xffff0000, v74
	v_and_b32_e32 v31, 0xffff0000, v85
	v_and_b32_e32 v30, 0xffff0000, v84
	v_pk_fma_f32 v[54:55], v[214:215], v[30:31], v[24:25] neg_lo:[1,0,0] neg_hi:[1,0,0]
	v_mov_b32_e32 v24, v42
	v_mov_b32_e32 v25, v54
	v_mul_f32_e32 v30, v54, v54
	v_pk_fma_f32 v[74:75], v[24:25], v[24:25], v[30:31] op_sel_hi:[1,1,0]
	v_mov_b32_e32 v24, v43
	v_mov_b32_e32 v25, v55
	v_mul_f32_e32 v30, v55, v55
	v_pk_fma_f32 v[84:85], v[24:25], v[24:25], v[30:31] op_sel_hi:[1,1,0]
	v_lshlrev_b32_e32 v25, 16, v87
	v_lshlrev_b32_e32 v24, 16, v86
	v_lshlrev_b32_e32 v31, 16, v89
	v_lshlrev_b32_e32 v30, 16, v88
	v_pk_fma_f32 v[24:25], v[214:215], v[30:31], v[24:25] neg_lo:[1,0,0] neg_hi:[1,0,0]
	v_and_b32_e32 v31, 0xffff0000, v87
	v_and_b32_e32 v30, 0xffff0000, v86
	v_and_b32_e32 v87, 0xffff0000, v89
	v_and_b32_e32 v86, 0xffff0000, v88
	v_pk_fma_f32 v[30:31], v[214:215], v[86:87], v[30:31] neg_lo:[1,0,0] neg_hi:[1,0,0]
	v_pk_mul_f32 v[86:87], v[24:25], v[24:25]
	v_pk_mul_f32 v[88:89], v[30:31], v[30:31]
	v_mov_b32_e32 v93, v86
	v_mov_b32_e32 v61, v88
	v_mov_b32_e32 v75, v87
	v_mov_b32_e32 v85, v89
	v_pk_add_f32 v[60:61], v[92:93], v[60:61]
	v_pk_add_f32 v[74:75], v[74:75], v[84:85]
	v_lshlrev_b32_e32 v89, 16, v37
	v_pk_add_f32 v[60:61], v[60:61], v[74:75]
	v_lshlrev_b32_e32 v75, 16, v29
	v_pk_add_f32 v[84:85], v[60:61], v[60:61] op_sel:[0,1] op_sel_hi:[1,0]
	v_lshlrev_b32_e32 v61, 16, v91
	v_lshlrev_b32_e32 v60, 16, v90
	v_lshlrev_b32_e32 v74, 16, v28
	v_pk_fma_f32 v[60:61], v[214:215], v[74:75], v[60:61] neg_lo:[1,0,0] neg_hi:[1,0,0]
	v_and_b32_e32 v75, 0xffff0000, v91
	v_and_b32_e32 v74, 0xffff0000, v90
	v_and_b32_e32 v29, 0xffff0000, v29
	v_and_b32_e32 v28, 0xffff0000, v28
	v_pk_fma_f32 v[74:75], v[214:215], v[28:29], v[74:75] neg_lo:[1,0,0] neg_hi:[1,0,0]
	v_lshlrev_b32_e32 v88, 16, v36
	v_pk_mul_f32 v[28:29], v[74:75], v[74:75]
	v_and_b32_e32 v37, 0xffff0000, v37
	v_pk_fma_f32 v[28:29], v[60:61], v[60:61], v[28:29]
	v_and_b32_e32 v36, 0xffff0000, v36
	v_pk_add_f32 v[86:87], v[28:29], v[28:29] op_sel:[0,1] op_sel_hi:[1,0]
	v_lshlrev_b32_e32 v29, 16, v59
	v_lshlrev_b32_e32 v28, 16, v58
	v_and_b32_e32 v59, 0xffff0000, v59
	v_and_b32_e32 v58, 0xffff0000, v58
	v_pk_fma_f32 v[28:29], v[214:215], v[88:89], v[28:29] neg_lo:[1,0,0] neg_hi:[1,0,0]
	v_pk_fma_f32 v[36:37], v[214:215], v[36:37], v[58:59] neg_lo:[1,0,0] neg_hi:[1,0,0]
	v_mov_b32_e32 v58, v28
	v_mov_b32_e32 v59, v36
	v_mul_f32_e32 v88, v36, v36
	v_pk_fma_f32 v[88:89], v[58:59], v[58:59], v[88:89] op_sel_hi:[1,1,0]
	v_mov_b32_e32 v58, v29
	v_mov_b32_e32 v59, v37
	v_mul_f32_e32 v90, v37, v37
	v_pk_fma_f32 v[90:91], v[58:59], v[58:59], v[90:91] op_sel_hi:[1,1,0]
	v_lshlrev_b32_e32 v59, 16, v67
	v_lshlrev_b32_e32 v58, 16, v66
	v_lshlrev_b32_e32 v93, 16, v45
	v_lshlrev_b32_e32 v92, 16, v44
	v_and_b32_e32 v67, 0xffff0000, v67
	v_and_b32_e32 v66, 0xffff0000, v66
	v_and_b32_e32 v45, 0xffff0000, v45
	v_and_b32_e32 v44, 0xffff0000, v44
	v_pk_fma_f32 v[58:59], v[214:215], v[92:93], v[58:59] neg_lo:[1,0,0] neg_hi:[1,0,0]
	v_pk_fma_f32 v[66:67], v[214:215], v[44:45], v[66:67] neg_lo:[1,0,0] neg_hi:[1,0,0]
	v_pk_mul_f32 v[44:45], v[58:59], v[58:59]
	v_pk_mul_f32 v[92:93], v[66:67], v[66:67]
	v_mov_b32_e32 v85, v44
	v_mov_b32_e32 v87, v92
	v_mov_b32_e32 v89, v45
	v_mov_b32_e32 v91, v93
	v_pk_add_f32 v[84:85], v[84:85], v[86:87]
	v_pk_add_f32 v[44:45], v[88:89], v[90:91]
	v_lshlrev_b32_e32 v87, 16, v53
	v_pk_add_f32 v[44:45], v[84:85], v[44:45]
	v_lshlrev_b32_e32 v86, 16, v52
	v_pk_add_f32 v[84:85], v[44:45], v[44:45] op_sel:[0,1] op_sel_hi:[1,0]
	v_lshlrev_b32_e32 v45, 16, v63
	v_lshlrev_b32_e32 v44, 16, v62
	v_and_b32_e32 v63, 0xffff0000, v63
	v_and_b32_e32 v62, 0xffff0000, v62
	v_and_b32_e32 v53, 0xffff0000, v53
	v_and_b32_e32 v52, 0xffff0000, v52
	v_pk_fma_f32 v[52:53], v[214:215], v[52:53], v[62:63] neg_lo:[1,0,0] neg_hi:[1,0,0]
	v_pk_fma_f32 v[44:45], v[214:215], v[86:87], v[44:45] neg_lo:[1,0,0] neg_hi:[1,0,0]
	v_pk_mul_f32 v[62:63], v[52:53], v[52:53]
	v_lshlrev_b32_e32 v89, 16, v33
	v_pk_fma_f32 v[62:63], v[44:45], v[44:45], v[62:63]
	v_lshlrev_b32_e32 v88, 16, v32
	v_pk_add_f32 v[86:87], v[62:63], v[62:63] op_sel:[0,1] op_sel_hi:[1,0]
	v_lshlrev_b32_e32 v63, 16, v77
	v_lshlrev_b32_e32 v62, 16, v76
	v_and_b32_e32 v77, 0xffff0000, v77
	v_and_b32_e32 v76, 0xffff0000, v76
	v_and_b32_e32 v33, 0xffff0000, v33
	v_and_b32_e32 v32, 0xffff0000, v32
	v_pk_fma_f32 v[62:63], v[214:215], v[88:89], v[62:63] neg_lo:[1,0,0] neg_hi:[1,0,0]
	v_pk_fma_f32 v[76:77], v[214:215], v[32:33], v[76:77] neg_lo:[1,0,0] neg_hi:[1,0,0]
	v_mov_b32_e32 v32, v62
	v_mov_b32_e32 v33, v76
	v_mul_f32_e32 v88, v76, v76
	v_pk_fma_f32 v[88:89], v[32:33], v[32:33], v[88:89] op_sel_hi:[1,1,0]
	v_mov_b32_e32 v32, v63
	v_mov_b32_e32 v33, v77
	v_mul_f32_e32 v90, v77, v77
	v_pk_fma_f32 v[90:91], v[32:33], v[32:33], v[90:91] op_sel_hi:[1,1,0]
	v_lshlrev_b32_e32 v33, 16, v69
	v_lshlrev_b32_e32 v32, 16, v68
	v_lshlrev_b32_e32 v93, 16, v39
	v_lshlrev_b32_e32 v92, 16, v38
	v_and_b32_e32 v69, 0xffff0000, v69
	v_and_b32_e32 v68, 0xffff0000, v68
	v_and_b32_e32 v39, 0xffff0000, v39
	v_and_b32_e32 v38, 0xffff0000, v38
	v_pk_fma_f32 v[32:33], v[214:215], v[92:93], v[32:33] neg_lo:[1,0,0] neg_hi:[1,0,0]
	v_pk_fma_f32 v[38:39], v[214:215], v[38:39], v[68:69] neg_lo:[1,0,0] neg_hi:[1,0,0]
	v_pk_mul_f32 v[68:69], v[32:33], v[32:33]
	v_pk_mul_f32 v[92:93], v[38:39], v[38:39]
	v_mov_b32_e32 v85, v68
	v_mov_b32_e32 v87, v92
	v_mov_b32_e32 v89, v69
	v_mov_b32_e32 v91, v93
	v_pk_add_f32 v[84:85], v[84:85], v[86:87]
	v_pk_add_f32 v[68:69], v[88:89], v[90:91]
	v_lshlrev_b32_e32 v87, 16, v21
	v_pk_add_f32 v[68:69], v[84:85], v[68:69]
	v_lshlrev_b32_e32 v86, 16, v20
	v_pk_add_f32 v[84:85], v[68:69], v[68:69] op_sel:[0,1] op_sel_hi:[1,0]
	v_lshlrev_b32_e32 v69, 16, v81
	v_lshlrev_b32_e32 v68, 16, v80
	v_and_b32_e32 v81, 0xffff0000, v81
	v_and_b32_e32 v80, 0xffff0000, v80
	v_and_b32_e32 v21, 0xffff0000, v21
	v_and_b32_e32 v20, 0xffff0000, v20
	v_pk_fma_f32 v[80:81], v[214:215], v[20:21], v[80:81] neg_lo:[1,0,0] neg_hi:[1,0,0]
	v_pk_fma_f32 v[68:69], v[214:215], v[86:87], v[68:69] neg_lo:[1,0,0] neg_hi:[1,0,0]
	v_pk_mul_f32 v[20:21], v[80:81], v[80:81]
	v_lshlrev_b32_e32 v89, 16, v23
	v_pk_fma_f32 v[20:21], v[68:69], v[68:69], v[20:21]
	v_lshlrev_b32_e32 v88, 16, v22
	v_pk_add_f32 v[86:87], v[20:21], v[20:21] op_sel:[0,1] op_sel_hi:[1,0]
	v_lshlrev_b32_e32 v21, 16, v47
	v_lshlrev_b32_e32 v20, 16, v46
	v_and_b32_e32 v47, 0xffff0000, v47
	v_and_b32_e32 v46, 0xffff0000, v46
	v_and_b32_e32 v23, 0xffff0000, v23
	v_and_b32_e32 v22, 0xffff0000, v22
	v_pk_fma_f32 v[20:21], v[214:215], v[88:89], v[20:21] neg_lo:[1,0,0] neg_hi:[1,0,0]
	v_pk_fma_f32 v[22:23], v[214:215], v[22:23], v[46:47] neg_lo:[1,0,0] neg_hi:[1,0,0]
	v_mov_b32_e32 v46, v20
	v_mov_b32_e32 v47, v22
	v_mul_f32_e32 v88, v22, v22
	v_pk_fma_f32 v[88:89], v[46:47], v[46:47], v[88:89] op_sel_hi:[1,1,0]
	v_mov_b32_e32 v46, v21
	v_mov_b32_e32 v47, v23
	v_mul_f32_e32 v90, v23, v23
	v_pk_fma_f32 v[90:91], v[46:47], v[46:47], v[90:91] op_sel_hi:[1,1,0]
	v_lshlrev_b32_e32 v47, 16, v57
	v_lshlrev_b32_e32 v46, 16, v56
	v_lshlrev_b32_e32 v93, 16, v49
	v_lshlrev_b32_e32 v92, 16, v48
	v_and_b32_e32 v57, 0xffff0000, v57
	v_and_b32_e32 v56, 0xffff0000, v56
	v_and_b32_e32 v49, 0xffff0000, v49
	v_and_b32_e32 v48, 0xffff0000, v48
	v_pk_fma_f32 v[46:47], v[214:215], v[92:93], v[46:47] neg_lo:[1,0,0] neg_hi:[1,0,0]
	v_pk_fma_f32 v[48:49], v[214:215], v[48:49], v[56:57] neg_lo:[1,0,0] neg_hi:[1,0,0]
	v_pk_mul_f32 v[56:57], v[46:47], v[46:47]
	v_pk_mul_f32 v[92:93], v[48:49], v[48:49]
	v_mov_b32_e32 v85, v56
	v_mov_b32_e32 v87, v92
	v_mov_b32_e32 v89, v57
	v_mov_b32_e32 v91, v93
	v_pk_add_f32 v[84:85], v[84:85], v[86:87]
	v_pk_add_f32 v[56:57], v[88:89], v[90:91]
	v_mov_b32_e32 v10, v9
	v_pk_add_f32 v[56:57], v[84:85], v[56:57]
	s_nop 0
	v_add_f32_e32 v56, v56, v57
	ds_bpermute_b32 v57, v83, v56
	s_waitcnt lgkmcnt(0)
	v_add_f32_e32 v2, v56, v57
	v_fmamk_f32 v2, v2, 0x3c000000, v1
	v_mul_f32_e32 v14, 0x4f800000, v2
	v_cmp_gt_f32_e32 vcc, s0, v2
	s_nop 1
	v_cndmask_b32_e32 v2, v2, v14, vcc
	v_sqrt_f32_e32 v56, v2
	v_mov_b32_e32 v14, v8
	v_add_u32_e32 v8, -1, v56
	v_fma_f32 v9, -v8, v56, v2
	v_cmp_ge_f32_e64 s[0:1], 0, v9
	v_add_u32_e32 v9, 1, v56
	s_nop 0
	v_cndmask_b32_e64 v8, v56, v8, s[0:1]
	v_fma_f32 v56, -v9, v56, v2
	v_cmp_lt_f32_e64 s[0:1], 0, v56
	s_nop 1
	v_cndmask_b32_e64 v8, v8, v9, s[0:1]
	v_mul_f32_e32 v9, 0x37800000, v8
	v_cndmask_b32_e32 v8, v8, v9, vcc
	v_cmp_class_f32_e32 vcc, v2, v226
	v_mov_b32_e32 v9, v6
	v_mov_b32_e32 v6, v5
	v_cndmask_b32_e32 v2, v8, v2, vcc
	v_div_scale_f32 v56, s[0:1], v2, v2, 1.0
	v_rcp_f32_e32 v57, v56
	v_mov_b32_e32 v8, v4
	v_fma_f32 v4, -v56, v57, 1.0
	v_fmac_f32_e32 v57, v4, v57
	v_div_scale_f32 v4, vcc, 1.0, v2, 1.0
	v_mul_f32_e32 v5, v4, v57
	v_fma_f32 v83, -v56, v5, v4
	v_fmac_f32_e32 v5, v83, v57
	v_fma_f32 v4, -v56, v5, v4
	v_div_fmas_f32 v4, v4, v57, v5
	v_div_fixup_f32 v2, v4, v2, 1.0
	v_mul_f32_e32 v2, 0x3f4ccccd, v2
	v_pk_mul_f32 v[4:5], v[78:79], v[2:3] op_sel_hi:[1,0]
	v_pk_mul_f32 v[16:17], v[16:17], v[2:3] op_sel_hi:[1,0]
	v_pk_mul_f32 v[4:5], v[14:15], v[4:5]
	v_pk_mul_f32 v[14:15], v[72:73], v[2:3] op_sel_hi:[1,0]
	s_nop 0
	v_pk_mul_f32 v[10:11], v[10:11], v[14:15]
	v_pk_mul_f32 v[14:15], v[70:71], v[2:3] op_sel_hi:[1,0]
	v_bfe_u32 v56, v11, 16, 1
	v_pk_mul_f32 v[8:9], v[8:9], v[14:15]
	v_pk_mul_f32 v[14:15], v[64:65], v[2:3] op_sel_hi:[1,0]
	v_bfe_u32 v57, v10, 16, 1
	v_pk_mul_f32 v[6:7], v[6:7], v[14:15]
	v_add3_u32 v10, v10, v57, s81
	v_bfe_u32 v14, v7, 16, 1
	v_bfe_u32 v15, v6, 16, 1
	v_add3_u32 v11, v11, v56, s81
	v_add3_u32 v6, v6, v15, s81
	v_add3_u32 v7, v7, v14, s81
	v_bfe_u32 v14, v4, 16, 1
	v_bfe_u32 v15, v5, 16, 1
	v_bfe_u32 v56, v8, 16, 1
	v_bfe_u32 v57, v9, 16, 1
	v_add3_u32 v9, v9, v57, s81
	v_add3_u32 v8, v8, v56, s81
	v_add3_u32 v5, v5, v15, s81
	v_add3_u32 v4, v4, v14, s81
	v_lshrrev_b32_e32 v4, 16, v4
	v_lshrrev_b32_e32 v5, 16, v5
	v_lshrrev_b32_e32 v8, 16, v8
	v_lshrrev_b32_e32 v9, 16, v9
	v_and_or_b32 v7, v7, s80, v9
	v_and_or_b32 v6, v6, s80, v8
	v_and_or_b32 v5, v11, s80, v5
	v_and_or_b32 v4, v10, s80, v4
	global_store_dwordx4 v[12:13], v[4:7], off offset:1024
	global_load_dwordx4 v[4:7], v82, s[58:59] offset:32
	s_nop 0
	global_load_dwordx4 v[8:11], v82, s[58:59] offset:48
	v_pk_mul_f32 v[14:15], v[18:19], v[2:3] op_sel_hi:[1,0]
	s_waitcnt vmcnt(1)
	v_mov_b32_e32 v19, v6
	v_mov_b32_e32 v6, v5
	v_mov_b32_e32 v18, v4
	v_pk_mul_f32 v[4:5], v[6:7], v[16:17]
	v_pk_mul_f32 v[6:7], v[40:41], v[2:3] op_sel_hi:[1,0]
	s_waitcnt vmcnt(0)
	v_mov_b32_e32 v16, v8
	v_mov_b32_e32 v17, v10
	v_pk_mul_f32 v[6:7], v[16:17], v[6:7]
	v_pk_mul_f32 v[16:17], v[50:51], v[2:3] op_sel_hi:[1,0]
	v_mov_b32_e32 v10, v9
	v_pk_mul_f32 v[8:9], v[10:11], v[16:17]
	v_pk_mul_f32 v[14:15], v[18:19], v[14:15]
	v_bfe_u32 v10, v9, 16, 1
	v_bfe_u32 v11, v8, 16, 1
	v_bfe_u32 v16, v5, 16, 1
	v_bfe_u32 v17, v4, 16, 1
	v_add3_u32 v4, v4, v17, s81
	v_add3_u32 v5, v5, v16, s81
	v_add3_u32 v8, v8, v11, s81
	v_add3_u32 v9, v9, v10, s81
	v_bfe_u32 v10, v14, 16, 1
	v_bfe_u32 v11, v15, 16, 1
	v_bfe_u32 v16, v6, 16, 1
	v_bfe_u32 v17, v7, 16, 1
	v_add3_u32 v7, v7, v17, s81
	v_add3_u32 v6, v6, v16, s81
	v_add3_u32 v11, v15, v11, s81
	v_add3_u32 v10, v14, v10, s81
	v_lshrrev_b32_e32 v10, 16, v10
	v_lshrrev_b32_e32 v11, 16, v11
	v_lshrrev_b32_e32 v6, 16, v6
	v_lshrrev_b32_e32 v7, 16, v7
	v_and_or_b32 v7, v9, s80, v7
	v_and_or_b32 v6, v8, s80, v6
	v_and_or_b32 v5, v5, s80, v11
	v_and_or_b32 v4, v4, s80, v10
	global_store_dwordx4 v[12:13], v[4:7], off offset:1040
	global_load_dwordx4 v[4:7], v82, s[58:59] offset:64
	s_nop 0
	global_load_dwordx4 v[8:11], v82, s[58:59] offset:80
	v_pk_mul_f32 v[14:15], v[26:27], v[2:3] op_sel_hi:[1,0]
	v_pk_mul_f32 v[18:19], v[62:63], v[2:3] op_sel_hi:[1,0]
	s_waitcnt vmcnt(1)
	v_mov_b32_e32 v16, v4
	v_mov_b32_e32 v17, v6
	v_pk_mul_f32 v[14:15], v[14:15], v[16:17]
	v_pk_mul_f32 v[16:17], v[34:35], v[2:3] op_sel_hi:[1,0]
	v_mov_b32_e32 v6, v5
	v_pk_mul_f32 v[4:5], v[16:17], v[6:7]
	v_pk_mul_f32 v[6:7], v[42:43], v[2:3] op_sel_hi:[1,0]
	s_waitcnt vmcnt(0)
	v_mov_b32_e32 v16, v8
	v_mov_b32_e32 v17, v10
	v_pk_mul_f32 v[6:7], v[6:7], v[16:17]
	v_pk_mul_f32 v[16:17], v[54:55], v[2:3] op_sel_hi:[1,0]
	v_mov_b32_e32 v10, v9
	v_pk_mul_f32 v[8:9], v[16:17], v[10:11]
	v_bfe_u32 v16, v5, 16, 1
	v_bfe_u32 v10, v9, 16, 1
	v_bfe_u32 v11, v8, 16, 1
	v_bfe_u32 v17, v4, 16, 1
	v_add3_u32 v4, v4, v17, s81
	v_add3_u32 v5, v5, v16, s81
	v_add3_u32 v8, v8, v11, s81
	v_add3_u32 v9, v9, v10, s81
	v_bfe_u32 v10, v14, 16, 1
	v_bfe_u32 v11, v15, 16, 1
	v_bfe_u32 v16, v6, 16, 1
	v_bfe_u32 v17, v7, 16, 1
	v_add3_u32 v7, v7, v17, s81
	v_add3_u32 v6, v6, v16, s81
	v_add3_u32 v11, v15, v11, s81
	v_add3_u32 v10, v14, v10, s81
	v_lshrrev_b32_e32 v10, 16, v10
	v_lshrrev_b32_e32 v11, 16, v11
	v_lshrrev_b32_e32 v6, 16, v6
	v_lshrrev_b32_e32 v7, 16, v7
	v_and_or_b32 v7, v9, s80, v7
	v_and_or_b32 v6, v8, s80, v6
	v_and_or_b32 v5, v5, s80, v11
	v_and_or_b32 v4, v4, s80, v10
	global_store_dwordx4 v[12:13], v[4:7], off offset:1056
	global_load_dwordx4 v[4:7], v82, s[58:59] offset:96
	s_nop 0
	global_load_dwordx4 v[8:11], v82, s[58:59] offset:112
	v_pk_mul_f32 v[14:15], v[24:25], v[2:3] op_sel_hi:[1,0]
	v_pk_mul_f32 v[24:25], v[76:77], v[2:3] op_sel_hi:[1,0]
	s_waitcnt vmcnt(1)
	v_mov_b32_e32 v16, v4
	v_mov_b32_e32 v17, v6
	v_pk_mul_f32 v[14:15], v[14:15], v[16:17]
	v_pk_mul_f32 v[16:17], v[30:31], v[2:3] op_sel_hi:[1,0]
	v_mov_b32_e32 v6, v5
	v_pk_mul_f32 v[4:5], v[16:17], v[6:7]
	v_pk_mul_f32 v[6:7], v[60:61], v[2:3] op_sel_hi:[1,0]
	s_waitcnt vmcnt(0)
	v_mov_b32_e32 v16, v8
	v_mov_b32_e32 v17, v10
	v_pk_mul_f32 v[6:7], v[6:7], v[16:17]
	v_pk_mul_f32 v[16:17], v[74:75], v[2:3] op_sel_hi:[1,0]
	v_mov_b32_e32 v10, v9
	v_pk_mul_f32 v[8:9], v[16:17], v[10:11]
	v_bfe_u32 v16, v5, 16, 1
	v_bfe_u32 v10, v9, 16, 1
	v_bfe_u32 v11, v8, 16, 1
	v_bfe_u32 v17, v4, 16, 1
	v_add3_u32 v4, v4, v17, s81
	v_add3_u32 v5, v5, v16, s81
	v_add3_u32 v8, v8, v11, s81
	v_add3_u32 v9, v9, v10, s81
	v_bfe_u32 v10, v14, 16, 1
	v_bfe_u32 v11, v15, 16, 1
	v_bfe_u32 v16, v6, 16, 1
	v_bfe_u32 v17, v7, 16, 1
	v_add3_u32 v7, v7, v17, s81
	v_add3_u32 v6, v6, v16, s81
	v_add3_u32 v11, v15, v11, s81
	v_add3_u32 v10, v14, v10, s81
	v_lshrrev_b32_e32 v10, 16, v10
	v_lshrrev_b32_e32 v11, 16, v11
	v_lshrrev_b32_e32 v6, 16, v6
	v_lshrrev_b32_e32 v7, 16, v7
	v_and_or_b32 v7, v9, s80, v7
	v_and_or_b32 v6, v8, s80, v6
	v_and_or_b32 v5, v5, s80, v11
	v_and_or_b32 v4, v4, s80, v10
	global_store_dwordx4 v[12:13], v[4:7], off offset:1072
	global_load_dwordx4 v[4:7], v82, s[58:59] offset:128
	s_nop 0
	global_load_dwordx4 v[8:11], v82, s[58:59] offset:144
	v_pk_mul_f32 v[14:15], v[28:29], v[2:3] op_sel_hi:[1,0]
	s_waitcnt vmcnt(1)
	v_mov_b32_e32 v16, v4
	v_mov_b32_e32 v17, v6
	v_pk_mul_f32 v[14:15], v[14:15], v[16:17]
	v_pk_mul_f32 v[16:17], v[36:37], v[2:3] op_sel_hi:[1,0]
	v_mov_b32_e32 v6, v5
	v_pk_mul_f32 v[4:5], v[16:17], v[6:7]
	v_pk_mul_f32 v[6:7], v[58:59], v[2:3] op_sel_hi:[1,0]
	s_waitcnt vmcnt(0)
	v_mov_b32_e32 v16, v8
	v_mov_b32_e32 v17, v10
	v_pk_mul_f32 v[6:7], v[6:7], v[16:17]
	v_pk_mul_f32 v[16:17], v[66:67], v[2:3] op_sel_hi:[1,0]
	v_mov_b32_e32 v10, v9
	v_pk_mul_f32 v[8:9], v[16:17], v[10:11]
	v_bfe_u32 v16, v5, 16, 1
	v_bfe_u32 v10, v9, 16, 1
	v_bfe_u32 v11, v8, 16, 1
	v_bfe_u32 v17, v4, 16, 1
	v_add3_u32 v4, v4, v17, s81
	v_add3_u32 v5, v5, v16, s81
	v_add3_u32 v8, v8, v11, s81
	v_add3_u32 v9, v9, v10, s81
	v_bfe_u32 v10, v14, 16, 1
	v_bfe_u32 v11, v15, 16, 1
	v_bfe_u32 v16, v6, 16, 1
	v_bfe_u32 v17, v7, 16, 1
	v_add3_u32 v7, v7, v17, s81
	v_add3_u32 v6, v6, v16, s81
	v_add3_u32 v11, v15, v11, s81
	v_add3_u32 v10, v14, v10, s81
	v_lshrrev_b32_e32 v10, 16, v10
	v_lshrrev_b32_e32 v11, 16, v11
	v_lshrrev_b32_e32 v6, 16, v6
	v_lshrrev_b32_e32 v7, 16, v7
	v_and_or_b32 v7, v9, s80, v7
	v_and_or_b32 v6, v8, s80, v6
	v_and_or_b32 v5, v5, s80, v11
	v_and_or_b32 v4, v4, s80, v10
	global_store_dwordx4 v[12:13], v[4:7], off offset:1088
	global_load_dwordx4 v[4:7], v82, s[58:59] offset:160
	s_nop 0
	global_load_dwordx4 v[8:11], v82, s[58:59] offset:176
	v_pk_mul_f32 v[16:17], v[52:53], v[2:3] op_sel_hi:[1,0]
	v_pk_mul_f32 v[14:15], v[44:45], v[2:3] op_sel_hi:[1,0]
	s_waitcnt vmcnt(1)
	v_mov_b32_e32 v27, v6
	v_mov_b32_e32 v6, v5
	s_waitcnt vmcnt(0)
	v_mov_b32_e32 v5, v10
	v_mov_b32_e32 v10, v9
	v_mov_b32_e32 v26, v4
	v_mov_b32_e32 v4, v8
	v_pk_mul_f32 v[6:7], v[16:17], v[6:7]
	v_pk_mul_f32 v[10:11], v[24:25], v[10:11]
	v_pk_mul_f32 v[8:9], v[14:15], v[26:27]
	v_pk_mul_f32 v[4:5], v[18:19], v[4:5]
	v_bfe_u32 v14, v11, 16, 1
	v_bfe_u32 v15, v10, 16, 1
	v_bfe_u32 v16, v7, 16, 1
	v_bfe_u32 v17, v6, 16, 1
	v_add3_u32 v17, v6, v17, s81
	v_add3_u32 v16, v7, v16, s81
	v_add3_u32 v6, v10, v15, s81
	v_add3_u32 v7, v11, v14, s81
	v_bfe_u32 v10, v8, 16, 1
	v_bfe_u32 v11, v9, 16, 1
	v_bfe_u32 v14, v4, 16, 1
	v_bfe_u32 v15, v5, 16, 1
	v_add3_u32 v5, v5, v15, s81
	v_add3_u32 v4, v4, v14, s81
	v_add3_u32 v9, v9, v11, s81
	v_add3_u32 v8, v8, v10, s81
	v_lshrrev_b32_e32 v8, 16, v8
	v_lshrrev_b32_e32 v9, 16, v9
	v_lshrrev_b32_e32 v4, 16, v4
	v_lshrrev_b32_e32 v5, 16, v5
	v_and_or_b32 v7, v7, s80, v5
	v_and_or_b32 v6, v6, s80, v4
	v_and_or_b32 v5, v16, s80, v9
	v_and_or_b32 v4, v17, s80, v8
	global_store_dwordx4 v[12:13], v[4:7], off offset:1104
	global_load_dwordx4 v[4:7], v82, s[58:59] offset:192
	s_nop 0
	global_load_dwordx4 v[8:11], v82, s[58:59] offset:208
	v_pk_mul_f32 v[14:15], v[32:33], v[2:3] op_sel_hi:[1,0]
	v_pk_mul_f32 v[18:19], v[68:69], v[2:3] op_sel_hi:[1,0]
	v_pk_mul_f32 v[16:17], v[38:39], v[2:3] op_sel_hi:[1,0]
	v_pk_mul_f32 v[24:25], v[80:81], v[2:3] op_sel_hi:[1,0]
	s_waitcnt vmcnt(1)
	v_mov_b32_e32 v26, v4
	v_mov_b32_e32 v27, v6
	v_mov_b32_e32 v6, v5
	s_waitcnt vmcnt(0)
	v_mov_b32_e32 v4, v8
	v_mov_b32_e32 v5, v10
	v_mov_b32_e32 v10, v9
	v_pk_mul_f32 v[8:9], v[14:15], v[26:27]
	v_pk_mul_f32 v[4:5], v[18:19], v[4:5]
	v_pk_mul_f32 v[6:7], v[16:17], v[6:7]
	v_pk_mul_f32 v[10:11], v[24:25], v[10:11]
	v_bfe_u32 v18, v8, 16, 1
	v_bfe_u32 v19, v9, 16, 1
	v_bfe_u32 v24, v4, 16, 1
	v_bfe_u32 v25, v5, 16, 1
	v_bfe_u32 v14, v11, 16, 1
	v_bfe_u32 v15, v10, 16, 1
	v_bfe_u32 v16, v7, 16, 1
	v_bfe_u32 v17, v6, 16, 1
	v_add3_u32 v5, v5, v25, s81
	v_add3_u32 v4, v4, v24, s81
	v_add3_u32 v9, v9, v19, s81
	v_add3_u32 v8, v8, v18, s81
	v_add3_u32 v17, v6, v17, s81
	v_add3_u32 v16, v7, v16, s81
	v_add3_u32 v6, v10, v15, s81
	v_add3_u32 v7, v11, v14, s81
	v_lshrrev_b32_e32 v8, 16, v8
	v_lshrrev_b32_e32 v9, 16, v9
	v_lshrrev_b32_e32 v4, 16, v4
	v_lshrrev_b32_e32 v5, 16, v5
	v_and_or_b32 v7, v7, s80, v5
	v_and_or_b32 v6, v6, s80, v4
	v_and_or_b32 v5, v16, s80, v9
	v_and_or_b32 v4, v17, s80, v8
	global_store_dwordx4 v[12:13], v[4:7], off offset:1120
	global_load_dwordx4 v[4:7], v82, s[58:59] offset:224
	s_nop 0
	global_load_dwordx4 v[8:11], v82, s[58:59] offset:240
	v_pk_mul_f32 v[14:15], v[20:21], v[2:3] op_sel_hi:[1,0]
	v_pk_mul_f32 v[16:17], v[22:23], v[2:3] op_sel_hi:[1,0]
	v_pk_mul_f32 v[18:19], v[46:47], v[2:3] op_sel_hi:[1,0]
	v_pk_mul_f32 v[20:21], v[48:49], v[2:3] op_sel_hi:[1,0]
	s_waitcnt vmcnt(1)
	v_mov_b32_e32 v22, v4
	v_mov_b32_e32 v23, v6
	v_mov_b32_e32 v6, v5
	s_waitcnt vmcnt(0)
	v_mov_b32_e32 v4, v8
	v_mov_b32_e32 v5, v10
	v_mov_b32_e32 v10, v9
	v_pk_mul_f32 v[8:9], v[14:15], v[22:23]
	v_pk_mul_f32 v[6:7], v[16:17], v[6:7]
	v_pk_mul_f32 v[4:5], v[18:19], v[4:5]
	v_pk_mul_f32 v[10:11], v[20:21], v[10:11]
	v_bfe_u32 v15, v7, 16, 1
	v_bfe_u32 v17, v8, 16, 1
	v_bfe_u32 v18, v9, 16, 1
	v_bfe_u32 v19, v4, 16, 1
	v_bfe_u32 v14, v10, 16, 1
	v_bfe_u32 v16, v6, 16, 1
	v_add3_u32 v15, v7, v15, s81
	v_add3_u32 v4, v4, v19, s81
	v_add3_u32 v7, v9, v18, s81
	v_add3_u32 v8, v8, v17, s81
	v_add3_u32 v16, v6, v16, s81
	v_add3_u32 v6, v10, v14, s81
	v_lshrrev_b32_e32 v8, 16, v8
	v_lshrrev_b32_e32 v9, 16, v7
	v_lshrrev_b32_e32 v4, 16, v4
	v_cvt_pk_bf16_f32 v7, v5, v11
	v_and_or_b32 v6, v6, s80, v4
	v_and_or_b32 v5, v15, s80, v9
	v_and_or_b32 v4, v16, s80, v8
	global_store_dwordx4 v[12:13], v[4:7], off offset:1136
	s_branch .LBB0_259

.LBB0_377:
	s_or_b64 exec, exec, s[20:21]
	v_min_i32_e32 v34, 2, v56
	v_cvt_f32_i32_e32 v34, v34
	v_lshlrev_b32_e32 v35, 2, v59
	v_add3_u32 v53, 0, v50, v35
	v_lshlrev_b32_e32 v51, 1, v59
	v_div_scale_f32 v46, s[20:21], v34, v34, 1.0
	v_rcp_f32_e32 v47, v46
	v_div_scale_f32 v35, vcc, 1.0, v34, 1.0
	s_movk_i32 s20, 0x90
	v_fma_f32 v48, -v46, v47, 1.0
	v_fmac_f32_e32 v47, v48, v47
	v_mul_f32_e32 v48, v35, v47
	v_fma_f32 v49, -v46, v48, v35
	v_fmac_f32_e32 v48, v49, v47
	v_fma_f32 v35, -v46, v48, v35
	v_div_fmas_f32 v35, v35, v47, v48
	ds_read_b128 v[46:49], v53 offset:3840
	v_div_fixup_f32 v34, v35, v34, 1.0
	v_mul_lo_u32 v35, v58, s20
	v_add3_u32 v51, 0, v35, v51
	s_movk_i32 s20, 0x7fff
	s_waitcnt lgkmcnt(0)
	v_xor_b32_e32 v49, 0x80000000, v49
	v_xor_b32_e32 v48, 0x80000000, v48
	v_pk_fma_f32 v[44:45], v[34:35], v[44:45], v[46:47] op_sel_hi:[0,1,1] neg_lo:[0,0,1] neg_hi:[0,0,1]
	v_pk_fma_f32 v[36:37], v[34:35], v[36:37], v[48:49] op_sel_hi:[0,1,1]
	s_mov_b32 s21, 0xffff0000
	v_cvt_pk_bf16_f32 v44, v44, v45
	v_cvt_pk_bf16_f32 v45, v36, v37
	ds_write_b64 v51, v[44:45] offset:40960
	v_mov_b32_e32 v45, 0
	v_mov_b32_e32 v44, v45
	v_mov_b32_e32 v37, v45
	v_mov_b32_e32 v36, v45
	s_and_saveexec_b64 s[20:21], s[2:3]
	s_cbranch_execz .LBB0_381
	v_lshlrev_b32_e32 v35, 6, v1
	v_add3_u32 v35, v50, v35, 0
	v_mov_b32_e32 v36, 0
	v_add_u32_e32 v35, 0xf10, v35
	s_mov_b64 s[22:23], 0
	v_mov_b32_e32 v46, v39
	v_mov_b32_e32 v37, v36
	v_mov_b32_e32 v44, v36
	v_mov_b32_e32 v45, v36

.LBB0_381:
	s_or_b64 exec, exec, s[20:21]
	ds_read_b128 v[46:49], v53 offset:3856
	v_mov_b32_e32 v35, v34
	s_movk_i32 s20, 0x7fff
	v_mov_b32_e32 v60, v34
	v_mov_b32_e32 v61, v34
	s_waitcnt lgkmcnt(0)
	v_pk_fma_f32 v[36:37], v[34:35], v[36:37], v[46:47] neg_lo:[0,0,1] neg_hi:[0,0,1]
	v_xor_b32_e32 v49, 0x80000000, v49
	v_xor_b32_e32 v48, 0x80000000, v48
	v_pk_fma_f32 v[44:45], v[60:61], v[44:45], v[48:49]
	s_mov_b32 s21, 0xffff0000
	v_cvt_pk_bf16_f32 v36, v36, v37
	v_cvt_pk_bf16_f32 v37, v44, v45
	v_mov_b32_e32 v45, 0
	ds_write_b64 v51, v[36:37] offset:40968
	v_mov_b32_e32 v44, v45
	v_mov_b32_e32 v37, v45
	v_mov_b32_e32 v36, v45
	s_and_saveexec_b64 s[20:21], s[2:3]
	s_cbranch_execz .LBB0_385
	v_lshlrev_b32_e32 v36, 6, v1
	v_add3_u32 v36, v50, v36, 0
	v_add_u32_e32 v46, 0xf20, v36
	v_mov_b32_e32 v36, 0
	s_mov_b64 s[22:23], 0
	v_mov_b32_e32 v47, v39
	v_mov_b32_e32 v37, v36
	v_mov_b32_e32 v44, v36
	v_mov_b32_e32 v45, v36

.LBB0_385:
	s_or_b64 exec, exec, s[20:21]
	ds_read_b128 v[46:49], v53 offset:3872
	s_movk_i32 s20, 0x7fff
	v_mov_b32_e32 v60, v34
	v_mov_b32_e32 v61, v34
	s_mov_b32 s21, 0xffff0000
	s_waitcnt lgkmcnt(0)
	v_pk_fma_f32 v[36:37], v[34:35], v[36:37], v[46:47] neg_lo:[0,0,1] neg_hi:[0,0,1]
	v_xor_b32_e32 v49, 0x80000000, v49
	v_xor_b32_e32 v48, 0x80000000, v48
	v_pk_fma_f32 v[44:45], v[60:61], v[44:45], v[48:49]
	v_cvt_pk_bf16_f32 v36, v36, v37
	v_cvt_pk_bf16_f32 v37, v44, v45
	v_mov_b32_e32 v45, 0
	ds_write_b64 v51, v[36:37] offset:40976
	v_mov_b32_e32 v44, v45
	v_mov_b32_e32 v37, v45
	v_mov_b32_e32 v36, v45
	s_and_saveexec_b64 s[20:21], s[2:3]
	s_cbranch_execz .LBB0_389
	v_lshlrev_b32_e32 v36, 6, v1
	v_add3_u32 v36, v50, v36, 0
	v_add_u32_e32 v46, 0xf30, v36
	v_mov_b32_e32 v36, 0
	s_mov_b64 s[22:23], 0
	v_mov_b32_e32 v37, v36
	v_mov_b32_e32 v44, v36
	v_mov_b32_e32 v45, v36

.LBB0_389:
	s_or_b64 exec, exec, s[20:21]
	ds_read_b128 v[46:49], v53 offset:3888
	v_mov_b32_e32 v60, v34
	v_mov_b32_e32 v61, v34
	s_movk_i32 s22, 0x7fff
	s_mov_b32 s23, 0xffff0000
	s_waitcnt lgkmcnt(0)
	v_pk_fma_f32 v[34:35], v[34:35], v[36:37], v[46:47] neg_lo:[0,0,1] neg_hi:[0,0,1]
	v_xor_b32_e32 v49, 0x80000000, v49
	v_xor_b32_e32 v48, 0x80000000, v48
	v_pk_fma_f32 v[44:45], v[60:61], v[44:45], v[48:49]
	v_or_b32_e32 v68, s36, v55
	s_movk_i32 s20, 0x90
	v_cvt_pk_bf16_f32 v34, v34, v35
	v_mul_lo_u32 v39, v68, s20
	v_add_u32_e32 v39, 0, v39
	v_cvt_pk_bf16_f32 v35, v44, v45
	v_add_u32_e32 v55, v39, v38
	ds_write_b64 v51, v[34:35] offset:40984
	s_waitcnt lgkmcnt(0)
	s_barrier
	ds_read_b128 v[34:37], v55 offset:40960
	ds_read_b128 v[44:47], v55 offset:41024
	s_waitcnt vmcnt(10) lgkmcnt(1)
	v_mfma_f32_16x16x32_bf16 v[60:63], v[26:29], v[34:37], 0
	v_lshlrev_b32_e32 v26, 4, v41
	v_ashrrev_i32_e32 v69, 31, v68
	s_waitcnt vmcnt(9)
	v_mfma_f32_16x16x32_bf16 v[30:33], v[30:33], v[34:37], 0
	s_movk_i32 s26, 0x1200
	v_mov_b64_e32 v[28:29], s[10:11]
	v_lshl_add_u64 v[38:39], s[0:1], 0, v[68:69]
	s_waitcnt lgkmcnt(0)
	v_mfma_f32_16x16x32_bf16 v[14:17], v[14:17], v[44:47], v[30:33]
	v_mad_u64_u32 v[28:29], s[20:21], v38, s26, v[28:29]
	v_mov_b32_e32 v41, 0
	v_mad_i32_i24 v29, v39, s26, v29
	v_lshl_add_u64 v[38:39], v[28:29], 0, v[40:41]
	s_waitcnt vmcnt(8)
	v_mfma_f32_16x16x32_bf16 v[10:13], v[10:13], v[44:47], v[60:63]
	s_waitcnt vmcnt(0)
	s_nop 0
	v_pk_mul_f32 v[16:17], v[16:17], v[102:103]
	v_pk_mul_f32 v[14:15], v[14:15], v[100:101]
	v_cvt_pk_bf16_f32 v14, v14, v15
	v_cvt_pk_bf16_f32 v15, v16, v17
	global_store_dwordx2 v[38:39], v[14:15], off offset:512
	v_mfma_f32_16x16x32_bf16 v[22:25], v[22:25], v[34:37], 0
	v_mov_b32_e32 v27, v41
	v_pk_mul_f32 v[12:13], v[12:13], v[106:107]
	v_pk_mul_f32 v[10:11], v[10:11], v[104:105]
	v_cvt_pk_bf16_f32 v10, v10, v11
	v_cvt_pk_bf16_f32 v11, v12, v13
	global_store_dwordx2 v[38:39], v[10:11], off offset:544
	v_mfma_f32_16x16x32_bf16 v[6:9], v[6:9], v[44:47], v[22:25]
	v_mfma_f32_16x16x32_bf16 v[18:21], v[18:21], v[34:37], 0
	v_mfma_f32_16x16x32_bf16 v[2:5], v[2:5], v[44:47], v[18:21]
	s_nop 5
	v_pk_mul_f32 v[8:9], v[8:9], v[110:111]
	v_pk_mul_f32 v[6:7], v[6:7], v[108:109]
	v_cvt_pk_bf16_f32 v6, v6, v7
	v_cvt_pk_bf16_f32 v7, v8, v9
	global_store_dwordx2 v[38:39], v[6:7], off offset:576
	v_pk_mul_f32 v[4:5], v[4:5], v[114:115]
	v_pk_mul_f32 v[2:3], v[2:3], v[112:113]
	v_cvt_pk_bf16_f32 v2, v2, v3
	v_cvt_pk_bf16_f32 v3, v4, v5
	global_store_dwordx2 v[38:39], v[2:3], off offset:608
	s_barrier
	v_lshlrev_b32_e32 v180, 16, v130
	v_and_b32_e32 v181, 0xffff0000, v130
	v_lshlrev_b32_e32 v182, 16, v131
	v_and_b32_e32 v183, 0xffff0000, v131
	v_lshlrev_b32_e32 v184, 16, v132
	v_and_b32_e32 v185, 0xffff0000, v132
	v_lshlrev_b32_e32 v186, 16, v133
	v_and_b32_e32 v187, 0xffff0000, v133
	v_lshlrev_b32_e32 v188, 16, v134
	v_and_b32_e32 v189, 0xffff0000, v134
	v_lshlrev_b32_e32 v190, 16, v135
	v_and_b32_e32 v191, 0xffff0000, v135
	v_lshlrev_b32_e32 v192, 16, v136
	v_and_b32_e32 v193, 0xffff0000, v136
	v_lshlrev_b32_e32 v194, 16, v137
	v_and_b32_e32 v195, 0xffff0000, v137
	v_lshlrev_b32_e32 v196, 16, v138
	v_and_b32_e32 v197, 0xffff0000, v138
	v_lshlrev_b32_e32 v198, 16, v139
	v_and_b32_e32 v199, 0xffff0000, v139
	v_lshlrev_b32_e32 v200, 16, v140
	v_and_b32_e32 v201, 0xffff0000, v140
	v_lshlrev_b32_e32 v202, 16, v141
	v_and_b32_e32 v203, 0xffff0000, v141
	ds_write_b128 v204, v[180:183]
	ds_write_b128 v204, v[184:187] offset:16
	ds_write_b128 v204, v[188:191] offset:16384
	ds_write_b128 v204, v[192:195] offset:16400
	s_mov_b64 s[98:99], exec
	v_cmp_gt_u32_e32 vcc, 0x78, v52
	s_and_b64 exec, s[98:99], vcc
	ds_write_b128 v204, v[196:199] offset:32768
	ds_write_b128 v204, v[200:203] offset:32784
	s_mov_b64 exec, s[98:99]
	v_add_co_u32_e32 v2, vcc, 0x2000, v42
	v_lshl_add_u64 v[40:41], s[64:65], 0, v[26:27]
	s_nop 0
	v_addc_co_u32_e32 v3, vcc, 0, v43, vcc
	global_load_dwordx4 v[18:21], v[2:3], off
	global_load_dwordx4 v[14:17], v[2:3], off offset:64
	global_load_dwordx4 v[22:25], v[2:3], off offset:2048
	global_load_dwordx4 v[10:13], v[2:3], off offset:2112
	v_add_co_u32_e32 v2, vcc, 0x3000, v42
	v_max_i32_e32 v34, 0, v54
	s_nop 0
	v_addc_co_u32_e32 v3, vcc, 0, v43, vcc
	global_load_dwordx4 v[26:29], v[2:3], off
	global_load_dwordx4 v[6:9], v[2:3], off offset:64
	global_load_dwordx4 v[30:33], v[2:3], off offset:2048
	s_nop 0
	global_load_dwordx4 v[2:5], v[2:3], off offset:2112
	global_load_dwordx4 v[100:103], v[40:41], off offset:256
	global_load_dwordx4 v[104:107], v[40:41], off offset:320
	global_load_dwordx4 v[108:111], v[40:41], off offset:384
	global_load_dwordx4 v[112:115], v[40:41], off offset:448
	v_add_u32_e32 v60, 1, v34
	v_mov_b32_e32 v45, 0
	v_min_u32_e32 v46, 4, v60
	v_mov_b32_e32 v44, v45
	v_mov_b32_e32 v37, v45
	v_mov_b32_e32 v36, v45
	s_waitcnt lgkmcnt(0)
	s_barrier
	s_and_saveexec_b64 s[20:21], s[2:3]
	s_cbranch_execz .LBB0_398
	v_lshlrev_b32_e32 v34, 6, v1
	v_add3_u32 v34, v50, v34, 0
	v_mov_b32_e32 v36, 0
	v_add_u32_e32 v34, 0xf00, v34
	s_mov_b64 s[22:23], 0
	v_mov_b32_e32 v35, v46
	v_mov_b32_e32 v37, v36
	v_mov_b32_e32 v44, v36
	v_mov_b32_e32 v45, v36

.LBB0_398:
	s_or_b64 exec, exec, s[20:21]
	v_min_i32_e32 v34, 4, v56
	v_cvt_f32_i32_e32 v34, v34
	ds_read_b128 v[62:65], v53 offset:3840
	v_div_scale_f32 v35, s[20:21], v34, v34, 1.0
	v_rcp_f32_e32 v47, v35
	v_div_scale_f32 v48, vcc, 1.0, v34, 1.0
	s_waitcnt lgkmcnt(0)
	v_xor_b32_e32 v49, 0x80000000, v65
	v_fma_f32 v61, -v35, v47, 1.0
	v_fmac_f32_e32 v47, v61, v47
	v_mul_f32_e32 v61, v48, v47
	v_fma_f32 v65, -v35, v61, v48
	v_fmac_f32_e32 v61, v65, v47
	v_fma_f32 v35, -v35, v61, v48
	v_div_fmas_f32 v35, v35, v47, v61
	v_div_fixup_f32 v34, v35, v34, 1.0
	v_xor_b32_e32 v48, 0x80000000, v64
	v_pk_fma_f32 v[36:37], v[34:35], v[36:37], v[62:63] op_sel_hi:[0,1,1] neg_lo:[0,0,1] neg_hi:[0,0,1]
	v_pk_fma_f32 v[44:45], v[34:35], v[44:45], v[48:49] op_sel_hi:[0,1,1]
	s_movk_i32 s20, 0x7fff
	s_mov_b32 s21, 0xffff0000
	v_cvt_pk_bf16_f32 v36, v36, v37
	v_cvt_pk_bf16_f32 v37, v44, v45
	v_mov_b32_e32 v45, 0
	ds_write_b64 v51, v[36:37] offset:40960
	v_mov_b32_e32 v44, v45
	v_mov_b32_e32 v37, v45
	v_mov_b32_e32 v36, v45
	s_and_saveexec_b64 s[20:21], s[2:3]
	s_cbranch_execz .LBB0_402
	v_lshlrev_b32_e32 v35, 6, v1
	v_add3_u32 v35, v50, v35, 0
	v_mov_b32_e32 v36, 0
	v_add_u32_e32 v35, 0xf10, v35
	s_mov_b64 s[22:23], 0
	v_mov_b32_e32 v47, v46
	v_mov_b32_e32 v37, v36
	v_mov_b32_e32 v44, v36
	v_mov_b32_e32 v45, v36

.LBB0_402:
	s_or_b64 exec, exec, s[20:21]
	ds_read_b128 v[62:65], v53 offset:3856
	v_mov_b32_e32 v35, v34
	s_movk_i32 s20, 0x7fff
	v_mov_b32_e32 v48, v34
	v_mov_b32_e32 v49, v34
	s_waitcnt lgkmcnt(0)
	v_pk_fma_f32 v[36:37], v[34:35], v[36:37], v[62:63] neg_lo:[0,0,1] neg_hi:[0,0,1]
	v_xor_b32_e32 v65, 0x80000000, v65
	v_xor_b32_e32 v64, 0x80000000, v64
	v_pk_fma_f32 v[44:45], v[48:49], v[44:45], v[64:65]
	s_mov_b32 s21, 0xffff0000
	v_cvt_pk_bf16_f32 v36, v36, v37
	v_cvt_pk_bf16_f32 v37, v44, v45
	v_mov_b32_e32 v45, 0
	ds_write_b64 v51, v[36:37] offset:40968
	v_mov_b32_e32 v44, v45
	v_mov_b32_e32 v37, v45
	v_mov_b32_e32 v36, v45
	s_and_saveexec_b64 s[20:21], s[2:3]
	s_cbranch_execz .LBB0_406
	v_lshlrev_b32_e32 v36, 6, v1
	v_add3_u32 v36, v50, v36, 0
	v_add_u32_e32 v47, 0xf20, v36
	v_mov_b32_e32 v36, 0
	s_mov_b64 s[22:23], 0
	v_mov_b32_e32 v48, v46
	v_mov_b32_e32 v37, v36
	v_mov_b32_e32 v44, v36
	v_mov_b32_e32 v45, v36

.LBB0_406:
	s_or_b64 exec, exec, s[20:21]
	ds_read_b128 v[62:65], v53 offset:3872
	s_movk_i32 s20, 0x7fff
	v_mov_b32_e32 v48, v34
	v_mov_b32_e32 v49, v34
	s_mov_b32 s21, 0xffff0000
	s_waitcnt lgkmcnt(0)
	v_pk_fma_f32 v[36:37], v[34:35], v[36:37], v[62:63] neg_lo:[0,0,1] neg_hi:[0,0,1]
	v_xor_b32_e32 v65, 0x80000000, v65
	v_xor_b32_e32 v64, 0x80000000, v64
	v_pk_fma_f32 v[44:45], v[48:49], v[44:45], v[64:65]
	v_cvt_pk_bf16_f32 v36, v36, v37
	v_cvt_pk_bf16_f32 v37, v44, v45
	v_mov_b32_e32 v45, 0
	ds_write_b64 v51, v[36:37] offset:40976
	v_mov_b32_e32 v44, v45
	v_mov_b32_e32 v37, v45
	v_mov_b32_e32 v36, v45
	s_and_saveexec_b64 s[20:21], s[2:3]
	s_cbranch_execz .LBB0_410
	v_lshlrev_b32_e32 v36, 6, v1
	v_add3_u32 v36, v50, v36, 0
	v_add_u32_e32 v47, 0xf30, v36
	v_mov_b32_e32 v36, 0
	s_mov_b64 s[22:23], 0
	v_mov_b32_e32 v37, v36
	v_mov_b32_e32 v44, v36
	v_mov_b32_e32 v45, v36

.LBB0_410:
	s_or_b64 exec, exec, s[20:21]
	ds_read_b128 v[46:49], v53 offset:3888
	v_mov_b32_e32 v62, v34
	v_mov_b32_e32 v63, v34
	s_movk_i32 s20, 0x7fff
	s_mov_b32 s21, 0xffff0000
	s_waitcnt lgkmcnt(0)
	v_xor_b32_e32 v49, 0x80000000, v49
	v_xor_b32_e32 v48, 0x80000000, v48
	v_pk_fma_f32 v[34:35], v[34:35], v[36:37], v[46:47] neg_lo:[0,0,1] neg_hi:[0,0,1]
	v_pk_fma_f32 v[36:37], v[62:63], v[44:45], v[48:49]
	v_cvt_pk_bf16_f32 v34, v34, v35
	v_cvt_pk_bf16_f32 v35, v36, v37
	ds_write_b64 v51, v[34:35] offset:40984
	s_waitcnt lgkmcnt(0)
	s_barrier
	ds_read_b128 v[34:37], v55 offset:40960
	ds_read_b128 v[44:47], v55 offset:41024
	s_waitcnt vmcnt(11) lgkmcnt(1)
	v_mfma_f32_16x16x32_bf16 v[18:21], v[18:21], v[34:37], 0
	s_waitcnt vmcnt(9)
	v_mfma_f32_16x16x32_bf16 v[22:25], v[22:25], v[34:37], 0
	s_waitcnt vmcnt(7)
	v_mfma_f32_16x16x32_bf16 v[26:29], v[26:29], v[34:37], 0
	s_waitcnt vmcnt(5)
	v_mfma_f32_16x16x32_bf16 v[30:33], v[30:33], v[34:37], 0
	s_waitcnt lgkmcnt(0)
	v_mfma_f32_16x16x32_bf16 v[14:17], v[14:17], v[44:47], v[18:21]
	v_mfma_f32_16x16x32_bf16 v[10:13], v[10:13], v[44:47], v[22:25]
	v_mfma_f32_16x16x32_bf16 v[6:9], v[6:9], v[44:47], v[26:29]
	s_waitcnt vmcnt(0)
	s_nop 4
	v_pk_mul_f32 v[16:17], v[16:17], v[102:103]
	v_pk_mul_f32 v[14:15], v[14:15], v[100:101]
	v_cvt_pk_bf16_f32 v14, v14, v15
	v_cvt_pk_bf16_f32 v15, v16, v17
	global_store_dwordx2 v[38:39], v[14:15], off offset:640
	v_mfma_f32_16x16x32_bf16 v[2:5], v[2:5], v[44:47], v[30:33]
	v_pk_mul_f32 v[12:13], v[12:13], v[106:107]
	v_pk_mul_f32 v[10:11], v[10:11], v[104:105]
	v_cvt_pk_bf16_f32 v10, v10, v11
	v_cvt_pk_bf16_f32 v11, v12, v13
	global_store_dwordx2 v[38:39], v[10:11], off offset:672
	v_pk_mul_f32 v[8:9], v[8:9], v[110:111]
	v_pk_mul_f32 v[6:7], v[6:7], v[108:109]
	v_cvt_pk_bf16_f32 v6, v6, v7
	v_cvt_pk_bf16_f32 v7, v8, v9
	global_store_dwordx2 v[38:39], v[6:7], off offset:704
	v_pk_mul_f32 v[4:5], v[4:5], v[114:115]
	v_pk_mul_f32 v[2:3], v[2:3], v[112:113]
	v_cvt_pk_bf16_f32 v2, v2, v3
	v_cvt_pk_bf16_f32 v3, v4, v5
	global_store_dwordx2 v[38:39], v[2:3], off offset:736
	s_barrier
	v_lshlrev_b32_e32 v180, 16, v142
	v_and_b32_e32 v181, 0xffff0000, v142
	v_lshlrev_b32_e32 v182, 16, v143
	v_and_b32_e32 v183, 0xffff0000, v143
	v_lshlrev_b32_e32 v184, 16, v144
	v_and_b32_e32 v185, 0xffff0000, v144
	v_lshlrev_b32_e32 v186, 16, v145
	v_and_b32_e32 v187, 0xffff0000, v145
	v_lshlrev_b32_e32 v188, 16, v146
	v_and_b32_e32 v189, 0xffff0000, v146
	v_lshlrev_b32_e32 v190, 16, v147
	v_and_b32_e32 v191, 0xffff0000, v147
	v_lshlrev_b32_e32 v192, 16, v148
	v_and_b32_e32 v193, 0xffff0000, v148
	v_lshlrev_b32_e32 v194, 16, v149
	v_and_b32_e32 v195, 0xffff0000, v149
	v_lshlrev_b32_e32 v196, 16, v150
	v_and_b32_e32 v197, 0xffff0000, v150
	v_lshlrev_b32_e32 v198, 16, v151
	v_and_b32_e32 v199, 0xffff0000, v151
	v_lshlrev_b32_e32 v200, 16, v152
	v_and_b32_e32 v201, 0xffff0000, v152
	v_lshlrev_b32_e32 v202, 16, v153
	v_and_b32_e32 v203, 0xffff0000, v153
	ds_write_b128 v204, v[180:183]
	ds_write_b128 v204, v[184:187] offset:16
	ds_write_b128 v204, v[188:191] offset:16384
	ds_write_b128 v204, v[192:195] offset:16400
	s_mov_b64 s[98:99], exec
	v_cmp_gt_u32_e32 vcc, 0x78, v52
	s_and_b64 exec, s[98:99], vcc
	ds_write_b128 v204, v[196:199] offset:32768
	ds_write_b128 v204, v[200:203] offset:32784
	s_mov_b64 exec, s[98:99]
	v_add_co_u32_e32 v2, vcc, 0x4000, v42
	s_nop 1
	v_addc_co_u32_e32 v3, vcc, 0, v43, vcc
	global_load_dwordx4 v[18:21], v[2:3], off
	global_load_dwordx4 v[14:17], v[2:3], off offset:64
	global_load_dwordx4 v[22:25], v[2:3], off offset:2048
	global_load_dwordx4 v[10:13], v[2:3], off offset:2112
	v_add_co_u32_e32 v2, vcc, 0x5000, v42
	s_nop 1
	v_addc_co_u32_e32 v3, vcc, 0, v43, vcc
	global_load_dwordx4 v[26:29], v[2:3], off
	global_load_dwordx4 v[6:9], v[2:3], off offset:64
	global_load_dwordx4 v[30:33], v[2:3], off offset:2048
	s_nop 0
	global_load_dwordx4 v[2:5], v[2:3], off offset:2112
	global_load_dwordx4 v[100:103], v[40:41], off offset:512
	global_load_dwordx4 v[104:107], v[40:41], off offset:576
	global_load_dwordx4 v[108:111], v[40:41], off offset:640
	global_load_dwordx4 v[112:115], v[40:41], off offset:704
	s_waitcnt lgkmcnt(0)
	s_barrier
	s_and_saveexec_b64 s[20:21], s[8:9]
	s_xor_b64 s[20:21], exec, s[20:21]
	ds_read_b128 v[34:37], v53 offset:3840
	s_or_saveexec_b64 s[20:21], s[20:21]
	v_lshl_add_u32 v59, v59, 2, 0
	v_add_u32_e32 v44, 15, v58
	v_mov_b32_e32 v46, 0
	v_lshl_add_u32 v58, v44, 8, v59
	v_mov_b32_e32 v47, 0
	v_mov_b32_e32 v48, 0
	v_mov_b32_e32 v49, 0
	s_xor_b64 exec, exec, s[20:21]
	s_cbranch_execz .LBB0_433
	s_waitcnt lgkmcnt(0)
	ds_read_b128 v[34:37], v58
	s_waitcnt lgkmcnt(0)
	v_pk_add_f32 v[48:49], v[36:37], 0 op_sel_hi:[1,0]
	v_pk_add_f32 v[46:47], v[34:35], 0 op_sel_hi:[1,0]
	s_and_saveexec_b64 s[22:23], s[6:7]
	s_cbranch_execz .LBB0_432
	v_add_u32_e32 v44, v59, v50
	ds_read_b128 v[62:65], v44 offset:3584
	v_cmp_ne_u32_e32 vcc, 2, v60
	s_waitcnt lgkmcnt(0)
	v_pk_add_f32 v[48:49], v[48:49], v[64:65]
	v_pk_add_f32 v[46:47], v[46:47], v[62:63]
	s_and_saveexec_b64 s[24:25], vcc
	s_cbranch_execz .LBB0_431
	ds_read_b128 v[62:65], v44 offset:3328
	v_cmp_ne_u32_e32 vcc, 3, v60
	s_waitcnt lgkmcnt(0)
	v_pk_add_f32 v[48:49], v[48:49], v[64:65]
	v_pk_add_f32 v[46:47], v[46:47], v[62:63]
	s_and_saveexec_b64 s[26:27], vcc
	s_cbranch_execz .LBB0_430
	ds_read_b128 v[62:65], v44 offset:3072
	v_cmp_ne_u32_e32 vcc, 4, v60
	s_waitcnt lgkmcnt(0)
	v_pk_add_f32 v[48:49], v[48:49], v[64:65]
	v_pk_add_f32 v[46:47], v[46:47], v[62:63]
	s_and_saveexec_b64 s[28:29], vcc
	s_cbranch_execz .LBB0_429
	ds_read_b128 v[62:65], v44 offset:2816
	v_cmp_ne_u32_e32 vcc, 5, v60
	s_waitcnt lgkmcnt(0)
	v_pk_add_f32 v[48:49], v[48:49], v[64:65]
	v_pk_add_f32 v[46:47], v[46:47], v[62:63]
	s_and_saveexec_b64 s[30:31], vcc
	s_cbranch_execz .LBB0_428
	ds_read_b128 v[62:65], v44 offset:2560
	v_cmp_ne_u32_e32 vcc, 6, v60
	s_waitcnt lgkmcnt(0)
	v_pk_add_f32 v[48:49], v[48:49], v[64:65]
	v_pk_add_f32 v[46:47], v[46:47], v[62:63]
	s_and_saveexec_b64 s[34:35], vcc
	s_cbranch_execz .LBB0_427
	ds_read_b128 v[62:65], v44 offset:2304
	v_cmp_ne_u32_e32 vcc, 7, v60
	s_waitcnt lgkmcnt(0)
	v_pk_add_f32 v[48:49], v[48:49], v[64:65]
	v_pk_add_f32 v[46:47], v[46:47], v[62:63]
	s_and_saveexec_b64 s[36:37], vcc
	s_cbranch_execz .LBB0_426
	ds_read_b128 v[62:65], v44 offset:2048
	s_waitcnt lgkmcnt(0)
	v_pk_add_f32 v[48:49], v[48:49], v[64:65]
	v_pk_add_f32 v[46:47], v[46:47], v[62:63]

.LBB0_433:
	s_or_b64 exec, exec, s[20:21]
	v_min_i32_e32 v44, 8, v56
	v_cvt_f32_i32_e32 v44, v44
	s_waitcnt lgkmcnt(0)
	v_xor_b32_e32 v37, 0x80000000, v37
	v_xor_b32_e32 v36, 0x80000000, v36
	v_div_scale_f32 v45, s[20:21], v44, v44, 1.0
	v_rcp_f32_e32 v61, v45
	v_div_scale_f32 v62, vcc, 1.0, v44, 1.0
	s_movk_i32 s20, 0x7fff
	v_fma_f32 v63, -v45, v61, 1.0
	v_fmac_f32_e32 v61, v63, v61
	v_mul_f32_e32 v63, v62, v61
	v_fma_f32 v64, -v45, v63, v62
	v_fmac_f32_e32 v63, v64, v61
	v_fma_f32 v45, -v45, v63, v62
	v_div_fmas_f32 v45, v45, v61, v63
	v_div_fixup_f32 v44, v45, v44, 1.0
	v_pk_fma_f32 v[34:35], v[44:45], v[46:47], v[34:35] op_sel_hi:[0,1,1] neg_lo:[0,0,1] neg_hi:[0,0,1]
	v_pk_fma_f32 v[36:37], v[44:45], v[48:49], v[36:37] op_sel_hi:[0,1,1]
	s_mov_b32 s21, 0xffff0000
	v_cvt_pk_bf16_f32 v34, v34, v35
	v_cvt_pk_bf16_f32 v35, v36, v37
	ds_write_b64 v51, v[34:35] offset:40960
	s_and_saveexec_b64 s[20:21], s[8:9]
	s_xor_b64 s[20:21], exec, s[20:21]
	ds_read_b128 v[34:37], v53 offset:3856
	s_or_saveexec_b64 s[20:21], s[20:21]
	v_mov_b32_e32 v45, v44
	v_mov_b32_e32 v46, 0
	v_mov_b32_e32 v47, 0
	v_mov_b32_e32 v48, 0
	v_mov_b32_e32 v49, 0
	s_xor_b64 exec, exec, s[20:21]
	s_cbranch_execz .LBB0_451
	s_waitcnt lgkmcnt(0)
	ds_read_b128 v[34:37], v58 offset:16
	s_waitcnt lgkmcnt(0)
	v_pk_add_f32 v[48:49], v[36:37], 0 op_sel_hi:[1,0]
	v_pk_add_f32 v[46:47], v[34:35], 0 op_sel_hi:[1,0]
	s_and_saveexec_b64 s[22:23], s[6:7]
	s_cbranch_execz .LBB0_450
	v_add_u32_e32 v61, v59, v50
	ds_read_b128 v[62:65], v61 offset:3600
	v_cmp_ne_u32_e32 vcc, 2, v60
	s_waitcnt lgkmcnt(0)
	v_pk_add_f32 v[48:49], v[48:49], v[64:65]
	v_pk_add_f32 v[46:47], v[46:47], v[62:63]
	s_and_saveexec_b64 s[24:25], vcc
	s_cbranch_execz .LBB0_449
	ds_read_b128 v[62:65], v61 offset:3344
	v_cmp_ne_u32_e32 vcc, 3, v60
	s_waitcnt lgkmcnt(0)
	v_pk_add_f32 v[48:49], v[48:49], v[64:65]
	v_pk_add_f32 v[46:47], v[46:47], v[62:63]
	s_and_saveexec_b64 s[26:27], vcc
	s_cbranch_execz .LBB0_448
	ds_read_b128 v[62:65], v61 offset:3088
	v_cmp_ne_u32_e32 vcc, 4, v60
	s_waitcnt lgkmcnt(0)
	v_pk_add_f32 v[48:49], v[48:49], v[64:65]
	v_pk_add_f32 v[46:47], v[46:47], v[62:63]
	s_and_saveexec_b64 s[28:29], vcc
	s_cbranch_execz .LBB0_447
	ds_read_b128 v[62:65], v61 offset:2832
	v_cmp_ne_u32_e32 vcc, 5, v60
	s_waitcnt lgkmcnt(0)
	v_pk_add_f32 v[48:49], v[48:49], v[64:65]
	v_pk_add_f32 v[46:47], v[46:47], v[62:63]
	s_and_saveexec_b64 s[30:31], vcc
	s_cbranch_execz .LBB0_446
	ds_read_b128 v[62:65], v61 offset:2576
	v_cmp_ne_u32_e32 vcc, 6, v60
	s_waitcnt lgkmcnt(0)
	v_pk_add_f32 v[48:49], v[48:49], v[64:65]
	v_pk_add_f32 v[46:47], v[46:47], v[62:63]
	s_and_saveexec_b64 s[34:35], vcc
	s_cbranch_execz .LBB0_445
	ds_read_b128 v[62:65], v61 offset:2320
	v_cmp_ne_u32_e32 vcc, 7, v60
	s_waitcnt lgkmcnt(0)
	v_pk_add_f32 v[48:49], v[48:49], v[64:65]
	v_pk_add_f32 v[46:47], v[46:47], v[62:63]
	s_and_saveexec_b64 s[36:37], vcc
	s_cbranch_execz .LBB0_444
	ds_read_b128 v[62:65], v61 offset:2064
	s_waitcnt lgkmcnt(0)
	v_pk_add_f32 v[48:49], v[48:49], v[64:65]
	v_pk_add_f32 v[46:47], v[46:47], v[62:63]

.LBB0_451:
	s_or_b64 exec, exec, s[20:21]
	s_waitcnt lgkmcnt(0)
	v_pk_fma_f32 v[34:35], v[44:45], v[46:47], v[34:35] neg_lo:[0,0,1] neg_hi:[0,0,1]
	s_movk_i32 s20, 0x7fff
	v_xor_b32_e32 v37, 0x80000000, v37
	v_xor_b32_e32 v36, 0x80000000, v36
	v_mov_b32_e32 v62, v44
	v_mov_b32_e32 v63, v44
	v_pk_fma_f32 v[36:37], v[62:63], v[48:49], v[36:37]
	s_mov_b32 s21, 0xffff0000
	v_cvt_pk_bf16_f32 v34, v34, v35
	v_cvt_pk_bf16_f32 v35, v36, v37
	ds_write_b64 v51, v[34:35] offset:40968
	s_and_saveexec_b64 s[20:21], s[8:9]
	s_xor_b64 s[20:21], exec, s[20:21]
	ds_read_b128 v[34:37], v53 offset:3872
	s_or_saveexec_b64 s[20:21], s[20:21]
	v_mov_b32_e32 v46, 0
	v_mov_b32_e32 v47, 0
	v_mov_b32_e32 v48, 0
	v_mov_b32_e32 v49, 0
	s_xor_b64 exec, exec, s[20:21]
	s_cbranch_execz .LBB0_469
	s_waitcnt lgkmcnt(0)
	ds_read_b128 v[34:37], v58 offset:32
	s_waitcnt lgkmcnt(0)
	v_pk_add_f32 v[48:49], v[36:37], 0 op_sel_hi:[1,0]
	v_pk_add_f32 v[46:47], v[34:35], 0 op_sel_hi:[1,0]
	s_and_saveexec_b64 s[22:23], s[6:7]
	s_cbranch_execz .LBB0_468
	v_add_u32_e32 v61, v59, v50
	ds_read_b128 v[62:65], v61 offset:3616
	v_cmp_ne_u32_e32 vcc, 2, v60
	s_waitcnt lgkmcnt(0)
	v_pk_add_f32 v[48:49], v[48:49], v[64:65]
	v_pk_add_f32 v[46:47], v[46:47], v[62:63]
	s_and_saveexec_b64 s[24:25], vcc
	s_cbranch_execz .LBB0_467
	ds_read_b128 v[62:65], v61 offset:3360
	v_cmp_ne_u32_e32 vcc, 3, v60
	s_waitcnt lgkmcnt(0)
	v_pk_add_f32 v[48:49], v[48:49], v[64:65]
	v_pk_add_f32 v[46:47], v[46:47], v[62:63]
	s_and_saveexec_b64 s[26:27], vcc
	s_cbranch_execz .LBB0_466
	ds_read_b128 v[62:65], v61 offset:3104
	v_cmp_ne_u32_e32 vcc, 4, v60
	s_waitcnt lgkmcnt(0)
	v_pk_add_f32 v[48:49], v[48:49], v[64:65]
	v_pk_add_f32 v[46:47], v[46:47], v[62:63]
	s_and_saveexec_b64 s[28:29], vcc
	s_cbranch_execz .LBB0_465
	ds_read_b128 v[62:65], v61 offset:2848
	v_cmp_ne_u32_e32 vcc, 5, v60
	s_waitcnt lgkmcnt(0)
	v_pk_add_f32 v[48:49], v[48:49], v[64:65]
	v_pk_add_f32 v[46:47], v[46:47], v[62:63]
	s_and_saveexec_b64 s[30:31], vcc
	s_cbranch_execz .LBB0_464
	ds_read_b128 v[62:65], v61 offset:2592
	v_cmp_ne_u32_e32 vcc, 6, v60
	s_waitcnt lgkmcnt(0)
	v_pk_add_f32 v[48:49], v[48:49], v[64:65]
	v_pk_add_f32 v[46:47], v[46:47], v[62:63]
	s_and_saveexec_b64 s[34:35], vcc
	s_cbranch_execz .LBB0_463
	ds_read_b128 v[62:65], v61 offset:2336
	v_cmp_ne_u32_e32 vcc, 7, v60
	s_waitcnt lgkmcnt(0)
	v_pk_add_f32 v[48:49], v[48:49], v[64:65]
	v_pk_add_f32 v[46:47], v[46:47], v[62:63]
	s_and_saveexec_b64 s[36:37], vcc
	s_cbranch_execz .LBB0_462
	ds_read_b128 v[62:65], v61 offset:2080
	s_waitcnt lgkmcnt(0)
	v_pk_add_f32 v[48:49], v[48:49], v[64:65]
	v_pk_add_f32 v[46:47], v[46:47], v[62:63]

.LBB0_469:
	s_or_b64 exec, exec, s[20:21]
	s_waitcnt lgkmcnt(0)
	v_pk_fma_f32 v[34:35], v[44:45], v[46:47], v[34:35] neg_lo:[0,0,1] neg_hi:[0,0,1]
	s_movk_i32 s20, 0x7fff
	v_xor_b32_e32 v37, 0x80000000, v37
	v_xor_b32_e32 v36, 0x80000000, v36
	v_mov_b32_e32 v62, v44
	v_mov_b32_e32 v63, v44
	v_pk_fma_f32 v[36:37], v[62:63], v[48:49], v[36:37]
	s_mov_b32 s21, 0xffff0000
	v_cvt_pk_bf16_f32 v34, v34, v35
	v_cvt_pk_bf16_f32 v35, v36, v37
	ds_write_b64 v51, v[34:35] offset:40976
	s_and_saveexec_b64 s[20:21], s[8:9]
	s_xor_b64 s[8:9], exec, s[20:21]
	ds_read_b128 v[34:37], v53 offset:3888
	s_or_saveexec_b64 s[8:9], s[8:9]
	v_mov_b32_e32 v46, 0
	v_mov_b32_e32 v47, 0
	v_mov_b32_e32 v48, 0
	v_mov_b32_e32 v49, 0
	s_xor_b64 exec, exec, s[8:9]
	s_cbranch_execz .LBB0_487
	s_waitcnt lgkmcnt(0)
	ds_read_b128 v[34:37], v58 offset:48
	s_waitcnt lgkmcnt(0)
	v_pk_add_f32 v[48:49], v[36:37], 0 op_sel_hi:[1,0]
	v_pk_add_f32 v[46:47], v[34:35], 0 op_sel_hi:[1,0]
	s_and_saveexec_b64 s[20:21], s[6:7]
	s_cbranch_execz .LBB0_486
	v_add_u32_e32 v58, v59, v50
	ds_read_b128 v[62:65], v58 offset:3632
	v_cmp_ne_u32_e32 vcc, 2, v60
	s_waitcnt lgkmcnt(0)
	v_pk_add_f32 v[48:49], v[48:49], v[64:65]
	v_pk_add_f32 v[46:47], v[46:47], v[62:63]
	s_and_saveexec_b64 s[6:7], vcc
	s_cbranch_execz .LBB0_485
	ds_read_b128 v[62:65], v58 offset:3376
	v_cmp_ne_u32_e32 vcc, 3, v60
	s_waitcnt lgkmcnt(0)
	v_pk_add_f32 v[48:49], v[48:49], v[64:65]
	v_pk_add_f32 v[46:47], v[46:47], v[62:63]
	s_and_saveexec_b64 s[22:23], vcc
	s_cbranch_execz .LBB0_484
	ds_read_b128 v[62:65], v58 offset:3120
	v_cmp_ne_u32_e32 vcc, 4, v60
	s_waitcnt lgkmcnt(0)
	v_pk_add_f32 v[48:49], v[48:49], v[64:65]
	v_pk_add_f32 v[46:47], v[46:47], v[62:63]
	s_and_saveexec_b64 s[24:25], vcc
	s_cbranch_execz .LBB0_483
	ds_read_b128 v[62:65], v58 offset:2864
	v_cmp_ne_u32_e32 vcc, 5, v60
	s_waitcnt lgkmcnt(0)
	v_pk_add_f32 v[48:49], v[48:49], v[64:65]
	v_pk_add_f32 v[46:47], v[46:47], v[62:63]
	s_and_saveexec_b64 s[26:27], vcc
	s_cbranch_execz .LBB0_482
	ds_read_b128 v[62:65], v58 offset:2608
	v_cmp_ne_u32_e32 vcc, 6, v60
	s_waitcnt lgkmcnt(0)
	v_pk_add_f32 v[48:49], v[48:49], v[64:65]
	v_pk_add_f32 v[46:47], v[46:47], v[62:63]
	s_and_saveexec_b64 s[28:29], vcc
	s_cbranch_execz .LBB0_481
	ds_read_b128 v[62:65], v58 offset:2352
	v_cmp_ne_u32_e32 vcc, 7, v60
	s_waitcnt lgkmcnt(0)
	v_pk_add_f32 v[48:49], v[48:49], v[64:65]
	v_pk_add_f32 v[46:47], v[46:47], v[62:63]
	s_and_saveexec_b64 s[30:31], vcc
	s_cbranch_execz .LBB0_480
	ds_read_b128 v[62:65], v58 offset:2096
	s_waitcnt lgkmcnt(0)
	v_pk_add_f32 v[48:49], v[48:49], v[64:65]
	v_pk_add_f32 v[46:47], v[46:47], v[62:63]

.LBB0_487:
	s_or_b64 exec, exec, s[8:9]
	s_waitcnt lgkmcnt(0)
	v_pk_fma_f32 v[34:35], v[44:45], v[46:47], v[34:35] neg_lo:[0,0,1] neg_hi:[0,0,1]
	v_mov_b32_e32 v58, v44
	v_mov_b32_e32 v59, v44
	s_movk_i32 s6, 0x7fff
	v_xor_b32_e32 v37, 0x80000000, v37
	v_xor_b32_e32 v36, 0x80000000, v36
	v_pk_fma_f32 v[36:37], v[58:59], v[48:49], v[36:37]
	s_mov_b32 s7, 0xffff0000
	v_cvt_pk_bf16_f32 v34, v34, v35
	v_cvt_pk_bf16_f32 v35, v36, v37
	ds_write_b64 v51, v[34:35] offset:40984
	s_waitcnt lgkmcnt(0)
	s_barrier
	ds_read_b128 v[34:37], v55 offset:40960
	ds_read_b128 v[44:47], v55 offset:41024
	s_waitcnt vmcnt(11) lgkmcnt(1)
	v_mfma_f32_16x16x32_bf16 v[18:21], v[18:21], v[34:37], 0
	s_waitcnt vmcnt(9)
	v_mfma_f32_16x16x32_bf16 v[22:25], v[22:25], v[34:37], 0
	s_waitcnt vmcnt(7)
	v_mfma_f32_16x16x32_bf16 v[26:29], v[26:29], v[34:37], 0
	s_waitcnt vmcnt(5)
	v_mfma_f32_16x16x32_bf16 v[30:33], v[30:33], v[34:37], 0
	s_waitcnt lgkmcnt(0)
	v_mfma_f32_16x16x32_bf16 v[14:17], v[14:17], v[44:47], v[18:21]
	v_mfma_f32_16x16x32_bf16 v[10:13], v[10:13], v[44:47], v[22:25]
	v_mfma_f32_16x16x32_bf16 v[6:9], v[6:9], v[44:47], v[26:29]
	s_waitcnt vmcnt(0)
	s_nop 4
	v_pk_mul_f32 v[16:17], v[16:17], v[102:103]
	v_pk_mul_f32 v[14:15], v[14:15], v[100:101]
	v_cvt_pk_bf16_f32 v14, v14, v15
	v_cvt_pk_bf16_f32 v15, v16, v17
	global_store_dwordx2 v[38:39], v[14:15], off offset:768
	v_mfma_f32_16x16x32_bf16 v[2:5], v[2:5], v[44:47], v[30:33]
	v_pk_mul_f32 v[12:13], v[12:13], v[106:107]
	v_pk_mul_f32 v[10:11], v[10:11], v[104:105]
	v_cvt_pk_bf16_f32 v10, v10, v11
	v_cvt_pk_bf16_f32 v11, v12, v13
	global_store_dwordx2 v[38:39], v[10:11], off offset:800
	v_pk_mul_f32 v[8:9], v[8:9], v[110:111]
	v_pk_mul_f32 v[6:7], v[6:7], v[108:109]
	v_cvt_pk_bf16_f32 v6, v6, v7
	v_cvt_pk_bf16_f32 v7, v8, v9
	global_store_dwordx2 v[38:39], v[6:7], off offset:832
	v_pk_mul_f32 v[4:5], v[4:5], v[114:115]
	v_pk_mul_f32 v[2:3], v[2:3], v[112:113]
	v_cvt_pk_bf16_f32 v2, v2, v3
	v_cvt_pk_bf16_f32 v3, v4, v5
	global_store_dwordx2 v[38:39], v[2:3], off offset:864
	s_barrier
	v_lshlrev_b32_e32 v180, 16, v154
	v_and_b32_e32 v181, 0xffff0000, v154
	v_lshlrev_b32_e32 v182, 16, v155
	v_and_b32_e32 v183, 0xffff0000, v155
	v_lshlrev_b32_e32 v184, 16, v156
	v_and_b32_e32 v185, 0xffff0000, v156
	v_lshlrev_b32_e32 v186, 16, v157
	v_and_b32_e32 v187, 0xffff0000, v157
	v_lshlrev_b32_e32 v188, 16, v158
	v_and_b32_e32 v189, 0xffff0000, v158
	v_lshlrev_b32_e32 v190, 16, v159
	v_and_b32_e32 v191, 0xffff0000, v159
	v_lshlrev_b32_e32 v192, 16, v160
	v_and_b32_e32 v193, 0xffff0000, v160
	v_lshlrev_b32_e32 v194, 16, v161
	v_and_b32_e32 v195, 0xffff0000, v161
	v_lshlrev_b32_e32 v196, 16, v162
	v_and_b32_e32 v197, 0xffff0000, v162
	v_lshlrev_b32_e32 v198, 16, v163
	v_and_b32_e32 v199, 0xffff0000, v163
	v_lshlrev_b32_e32 v200, 16, v164
	v_and_b32_e32 v201, 0xffff0000, v164
	v_lshlrev_b32_e32 v202, 16, v165
	v_and_b32_e32 v203, 0xffff0000, v165
	ds_write_b128 v204, v[180:183]
	ds_write_b128 v204, v[184:187] offset:16
	ds_write_b128 v204, v[188:191] offset:16384
	ds_write_b128 v204, v[192:195] offset:16400
	s_mov_b64 s[98:99], exec
	v_cmp_gt_u32_e32 vcc, 0x78, v52
	s_and_b64 exec, s[98:99], vcc
	ds_write_b128 v204, v[196:199] offset:32768
	ds_write_b128 v204, v[200:203] offset:32784
	s_mov_b64 exec, s[98:99]
	v_add_co_u32_e32 v2, vcc, 0x6000, v42
	v_min_u32_e32 v44, 16, v60
	s_nop 0
	v_addc_co_u32_e32 v3, vcc, 0, v43, vcc
	v_add_co_u32_e32 v34, vcc, 0x7000, v42
	global_load_dwordx4 v[18:21], v[2:3], off
	global_load_dwordx4 v[14:17], v[2:3], off offset:64
	global_load_dwordx4 v[22:25], v[2:3], off offset:2048
	global_load_dwordx4 v[10:13], v[2:3], off offset:2112
	v_addc_co_u32_e32 v35, vcc, 0, v43, vcc
	global_load_dwordx4 v[26:29], v[34:35], off
	global_load_dwordx4 v[6:9], v[34:35], off offset:64
	global_load_dwordx4 v[30:33], v[34:35], off offset:2048
	global_load_dwordx4 v[2:5], v[34:35], off offset:2112
	global_load_dwordx4 v[100:103], v[40:41], off offset:768
	global_load_dwordx4 v[104:107], v[40:41], off offset:832
	global_load_dwordx4 v[108:111], v[40:41], off offset:896
	global_load_dwordx4 v[112:115], v[40:41], off offset:960
	v_mov_b32_e32 v43, 0
	v_mov_b32_e32 v42, 0
	v_mov_b32_e32 v37, 0
	v_mov_b32_e32 v36, 0
	s_waitcnt lgkmcnt(0)
	s_barrier
	s_and_saveexec_b64 s[0:1], s[2:3]
	s_cbranch_execz .LBB0_502
	v_mov_b32_e32 v36, 0
	v_cmp_lt_i32_e32 vcc, 6, v54
	s_mov_b32 s8, 0
	v_mov_b32_e32 v37, v36
	v_mov_b32_e32 v42, v36
	v_mov_b32_e32 v43, v36
	v_mov_b32_e32 v34, v36
	s_and_saveexec_b64 s[4:5], vcc
	s_cbranch_execz .LBB0_497
	v_lshlrev_b32_e32 v35, 6, v1
	v_add3_u32 v35, v50, v35, 0
	v_mov_b32_e32 v36, 0
	v_and_b32_e32 v34, 24, v44
	v_add_u32_e32 v35, 0x800, v35
	s_mov_b64 s[6:7], 0
	v_mov_b32_e32 v37, v36
	v_mov_b32_e32 v42, v36
	v_mov_b32_e32 v43, v36

.LBB0_502:
	s_or_b64 exec, exec, s[0:1]
	v_min_i32_e32 v34, 16, v56
	v_cvt_f32_i32_e32 v34, v34
	ds_read_b128 v[46:49], v53 offset:3840
	v_div_scale_f32 v35, s[0:1], v34, v34, 1.0
	v_rcp_f32_e32 v45, v35
	v_div_scale_f32 v52, vcc, 1.0, v34, 1.0
	s_waitcnt lgkmcnt(0)
	v_xor_b32_e32 v49, 0x80000000, v49
	v_fma_f32 v56, -v35, v45, 1.0
	v_fmac_f32_e32 v45, v56, v45
	v_mul_f32_e32 v56, v52, v45
	v_fma_f32 v57, -v35, v56, v52
	v_fmac_f32_e32 v56, v57, v45
	v_fma_f32 v35, -v35, v56, v52
	v_div_fmas_f32 v35, v35, v45, v56
	v_div_fixup_f32 v34, v35, v34, 1.0
	v_xor_b32_e32 v48, 0x80000000, v48
	v_pk_fma_f32 v[36:37], v[34:35], v[36:37], v[46:47] op_sel_hi:[0,1,1] neg_lo:[0,0,1] neg_hi:[0,0,1]
	v_pk_fma_f32 v[42:43], v[34:35], v[42:43], v[48:49] op_sel_hi:[0,1,1]
	s_movk_i32 s0, 0x7fff
	s_mov_b32 s1, 0xffff0000
	v_cvt_pk_bf16_f32 v36, v36, v37
	v_cvt_pk_bf16_f32 v37, v42, v43
	ds_write_b64 v51, v[36:37] offset:40960
	v_mov_b32_e32 v43, 0
	v_mov_b32_e32 v42, 0
	v_mov_b32_e32 v37, 0
	v_mov_b32_e32 v36, 0
	s_and_saveexec_b64 s[0:1], s[2:3]
	s_cbranch_execz .LBB0_512
	v_mov_b32_e32 v36, 0
	v_cmp_lt_i32_e32 vcc, 6, v54
	s_mov_b32 s8, 0
	v_mov_b32_e32 v37, v36
	v_mov_b32_e32 v42, v36
	v_mov_b32_e32 v43, v36
	v_mov_b32_e32 v35, v36
	s_and_saveexec_b64 s[4:5], vcc
	s_cbranch_execz .LBB0_507
	v_lshlrev_b32_e32 v36, 6, v1
	v_add3_u32 v36, v50, v36, 0
	v_add_u32_e32 v45, 0x810, v36
	v_mov_b32_e32 v36, 0
	v_and_b32_e32 v35, 24, v44
	s_mov_b64 s[6:7], 0
	v_mov_b32_e32 v37, v36
	v_mov_b32_e32 v42, v36
	v_mov_b32_e32 v43, v36

.LBB0_512:
	s_or_b64 exec, exec, s[0:1]
	ds_read_b128 v[46:49], v53 offset:3856
	v_mov_b32_e32 v35, v34
	s_movk_i32 s0, 0x7fff
	v_mov_b32_e32 v56, v34
	v_mov_b32_e32 v57, v34
	s_waitcnt lgkmcnt(0)
	v_pk_fma_f32 v[36:37], v[34:35], v[36:37], v[46:47] neg_lo:[0,0,1] neg_hi:[0,0,1]
	v_xor_b32_e32 v49, 0x80000000, v49
	v_xor_b32_e32 v48, 0x80000000, v48
	v_pk_fma_f32 v[42:43], v[56:57], v[42:43], v[48:49]
	s_mov_b32 s1, 0xffff0000
	v_cvt_pk_bf16_f32 v36, v36, v37
	v_cvt_pk_bf16_f32 v37, v42, v43
	ds_write_b64 v51, v[36:37] offset:40968
	v_mov_b32_e32 v43, 0
	v_mov_b32_e32 v42, 0
	v_mov_b32_e32 v37, 0
	v_mov_b32_e32 v36, 0
	s_and_saveexec_b64 s[0:1], s[2:3]
	s_cbranch_execz .LBB0_522
	v_mov_b32_e32 v36, 0
	v_cmp_lt_i32_e32 vcc, 6, v54
	s_mov_b32 s8, 0
	v_mov_b32_e32 v37, v36
	v_mov_b32_e32 v42, v36
	v_mov_b32_e32 v43, v36
	v_mov_b32_e32 v45, v36
	s_and_saveexec_b64 s[4:5], vcc
	s_cbranch_execz .LBB0_517
	v_lshlrev_b32_e32 v36, 6, v1
	v_add3_u32 v36, v50, v36, 0
	v_add_u32_e32 v46, 0x820, v36
	v_mov_b32_e32 v36, 0
	v_and_b32_e32 v45, 24, v44
	s_mov_b64 s[6:7], 0
	v_mov_b32_e32 v37, v36
	v_mov_b32_e32 v42, v36
	v_mov_b32_e32 v43, v36

.LBB0_522:
	s_or_b64 exec, exec, s[0:1]
	ds_read_b128 v[46:49], v53 offset:3872
	s_movk_i32 s0, 0x7fff
	v_mov_b32_e32 v56, v34
	v_mov_b32_e32 v57, v34
	s_mov_b32 s1, 0xffff0000
	s_waitcnt lgkmcnt(0)
	v_pk_fma_f32 v[36:37], v[34:35], v[36:37], v[46:47] neg_lo:[0,0,1] neg_hi:[0,0,1]
	v_xor_b32_e32 v49, 0x80000000, v49
	v_xor_b32_e32 v48, 0x80000000, v48
	v_pk_fma_f32 v[42:43], v[56:57], v[42:43], v[48:49]
	v_cvt_pk_bf16_f32 v36, v36, v37
	v_cvt_pk_bf16_f32 v37, v42, v43
	ds_write_b64 v51, v[36:37] offset:40976
	v_mov_b32_e32 v43, 0
	v_mov_b32_e32 v42, 0
	v_mov_b32_e32 v37, 0
	v_mov_b32_e32 v36, 0
	s_and_saveexec_b64 s[0:1], s[2:3]
	s_cbranch_execz .LBB0_532
	v_mov_b32_e32 v36, 0
	v_cmp_lt_i32_e32 vcc, 6, v54
	s_mov_b32 s6, 0
	v_mov_b32_e32 v37, v36
	v_mov_b32_e32 v42, v36
	v_mov_b32_e32 v43, v36
	v_mov_b32_e32 v45, v36
	s_and_saveexec_b64 s[2:3], vcc
	s_cbranch_execz .LBB0_527
	v_lshlrev_b32_e32 v36, 6, v1
	v_add3_u32 v36, v50, v36, 0
	v_add_u32_e32 v46, 0x830, v36
	v_mov_b32_e32 v36, 0
	v_and_b32_e32 v45, 24, v44
	s_mov_b64 s[4:5], 0
	v_mov_b32_e32 v37, v36
	v_mov_b32_e32 v42, v36
	v_mov_b32_e32 v43, v36

.LBB0_532:
	s_or_b64 exec, exec, s[0:1]
	ds_read_b128 v[44:47], v53 offset:3888
	v_mov_b32_e32 v48, v34
	v_mov_b32_e32 v49, v34
	s_movk_i32 s0, 0x7fff
	s_mov_b32 s1, 0xffff0000
	s_waitcnt lgkmcnt(0)
	v_pk_fma_f32 v[34:35], v[34:35], v[36:37], v[44:45] neg_lo:[0,0,1] neg_hi:[0,0,1]
	v_xor_b32_e32 v47, 0x80000000, v47
	v_xor_b32_e32 v46, 0x80000000, v46
	v_pk_fma_f32 v[36:37], v[48:49], v[42:43], v[46:47]
	v_cvt_pk_bf16_f32 v34, v34, v35
	v_cvt_pk_bf16_f32 v35, v36, v37
	ds_write_b64 v51, v[34:35] offset:40984
	s_waitcnt lgkmcnt(0)
	s_barrier
	ds_read_b128 v[34:37], v55 offset:40960
	ds_read_b128 v[42:45], v55 offset:41024
	s_waitcnt vmcnt(11) lgkmcnt(1)
	v_mfma_f32_16x16x32_bf16 v[18:21], v[18:21], v[34:37], 0
	s_mov_b32 s3, 0
	s_waitcnt vmcnt(9)
	v_mfma_f32_16x16x32_bf16 v[22:25], v[22:25], v[34:37], 0
	s_waitcnt vmcnt(7)
	v_mfma_f32_16x16x32_bf16 v[26:29], v[26:29], v[34:37], 0
	s_waitcnt vmcnt(5)
	v_mfma_f32_16x16x32_bf16 v[30:33], v[30:33], v[34:37], 0
	s_waitcnt lgkmcnt(0)
	v_mfma_f32_16x16x32_bf16 v[14:17], v[14:17], v[42:45], v[18:21]
	v_mfma_f32_16x16x32_bf16 v[10:13], v[10:13], v[42:45], v[22:25]
	v_mfma_f32_16x16x32_bf16 v[6:9], v[6:9], v[42:45], v[26:29]
	s_waitcnt vmcnt(0)
	s_nop 4
	v_pk_mul_f32 v[16:17], v[16:17], v[102:103]
	v_pk_mul_f32 v[14:15], v[14:15], v[100:101]
	v_bfe_u32 v19, v16, 16, 1
	v_bfe_u32 v1, v14, 16, 1
	v_bfe_u32 v18, v15, 16, 1
	v_bfe_u32 v20, v17, 16, 1
	v_add3_u32 v1, v14, v1, s0
	v_add3_u32 v14, v15, v18, s0
	v_add3_u32 v15, v16, v19, s0
	v_add3_u32 v16, v17, v20, s0
	v_lshrrev_b32_e32 v1, 16, v1
	v_lshrrev_b32_e32 v15, 16, v15
	v_and_or_b32 v14, v14, s1, v1
	v_and_or_b32 v15, v16, s1, v15
	global_store_dwordx2 v[38:39], v[14:15], off offset:896
	v_mfma_f32_16x16x32_bf16 v[2:5], v[2:5], v[42:45], v[30:33]
	v_pk_mul_f32 v[12:13], v[12:13], v[106:107]
	v_pk_mul_f32 v[10:11], v[10:11], v[104:105]
	v_bfe_u32 v15, v12, 16, 1
	v_bfe_u32 v1, v10, 16, 1
	v_bfe_u32 v14, v11, 16, 1
	v_bfe_u32 v16, v13, 16, 1
	v_add3_u32 v1, v10, v1, s0
	v_add3_u32 v10, v11, v14, s0
	v_add3_u32 v11, v12, v15, s0
	v_add3_u32 v12, v13, v16, s0
	v_lshrrev_b32_e32 v1, 16, v1
	v_lshrrev_b32_e32 v11, 16, v11
	v_and_or_b32 v10, v10, s1, v1
	v_and_or_b32 v11, v12, s1, v11
	global_store_dwordx2 v[38:39], v[10:11], off offset:928
	v_pk_mul_f32 v[8:9], v[8:9], v[110:111]
	v_pk_mul_f32 v[6:7], v[6:7], v[108:109]
	v_bfe_u32 v11, v8, 16, 1
	v_bfe_u32 v1, v6, 16, 1
	v_bfe_u32 v10, v7, 16, 1
	v_bfe_u32 v12, v9, 16, 1
	v_add3_u32 v1, v6, v1, s0
	v_add3_u32 v6, v7, v10, s0
	v_add3_u32 v7, v8, v11, s0
	v_add3_u32 v8, v9, v12, s0
	v_lshrrev_b32_e32 v1, 16, v1
	v_lshrrev_b32_e32 v7, 16, v7
	v_and_or_b32 v6, v6, s1, v1
	v_and_or_b32 v7, v8, s1, v7
	global_store_dwordx2 v[38:39], v[6:7], off offset:960
	v_pk_mul_f32 v[4:5], v[4:5], v[114:115]
	v_pk_mul_f32 v[2:3], v[2:3], v[112:113]
	v_bfe_u32 v7, v4, 16, 1
	v_bfe_u32 v1, v2, 16, 1
	v_bfe_u32 v6, v3, 16, 1
	v_bfe_u32 v8, v5, 16, 1
	v_add3_u32 v1, v2, v1, s0
	v_add3_u32 v2, v3, v6, s0
	v_add3_u32 v3, v4, v7, s0
	v_add3_u32 v4, v5, v8, s0
	v_lshrrev_b32_e32 v1, 16, v1
	v_lshrrev_b32_e32 v3, 16, v3
	v_and_or_b32 v2, v2, s1, v1
	v_and_or_b32 v3, v4, s1, v3
	global_store_dwordx2 v[38:39], v[2:3], off offset:992
	s_barrier
	s_waitcnt vmcnt(0)
	s_barrier
	s_mov_b64 s[0:1], exec
	v_readlane_b32 s4, v254, 2
	v_readlane_b32 s5, v254, 3
	s_and_b64 s[4:5], s[0:1], s[4:5]
	s_mov_b64 exec, s[4:5]
	s_cbranch_execz .LBB0_584
	s_mov_b32 s2, 0
	s_lshl_b64 s[2:3], s[2:3], 2
	v_readlane_b32 s4, v254, 0
	v_readlane_b32 s5, v254, 1
	s_add_u32 s2, s4, s2
	s_addc_u32 s3, s5, s3
	s_add_i32 s4, 0, 0x20160
	v_mov_b32_e32 v1, s4
	s_waitcnt vmcnt(0) expcnt(0) lgkmcnt(0)
	ds_read_b32 v3, v1
	s_add_i32 s4, 0, 0x20164
	v_mov_b32_e32 v1, s4
	ds_read_b32 v1, v1
	s_waitcnt lgkmcnt(1)
	v_cmp_ne_u32_e32 vcc, 0, v3
	s_cbranch_vccnz .LBB0_548
	v_readlane_b32 s4, v254, 20
	v_readlane_b32 s5, v254, 21
	s_load_dwordx2 s[8:9], s[4:5], 0x4
	s_add_u32 s4, s2, 0x1000
	s_addc_u32 s5, s3, 0
	s_add_u32 s6, s2, 0x1100
	s_addc_u32 s7, s3, 0
	v_readlane_b32 s10, v254, 22
	s_waitcnt lgkmcnt(0)
	s_mul_i32 s26, s8, s10
	s_add_u32 s8, s2, 0x1200
	s_mul_i32 s26, s26, s9
	s_addc_u32 s9, s3, 0
	s_add_u32 s10, s2, 0x1300
	s_addc_u32 s11, s3, 0
	s_mov_b32 s27, 1
	v_mov_b32_e32 v17, 0
	s_branch .LBB0_536

.LBB0_595:
	v_lshl_add_u32 v146, s38, 8, v152
	s_lshl_b32 s26, s55, 8
	s_ashr_i32 s27, s26, 31
	v_ashrrev_i32_e32 v147, 31, v146
	v_lshl_add_u64 v[144:145], s[26:27], 1, v[138:139]
	v_lshlrev_b64 v[148:149], 11, v[146:147]
	v_lshl_add_u64 v[150:151], v[144:145], 0, v[148:149]
	global_load_dwordx4 v[156:159], v[150:151], off
	global_load_dwordx4 v[160:163], v[150:151], off offset:256
	v_or_b32_e32 v148, 16, v146
	v_ashrrev_i32_e32 v149, 31, v148
	v_lshlrev_b64 v[148:149], 11, v[148:149]
	v_lshl_add_u64 v[148:149], v[144:145], 0, v[148:149]
	global_load_dwordx4 v[164:167], v[148:149], off
	global_load_dwordx4 v[168:171], v[148:149], off offset:256
	v_or_b32_e32 v172, 32, v146
	s_and_b64 vcc, exec, s[2:3]
	s_mov_b64 s[2:3], -1
	s_waitcnt vmcnt(0)
	v_lshlrev_b32_e32 v174, 16, v156
	v_and_b32_e32 v175, 0xffff0000, v156
	v_lshlrev_b32_e32 v156, 16, v157
	v_and_b32_e32 v157, 0xffff0000, v157
	v_lshlrev_b32_e32 v176, 16, v158
	v_and_b32_e32 v177, 0xffff0000, v158
	v_lshlrev_b32_e32 v158, 16, v159
	v_and_b32_e32 v159, 0xffff0000, v159
	v_lshlrev_b32_e32 v178, 16, v160
	v_and_b32_e32 v179, 0xffff0000, v160
	v_lshlrev_b32_e32 v160, 16, v161
	v_and_b32_e32 v161, 0xffff0000, v161
	v_lshlrev_b32_e32 v180, 16, v162
	v_and_b32_e32 v181, 0xffff0000, v162
	v_lshlrev_b32_e32 v162, 16, v163
	v_and_b32_e32 v163, 0xffff0000, v163
	v_pk_fma_f32 v[128:129], v[156:157], s[20:21], v[128:129] op_sel_hi:[1,0,1]
	v_pk_fma_f32 v[126:127], v[174:175], s[20:21], v[126:127] op_sel_hi:[1,0,1]
	v_pk_fma_f32 v[124:125], v[158:159], s[20:21], v[124:125] op_sel_hi:[1,0,1]
	v_pk_fma_f32 v[122:123], v[176:177], s[20:21], v[122:123] op_sel_hi:[1,0,1]
	v_pk_fma_f32 v[120:121], v[160:161], s[20:21], v[120:121] op_sel_hi:[1,0,1]
	v_pk_fma_f32 v[118:119], v[178:179], s[20:21], v[118:119] op_sel_hi:[1,0,1]
	v_pk_fma_f32 v[116:117], v[162:163], s[20:21], v[116:117] op_sel_hi:[1,0,1]
	v_pk_fma_f32 v[114:115], v[180:181], s[20:21], v[114:115] op_sel_hi:[1,0,1]
	v_bfe_u32 v147, v126, 16, 1
	v_bfe_u32 v158, v128, 16, 1
	v_bfe_u32 v157, v127, 16, 1
	v_bfe_u32 v159, v129, 16, 1
	v_bfe_u32 v173, v118, 16, 1
	v_bfe_u32 v175, v120, 16, 1
	v_bfe_u32 v177, v114, 16, 1
	v_bfe_u32 v178, v115, 16, 1
	v_bfe_u32 v179, v116, 16, 1
	v_bfe_u32 v180, v117, 16, 1
	v_add3_u32 v126, v126, v147, s51
	v_add3_u32 v128, v128, v158, s51
	v_bfe_u32 v174, v119, 16, 1
	v_bfe_u32 v176, v121, 16, 1
	v_add3_u32 v127, v127, v157, s51
	v_add3_u32 v129, v129, v159, s51
	v_add3_u32 v118, v118, v173, s51
	v_add3_u32 v120, v120, v175, s51
	v_add3_u32 v114, v114, v177, s51
	v_add3_u32 v147, v115, v178, s51
	v_add3_u32 v115, v116, v179, s51
	v_add3_u32 v157, v117, v180, s51
	v_lshrrev_b32_e32 v116, 16, v126
	v_lshrrev_b32_e32 v117, 16, v128
	v_add3_u32 v119, v119, v174, s51
	v_add3_u32 v121, v121, v176, s51
	v_lshrrev_b32_e32 v118, 16, v118
	v_lshrrev_b32_e32 v120, 16, v120
	v_lshrrev_b32_e32 v126, 16, v114
	v_lshrrev_b32_e32 v128, 16, v115
	v_and_or_b32 v114, v127, s50, v116
	v_and_or_b32 v115, v129, s50, v117
	v_cvt_pk_bf16_f32 v116, v122, v123
	v_cvt_pk_bf16_f32 v117, v124, v125
	v_ashrrev_i32_e32 v173, 31, v172
	v_and_or_b32 v118, v119, s50, v118
	v_and_or_b32 v119, v121, s50, v120
	v_and_or_b32 v120, v147, s50, v126
	v_and_or_b32 v121, v157, s50, v128
	global_store_dwordx4 v[150:151], v[114:117], off
	global_store_dwordx4 v[150:151], v[118:121], off offset:256
	v_lshlrev_b32_e32 v156, 16, v164
	v_lshlrev_b64 v[114:115], 11, v[172:173]
	v_lshl_add_u64 v[114:115], v[144:145], 0, v[114:115]
	global_load_dwordx4 v[116:119], v[114:115], off
	global_load_dwordx4 v[120:123], v[114:115], off offset:256
	v_and_b32_e32 v157, 0xffff0000, v164
	v_lshlrev_b32_e32 v124, 16, v165
	v_and_b32_e32 v125, 0xffff0000, v165
	v_lshlrev_b32_e32 v126, 16, v166
	v_and_b32_e32 v127, 0xffff0000, v166
	v_lshlrev_b32_e32 v128, 16, v167
	v_and_b32_e32 v129, 0xffff0000, v167
	v_pk_fma_f32 v[110:111], v[156:157], s[20:21], v[110:111] op_sel_hi:[1,0,1]
	v_pk_fma_f32 v[112:113], v[124:125], s[20:21], v[112:113] op_sel_hi:[1,0,1]
	v_pk_fma_f32 v[124:125], v[128:129], s[20:21], v[108:109] op_sel_hi:[1,0,1]
	v_pk_fma_f32 v[108:109], v[126:127], s[20:21], v[106:107] op_sel_hi:[1,0,1]
	v_cvt_pk_bf16_f32 v106, v110, v111
	v_cvt_pk_bf16_f32 v107, v112, v113
	v_cvt_pk_bf16_f32 v108, v108, v109
	v_lshlrev_b32_e32 v150, 16, v168
	v_and_b32_e32 v151, 0xffff0000, v168
	v_lshlrev_b32_e32 v162, 16, v171
	v_and_b32_e32 v163, 0xffff0000, v171
	v_cvt_pk_bf16_f32 v109, v124, v125
	v_pk_fma_f32 v[102:103], v[150:151], s[20:21], v[102:103] op_sel_hi:[1,0,1]
	global_store_dwordx4 v[148:149], v[106:109], off
	v_lshlrev_b32_e32 v158, 16, v169
	v_and_b32_e32 v159, 0xffff0000, v169
	v_pk_fma_f32 v[108:109], v[162:163], s[20:21], v[100:101] op_sel_hi:[1,0,1]
	v_pk_fma_f32 v[104:105], v[158:159], s[20:21], v[104:105] op_sel_hi:[1,0,1]
	v_cvt_pk_bf16_f32 v100, v102, v103
	v_lshlrev_b32_e32 v160, 16, v170
	v_and_b32_e32 v161, 0xffff0000, v170
	v_pk_fma_f32 v[98:99], v[160:161], s[20:21], v[98:99] op_sel_hi:[1,0,1]
	v_cvt_pk_bf16_f32 v101, v104, v105
	v_cvt_pk_bf16_f32 v102, v98, v99
	v_bfe_u32 v98, v108, 16, 1
	v_add3_u32 v98, v108, v98, s51
	v_lshrrev_b32_e32 v103, 16, v98
	v_or_b32_e32 v98, 48, v146
	v_ashrrev_i32_e32 v99, 31, v98
	v_lshlrev_b64 v[98:99], 11, v[98:99]
	v_lshl_add_u64 v[98:99], v[144:145], 0, v[98:99]
	global_load_dwordx4 v[104:107], v[98:99], off
	v_bfe_u32 v108, v109, 16, 1
	v_add3_u32 v108, v109, v108, s51
	v_and_or_b32 v103, v108, s50, v103
	global_store_dwordx4 v[148:149], v[100:103], off offset:256
	global_load_dwordx4 v[100:103], v[98:99], off offset:256
	s_waitcnt vmcnt(5)
	v_lshlrev_b32_e32 v108, 16, v116
	v_and_b32_e32 v109, 0xffff0000, v116
	v_lshlrev_b32_e32 v110, 16, v117
	v_and_b32_e32 v111, 0xffff0000, v117
	v_lshlrev_b32_e32 v112, 16, v118
	v_and_b32_e32 v113, 0xffff0000, v118
	v_lshlrev_b32_e32 v116, 16, v119
	v_and_b32_e32 v117, 0xffff0000, v119
	v_pk_fma_f32 v[94:95], v[108:109], s[20:21], v[94:95] op_sel_hi:[1,0,1]
	v_pk_fma_f32 v[108:109], v[116:117], s[20:21], v[92:93] op_sel_hi:[1,0,1]
	v_pk_fma_f32 v[92:93], v[112:113], s[20:21], v[90:91] op_sel_hi:[1,0,1]
	v_pk_fma_f32 v[96:97], v[110:111], s[20:21], v[96:97] op_sel_hi:[1,0,1]
	v_cvt_pk_bf16_f32 v90, v94, v95
	v_cvt_pk_bf16_f32 v91, v96, v97
	v_cvt_pk_bf16_f32 v92, v92, v93
	s_waitcnt vmcnt(4)
	v_lshlrev_b32_e32 v118, 16, v120
	v_and_b32_e32 v119, 0xffff0000, v120
	v_lshlrev_b32_e32 v124, 16, v122
	v_and_b32_e32 v125, 0xffff0000, v122
	v_lshlrev_b32_e32 v122, 16, v123
	v_and_b32_e32 v123, 0xffff0000, v123
	v_cvt_pk_bf16_f32 v93, v108, v109
	v_pk_fma_f32 v[86:87], v[118:119], s[20:21], v[86:87] op_sel_hi:[1,0,1]
	global_store_dwordx4 v[114:115], v[90:93], off
	v_lshlrev_b32_e32 v120, 16, v121
	v_and_b32_e32 v121, 0xffff0000, v121
	v_pk_fma_f32 v[90:91], v[122:123], s[20:21], v[84:85] op_sel_hi:[1,0,1]
	v_pk_fma_f32 v[84:85], v[124:125], s[20:21], v[82:83] op_sel_hi:[1,0,1]
	v_pk_fma_f32 v[88:89], v[120:121], s[20:21], v[88:89] op_sel_hi:[1,0,1]
	v_cvt_pk_bf16_f32 v82, v86, v87
	v_cvt_pk_bf16_f32 v83, v88, v89
	v_cvt_pk_bf16_f32 v84, v84, v85
	v_cvt_pk_bf16_f32 v85, v90, v91
	global_store_dwordx4 v[114:115], v[82:85], off offset:256
	s_waitcnt vmcnt(4)
	v_lshlrev_b32_e32 v92, 16, v104
	v_and_b32_e32 v93, 0xffff0000, v104
	v_add_u32_e32 v82, 0x80, v146
	v_ashrrev_i32_e32 v83, 31, v82
	v_lshlrev_b64 v[82:83], 11, v[82:83]
	v_lshl_add_u64 v[82:83], v[144:145], 0, v[82:83]
	global_load_dwordx4 v[84:87], v[82:83], off
	global_load_dwordx4 v[88:91], v[82:83], off offset:256
	v_lshlrev_b32_e32 v94, 16, v105
	v_and_b32_e32 v95, 0xffff0000, v105
	v_lshlrev_b32_e32 v96, 16, v106
	v_and_b32_e32 v97, 0xffff0000, v106
	v_lshlrev_b32_e32 v104, 16, v107
	v_and_b32_e32 v105, 0xffff0000, v107
	v_pk_fma_f32 v[78:79], v[92:93], s[20:21], v[78:79] op_sel_hi:[1,0,1]
	v_pk_fma_f32 v[92:93], v[104:105], s[20:21], v[76:77] op_sel_hi:[1,0,1]
	v_pk_fma_f32 v[76:77], v[96:97], s[20:21], v[74:75] op_sel_hi:[1,0,1]
	v_pk_fma_f32 v[80:81], v[94:95], s[20:21], v[80:81] op_sel_hi:[1,0,1]
	v_cvt_pk_bf16_f32 v74, v78, v79
	v_cvt_pk_bf16_f32 v75, v80, v81
	v_cvt_pk_bf16_f32 v76, v76, v77
	s_waitcnt vmcnt(4)
	v_lshlrev_b32_e32 v106, 16, v100
	v_and_b32_e32 v107, 0xffff0000, v100
	v_lshlrev_b32_e32 v108, 16, v102
	v_and_b32_e32 v109, 0xffff0000, v102
	v_lshlrev_b32_e32 v102, 16, v103
	v_and_b32_e32 v103, 0xffff0000, v103
	v_cvt_pk_bf16_f32 v77, v92, v93
	v_pk_fma_f32 v[70:71], v[106:107], s[20:21], v[70:71] op_sel_hi:[1,0,1]
	global_store_dwordx4 v[98:99], v[74:77], off
	v_lshlrev_b32_e32 v100, 16, v101
	v_and_b32_e32 v101, 0xffff0000, v101
	v_pk_fma_f32 v[76:77], v[102:103], s[20:21], v[68:69] op_sel_hi:[1,0,1]
	v_pk_fma_f32 v[72:73], v[100:101], s[20:21], v[72:73] op_sel_hi:[1,0,1]
	v_cvt_pk_bf16_f32 v68, v70, v71
	v_pk_fma_f32 v[66:67], v[108:109], s[20:21], v[66:67] op_sel_hi:[1,0,1]
	v_cvt_pk_bf16_f32 v69, v72, v73
	v_cvt_pk_bf16_f32 v70, v66, v67
	v_bfe_u32 v66, v76, 16, 1
	v_add3_u32 v66, v76, v66, s51
	v_lshrrev_b32_e32 v71, 16, v66
	v_add_u32_e32 v66, 0x90, v146
	v_ashrrev_i32_e32 v67, 31, v66
	v_lshlrev_b64 v[66:67], 11, v[66:67]
	v_lshl_add_u64 v[66:67], v[144:145], 0, v[66:67]
	global_load_dwordx4 v[72:75], v[66:67], off
	v_bfe_u32 v76, v77, 16, 1
	v_add3_u32 v76, v77, v76, s51
	v_and_or_b32 v71, v76, s50, v71
	global_store_dwordx4 v[98:99], v[68:71], off offset:256
	global_load_dwordx4 v[68:71], v[66:67], off offset:256
	s_waitcnt vmcnt(5)
	v_lshlrev_b32_e32 v76, 16, v84
	v_and_b32_e32 v77, 0xffff0000, v84
	v_lshlrev_b32_e32 v78, 16, v85
	v_and_b32_e32 v79, 0xffff0000, v85
	v_lshlrev_b32_e32 v80, 16, v86
	v_and_b32_e32 v81, 0xffff0000, v86
	v_lshlrev_b32_e32 v84, 16, v87
	v_and_b32_e32 v85, 0xffff0000, v87
	v_pk_fma_f32 v[62:63], v[76:77], s[20:21], v[62:63] op_sel_hi:[1,0,1]
	v_pk_fma_f32 v[76:77], v[84:85], s[20:21], v[60:61] op_sel_hi:[1,0,1]
	v_pk_fma_f32 v[60:61], v[80:81], s[20:21], v[58:59] op_sel_hi:[1,0,1]
	v_pk_fma_f32 v[64:65], v[78:79], s[20:21], v[64:65] op_sel_hi:[1,0,1]
	v_cvt_pk_bf16_f32 v58, v62, v63
	v_cvt_pk_bf16_f32 v59, v64, v65
	v_cvt_pk_bf16_f32 v60, v60, v61
	s_waitcnt vmcnt(4)
	v_lshlrev_b32_e32 v86, 16, v88
	v_and_b32_e32 v87, 0xffff0000, v88
	v_lshlrev_b32_e32 v92, 16, v90
	v_and_b32_e32 v93, 0xffff0000, v90
	v_lshlrev_b32_e32 v90, 16, v91
	v_and_b32_e32 v91, 0xffff0000, v91
	v_cvt_pk_bf16_f32 v61, v76, v77
	v_pk_fma_f32 v[54:55], v[86:87], s[20:21], v[54:55] op_sel_hi:[1,0,1]
	global_store_dwordx4 v[82:83], v[58:61], off
	v_lshlrev_b32_e32 v88, 16, v89
	v_and_b32_e32 v89, 0xffff0000, v89
	v_pk_fma_f32 v[58:59], v[90:91], s[20:21], v[52:53] op_sel_hi:[1,0,1]
	v_pk_fma_f32 v[52:53], v[92:93], s[20:21], v[50:51] op_sel_hi:[1,0,1]
	v_pk_fma_f32 v[56:57], v[88:89], s[20:21], v[56:57] op_sel_hi:[1,0,1]
	v_cvt_pk_bf16_f32 v50, v54, v55
	v_cvt_pk_bf16_f32 v51, v56, v57
	v_cvt_pk_bf16_f32 v52, v52, v53
	v_cvt_pk_bf16_f32 v53, v58, v59
	global_store_dwordx4 v[82:83], v[50:53], off offset:256
	s_waitcnt vmcnt(4)
	v_lshlrev_b32_e32 v60, 16, v72
	v_and_b32_e32 v61, 0xffff0000, v72
	v_add_u32_e32 v50, 0xa0, v146
	v_ashrrev_i32_e32 v51, 31, v50
	v_lshlrev_b64 v[50:51], 11, v[50:51]
	v_lshl_add_u64 v[50:51], v[144:145], 0, v[50:51]
	global_load_dwordx4 v[52:55], v[50:51], off
	global_load_dwordx4 v[56:59], v[50:51], off offset:256
	v_lshlrev_b32_e32 v62, 16, v73
	v_and_b32_e32 v63, 0xffff0000, v73
	v_lshlrev_b32_e32 v64, 16, v74
	v_and_b32_e32 v65, 0xffff0000, v74
	v_lshlrev_b32_e32 v72, 16, v75
	v_and_b32_e32 v73, 0xffff0000, v75
	v_pk_fma_f32 v[46:47], v[60:61], s[20:21], v[46:47] op_sel_hi:[1,0,1]
	v_pk_fma_f32 v[60:61], v[72:73], s[20:21], v[44:45] op_sel_hi:[1,0,1]
	v_pk_fma_f32 v[44:45], v[64:65], s[20:21], v[42:43] op_sel_hi:[1,0,1]
	v_pk_fma_f32 v[48:49], v[62:63], s[20:21], v[48:49] op_sel_hi:[1,0,1]
	v_cvt_pk_bf16_f32 v42, v46, v47
	v_cvt_pk_bf16_f32 v43, v48, v49
	v_cvt_pk_bf16_f32 v44, v44, v45
	s_waitcnt vmcnt(4)
	v_lshlrev_b32_e32 v74, 16, v68
	v_and_b32_e32 v75, 0xffff0000, v68
	v_lshlrev_b32_e32 v76, 16, v70
	v_and_b32_e32 v77, 0xffff0000, v70
	v_lshlrev_b32_e32 v70, 16, v71
	v_and_b32_e32 v71, 0xffff0000, v71
	v_cvt_pk_bf16_f32 v45, v60, v61
	v_pk_fma_f32 v[38:39], v[74:75], s[20:21], v[38:39] op_sel_hi:[1,0,1]
	global_store_dwordx4 v[66:67], v[42:45], off
	v_lshlrev_b32_e32 v68, 16, v69
	v_and_b32_e32 v69, 0xffff0000, v69
	v_pk_fma_f32 v[42:43], v[70:71], s[20:21], v[36:37] op_sel_hi:[1,0,1]
	v_pk_fma_f32 v[36:37], v[76:77], s[20:21], v[34:35] op_sel_hi:[1,0,1]
	v_pk_fma_f32 v[40:41], v[68:69], s[20:21], v[40:41] op_sel_hi:[1,0,1]
	v_cvt_pk_bf16_f32 v34, v38, v39
	v_cvt_pk_bf16_f32 v35, v40, v41
	v_bfe_u32 v38, v36, 16, 1
	v_add3_u32 v36, v36, v38, s51
	v_bfe_u32 v38, v37, 16, 1
	v_add3_u32 v37, v37, v38, s51
	v_add_u32_e32 v38, 0xb0, v146
	v_ashrrev_i32_e32 v39, 31, v38
	v_lshlrev_b64 v[38:39], 11, v[38:39]
	v_lshl_add_u64 v[44:45], v[144:145], 0, v[38:39]
	global_load_dwordx4 v[38:41], v[44:45], off
	v_lshrrev_b32_e32 v36, 16, v36
	v_and_or_b32 v36, v37, s50, v36
	v_cvt_pk_bf16_f32 v37, v42, v43
	global_store_dwordx4 v[66:67], v[34:37], off offset:256
	global_load_dwordx4 v[34:37], v[44:45], off offset:256
	s_waitcnt vmcnt(5)
	v_lshlrev_b32_e32 v42, 16, v52
	v_and_b32_e32 v43, 0xffff0000, v52
	v_lshlrev_b32_e32 v46, 16, v53
	v_and_b32_e32 v47, 0xffff0000, v53
	v_lshlrev_b32_e32 v48, 16, v54
	v_and_b32_e32 v49, 0xffff0000, v54
	v_lshlrev_b32_e32 v52, 16, v55
	v_and_b32_e32 v53, 0xffff0000, v55
	v_pk_fma_f32 v[30:31], v[42:43], s[20:21], v[30:31] op_sel_hi:[1,0,1]
	v_pk_fma_f32 v[42:43], v[52:53], s[20:21], v[28:29] op_sel_hi:[1,0,1]
	v_pk_fma_f32 v[28:29], v[48:49], s[20:21], v[26:27] op_sel_hi:[1,0,1]
	v_pk_fma_f32 v[32:33], v[46:47], s[20:21], v[32:33] op_sel_hi:[1,0,1]
	v_cvt_pk_bf16_f32 v26, v30, v31
	v_cvt_pk_bf16_f32 v27, v32, v33
	v_cvt_pk_bf16_f32 v28, v28, v29
	s_waitcnt vmcnt(4)
	v_lshlrev_b32_e32 v54, 16, v56
	v_and_b32_e32 v55, 0xffff0000, v56
	v_lshlrev_b32_e32 v60, 16, v58
	v_and_b32_e32 v61, 0xffff0000, v58
	v_lshlrev_b32_e32 v58, 16, v59
	v_and_b32_e32 v59, 0xffff0000, v59
	v_cvt_pk_bf16_f32 v29, v42, v43
	v_pk_fma_f32 v[22:23], v[54:55], s[20:21], v[22:23] op_sel_hi:[1,0,1]
	global_store_dwordx4 v[50:51], v[26:29], off
	v_lshlrev_b32_e32 v56, 16, v57
	v_and_b32_e32 v57, 0xffff0000, v57
	v_pk_fma_f32 v[26:27], v[58:59], s[20:21], v[20:21] op_sel_hi:[1,0,1]
	v_pk_fma_f32 v[20:21], v[60:61], s[20:21], v[18:19] op_sel_hi:[1,0,1]
	v_pk_fma_f32 v[24:25], v[56:57], s[20:21], v[24:25] op_sel_hi:[1,0,1]
	v_cvt_pk_bf16_f32 v18, v22, v23
	v_cvt_pk_bf16_f32 v19, v24, v25
	v_cvt_pk_bf16_f32 v20, v20, v21
	v_cvt_pk_bf16_f32 v21, v26, v27
	global_store_dwordx4 v[50:51], v[18:21], off offset:256
	s_waitcnt vmcnt(4)
	v_lshlrev_b32_e32 v22, 16, v40
	v_and_b32_e32 v23, 0xffff0000, v40
	v_lshlrev_b32_e32 v18, 16, v38
	v_and_b32_e32 v19, 0xffff0000, v38
	v_lshlrev_b32_e32 v24, 16, v41
	v_and_b32_e32 v25, 0xffff0000, v41
	v_pk_fma_f32 v[14:15], v[18:19], s[20:21], v[14:15] op_sel_hi:[1,0,1]
	v_pk_fma_f32 v[18:19], v[24:25], s[20:21], v[12:13] op_sel_hi:[1,0,1]
	v_pk_fma_f32 v[12:13], v[22:23], s[20:21], v[10:11] op_sel_hi:[1,0,1]
	v_lshlrev_b32_e32 v20, 16, v39
	v_and_b32_e32 v21, 0xffff0000, v39
	v_pk_fma_f32 v[16:17], v[20:21], s[20:21], v[16:17] op_sel_hi:[1,0,1]
	v_cvt_pk_bf16_f32 v10, v14, v15
	v_cvt_pk_bf16_f32 v11, v16, v17
	v_cvt_pk_bf16_f32 v12, v12, v13
	s_waitcnt vmcnt(2)
	v_lshlrev_b32_e32 v26, 16, v34
	v_and_b32_e32 v27, 0xffff0000, v34
	v_lshlrev_b32_e32 v30, 16, v36
	v_and_b32_e32 v31, 0xffff0000, v36
	v_lshlrev_b32_e32 v32, 16, v37
	v_and_b32_e32 v33, 0xffff0000, v37
	v_cvt_pk_bf16_f32 v13, v18, v19
	v_pk_fma_f32 v[6:7], v[26:27], s[20:21], v[6:7] op_sel_hi:[1,0,1]
	global_store_dwordx4 v[44:45], v[10:13], off
	v_lshlrev_b32_e32 v28, 16, v35
	v_and_b32_e32 v29, 0xffff0000, v35
	v_pk_fma_f32 v[10:11], v[32:33], s[20:21], v[4:5] op_sel_hi:[1,0,1]
	v_pk_fma_f32 v[4:5], v[30:31], s[20:21], v[2:3] op_sel_hi:[1,0,1]
	v_pk_fma_f32 v[8:9], v[28:29], s[20:21], v[8:9] op_sel_hi:[1,0,1]
	v_cvt_pk_bf16_f32 v2, v6, v7
	v_cvt_pk_bf16_f32 v3, v8, v9
	v_cvt_pk_bf16_f32 v4, v4, v5
	v_cvt_pk_bf16_f32 v5, v10, v11
	global_store_dwordx4 v[44:45], v[2:5], off offset:256
	s_cbranch_vccnz .LBB0_588
	s_andn2_b64 vcc, exec, s[4:5]
	s_cbranch_vccnz .LBB0_587
	s_barrier
	s_branch .LBB0_587

.LBB0_617:
	s_waitcnt vmcnt(7)
	v_lshlrev_b32_e32 v87, 16, v59
	v_lshlrev_b32_e32 v86, 16, v58
	v_and_b32_e32 v59, 0xffff0000, v59
	v_and_b32_e32 v58, 0xffff0000, v58
	v_pk_add_f32 v[88:89], v[86:87], v[58:59]
	s_waitcnt vmcnt(6)
	v_lshlrev_b32_e32 v82, 16, v65
	v_and_b32_e32 v84, 0xffff0000, v65
	v_add_f32_e32 v65, v88, v89
	v_lshlrev_b32_e32 v89, 16, v61
	v_lshlrev_b32_e32 v88, 16, v60
	v_and_b32_e32 v61, 0xffff0000, v61
	v_and_b32_e32 v60, 0xffff0000, v60
	v_pk_add_f32 v[90:91], v[88:89], v[60:61]
	v_lshlrev_b32_e32 v72, 16, v62
	v_and_b32_e32 v73, 0xffff0000, v62
	v_lshlrev_b32_e32 v62, 16, v63
	v_and_b32_e32 v63, 0xffff0000, v63
	v_pk_add_f32 v[90:91], v[90:91], v[90:91] op_sel_hi:[0,1]
	v_lshlrev_b32_e32 v80, 16, v64
	v_and_b32_e32 v64, 0xffff0000, v64
	v_add_f32_e32 v85, 0, v65
	v_add_f32_e32 v81, v72, v73
	v_add_f32_e32 v65, v62, v63
	v_mov_b32_e32 v83, v91
	v_pk_add_f32 v[92:93], v[80:81], v[64:65]
	v_pk_add_f32 v[90:91], v[82:83], v[84:85]
	s_add_i32 s4, s4, 4
	v_pk_add_f32 v[90:91], v[92:93], v[90:91]
	s_cmp_lt_u32 s4, 12
	v_add_f32_e32 v65, v90, v91
	s_waitcnt lgkmcnt(0)
	s_nop 1
	v_add_f32_dpp v65, v65, v65 quad_perm:[1,0,3,2] row_mask:0xf bank_mask:0xf
	s_nop 1
	v_add_f32_dpp v65, v65, v65 quad_perm:[2,3,0,1] row_mask:0xf bank_mask:0xf
	s_nop 1
	v_add_f32_dpp v65, v65, v65 row_half_mirror row_mask:0xf bank_mask:0xf
	s_nop 1
	v_add_f32_dpp v65, v65, v65 row_mirror row_mask:0xf bank_mask:0xf
	v_mov_b32_e32 v81, v65
	s_nop 1
	v_permlane16_swap_b32_e32 v65, v81
	v_add_f32_e32 v65, v65, v81
	v_mov_b32_e32 v81, v65
	s_nop 1
	v_permlane32_swap_b32_e32 v65, v81
	v_add_f32_e32 v65, v65, v81
	v_fmac_f32_e32 v58, 0xba800000, v65
	v_fmac_f32_e32 v59, 0xba800000, v65
	v_fmac_f32_e32 v87, 0xba800000, v65
	v_fmac_f32_e32 v86, 0xba800000, v65
	v_mov_b32_e32 v90, v87
	v_mov_b32_e32 v91, v59
	v_mov_b32_e32 v87, v58
	v_pk_mul_f32 v[92:93], v[90:91], v[90:91]
	v_pk_mul_f32 v[58:59], v[86:87], v[86:87]
	v_fmac_f32_e32 v60, 0xba800000, v65
	v_pk_mov_b32 v[94:95], v[58:59], v[92:93] op_sel:[1,0]
	v_mov_b32_e32 v59, v93
	v_fmac_f32_e32 v61, 0xba800000, v65
	v_fmac_f32_e32 v89, 0xba800000, v65
	v_pk_add_f32 v[58:59], v[94:95], v[58:59]
	v_fmac_f32_e32 v88, 0xba800000, v65
	v_mov_b32_e32 v92, v89
	v_mov_b32_e32 v93, v61
	v_mov_b32_e32 v89, v60
	v_pk_add_f32 v[58:59], v[58:59], v[58:59] op_sel_hi:[0,1]
	v_pk_mul_f32 v[94:95], v[92:93], v[92:93]
	v_pk_mul_f32 v[60:61], v[88:89], v[88:89]
	v_fmac_f32_e32 v72, 0xba800000, v65
	v_pk_mov_b32 v[96:97], v[60:61], v[94:95] op_sel:[1,0]
	v_mov_b32_e32 v61, v95
	v_fmac_f32_e32 v73, 0xba800000, v65
	v_fmac_f32_e32 v62, 0xba800000, v65
	v_mul_f32_e32 v58, v72, v72
	v_pk_add_f32 v[60:61], v[96:97], v[60:61]
	v_fmac_f32_e32 v63, 0xba800000, v65
	v_pk_fma_f32 v[94:95], v[72:73], v[72:73], v[58:59] op_sel_hi:[1,1,0]
	v_mul_f32_e32 v58, v62, v62
	v_pk_add_f32 v[60:61], v[60:61], v[60:61] op_sel_hi:[0,1]
	v_pk_fma_f32 v[96:97], v[62:63], v[62:63], v[58:59] op_sel_hi:[1,1,0]
	v_fmac_f32_e32 v84, 0xba800000, v65
	v_fmac_f32_e32 v82, 0xba800000, v65
	v_fmac_f32_e32 v64, 0xba800000, v65
	v_fmac_f32_e32 v80, 0xba800000, v65
	v_mul_f32_e32 v94, v80, v80
	v_mul_f32_e32 v96, v64, v64
	v_mul_f32_e32 v58, v82, v82
	v_mul_f32_e32 v60, v84, v84
	v_pk_add_f32 v[94:95], v[94:95], v[96:97]
	v_pk_add_f32 v[58:59], v[58:59], v[60:61]
	v_mov_b32_e32 v83, v84
	v_pk_add_f32 v[58:59], v[94:95], v[58:59]
	s_nop 0
	v_add_f32_e32 v58, v58, v59
	s_waitcnt lgkmcnt(0)
	s_nop 1
	v_add_f32_dpp v58, v58, v58 quad_perm:[1,0,3,2] row_mask:0xf bank_mask:0xf
	s_nop 1
	v_add_f32_dpp v58, v58, v58 quad_perm:[2,3,0,1] row_mask:0xf bank_mask:0xf
	s_nop 1
	v_add_f32_dpp v58, v58, v58 row_half_mirror row_mask:0xf bank_mask:0xf
	s_nop 1
	v_add_f32_dpp v58, v58, v58 row_mirror row_mask:0xf bank_mask:0xf
	v_mov_b32_e32 v59, v58
	s_nop 1
	v_permlane16_swap_b32_e32 v58, v59
	v_add_f32_e32 v58, v58, v59
	v_mov_b32_e32 v59, v58
	s_nop 1
	v_permlane32_swap_b32_e32 v58, v59
	v_add_f32_e32 v58, v58, v59
	v_fmamk_f32 v58, v58, 0x3a800000, v78
	v_mul_f32_e32 v59, 0x4f800000, v58
	v_cmp_gt_f32_e32 vcc, s6, v58
	s_nop 1
	v_cndmask_b32_e32 v58, v58, v59, vcc
	v_sqrt_f32_e32 v59, v58
	s_nop 0
	v_add_u32_e32 v60, -1, v59
	v_fma_f32 v61, -v60, v59, v58
	v_cmp_ge_f32_e64 s[0:1], 0, v61
	v_add_u32_e32 v61, 1, v59
	s_nop 0
	v_cndmask_b32_e64 v60, v59, v60, s[0:1]
	v_fma_f32 v59, -v61, v59, v58
	v_cmp_lt_f32_e64 s[0:1], 0, v59
	s_nop 1
	v_cndmask_b32_e64 v59, v60, v61, s[0:1]
	v_mul_f32_e32 v60, 0x37800000, v59
	v_cndmask_b32_e32 v59, v59, v60, vcc
	v_cmp_class_f32_e32 vcc, v58, v79
	s_nop 1
	v_cndmask_b32_e32 v58, v59, v58, vcc
	v_div_scale_f32 v59, s[0:1], v58, v58, 1.0
	v_rcp_f32_e32 v60, v59
	s_nop 0
	v_fma_f32 v61, -v59, v60, 1.0
	v_fmac_f32_e32 v60, v61, v60
	v_div_scale_f32 v61, vcc, 1.0, v58, 1.0
	v_mul_f32_e32 v65, v61, v60
	v_fma_f32 v81, -v59, v65, v61
	v_fmac_f32_e32 v65, v81, v60
	v_fma_f32 v59, -v59, v65, v61
	v_div_fmas_f32 v59, v59, v60, v65
	v_div_fixup_f32 v58, v59, v58, 1.0
	v_pk_mul_f32 v[60:61], v[86:87], v[58:59] op_sel_hi:[1,0]
	v_mov_b32_e32 v81, v64
	v_pk_mul_f32 v[86:87], v[90:91], v[58:59] op_sel_hi:[1,0]
	v_pk_fma_f32 v[60:61], v[10:11], v[60:61], v[14:15]
	v_pk_mul_f32 v[88:89], v[88:89], v[58:59] op_sel_hi:[1,0]
	v_pk_mul_f32 v[90:91], v[92:93], v[58:59] op_sel_hi:[1,0]
	v_pk_mul_f32 v[72:73], v[72:73], v[58:59] op_sel_hi:[1,0]
	v_pk_mul_f32 v[62:63], v[62:63], v[58:59] op_sel_hi:[1,0]
	v_pk_mul_f32 v[64:65], v[80:81], v[58:59] op_sel_hi:[1,0]
	v_pk_mul_f32 v[58:59], v[82:83], v[58:59] op_sel_hi:[1,0]
	v_pk_fma_f32 v[86:87], v[12:13], v[86:87], v[16:17]
	v_pk_fma_f32 v[80:81], v[20:21], v[58:59], v[24:25]
	v_cvt_pk_bf16_f32 v58, v60, v61
	v_pk_fma_f32 v[88:89], v[2:3], v[88:89], v[6:7]
	v_cvt_pk_bf16_f32 v59, v86, v87
	v_pk_fma_f32 v[90:91], v[4:5], v[90:91], v[8:9]
	v_cvt_pk_bf16_f32 v60, v88, v89
	v_pk_fma_f32 v[72:73], v[26:27], v[72:73], v[30:31]
	v_cvt_pk_bf16_f32 v61, v90, v91
	global_store_dwordx4 v[70:71], v[58:61], off offset:-1024
	v_pk_fma_f32 v[62:63], v[28:29], v[62:63], v[32:33]
	v_pk_fma_f32 v[64:65], v[18:19], v[64:65], v[22:23]
	v_cvt_pk_bf16_f32 v58, v72, v73
	v_cvt_pk_bf16_f32 v59, v62, v63
	v_cvt_pk_bf16_f32 v60, v64, v65
	v_cvt_pk_bf16_f32 v61, v80, v81
	global_store_dwordx4 v[70:71], v[58:61], off
	v_lshl_add_u64 v[70:71], v[70:71], 0, s[2:3]
	s_cbranch_scc0 .LBB0_624
.LBB0_618:
	s_waitcnt vmcnt(5)
	v_lshlrev_b32_e32 v91, 16, v35
	v_lshlrev_b32_e32 v90, 16, v34
	v_and_b32_e32 v59, 0xffff0000, v35
	v_and_b32_e32 v58, 0xffff0000, v34
	v_pk_add_f32 v[60:61], v[90:91], v[58:59]
	v_lshlrev_b32_e32 v93, 16, v37
	v_add_f32_e32 v60, v60, v61
	v_add_f32_e32 v89, 0, v60
	v_lshlrev_b32_e32 v92, 16, v36
	v_and_b32_e32 v61, 0xffff0000, v37
	v_and_b32_e32 v60, 0xffff0000, v36
	v_pk_add_f32 v[62:63], v[92:93], v[60:61]
	s_waitcnt vmcnt(4)
	v_lshlrev_b32_e32 v72, 16, v38
	v_and_b32_e32 v73, 0xffff0000, v38
	v_lshlrev_b32_e32 v80, 16, v39
	v_and_b32_e32 v81, 0xffff0000, v39
	v_pk_add_f32 v[62:63], v[62:63], v[62:63] op_sel_hi:[0,1]
	v_lshlrev_b32_e32 v82, 16, v40
	v_and_b32_e32 v84, 0xffff0000, v40
	v_lshlrev_b32_e32 v86, 16, v41
	v_and_b32_e32 v88, 0xffff0000, v41
	v_add_f32_e32 v83, v72, v73
	v_add_f32_e32 v85, v80, v81
	v_mov_b32_e32 v87, v63
	v_pk_add_f32 v[64:65], v[82:83], v[84:85]
	v_pk_add_f32 v[62:63], v[86:87], v[88:89]
	s_nop 0
	v_pk_add_f32 v[62:63], v[64:65], v[62:63]
	s_nop 0
	v_add_f32_e32 v62, v62, v63
	s_waitcnt lgkmcnt(0)
	s_nop 1
	v_add_f32_dpp v62, v62, v62 quad_perm:[1,0,3,2] row_mask:0xf bank_mask:0xf
	s_nop 1
	v_add_f32_dpp v62, v62, v62 quad_perm:[2,3,0,1] row_mask:0xf bank_mask:0xf
	s_nop 1
	v_add_f32_dpp v62, v62, v62 row_half_mirror row_mask:0xf bank_mask:0xf
	s_nop 1
	v_add_f32_dpp v62, v62, v62 row_mirror row_mask:0xf bank_mask:0xf
	v_mov_b32_e32 v63, v62
	s_nop 1
	v_permlane16_swap_b32_e32 v62, v63
	v_add_f32_e32 v62, v62, v63
	v_mov_b32_e32 v63, v62
	s_nop 1
	v_permlane32_swap_b32_e32 v62, v63
	v_add_f32_e32 v83, v62, v63
	v_fmac_f32_e32 v58, 0xba800000, v83
	v_fmac_f32_e32 v59, 0xba800000, v83
	v_fmac_f32_e32 v91, 0xba800000, v83
	v_fmac_f32_e32 v90, 0xba800000, v83
	v_mov_b32_e32 v94, v91
	v_mov_b32_e32 v95, v59
	v_mov_b32_e32 v91, v58
	v_pk_mul_f32 v[62:63], v[94:95], v[94:95]
	v_pk_mul_f32 v[58:59], v[90:91], v[90:91]
	v_fmac_f32_e32 v60, 0xba800000, v83
	v_pk_mov_b32 v[64:65], v[58:59], v[62:63] op_sel:[1,0]
	v_mov_b32_e32 v59, v63
	v_fmac_f32_e32 v61, 0xba800000, v83
	v_fmac_f32_e32 v93, 0xba800000, v83
	v_pk_add_f32 v[58:59], v[64:65], v[58:59]
	v_fmac_f32_e32 v92, 0xba800000, v83
	v_mov_b32_e32 v96, v93
	v_mov_b32_e32 v97, v61
	v_mov_b32_e32 v93, v60
	v_pk_add_f32 v[58:59], v[58:59], v[58:59] op_sel_hi:[0,1]
	v_pk_mul_f32 v[62:63], v[96:97], v[96:97]
	v_pk_mul_f32 v[60:61], v[92:93], v[92:93]
	v_fmac_f32_e32 v72, 0xba800000, v83
	v_pk_mov_b32 v[64:65], v[60:61], v[62:63] op_sel:[1,0]
	v_mov_b32_e32 v61, v63
	v_fmac_f32_e32 v73, 0xba800000, v83
	v_fmac_f32_e32 v80, 0xba800000, v83
	v_mul_f32_e32 v58, v72, v72
	v_pk_add_f32 v[60:61], v[64:65], v[60:61]
	v_fmac_f32_e32 v81, 0xba800000, v83
	v_pk_fma_f32 v[62:63], v[72:73], v[72:73], v[58:59] op_sel_hi:[1,1,0]
	v_mul_f32_e32 v58, v80, v80
	v_pk_add_f32 v[60:61], v[60:61], v[60:61] op_sel_hi:[0,1]
	v_pk_fma_f32 v[64:65], v[80:81], v[80:81], v[58:59] op_sel_hi:[1,1,0]
	v_fmac_f32_e32 v88, 0xba800000, v83
	v_fmac_f32_e32 v86, 0xba800000, v83
	v_fmac_f32_e32 v84, 0xba800000, v83
	v_fmac_f32_e32 v82, 0xba800000, v83
	v_mul_f32_e32 v62, v82, v82
	v_mul_f32_e32 v64, v84, v84
	v_mul_f32_e32 v58, v86, v86
	v_mul_f32_e32 v60, v88, v88
	v_pk_add_f32 v[62:63], v[62:63], v[64:65]
	v_pk_add_f32 v[58:59], v[58:59], v[60:61]
	s_nop 0
	v_pk_add_f32 v[58:59], v[62:63], v[58:59]
	s_nop 0
	v_add_f32_e32 v58, v58, v59
	s_waitcnt lgkmcnt(0)
	s_nop 1
	v_add_f32_dpp v58, v58, v58 quad_perm:[1,0,3,2] row_mask:0xf bank_mask:0xf
	s_nop 1
	v_add_f32_dpp v58, v58, v58 quad_perm:[2,3,0,1] row_mask:0xf bank_mask:0xf
	s_nop 1
	v_add_f32_dpp v58, v58, v58 row_half_mirror row_mask:0xf bank_mask:0xf
	s_nop 1
	v_add_f32_dpp v58, v58, v58 row_mirror row_mask:0xf bank_mask:0xf
	v_mov_b32_e32 v59, v58
	s_nop 1
	v_permlane16_swap_b32_e32 v58, v59
	v_add_f32_e32 v58, v58, v59
	v_mov_b32_e32 v59, v58
	s_nop 1
	v_permlane32_swap_b32_e32 v58, v59
	v_add_f32_e32 v58, v58, v59
	v_fmamk_f32 v58, v58, 0x3a800000, v78
	v_mul_f32_e32 v59, 0x4f800000, v58
	v_cmp_gt_f32_e32 vcc, s6, v58
	s_nop 1
	v_cndmask_b32_e32 v58, v58, v59, vcc
	v_sqrt_f32_e32 v59, v58
	s_nop 0
	v_add_u32_e32 v60, -1, v59
	v_fma_f32 v61, -v60, v59, v58
	v_cmp_ge_f32_e64 s[0:1], 0, v61
	v_add_u32_e32 v61, 1, v59
	s_nop 0
	v_cndmask_b32_e64 v60, v59, v60, s[0:1]
	v_fma_f32 v59, -v61, v59, v58
	v_cmp_lt_f32_e64 s[0:1], 0, v59
	s_nop 1
	v_cndmask_b32_e64 v59, v60, v61, s[0:1]
	v_mul_f32_e32 v60, 0x37800000, v59
	v_cndmask_b32_e32 v59, v59, v60, vcc
	v_cmp_class_f32_e32 vcc, v58, v79
	s_nop 1
	v_cndmask_b32_e32 v83, v59, v58, vcc
	global_load_dwordx4 v[58:61], v[70:71], off offset:-1024
	global_load_dwordx4 v[62:65], v[70:71], off
	v_div_scale_f32 v85, s[0:1], v83, v83, 1.0
	v_rcp_f32_e32 v87, v85
	s_add_i32 s0, s4, 5
	s_cmp_gt_u32 s0, 12
	v_fma_f32 v89, -v85, v87, 1.0
	v_fmac_f32_e32 v87, v89, v87
	v_div_scale_f32 v89, vcc, 1.0, v83, 1.0
	v_mul_f32_e32 v98, v89, v87
	v_fma_f32 v99, -v85, v98, v89
	v_fmac_f32_e32 v98, v99, v87
	v_fma_f32 v85, -v85, v98, v89
	v_div_fmas_f32 v85, v85, v87, v98
	v_div_fixup_f32 v98, v85, v83, 1.0
	v_pk_mul_f32 v[90:91], v[90:91], v[98:99] op_sel_hi:[1,0]
	v_pk_mul_f32 v[72:73], v[72:73], v[98:99] op_sel_hi:[1,0]
	v_mov_b32_e32 v83, v84
	v_pk_fma_f32 v[90:91], v[10:11], v[90:91], v[14:15]
	v_pk_mul_f32 v[80:81], v[80:81], v[98:99] op_sel_hi:[1,0]
	v_pk_fma_f32 v[102:103], v[26:27], v[72:73], v[30:31]
	v_pk_mul_f32 v[72:73], v[82:83], v[98:99] op_sel_hi:[1,0]
	v_mov_b32_e32 v87, v88
	v_pk_fma_f32 v[100:101], v[28:29], v[80:81], v[32:33]
	v_pk_mul_f32 v[80:81], v[86:87], v[98:99] op_sel_hi:[1,0]
	v_pk_fma_f32 v[86:87], v[18:19], v[72:73], v[22:23]
	v_pk_mul_f32 v[94:95], v[94:95], v[98:99] op_sel_hi:[1,0]
	v_pk_fma_f32 v[94:95], v[12:13], v[94:95], v[16:17]
	v_pk_fma_f32 v[84:85], v[20:21], v[80:81], v[24:25]
	v_cvt_pk_bf16_f32 v80, v90, v91
	v_pk_mul_f32 v[92:93], v[92:93], v[98:99] op_sel_hi:[1,0]
	v_pk_fma_f32 v[92:93], v[2:3], v[92:93], v[6:7]
	v_cvt_pk_bf16_f32 v81, v94, v95
	v_pk_mul_f32 v[96:97], v[96:97], v[98:99] op_sel_hi:[1,0]
	v_pk_fma_f32 v[96:97], v[4:5], v[96:97], v[8:9]
	v_cvt_pk_bf16_f32 v82, v92, v93
	v_cvt_pk_bf16_f32 v83, v96, v97
	v_add_co_u32_e32 v72, vcc, s8, v70
	s_nop 1
	v_addc_co_u32_e32 v73, vcc, -1, v71, vcc
	global_store_dwordx4 v[72:73], v[80:83], off offset:-3072
	s_nop 1
	v_cvt_pk_bf16_f32 v80, v102, v103
	v_cvt_pk_bf16_f32 v81, v100, v101
	v_cvt_pk_bf16_f32 v82, v86, v87
	v_cvt_pk_bf16_f32 v83, v84, v85
	global_store_dwordx4 v[72:73], v[80:83], off offset:-2048
	s_cbranch_scc1 .LBB0_620
	v_add3_u32 v34, v66, s4, 8
	v_ashrrev_i32_e32 v35, 31, v34
	v_lshlrev_b64 v[34:35], 11, v[34:35]
	v_lshl_add_u64 v[38:39], v[68:69], 0, v[34:35]
	global_load_dwordx4 v[34:37], v[38:39], off
	s_nop 0
	global_load_dwordx4 v[38:41], v[38:39], off offset:1024
.LBB0_620:
	s_waitcnt vmcnt(7)
	v_lshlrev_b32_e32 v93, 16, v43
	v_lshlrev_b32_e32 v92, 16, v42
	v_and_b32_e32 v95, 0xffff0000, v43
	v_and_b32_e32 v94, 0xffff0000, v42
	v_pk_add_f32 v[96:97], v[92:93], v[94:95]
	v_and_b32_e32 v99, 0xffff0000, v45
	v_add_f32_e32 v85, v96, v97
	v_lshlrev_b32_e32 v97, 16, v45
	v_lshlrev_b32_e32 v96, 16, v44
	v_and_b32_e32 v98, 0xffff0000, v44
	v_pk_add_f32 v[100:101], v[96:97], v[98:99]
	s_waitcnt vmcnt(6)
	v_lshlrev_b32_e32 v80, 16, v46
	v_and_b32_e32 v81, 0xffff0000, v46
	v_lshlrev_b32_e32 v82, 16, v47
	v_and_b32_e32 v83, 0xffff0000, v47
	v_pk_add_f32 v[100:101], v[100:101], v[100:101] op_sel_hi:[0,1]
	v_lshlrev_b32_e32 v84, 16, v48
	v_and_b32_e32 v86, 0xffff0000, v48
	v_lshlrev_b32_e32 v88, 16, v49
	v_and_b32_e32 v90, 0xffff0000, v49
	v_add_f32_e32 v91, 0, v85
	v_add_f32_e32 v85, v80, v81
	v_add_f32_e32 v87, v82, v83
	v_mov_b32_e32 v89, v101
	v_pk_add_f32 v[102:103], v[84:85], v[86:87]
	v_pk_add_f32 v[100:101], v[88:89], v[90:91]
	s_nop 0
	v_pk_add_f32 v[100:101], v[102:103], v[100:101]
	s_nop 0
	v_add_f32_e32 v85, v100, v101
	s_waitcnt lgkmcnt(0)
	s_nop 1
	v_add_f32_dpp v85, v85, v85 quad_perm:[1,0,3,2] row_mask:0xf bank_mask:0xf
	s_nop 1
	v_add_f32_dpp v85, v85, v85 quad_perm:[2,3,0,1] row_mask:0xf bank_mask:0xf
	s_nop 1
	v_add_f32_dpp v85, v85, v85 row_half_mirror row_mask:0xf bank_mask:0xf
	s_nop 1
	v_add_f32_dpp v85, v85, v85 row_mirror row_mask:0xf bank_mask:0xf
	v_mov_b32_e32 v87, v85
	s_nop 1
	v_permlane16_swap_b32_e32 v85, v87
	v_add_f32_e32 v85, v85, v87
	v_mov_b32_e32 v87, v85
	s_nop 1
	v_permlane32_swap_b32_e32 v85, v87
	v_add_f32_e32 v85, v85, v87
	v_fmac_f32_e32 v94, 0xba800000, v85
	v_fmac_f32_e32 v95, 0xba800000, v85
	v_fmac_f32_e32 v93, 0xba800000, v85
	v_fmac_f32_e32 v92, 0xba800000, v85
	v_mov_b32_e32 v100, v93
	v_mov_b32_e32 v101, v95
	v_mov_b32_e32 v93, v94
	v_pk_mul_f32 v[102:103], v[100:101], v[100:101]
	v_pk_mul_f32 v[94:95], v[92:93], v[92:93]
	v_fmac_f32_e32 v98, 0xba800000, v85
	v_pk_mov_b32 v[104:105], v[94:95], v[102:103] op_sel:[1,0]
	v_mov_b32_e32 v95, v103
	v_fmac_f32_e32 v99, 0xba800000, v85
	v_fmac_f32_e32 v97, 0xba800000, v85
	v_pk_add_f32 v[94:95], v[104:105], v[94:95]
	v_fmac_f32_e32 v96, 0xba800000, v85
	v_mov_b32_e32 v102, v97
	v_mov_b32_e32 v103, v99
	v_mov_b32_e32 v97, v98
	v_pk_add_f32 v[94:95], v[94:95], v[94:95] op_sel_hi:[0,1]
	v_pk_mul_f32 v[104:105], v[102:103], v[102:103]
	v_pk_mul_f32 v[98:99], v[96:97], v[96:97]
	v_fmac_f32_e32 v80, 0xba800000, v85
	v_pk_mov_b32 v[106:107], v[98:99], v[104:105] op_sel:[1,0]
	v_mov_b32_e32 v99, v105
	v_fmac_f32_e32 v81, 0xba800000, v85
	v_fmac_f32_e32 v82, 0xba800000, v85
	v_mul_f32_e32 v94, v80, v80
	v_pk_add_f32 v[98:99], v[106:107], v[98:99]
	v_fmac_f32_e32 v83, 0xba800000, v85
	v_pk_fma_f32 v[104:105], v[80:81], v[80:81], v[94:95] op_sel_hi:[1,1,0]
	v_mul_f32_e32 v94, v82, v82
	v_pk_add_f32 v[98:99], v[98:99], v[98:99] op_sel_hi:[0,1]
	v_pk_fma_f32 v[106:107], v[82:83], v[82:83], v[94:95] op_sel_hi:[1,1,0]
	v_fmac_f32_e32 v90, 0xba800000, v85
	v_fmac_f32_e32 v88, 0xba800000, v85
	v_fmac_f32_e32 v86, 0xba800000, v85
	v_fmac_f32_e32 v84, 0xba800000, v85
	v_mul_f32_e32 v104, v84, v84
	v_mul_f32_e32 v106, v86, v86
	v_mul_f32_e32 v94, v88, v88
	v_mul_f32_e32 v98, v90, v90
	v_pk_add_f32 v[104:105], v[104:105], v[106:107]
	v_pk_add_f32 v[94:95], v[94:95], v[98:99]
	s_nop 0
	v_pk_add_f32 v[94:95], v[104:105], v[94:95]
	s_nop 0
	v_add_f32_e32 v85, v94, v95
	s_waitcnt lgkmcnt(0)
	s_nop 1
	v_add_f32_dpp v85, v85, v85 quad_perm:[1,0,3,2] row_mask:0xf bank_mask:0xf
	s_nop 1
	v_add_f32_dpp v85, v85, v85 quad_perm:[2,3,0,1] row_mask:0xf bank_mask:0xf
	s_nop 1
	v_add_f32_dpp v85, v85, v85 row_half_mirror row_mask:0xf bank_mask:0xf
	s_nop 1
	v_add_f32_dpp v85, v85, v85 row_mirror row_mask:0xf bank_mask:0xf
	v_mov_b32_e32 v87, v85
	s_nop 1
	v_permlane16_swap_b32_e32 v85, v87
	v_add_f32_e32 v85, v85, v87
	v_mov_b32_e32 v87, v85
	s_nop 1
	v_permlane32_swap_b32_e32 v85, v87
	v_add_f32_e32 v85, v85, v87
	v_fmamk_f32 v85, v85, 0x3a800000, v78
	v_mul_f32_e32 v87, 0x4f800000, v85
	v_cmp_gt_f32_e32 vcc, s6, v85
	s_nop 1
	v_cndmask_b32_e32 v85, v85, v87, vcc
	v_sqrt_f32_e32 v87, v85
	s_nop 0
	v_add_u32_e32 v89, -1, v87
	v_fma_f32 v91, -v89, v87, v85
	v_cmp_ge_f32_e64 s[0:1], 0, v91
	v_add_u32_e32 v91, 1, v87
	s_nop 0
	v_cndmask_b32_e64 v89, v87, v89, s[0:1]
	v_fma_f32 v87, -v91, v87, v85
	v_cmp_lt_f32_e64 s[0:1], 0, v87
	s_nop 1
	v_cndmask_b32_e64 v87, v89, v91, s[0:1]
	v_mul_f32_e32 v89, 0x37800000, v87
	v_cndmask_b32_e32 v87, v87, v89, vcc
	v_cmp_class_f32_e32 vcc, v85, v79
	s_nop 1
	v_cndmask_b32_e32 v85, v87, v85, vcc
	v_div_scale_f32 v87, s[0:1], v85, v85, 1.0
	v_rcp_f32_e32 v89, v87
	s_add_i32 s0, s4, 6
	s_cmp_gt_u32 s0, 12
	v_fma_f32 v91, -v87, v89, 1.0
	v_fmac_f32_e32 v89, v91, v89
	v_div_scale_f32 v91, vcc, 1.0, v85, 1.0
	v_mul_f32_e32 v94, v91, v89
	v_fma_f32 v95, -v87, v94, v91
	v_fmac_f32_e32 v94, v95, v89
	v_fma_f32 v87, -v87, v94, v91
	v_div_fmas_f32 v87, v87, v89, v94
	v_div_fixup_f32 v94, v87, v85, 1.0
	v_pk_mul_f32 v[92:93], v[92:93], v[94:95] op_sel_hi:[1,0]
	v_pk_mul_f32 v[80:81], v[80:81], v[94:95] op_sel_hi:[1,0]
	v_mov_b32_e32 v85, v86
	v_pk_fma_f32 v[92:93], v[10:11], v[92:93], v[14:15]
	v_pk_fma_f32 v[104:105], v[26:27], v[80:81], v[30:31]
	v_pk_mul_f32 v[80:81], v[84:85], v[94:95] op_sel_hi:[1,0]
	v_pk_mul_f32 v[98:99], v[100:101], v[94:95] op_sel_hi:[1,0]
	v_pk_fma_f32 v[86:87], v[18:19], v[80:81], v[22:23]
	v_pk_fma_f32 v[98:99], v[12:13], v[98:99], v[16:17]
	v_pk_mul_f32 v[82:83], v[82:83], v[94:95] op_sel_hi:[1,0]
	v_mov_b32_e32 v89, v90
	v_pk_mul_f32 v[100:101], v[102:103], v[94:95] op_sel_hi:[1,0]
	v_pk_fma_f32 v[102:103], v[28:29], v[82:83], v[32:33]
	v_pk_mul_f32 v[82:83], v[88:89], v[94:95] op_sel_hi:[1,0]
	v_cvt_pk_bf16_f32 v80, v92, v93
	v_bfe_u32 v81, v98, 16, 1
	v_pk_mul_f32 v[96:97], v[96:97], v[94:95] op_sel_hi:[1,0]
	v_pk_fma_f32 v[84:85], v[20:21], v[82:83], v[24:25]
	v_add3_u32 v81, v98, v81, s7
	v_bfe_u32 v82, v99, 16, 1
	v_pk_fma_f32 v[96:97], v[2:3], v[96:97], v[6:7]
	v_lshrrev_b32_e32 v81, 16, v81
	v_add3_u32 v82, v99, v82, s7
	v_and_or_b32 v81, v82, s5, v81
	v_pk_fma_f32 v[100:101], v[4:5], v[100:101], v[8:9]
	v_cvt_pk_bf16_f32 v82, v96, v97
	v_cvt_pk_bf16_f32 v83, v100, v101
	global_store_dwordx4 v[72:73], v[80:83], off offset:-1024
	s_nop 1
	v_cvt_pk_bf16_f32 v80, v104, v105
	v_cvt_pk_bf16_f32 v81, v102, v103
	v_cvt_pk_bf16_f32 v82, v86, v87
	v_cvt_pk_bf16_f32 v83, v84, v85
	global_store_dwordx4 v[70:71], v[80:83], off offset:-4096
	s_cbranch_scc1 .LBB0_622
	v_add3_u32 v42, v66, s4, 9
	v_ashrrev_i32_e32 v43, 31, v42
	v_lshlrev_b64 v[42:43], 11, v[42:43]
	v_lshl_add_u64 v[46:47], v[68:69], 0, v[42:43]
	global_load_dwordx4 v[42:45], v[46:47], off
	s_nop 0
	global_load_dwordx4 v[46:49], v[46:47], off offset:1024
.LBB0_622:
	s_waitcnt vmcnt(7)
	v_lshlrev_b32_e32 v91, 16, v51
	v_lshlrev_b32_e32 v90, 16, v50
	v_and_b32_e32 v93, 0xffff0000, v51
	v_and_b32_e32 v92, 0xffff0000, v50
	v_pk_add_f32 v[94:95], v[90:91], v[92:93]
	v_and_b32_e32 v97, 0xffff0000, v53
	v_add_f32_e32 v83, v94, v95
	v_lshlrev_b32_e32 v95, 16, v53
	v_lshlrev_b32_e32 v94, 16, v52
	v_and_b32_e32 v96, 0xffff0000, v52
	v_pk_add_f32 v[98:99], v[94:95], v[96:97]
	s_waitcnt vmcnt(6)
	v_lshlrev_b32_e32 v72, 16, v54
	v_and_b32_e32 v73, 0xffff0000, v54
	v_lshlrev_b32_e32 v80, 16, v55
	v_and_b32_e32 v81, 0xffff0000, v55
	v_pk_add_f32 v[98:99], v[98:99], v[98:99] op_sel_hi:[0,1]
	v_lshlrev_b32_e32 v82, 16, v56
	v_and_b32_e32 v84, 0xffff0000, v56
	v_lshlrev_b32_e32 v86, 16, v57
	v_and_b32_e32 v88, 0xffff0000, v57
	v_add_f32_e32 v89, 0, v83
	v_add_f32_e32 v83, v72, v73
	v_add_f32_e32 v85, v80, v81
	v_mov_b32_e32 v87, v99
	v_pk_add_f32 v[100:101], v[82:83], v[84:85]
	v_pk_add_f32 v[98:99], v[86:87], v[88:89]
	s_nop 0
	v_pk_add_f32 v[98:99], v[100:101], v[98:99]
	s_nop 0
	v_add_f32_e32 v83, v98, v99
	s_waitcnt lgkmcnt(0)
	s_nop 1
	v_add_f32_dpp v83, v83, v83 quad_perm:[1,0,3,2] row_mask:0xf bank_mask:0xf
	s_nop 1
	v_add_f32_dpp v83, v83, v83 quad_perm:[2,3,0,1] row_mask:0xf bank_mask:0xf
	s_nop 1
	v_add_f32_dpp v83, v83, v83 row_half_mirror row_mask:0xf bank_mask:0xf
	s_nop 1
	v_add_f32_dpp v83, v83, v83 row_mirror row_mask:0xf bank_mask:0xf
	v_mov_b32_e32 v85, v83
	s_nop 1
	v_permlane16_swap_b32_e32 v83, v85
	v_add_f32_e32 v83, v83, v85
	v_mov_b32_e32 v85, v83
	s_nop 1
	v_permlane32_swap_b32_e32 v83, v85
	v_add_f32_e32 v83, v83, v85
	v_fmac_f32_e32 v92, 0xba800000, v83
	v_fmac_f32_e32 v93, 0xba800000, v83
	v_fmac_f32_e32 v91, 0xba800000, v83
	v_fmac_f32_e32 v90, 0xba800000, v83
	v_mov_b32_e32 v98, v91
	v_mov_b32_e32 v99, v93
	v_mov_b32_e32 v91, v92
	v_pk_mul_f32 v[100:101], v[98:99], v[98:99]
	v_pk_mul_f32 v[92:93], v[90:91], v[90:91]
	v_fmac_f32_e32 v96, 0xba800000, v83
	v_pk_mov_b32 v[102:103], v[92:93], v[100:101] op_sel:[1,0]
	v_mov_b32_e32 v93, v101
	v_fmac_f32_e32 v97, 0xba800000, v83
	v_fmac_f32_e32 v95, 0xba800000, v83
	v_pk_add_f32 v[92:93], v[102:103], v[92:93]
	v_fmac_f32_e32 v94, 0xba800000, v83
	v_mov_b32_e32 v100, v95
	v_mov_b32_e32 v101, v97
	v_mov_b32_e32 v95, v96
	v_pk_add_f32 v[92:93], v[92:93], v[92:93] op_sel_hi:[0,1]
	v_pk_mul_f32 v[102:103], v[100:101], v[100:101]
	v_pk_mul_f32 v[96:97], v[94:95], v[94:95]
	v_fmac_f32_e32 v72, 0xba800000, v83
	v_pk_mov_b32 v[104:105], v[96:97], v[102:103] op_sel:[1,0]
	v_mov_b32_e32 v97, v103
	v_fmac_f32_e32 v73, 0xba800000, v83
	v_fmac_f32_e32 v80, 0xba800000, v83
	v_mul_f32_e32 v92, v72, v72
	v_pk_add_f32 v[96:97], v[104:105], v[96:97]
	v_fmac_f32_e32 v81, 0xba800000, v83
	v_pk_fma_f32 v[102:103], v[72:73], v[72:73], v[92:93] op_sel_hi:[1,1,0]
	v_mul_f32_e32 v92, v80, v80
	v_pk_add_f32 v[96:97], v[96:97], v[96:97] op_sel_hi:[0,1]
	v_pk_fma_f32 v[104:105], v[80:81], v[80:81], v[92:93] op_sel_hi:[1,1,0]
	v_fmac_f32_e32 v88, 0xba800000, v83
	v_fmac_f32_e32 v86, 0xba800000, v83
	v_fmac_f32_e32 v84, 0xba800000, v83
	v_fmac_f32_e32 v82, 0xba800000, v83
	v_mul_f32_e32 v102, v82, v82
	v_mul_f32_e32 v104, v84, v84
	v_mul_f32_e32 v92, v86, v86
	v_mul_f32_e32 v96, v88, v88
	v_pk_add_f32 v[102:103], v[102:103], v[104:105]
	v_pk_add_f32 v[92:93], v[92:93], v[96:97]
	s_nop 0
	v_pk_add_f32 v[92:93], v[102:103], v[92:93]
	s_nop 0
	v_add_f32_e32 v83, v92, v93
	s_waitcnt lgkmcnt(0)
	s_nop 1
	v_add_f32_dpp v83, v83, v83 quad_perm:[1,0,3,2] row_mask:0xf bank_mask:0xf
	s_nop 1
	v_add_f32_dpp v83, v83, v83 quad_perm:[2,3,0,1] row_mask:0xf bank_mask:0xf
	s_nop 1
	v_add_f32_dpp v83, v83, v83 row_half_mirror row_mask:0xf bank_mask:0xf
	s_nop 1
	v_add_f32_dpp v83, v83, v83 row_mirror row_mask:0xf bank_mask:0xf
	v_mov_b32_e32 v85, v83
	s_nop 1
	v_permlane16_swap_b32_e32 v83, v85
	v_add_f32_e32 v83, v83, v85
	v_mov_b32_e32 v85, v83
	s_nop 1
	v_permlane32_swap_b32_e32 v83, v85
	v_add_f32_e32 v83, v83, v85
	v_fmamk_f32 v83, v83, 0x3a800000, v78
	v_mul_f32_e32 v85, 0x4f800000, v83
	v_cmp_gt_f32_e32 vcc, s6, v83
	s_nop 1
	v_cndmask_b32_e32 v83, v83, v85, vcc
	v_sqrt_f32_e32 v85, v83
	s_nop 0
	v_add_u32_e32 v87, -1, v85
	v_fma_f32 v89, -v87, v85, v83
	v_cmp_ge_f32_e64 s[0:1], 0, v89
	v_add_u32_e32 v89, 1, v85
	s_nop 0
	v_cndmask_b32_e64 v87, v85, v87, s[0:1]
	v_fma_f32 v85, -v89, v85, v83
	v_cmp_lt_f32_e64 s[0:1], 0, v85
	s_nop 1
	v_cndmask_b32_e64 v85, v87, v89, s[0:1]
	v_mul_f32_e32 v87, 0x37800000, v85
	v_cndmask_b32_e32 v85, v85, v87, vcc
	v_cmp_class_f32_e32 vcc, v83, v79
	s_nop 1
	v_cndmask_b32_e32 v83, v85, v83, vcc
	v_div_scale_f32 v85, s[0:1], v83, v83, 1.0
	v_rcp_f32_e32 v87, v85
	s_add_i32 s0, s4, 7
	s_cmp_gt_u32 s0, 12
	v_fma_f32 v89, -v85, v87, 1.0
	v_fmac_f32_e32 v87, v89, v87
	v_div_scale_f32 v89, vcc, 1.0, v83, 1.0
	v_mul_f32_e32 v92, v89, v87
	v_fma_f32 v93, -v85, v92, v89
	v_fmac_f32_e32 v92, v93, v87
	v_fma_f32 v85, -v85, v92, v89
	v_div_fmas_f32 v85, v85, v87, v92
	v_div_fixup_f32 v92, v85, v83, 1.0
	v_pk_mul_f32 v[90:91], v[90:91], v[92:93] op_sel_hi:[1,0]
	v_pk_mul_f32 v[80:81], v[80:81], v[92:93] op_sel_hi:[1,0]
	v_mov_b32_e32 v83, v84
	v_pk_mul_f32 v[96:97], v[98:99], v[92:93] op_sel_hi:[1,0]
	v_pk_fma_f32 v[90:91], v[10:11], v[90:91], v[14:15]
	v_pk_mul_f32 v[98:99], v[100:101], v[92:93] op_sel_hi:[1,0]
	v_pk_fma_f32 v[100:101], v[28:29], v[80:81], v[32:33]
	v_pk_mul_f32 v[80:81], v[82:83], v[92:93] op_sel_hi:[1,0]
	v_mov_b32_e32 v87, v88
	v_pk_mul_f32 v[82:83], v[86:87], v[92:93] op_sel_hi:[1,0]
	v_pk_fma_f32 v[86:87], v[18:19], v[80:81], v[22:23]
	v_pk_fma_f32 v[96:97], v[12:13], v[96:97], v[16:17]
	v_cvt_pk_bf16_f32 v80, v90, v91
	v_bfe_u32 v81, v96, 16, 1
	v_pk_mul_f32 v[94:95], v[94:95], v[92:93] op_sel_hi:[1,0]
	v_pk_fma_f32 v[84:85], v[20:21], v[82:83], v[24:25]
	v_add3_u32 v81, v96, v81, s7
	v_bfe_u32 v82, v97, 16, 1
	v_pk_fma_f32 v[94:95], v[2:3], v[94:95], v[6:7]
	v_lshrrev_b32_e32 v81, 16, v81
	v_add3_u32 v82, v97, v82, s7
	v_and_or_b32 v81, v82, s5, v81
	v_pk_fma_f32 v[98:99], v[4:5], v[98:99], v[8:9]
	v_cvt_pk_bf16_f32 v82, v94, v95
	v_pk_mul_f32 v[72:73], v[72:73], v[92:93] op_sel_hi:[1,0]
	v_pk_fma_f32 v[72:73], v[26:27], v[72:73], v[30:31]
	v_cvt_pk_bf16_f32 v83, v98, v99
	global_store_dwordx4 v[70:71], v[80:83], off offset:-3072
	s_nop 1
	v_cvt_pk_bf16_f32 v80, v72, v73
	v_cvt_pk_bf16_f32 v81, v100, v101
	v_cvt_pk_bf16_f32 v82, v86, v87
	v_cvt_pk_bf16_f32 v83, v84, v85
	global_store_dwordx4 v[70:71], v[80:83], off offset:-2048
	s_cbranch_scc1 .LBB0_617
	v_add3_u32 v50, v66, s4, 10
	v_ashrrev_i32_e32 v51, 31, v50
	v_lshlrev_b64 v[50:51], 11, v[50:51]
	v_lshl_add_u64 v[54:55], v[68:69], 0, v[50:51]
	global_load_dwordx4 v[50:53], v[54:55], off
	s_nop 0
	global_load_dwordx4 v[54:57], v[54:55], off offset:1024
	s_branch .LBB0_617

.LBB0_699:
	v_mov_b32_e32 v132, v0
	s_lshl_b32 s1, s36, 8
	s_lshl_b32 s22, s80, 8
	s_add_i32 s1, s1, s74
	s_ashr_i32 s23, s22, 31
	v_and_or_b32 v134, v132, 15, s1
	v_lshrrev_b32_e32 v132, 1, v132
	s_lshl_b64 s[22:23], s[22:23], 1
	v_and_or_b32 v132, v132, 24, s75
	s_add_u32 s22, s47, s22
	s_addc_u32 s23, s50, s23
	v_lshlrev_b32_e32 v132, 1, v132
	v_ashrrev_i32_e32 v135, 31, v134
	v_lshl_add_u64 v[136:137], s[22:23], 0, v[132:133]
	v_lshlrev_b64 v[138:139], 11, v[134:135]
	v_lshl_add_u64 v[162:163], v[136:137], 0, v[138:139]
	global_load_dwordx4 v[146:149], v[162:163], off
	global_load_dwordx4 v[150:153], v[162:163], off offset:256
	v_or_b32_e32 v138, 16, v134
	v_ashrrev_i32_e32 v139, 31, v138
	v_lshlrev_b64 v[138:139], 11, v[138:139]
	v_lshl_add_u64 v[138:139], v[136:137], 0, v[138:139]
	global_load_dwordx4 v[154:157], v[138:139], off
	global_load_dwordx4 v[158:161], v[138:139], off offset:256
	s_and_b64 vcc, exec, s[2:3]
	s_mov_b64 s[2:3], -1
	s_waitcnt vmcnt(3)
	v_lshlrev_b32_e32 v164, 16, v146
	v_and_b32_e32 v165, 0xffff0000, v146
	v_lshlrev_b32_e32 v146, 16, v147
	v_and_b32_e32 v147, 0xffff0000, v147
	v_lshlrev_b32_e32 v166, 16, v148
	v_and_b32_e32 v167, 0xffff0000, v148
	v_lshlrev_b32_e32 v148, 16, v149
	v_and_b32_e32 v149, 0xffff0000, v149
	s_waitcnt vmcnt(2)
	v_lshlrev_b32_e32 v170, 16, v152
	v_and_b32_e32 v171, 0xffff0000, v152
	v_lshlrev_b32_e32 v152, 16, v153
	v_and_b32_e32 v153, 0xffff0000, v153
	v_pk_fma_f32 v[128:129], v[146:147], s[8:9], v[128:129] op_sel_hi:[1,0,1]
	v_pk_fma_f32 v[126:127], v[164:165], s[8:9], v[126:127] op_sel_hi:[1,0,1]
	v_pk_fma_f32 v[124:125], v[148:149], s[8:9], v[124:125] op_sel_hi:[1,0,1]
	v_pk_fma_f32 v[122:123], v[166:167], s[8:9], v[122:123] op_sel_hi:[1,0,1]
	v_lshlrev_b32_e32 v168, 16, v150
	v_and_b32_e32 v169, 0xffff0000, v150
	v_lshlrev_b32_e32 v150, 16, v151
	v_and_b32_e32 v151, 0xffff0000, v151
	v_pk_fma_f32 v[146:147], v[152:153], s[8:9], v[116:117] op_sel_hi:[1,0,1]
	v_pk_fma_f32 v[114:115], v[170:171], s[8:9], v[114:115] op_sel_hi:[1,0,1]
	v_bfe_u32 v116, v126, 16, 1
	v_bfe_u32 v132, v128, 16, 1
	v_bfe_u32 v145, v122, 16, 1
	v_bfe_u32 v149, v124, 16, 1
	v_pk_fma_f32 v[120:121], v[150:151], s[8:9], v[120:121] op_sel_hi:[1,0,1]
	v_bfe_u32 v117, v127, 16, 1
	v_bfe_u32 v135, v129, 16, 1
	v_bfe_u32 v148, v123, 16, 1
	v_bfe_u32 v150, v125, 16, 1
	v_bfe_u32 v165, v114, 16, 1
	v_bfe_u32 v166, v115, 16, 1
	v_add3_u32 v116, v126, v116, s79
	v_add3_u32 v126, v128, v132, s79
	v_add3_u32 v122, v122, v145, s79
	v_add3_u32 v124, v124, v149, s79
	v_pk_fma_f32 v[118:119], v[168:169], s[8:9], v[118:119] op_sel_hi:[1,0,1]
	v_add3_u32 v117, v127, v117, s79
	v_add3_u32 v127, v129, v135, s79
	v_add3_u32 v123, v123, v148, s79
	v_add3_u32 v125, v125, v150, s79
	v_add3_u32 v114, v114, v165, s79
	v_add3_u32 v128, v115, v166, s79
	v_lshrrev_b32_e32 v115, 16, v116
	v_lshrrev_b32_e32 v116, 16, v126
	v_lshrrev_b32_e32 v122, 16, v122
	v_lshrrev_b32_e32 v124, 16, v124
	v_bfe_u32 v153, v120, 16, 1
	v_bfe_u32 v167, v146, 16, 1
	v_lshrrev_b32_e32 v126, 16, v114
	v_and_or_b32 v114, v117, s77, v115
	v_and_or_b32 v115, v127, s77, v116
	v_and_or_b32 v116, v123, s77, v122
	v_and_or_b32 v117, v125, s77, v124
	v_bfe_u32 v164, v121, 16, 1
	v_add3_u32 v120, v120, v153, s79
	v_add3_u32 v129, v146, v167, s79
	global_store_dwordx4 v[162:163], v[114:117], off
	s_nop 1
	v_add3_u32 v121, v121, v164, s79
	v_bfe_u32 v115, v147, 16, 1
	v_lshrrev_b32_e32 v120, 16, v120
	v_lshrrev_b32_e32 v114, 16, v129
	v_add3_u32 v115, v147, v115, s79
	v_cvt_pk_bf16_f32 v118, v118, v119
	v_and_or_b32 v119, v121, s77, v120
	v_and_or_b32 v121, v115, s77, v114
	v_or_b32_e32 v114, 32, v134
	v_ashrrev_i32_e32 v115, 31, v114
	v_lshlrev_b64 v[114:115], 11, v[114:115]
	v_and_or_b32 v120, v128, s77, v126
	v_lshl_add_u64 v[114:115], v[136:137], 0, v[114:115]
	global_store_dwordx4 v[162:163], v[118:121], off offset:256
	global_load_dwordx4 v[116:119], v[114:115], off
	s_waitcnt vmcnt(4)
	v_lshlrev_b32_e32 v124, 16, v154
	v_and_b32_e32 v125, 0xffff0000, v154
	v_lshlrev_b32_e32 v128, 16, v156
	v_and_b32_e32 v129, 0xffff0000, v156
	v_lshlrev_b32_e32 v146, 16, v157
	v_and_b32_e32 v147, 0xffff0000, v157
	v_pk_fma_f32 v[110:111], v[124:125], s[8:9], v[110:111] op_sel_hi:[1,0,1]
	v_pk_fma_f32 v[124:125], v[146:147], s[8:9], v[108:109] op_sel_hi:[1,0,1]
	v_pk_fma_f32 v[108:109], v[128:129], s[8:9], v[106:107] op_sel_hi:[1,0,1]
	v_lshlrev_b32_e32 v126, 16, v155
	v_and_b32_e32 v127, 0xffff0000, v155
	v_pk_fma_f32 v[112:113], v[126:127], s[8:9], v[112:113] op_sel_hi:[1,0,1]
	v_cvt_pk_bf16_f32 v106, v110, v111
	global_load_dwordx4 v[120:123], v[114:115], off offset:256
	v_cvt_pk_bf16_f32 v107, v112, v113
	v_cvt_pk_bf16_f32 v108, v108, v109
	s_waitcnt vmcnt(4)
	v_lshlrev_b32_e32 v148, 16, v158
	v_and_b32_e32 v149, 0xffff0000, v158
	v_lshlrev_b32_e32 v154, 16, v161
	v_and_b32_e32 v155, 0xffff0000, v161
	v_cvt_pk_bf16_f32 v109, v124, v125
	v_pk_fma_f32 v[102:103], v[148:149], s[8:9], v[102:103] op_sel_hi:[1,0,1]
	global_store_dwordx4 v[138:139], v[106:109], off
	v_lshlrev_b32_e32 v150, 16, v159
	v_and_b32_e32 v151, 0xffff0000, v159
	v_pk_fma_f32 v[108:109], v[154:155], s[8:9], v[100:101] op_sel_hi:[1,0,1]
	v_pk_fma_f32 v[104:105], v[150:151], s[8:9], v[104:105] op_sel_hi:[1,0,1]
	v_cvt_pk_bf16_f32 v100, v102, v103
	v_lshlrev_b32_e32 v152, 16, v160
	v_and_b32_e32 v153, 0xffff0000, v160
	v_pk_fma_f32 v[98:99], v[152:153], s[8:9], v[98:99] op_sel_hi:[1,0,1]
	v_cvt_pk_bf16_f32 v101, v104, v105
	v_cvt_pk_bf16_f32 v102, v98, v99
	v_bfe_u32 v98, v108, 16, 1
	v_add3_u32 v98, v108, v98, s79
	v_lshrrev_b32_e32 v103, 16, v98
	v_or_b32_e32 v98, 48, v134
	v_ashrrev_i32_e32 v99, 31, v98
	v_lshlrev_b64 v[98:99], 11, v[98:99]
	v_lshl_add_u64 v[98:99], v[136:137], 0, v[98:99]
	global_load_dwordx4 v[104:107], v[98:99], off
	v_bfe_u32 v108, v109, 16, 1
	v_add3_u32 v108, v109, v108, s79
	v_and_or_b32 v103, v108, s77, v103
	global_store_dwordx4 v[138:139], v[100:103], off offset:256
	global_load_dwordx4 v[100:103], v[98:99], off offset:256
	s_waitcnt vmcnt(5)
	v_lshlrev_b32_e32 v108, 16, v116
	v_and_b32_e32 v109, 0xffff0000, v116
	v_lshlrev_b32_e32 v110, 16, v117
	v_and_b32_e32 v111, 0xffff0000, v117
	v_lshlrev_b32_e32 v112, 16, v118
	v_and_b32_e32 v113, 0xffff0000, v118
	v_lshlrev_b32_e32 v116, 16, v119
	v_and_b32_e32 v117, 0xffff0000, v119
	v_pk_fma_f32 v[94:95], v[108:109], s[8:9], v[94:95] op_sel_hi:[1,0,1]
	v_pk_fma_f32 v[108:109], v[116:117], s[8:9], v[92:93] op_sel_hi:[1,0,1]
	v_pk_fma_f32 v[92:93], v[112:113], s[8:9], v[90:91] op_sel_hi:[1,0,1]
	v_pk_fma_f32 v[96:97], v[110:111], s[8:9], v[96:97] op_sel_hi:[1,0,1]
	v_cvt_pk_bf16_f32 v90, v94, v95
	v_cvt_pk_bf16_f32 v91, v96, v97
	v_cvt_pk_bf16_f32 v92, v92, v93
	s_waitcnt vmcnt(4)
	v_lshlrev_b32_e32 v118, 16, v120
	v_and_b32_e32 v119, 0xffff0000, v120
	v_lshlrev_b32_e32 v124, 16, v122
	v_and_b32_e32 v125, 0xffff0000, v122
	v_lshlrev_b32_e32 v122, 16, v123
	v_and_b32_e32 v123, 0xffff0000, v123
	v_cvt_pk_bf16_f32 v93, v108, v109
	v_pk_fma_f32 v[86:87], v[118:119], s[8:9], v[86:87] op_sel_hi:[1,0,1]
	global_store_dwordx4 v[114:115], v[90:93], off
	v_lshlrev_b32_e32 v120, 16, v121
	v_and_b32_e32 v121, 0xffff0000, v121
	v_pk_fma_f32 v[90:91], v[122:123], s[8:9], v[84:85] op_sel_hi:[1,0,1]
	v_pk_fma_f32 v[84:85], v[124:125], s[8:9], v[82:83] op_sel_hi:[1,0,1]
	v_pk_fma_f32 v[88:89], v[120:121], s[8:9], v[88:89] op_sel_hi:[1,0,1]
	v_cvt_pk_bf16_f32 v82, v86, v87
	v_cvt_pk_bf16_f32 v83, v88, v89
	v_cvt_pk_bf16_f32 v84, v84, v85
	v_cvt_pk_bf16_f32 v85, v90, v91
	global_store_dwordx4 v[114:115], v[82:85], off offset:256
	s_waitcnt vmcnt(4)
	v_lshlrev_b32_e32 v92, 16, v104
	v_and_b32_e32 v93, 0xffff0000, v104
	v_add_u32_e32 v82, 0x80, v134
	v_ashrrev_i32_e32 v83, 31, v82
	v_lshlrev_b64 v[82:83], 11, v[82:83]
	v_lshl_add_u64 v[82:83], v[136:137], 0, v[82:83]
	global_load_dwordx4 v[84:87], v[82:83], off
	global_load_dwordx4 v[88:91], v[82:83], off offset:256
	v_lshlrev_b32_e32 v94, 16, v105
	v_and_b32_e32 v95, 0xffff0000, v105
	v_lshlrev_b32_e32 v96, 16, v106
	v_and_b32_e32 v97, 0xffff0000, v106
	v_lshlrev_b32_e32 v104, 16, v107
	v_and_b32_e32 v105, 0xffff0000, v107
	v_pk_fma_f32 v[78:79], v[92:93], s[8:9], v[78:79] op_sel_hi:[1,0,1]
	v_pk_fma_f32 v[92:93], v[104:105], s[8:9], v[76:77] op_sel_hi:[1,0,1]
	v_pk_fma_f32 v[76:77], v[96:97], s[8:9], v[74:75] op_sel_hi:[1,0,1]
	v_pk_fma_f32 v[80:81], v[94:95], s[8:9], v[80:81] op_sel_hi:[1,0,1]
	v_cvt_pk_bf16_f32 v74, v78, v79
	v_cvt_pk_bf16_f32 v75, v80, v81
	v_cvt_pk_bf16_f32 v76, v76, v77
	s_waitcnt vmcnt(4)
	v_lshlrev_b32_e32 v106, 16, v100
	v_and_b32_e32 v107, 0xffff0000, v100
	v_lshlrev_b32_e32 v108, 16, v102
	v_and_b32_e32 v109, 0xffff0000, v102
	v_lshlrev_b32_e32 v102, 16, v103
	v_and_b32_e32 v103, 0xffff0000, v103
	v_cvt_pk_bf16_f32 v77, v92, v93
	v_pk_fma_f32 v[70:71], v[106:107], s[8:9], v[70:71] op_sel_hi:[1,0,1]
	global_store_dwordx4 v[98:99], v[74:77], off
	v_lshlrev_b32_e32 v100, 16, v101
	v_and_b32_e32 v101, 0xffff0000, v101
	v_pk_fma_f32 v[76:77], v[102:103], s[8:9], v[68:69] op_sel_hi:[1,0,1]
	v_pk_fma_f32 v[72:73], v[100:101], s[8:9], v[72:73] op_sel_hi:[1,0,1]
	v_cvt_pk_bf16_f32 v68, v70, v71
	v_pk_fma_f32 v[66:67], v[108:109], s[8:9], v[66:67] op_sel_hi:[1,0,1]
	v_cvt_pk_bf16_f32 v69, v72, v73
	v_cvt_pk_bf16_f32 v70, v66, v67
	v_bfe_u32 v66, v76, 16, 1
	v_add3_u32 v66, v76, v66, s79
	v_lshrrev_b32_e32 v71, 16, v66
	v_add_u32_e32 v66, 0x90, v134
	v_ashrrev_i32_e32 v67, 31, v66
	v_lshlrev_b64 v[66:67], 11, v[66:67]
	v_lshl_add_u64 v[66:67], v[136:137], 0, v[66:67]
	global_load_dwordx4 v[72:75], v[66:67], off
	v_bfe_u32 v76, v77, 16, 1
	v_add3_u32 v76, v77, v76, s79
	v_and_or_b32 v71, v76, s77, v71
	global_store_dwordx4 v[98:99], v[68:71], off offset:256
	global_load_dwordx4 v[68:71], v[66:67], off offset:256
	s_waitcnt vmcnt(5)
	v_lshlrev_b32_e32 v76, 16, v84
	v_and_b32_e32 v77, 0xffff0000, v84
	v_lshlrev_b32_e32 v78, 16, v85
	v_and_b32_e32 v79, 0xffff0000, v85
	v_lshlrev_b32_e32 v80, 16, v86
	v_and_b32_e32 v81, 0xffff0000, v86
	v_lshlrev_b32_e32 v84, 16, v87
	v_and_b32_e32 v85, 0xffff0000, v87
	v_pk_fma_f32 v[62:63], v[76:77], s[8:9], v[62:63] op_sel_hi:[1,0,1]
	v_pk_fma_f32 v[76:77], v[84:85], s[8:9], v[60:61] op_sel_hi:[1,0,1]
	v_pk_fma_f32 v[60:61], v[80:81], s[8:9], v[58:59] op_sel_hi:[1,0,1]
	v_pk_fma_f32 v[64:65], v[78:79], s[8:9], v[64:65] op_sel_hi:[1,0,1]
	v_cvt_pk_bf16_f32 v58, v62, v63
	v_cvt_pk_bf16_f32 v59, v64, v65
	v_cvt_pk_bf16_f32 v60, v60, v61
	s_waitcnt vmcnt(4)
	v_lshlrev_b32_e32 v86, 16, v88
	v_and_b32_e32 v87, 0xffff0000, v88
	v_lshlrev_b32_e32 v92, 16, v90
	v_and_b32_e32 v93, 0xffff0000, v90
	v_lshlrev_b32_e32 v90, 16, v91
	v_and_b32_e32 v91, 0xffff0000, v91
	v_cvt_pk_bf16_f32 v61, v76, v77
	v_pk_fma_f32 v[54:55], v[86:87], s[8:9], v[54:55] op_sel_hi:[1,0,1]
	global_store_dwordx4 v[82:83], v[58:61], off
	v_lshlrev_b32_e32 v88, 16, v89
	v_and_b32_e32 v89, 0xffff0000, v89
	v_pk_fma_f32 v[58:59], v[90:91], s[8:9], v[52:53] op_sel_hi:[1,0,1]
	v_pk_fma_f32 v[52:53], v[92:93], s[8:9], v[50:51] op_sel_hi:[1,0,1]
	v_pk_fma_f32 v[56:57], v[88:89], s[8:9], v[56:57] op_sel_hi:[1,0,1]
	v_cvt_pk_bf16_f32 v50, v54, v55
	v_cvt_pk_bf16_f32 v51, v56, v57
	v_cvt_pk_bf16_f32 v52, v52, v53
	v_cvt_pk_bf16_f32 v53, v58, v59
	global_store_dwordx4 v[82:83], v[50:53], off offset:256
	s_waitcnt vmcnt(4)
	v_lshlrev_b32_e32 v60, 16, v72
	v_and_b32_e32 v61, 0xffff0000, v72
	v_add_u32_e32 v50, 0xa0, v134
	v_ashrrev_i32_e32 v51, 31, v50
	v_lshlrev_b64 v[50:51], 11, v[50:51]
	v_lshl_add_u64 v[50:51], v[136:137], 0, v[50:51]
	global_load_dwordx4 v[52:55], v[50:51], off
	global_load_dwordx4 v[56:59], v[50:51], off offset:256
	v_lshlrev_b32_e32 v62, 16, v73
	v_and_b32_e32 v63, 0xffff0000, v73
	v_lshlrev_b32_e32 v64, 16, v74
	v_and_b32_e32 v65, 0xffff0000, v74
	v_lshlrev_b32_e32 v72, 16, v75
	v_and_b32_e32 v73, 0xffff0000, v75
	v_pk_fma_f32 v[46:47], v[60:61], s[8:9], v[46:47] op_sel_hi:[1,0,1]
	v_pk_fma_f32 v[60:61], v[72:73], s[8:9], v[44:45] op_sel_hi:[1,0,1]
	v_pk_fma_f32 v[44:45], v[64:65], s[8:9], v[42:43] op_sel_hi:[1,0,1]
	v_pk_fma_f32 v[48:49], v[62:63], s[8:9], v[48:49] op_sel_hi:[1,0,1]
	v_cvt_pk_bf16_f32 v42, v46, v47
	v_cvt_pk_bf16_f32 v43, v48, v49
	v_cvt_pk_bf16_f32 v44, v44, v45
	s_waitcnt vmcnt(4)
	v_lshlrev_b32_e32 v74, 16, v68
	v_and_b32_e32 v75, 0xffff0000, v68
	v_lshlrev_b32_e32 v76, 16, v70
	v_and_b32_e32 v77, 0xffff0000, v70
	v_lshlrev_b32_e32 v70, 16, v71
	v_and_b32_e32 v71, 0xffff0000, v71
	v_cvt_pk_bf16_f32 v45, v60, v61
	v_pk_fma_f32 v[38:39], v[74:75], s[8:9], v[38:39] op_sel_hi:[1,0,1]
	global_store_dwordx4 v[66:67], v[42:45], off
	v_lshlrev_b32_e32 v68, 16, v69
	v_and_b32_e32 v69, 0xffff0000, v69
	v_pk_fma_f32 v[42:43], v[70:71], s[8:9], v[36:37] op_sel_hi:[1,0,1]
	v_pk_fma_f32 v[36:37], v[76:77], s[8:9], v[34:35] op_sel_hi:[1,0,1]
	v_pk_fma_f32 v[40:41], v[68:69], s[8:9], v[40:41] op_sel_hi:[1,0,1]
	v_cvt_pk_bf16_f32 v34, v38, v39
	v_cvt_pk_bf16_f32 v35, v40, v41
	v_bfe_u32 v38, v36, 16, 1
	v_add3_u32 v36, v36, v38, s79
	v_bfe_u32 v38, v37, 16, 1
	v_add3_u32 v37, v37, v38, s79
	v_add_u32_e32 v38, 0xb0, v134
	v_ashrrev_i32_e32 v39, 31, v38
	v_lshlrev_b64 v[38:39], 11, v[38:39]
	v_lshl_add_u64 v[44:45], v[136:137], 0, v[38:39]
	global_load_dwordx4 v[38:41], v[44:45], off
	v_lshrrev_b32_e32 v36, 16, v36
	v_and_or_b32 v36, v37, s77, v36
	v_cvt_pk_bf16_f32 v37, v42, v43
	global_store_dwordx4 v[66:67], v[34:37], off offset:256
	global_load_dwordx4 v[34:37], v[44:45], off offset:256
	s_waitcnt vmcnt(5)
	v_lshlrev_b32_e32 v42, 16, v52
	v_and_b32_e32 v43, 0xffff0000, v52
	v_lshlrev_b32_e32 v46, 16, v53
	v_and_b32_e32 v47, 0xffff0000, v53
	v_lshlrev_b32_e32 v48, 16, v54
	v_and_b32_e32 v49, 0xffff0000, v54
	v_lshlrev_b32_e32 v52, 16, v55
	v_and_b32_e32 v53, 0xffff0000, v55
	v_pk_fma_f32 v[30:31], v[42:43], s[8:9], v[30:31] op_sel_hi:[1,0,1]
	v_pk_fma_f32 v[42:43], v[52:53], s[8:9], v[28:29] op_sel_hi:[1,0,1]
	v_pk_fma_f32 v[28:29], v[48:49], s[8:9], v[26:27] op_sel_hi:[1,0,1]
	v_pk_fma_f32 v[32:33], v[46:47], s[8:9], v[32:33] op_sel_hi:[1,0,1]
	v_cvt_pk_bf16_f32 v26, v30, v31
	v_cvt_pk_bf16_f32 v27, v32, v33
	v_cvt_pk_bf16_f32 v28, v28, v29
	s_waitcnt vmcnt(4)
	v_lshlrev_b32_e32 v54, 16, v56
	v_and_b32_e32 v55, 0xffff0000, v56
	v_lshlrev_b32_e32 v60, 16, v58
	v_and_b32_e32 v61, 0xffff0000, v58
	v_lshlrev_b32_e32 v58, 16, v59
	v_and_b32_e32 v59, 0xffff0000, v59
	v_cvt_pk_bf16_f32 v29, v42, v43
	v_pk_fma_f32 v[22:23], v[54:55], s[8:9], v[22:23] op_sel_hi:[1,0,1]
	global_store_dwordx4 v[50:51], v[26:29], off
	v_lshlrev_b32_e32 v56, 16, v57
	v_and_b32_e32 v57, 0xffff0000, v57
	v_pk_fma_f32 v[26:27], v[58:59], s[8:9], v[20:21] op_sel_hi:[1,0,1]
	v_pk_fma_f32 v[20:21], v[60:61], s[8:9], v[18:19] op_sel_hi:[1,0,1]
	v_pk_fma_f32 v[24:25], v[56:57], s[8:9], v[24:25] op_sel_hi:[1,0,1]
	v_cvt_pk_bf16_f32 v18, v22, v23
	v_cvt_pk_bf16_f32 v19, v24, v25
	v_cvt_pk_bf16_f32 v20, v20, v21
	v_cvt_pk_bf16_f32 v21, v26, v27
	global_store_dwordx4 v[50:51], v[18:21], off offset:256
	s_waitcnt vmcnt(4)
	v_lshlrev_b32_e32 v22, 16, v40
	v_and_b32_e32 v23, 0xffff0000, v40
	v_lshlrev_b32_e32 v18, 16, v38
	v_and_b32_e32 v19, 0xffff0000, v38
	v_lshlrev_b32_e32 v24, 16, v41
	v_and_b32_e32 v25, 0xffff0000, v41
	v_pk_fma_f32 v[14:15], v[18:19], s[8:9], v[14:15] op_sel_hi:[1,0,1]
	v_pk_fma_f32 v[18:19], v[24:25], s[8:9], v[12:13] op_sel_hi:[1,0,1]
	v_pk_fma_f32 v[12:13], v[22:23], s[8:9], v[10:11] op_sel_hi:[1,0,1]
	v_lshlrev_b32_e32 v20, 16, v39
	v_and_b32_e32 v21, 0xffff0000, v39
	v_pk_fma_f32 v[16:17], v[20:21], s[8:9], v[16:17] op_sel_hi:[1,0,1]
	v_cvt_pk_bf16_f32 v10, v14, v15
	v_cvt_pk_bf16_f32 v11, v16, v17
	v_cvt_pk_bf16_f32 v12, v12, v13
	s_waitcnt vmcnt(2)
	v_lshlrev_b32_e32 v26, 16, v34
	v_and_b32_e32 v27, 0xffff0000, v34
	v_lshlrev_b32_e32 v30, 16, v36
	v_and_b32_e32 v31, 0xffff0000, v36
	v_lshlrev_b32_e32 v32, 16, v37
	v_and_b32_e32 v33, 0xffff0000, v37
	v_cvt_pk_bf16_f32 v13, v18, v19
	v_pk_fma_f32 v[6:7], v[26:27], s[8:9], v[6:7] op_sel_hi:[1,0,1]
	global_store_dwordx4 v[44:45], v[10:13], off
	v_lshlrev_b32_e32 v28, 16, v35
	v_and_b32_e32 v29, 0xffff0000, v35
	v_pk_fma_f32 v[10:11], v[32:33], s[8:9], v[4:5] op_sel_hi:[1,0,1]
	v_pk_fma_f32 v[4:5], v[30:31], s[8:9], v[2:3] op_sel_hi:[1,0,1]
	v_pk_fma_f32 v[8:9], v[28:29], s[8:9], v[8:9] op_sel_hi:[1,0,1]
	v_cvt_pk_bf16_f32 v2, v6, v7
	v_cvt_pk_bf16_f32 v3, v8, v9
	v_cvt_pk_bf16_f32 v4, v4, v5
	v_cvt_pk_bf16_f32 v5, v10, v11
	global_store_dwordx4 v[44:45], v[2:5], off offset:256
	s_cbranch_vccnz .LBB0_686
	s_andn2_b64 vcc, exec, s[4:5]
	s_cbranch_vccnz .LBB0_685
	s_barrier
	s_branch .LBB0_685

.LBB0_721:
	s_waitcnt vmcnt(7)
	v_lshlrev_b32_e32 v87, 16, v59
	v_lshlrev_b32_e32 v86, 16, v58
	v_and_b32_e32 v59, 0xffff0000, v59
	v_and_b32_e32 v58, 0xffff0000, v58
	v_pk_add_f32 v[88:89], v[86:87], v[58:59]
	s_waitcnt vmcnt(6)
	v_lshlrev_b32_e32 v82, 16, v65
	v_and_b32_e32 v84, 0xffff0000, v65
	v_add_f32_e32 v65, v88, v89
	v_lshlrev_b32_e32 v89, 16, v61
	v_lshlrev_b32_e32 v88, 16, v60
	v_and_b32_e32 v61, 0xffff0000, v61
	v_and_b32_e32 v60, 0xffff0000, v60
	v_pk_add_f32 v[90:91], v[88:89], v[60:61]
	v_lshlrev_b32_e32 v72, 16, v62
	v_and_b32_e32 v73, 0xffff0000, v62
	v_lshlrev_b32_e32 v62, 16, v63
	v_and_b32_e32 v63, 0xffff0000, v63
	v_pk_add_f32 v[90:91], v[90:91], v[90:91] op_sel_hi:[0,1]
	v_lshlrev_b32_e32 v80, 16, v64
	v_and_b32_e32 v64, 0xffff0000, v64
	v_add_f32_e32 v85, 0, v65
	v_add_f32_e32 v81, v72, v73
	v_add_f32_e32 v65, v62, v63
	v_mov_b32_e32 v83, v91
	v_pk_add_f32 v[92:93], v[80:81], v[64:65]
	v_pk_add_f32 v[90:91], v[82:83], v[84:85]
	s_add_i32 s4, s4, 4
	v_pk_add_f32 v[90:91], v[92:93], v[90:91]
	s_cmp_gt_u32 s4, 11
	v_add_f32_e32 v65, v90, v91
	s_waitcnt lgkmcnt(0)
	s_nop 1
	v_add_f32_dpp v65, v65, v65 quad_perm:[1,0,3,2] row_mask:0xf bank_mask:0xf
	s_nop 1
	v_add_f32_dpp v65, v65, v65 quad_perm:[2,3,0,1] row_mask:0xf bank_mask:0xf
	s_nop 1
	v_add_f32_dpp v65, v65, v65 row_half_mirror row_mask:0xf bank_mask:0xf
	s_nop 1
	v_add_f32_dpp v65, v65, v65 row_mirror row_mask:0xf bank_mask:0xf
	v_mov_b32_e32 v81, v65
	s_nop 1
	v_permlane16_swap_b32_e32 v65, v81
	v_add_f32_e32 v65, v65, v81
	v_mov_b32_e32 v81, v65
	s_nop 1
	v_permlane32_swap_b32_e32 v65, v81
	v_add_f32_e32 v65, v65, v81
	v_fmac_f32_e32 v58, 0xba800000, v65
	v_fmac_f32_e32 v59, 0xba800000, v65
	v_fmac_f32_e32 v87, 0xba800000, v65
	v_fmac_f32_e32 v86, 0xba800000, v65
	v_mov_b32_e32 v90, v87
	v_mov_b32_e32 v91, v59
	v_mov_b32_e32 v87, v58
	v_pk_mul_f32 v[92:93], v[90:91], v[90:91]
	v_pk_mul_f32 v[58:59], v[86:87], v[86:87]
	v_fmac_f32_e32 v60, 0xba800000, v65
	v_pk_mov_b32 v[94:95], v[58:59], v[92:93] op_sel:[1,0]
	v_mov_b32_e32 v59, v93
	v_fmac_f32_e32 v61, 0xba800000, v65
	v_fmac_f32_e32 v89, 0xba800000, v65
	v_pk_add_f32 v[58:59], v[94:95], v[58:59]
	v_fmac_f32_e32 v88, 0xba800000, v65
	v_mov_b32_e32 v92, v89
	v_mov_b32_e32 v93, v61
	v_mov_b32_e32 v89, v60
	v_pk_add_f32 v[58:59], v[58:59], v[58:59] op_sel_hi:[0,1]
	v_pk_mul_f32 v[94:95], v[92:93], v[92:93]
	v_pk_mul_f32 v[60:61], v[88:89], v[88:89]
	v_fmac_f32_e32 v72, 0xba800000, v65
	v_pk_mov_b32 v[96:97], v[60:61], v[94:95] op_sel:[1,0]
	v_mov_b32_e32 v61, v95
	v_fmac_f32_e32 v73, 0xba800000, v65
	v_fmac_f32_e32 v62, 0xba800000, v65
	v_mul_f32_e32 v58, v72, v72
	v_pk_add_f32 v[60:61], v[96:97], v[60:61]
	v_fmac_f32_e32 v63, 0xba800000, v65
	v_pk_fma_f32 v[94:95], v[72:73], v[72:73], v[58:59] op_sel_hi:[1,1,0]
	v_mul_f32_e32 v58, v62, v62
	v_pk_add_f32 v[60:61], v[60:61], v[60:61] op_sel_hi:[0,1]
	v_pk_fma_f32 v[96:97], v[62:63], v[62:63], v[58:59] op_sel_hi:[1,1,0]
	v_fmac_f32_e32 v84, 0xba800000, v65
	v_fmac_f32_e32 v82, 0xba800000, v65
	v_fmac_f32_e32 v64, 0xba800000, v65
	v_fmac_f32_e32 v80, 0xba800000, v65
	v_mul_f32_e32 v94, v80, v80
	v_mul_f32_e32 v96, v64, v64
	v_mul_f32_e32 v58, v82, v82
	v_mul_f32_e32 v60, v84, v84
	v_pk_add_f32 v[94:95], v[94:95], v[96:97]
	v_pk_add_f32 v[58:59], v[58:59], v[60:61]
	v_mov_b32_e32 v83, v84
	v_pk_add_f32 v[58:59], v[94:95], v[58:59]
	s_nop 0
	v_add_f32_e32 v58, v58, v59
	s_waitcnt lgkmcnt(0)
	s_nop 1
	v_add_f32_dpp v58, v58, v58 quad_perm:[1,0,3,2] row_mask:0xf bank_mask:0xf
	s_nop 1
	v_add_f32_dpp v58, v58, v58 quad_perm:[2,3,0,1] row_mask:0xf bank_mask:0xf
	s_nop 1
	v_add_f32_dpp v58, v58, v58 row_half_mirror row_mask:0xf bank_mask:0xf
	s_nop 1
	v_add_f32_dpp v58, v58, v58 row_mirror row_mask:0xf bank_mask:0xf
	v_mov_b32_e32 v59, v58
	s_nop 1
	v_permlane16_swap_b32_e32 v58, v59
	v_add_f32_e32 v58, v58, v59
	v_mov_b32_e32 v59, v58
	s_nop 1
	v_permlane32_swap_b32_e32 v58, v59
	v_add_f32_e32 v58, v58, v59
	v_fmamk_f32 v58, v58, 0x3a800000, v78
	v_mul_f32_e32 v59, 0x4f800000, v58
	v_cmp_gt_f32_e32 vcc, s6, v58
	s_nop 1
	v_cndmask_b32_e32 v58, v58, v59, vcc
	v_sqrt_f32_e32 v59, v58
	s_nop 0
	v_add_u32_e32 v60, -1, v59
	v_fma_f32 v61, -v60, v59, v58
	v_cmp_ge_f32_e64 s[0:1], 0, v61
	v_add_u32_e32 v61, 1, v59
	s_nop 0
	v_cndmask_b32_e64 v60, v59, v60, s[0:1]
	v_fma_f32 v59, -v61, v59, v58
	v_cmp_lt_f32_e64 s[0:1], 0, v59
	s_nop 1
	v_cndmask_b32_e64 v59, v60, v61, s[0:1]
	v_mul_f32_e32 v60, 0x37800000, v59
	v_cndmask_b32_e32 v59, v59, v60, vcc
	v_cmp_class_f32_e32 vcc, v58, v79
	s_nop 1
	v_cndmask_b32_e32 v58, v59, v58, vcc
	v_div_scale_f32 v59, s[0:1], v58, v58, 1.0
	v_rcp_f32_e32 v60, v59
	s_nop 0
	v_fma_f32 v61, -v59, v60, 1.0
	v_fmac_f32_e32 v60, v61, v60
	v_div_scale_f32 v61, vcc, 1.0, v58, 1.0
	v_mul_f32_e32 v65, v61, v60
	v_fma_f32 v81, -v59, v65, v61
	v_fmac_f32_e32 v65, v81, v60
	v_fma_f32 v59, -v59, v65, v61
	v_div_fmas_f32 v59, v59, v60, v65
	v_div_fixup_f32 v58, v59, v58, 1.0
	v_pk_mul_f32 v[60:61], v[86:87], v[58:59] op_sel_hi:[1,0]
	v_mov_b32_e32 v81, v64
	v_pk_mul_f32 v[86:87], v[90:91], v[58:59] op_sel_hi:[1,0]
	v_pk_fma_f32 v[60:61], v[6:7], v[60:61], v[14:15]
	v_pk_mul_f32 v[88:89], v[88:89], v[58:59] op_sel_hi:[1,0]
	v_pk_mul_f32 v[90:91], v[92:93], v[58:59] op_sel_hi:[1,0]
	v_pk_mul_f32 v[72:73], v[72:73], v[58:59] op_sel_hi:[1,0]
	v_pk_mul_f32 v[62:63], v[62:63], v[58:59] op_sel_hi:[1,0]
	v_pk_mul_f32 v[64:65], v[80:81], v[58:59] op_sel_hi:[1,0]
	v_pk_mul_f32 v[58:59], v[82:83], v[58:59] op_sel_hi:[1,0]
	v_pk_fma_f32 v[86:87], v[8:9], v[86:87], v[16:17]
	v_pk_fma_f32 v[80:81], v[20:21], v[58:59], v[28:29]
	v_cvt_pk_bf16_f32 v58, v60, v61
	v_pk_fma_f32 v[88:89], v[2:3], v[88:89], v[10:11]
	v_cvt_pk_bf16_f32 v59, v86, v87
	v_pk_fma_f32 v[90:91], v[4:5], v[90:91], v[12:13]
	v_cvt_pk_bf16_f32 v60, v88, v89
	v_pk_fma_f32 v[72:73], v[22:23], v[72:73], v[30:31]
	v_cvt_pk_bf16_f32 v61, v90, v91
	global_store_dwordx4 v[70:71], v[58:61], off offset:-1024
	v_pk_fma_f32 v[62:63], v[24:25], v[62:63], v[32:33]
	v_pk_fma_f32 v[64:65], v[18:19], v[64:65], v[26:27]
	v_cvt_pk_bf16_f32 v58, v72, v73
	v_cvt_pk_bf16_f32 v59, v62, v63
	v_cvt_pk_bf16_f32 v60, v64, v65
	v_cvt_pk_bf16_f32 v61, v80, v81
	global_store_dwordx4 v[70:71], v[58:61], off
	v_lshl_add_u64 v[70:71], v[70:71], 0, s[2:3]
	s_cbranch_scc1 .LBB0_728
.LBB0_722:
	s_waitcnt vmcnt(5)
	v_lshlrev_b32_e32 v91, 16, v35
	v_lshlrev_b32_e32 v90, 16, v34
	v_and_b32_e32 v59, 0xffff0000, v35
	v_and_b32_e32 v58, 0xffff0000, v34
	v_pk_add_f32 v[60:61], v[90:91], v[58:59]
	v_lshlrev_b32_e32 v93, 16, v37
	v_add_f32_e32 v60, v60, v61
	v_add_f32_e32 v89, 0, v60
	v_lshlrev_b32_e32 v92, 16, v36
	v_and_b32_e32 v61, 0xffff0000, v37
	v_and_b32_e32 v60, 0xffff0000, v36
	v_pk_add_f32 v[62:63], v[92:93], v[60:61]
	s_waitcnt vmcnt(4)
	v_lshlrev_b32_e32 v72, 16, v38
	v_and_b32_e32 v73, 0xffff0000, v38
	v_lshlrev_b32_e32 v80, 16, v39
	v_and_b32_e32 v81, 0xffff0000, v39
	v_pk_add_f32 v[62:63], v[62:63], v[62:63] op_sel_hi:[0,1]
	v_lshlrev_b32_e32 v82, 16, v40
	v_and_b32_e32 v84, 0xffff0000, v40
	v_lshlrev_b32_e32 v86, 16, v41
	v_and_b32_e32 v88, 0xffff0000, v41
	v_add_f32_e32 v83, v72, v73
	v_add_f32_e32 v85, v80, v81
	v_mov_b32_e32 v87, v63
	v_pk_add_f32 v[64:65], v[82:83], v[84:85]
	v_pk_add_f32 v[62:63], v[86:87], v[88:89]
	s_nop 0
	v_pk_add_f32 v[62:63], v[64:65], v[62:63]
	s_nop 0
	v_add_f32_e32 v62, v62, v63
	s_waitcnt lgkmcnt(0)
	s_nop 1
	v_add_f32_dpp v62, v62, v62 quad_perm:[1,0,3,2] row_mask:0xf bank_mask:0xf
	s_nop 1
	v_add_f32_dpp v62, v62, v62 quad_perm:[2,3,0,1] row_mask:0xf bank_mask:0xf
	s_nop 1
	v_add_f32_dpp v62, v62, v62 row_half_mirror row_mask:0xf bank_mask:0xf
	s_nop 1
	v_add_f32_dpp v62, v62, v62 row_mirror row_mask:0xf bank_mask:0xf
	v_mov_b32_e32 v63, v62
	s_nop 1
	v_permlane16_swap_b32_e32 v62, v63
	v_add_f32_e32 v62, v62, v63
	v_mov_b32_e32 v63, v62
	s_nop 1
	v_permlane32_swap_b32_e32 v62, v63
	v_add_f32_e32 v83, v62, v63
	v_fmac_f32_e32 v58, 0xba800000, v83
	v_fmac_f32_e32 v59, 0xba800000, v83
	v_fmac_f32_e32 v91, 0xba800000, v83
	v_fmac_f32_e32 v90, 0xba800000, v83
	v_mov_b32_e32 v94, v91
	v_mov_b32_e32 v95, v59
	v_mov_b32_e32 v91, v58
	v_pk_mul_f32 v[62:63], v[94:95], v[94:95]
	v_pk_mul_f32 v[58:59], v[90:91], v[90:91]
	v_fmac_f32_e32 v60, 0xba800000, v83
	v_pk_mov_b32 v[64:65], v[58:59], v[62:63] op_sel:[1,0]
	v_mov_b32_e32 v59, v63
	v_fmac_f32_e32 v61, 0xba800000, v83
	v_fmac_f32_e32 v93, 0xba800000, v83
	v_pk_add_f32 v[58:59], v[64:65], v[58:59]
	v_fmac_f32_e32 v92, 0xba800000, v83
	v_mov_b32_e32 v96, v93
	v_mov_b32_e32 v97, v61
	v_mov_b32_e32 v93, v60
	v_pk_add_f32 v[58:59], v[58:59], v[58:59] op_sel_hi:[0,1]
	v_pk_mul_f32 v[62:63], v[96:97], v[96:97]
	v_pk_mul_f32 v[60:61], v[92:93], v[92:93]
	v_fmac_f32_e32 v72, 0xba800000, v83
	v_pk_mov_b32 v[64:65], v[60:61], v[62:63] op_sel:[1,0]
	v_mov_b32_e32 v61, v63
	v_fmac_f32_e32 v73, 0xba800000, v83
	v_fmac_f32_e32 v80, 0xba800000, v83
	v_mul_f32_e32 v58, v72, v72
	v_pk_add_f32 v[60:61], v[64:65], v[60:61]
	v_fmac_f32_e32 v81, 0xba800000, v83
	v_pk_fma_f32 v[62:63], v[72:73], v[72:73], v[58:59] op_sel_hi:[1,1,0]
	v_mul_f32_e32 v58, v80, v80
	v_pk_add_f32 v[60:61], v[60:61], v[60:61] op_sel_hi:[0,1]
	v_pk_fma_f32 v[64:65], v[80:81], v[80:81], v[58:59] op_sel_hi:[1,1,0]
	v_fmac_f32_e32 v88, 0xba800000, v83
	v_fmac_f32_e32 v86, 0xba800000, v83
	v_fmac_f32_e32 v84, 0xba800000, v83
	v_fmac_f32_e32 v82, 0xba800000, v83
	v_mul_f32_e32 v62, v82, v82
	v_mul_f32_e32 v64, v84, v84
	v_mul_f32_e32 v58, v86, v86
	v_mul_f32_e32 v60, v88, v88
	v_pk_add_f32 v[62:63], v[62:63], v[64:65]
	v_pk_add_f32 v[58:59], v[58:59], v[60:61]
	s_nop 0
	v_pk_add_f32 v[58:59], v[62:63], v[58:59]
	s_nop 0
	v_add_f32_e32 v58, v58, v59
	s_waitcnt lgkmcnt(0)
	s_nop 1
	v_add_f32_dpp v58, v58, v58 quad_perm:[1,0,3,2] row_mask:0xf bank_mask:0xf
	s_nop 1
	v_add_f32_dpp v58, v58, v58 quad_perm:[2,3,0,1] row_mask:0xf bank_mask:0xf
	s_nop 1
	v_add_f32_dpp v58, v58, v58 row_half_mirror row_mask:0xf bank_mask:0xf
	s_nop 1
	v_add_f32_dpp v58, v58, v58 row_mirror row_mask:0xf bank_mask:0xf
	v_mov_b32_e32 v59, v58
	s_nop 1
	v_permlane16_swap_b32_e32 v58, v59
	v_add_f32_e32 v58, v58, v59
	v_mov_b32_e32 v59, v58
	s_nop 1
	v_permlane32_swap_b32_e32 v58, v59
	v_add_f32_e32 v58, v58, v59
	v_fmamk_f32 v58, v58, 0x3a800000, v78
	v_mul_f32_e32 v59, 0x4f800000, v58
	v_cmp_gt_f32_e32 vcc, s6, v58
	s_nop 1
	v_cndmask_b32_e32 v58, v58, v59, vcc
	v_sqrt_f32_e32 v59, v58
	s_nop 0
	v_add_u32_e32 v60, -1, v59
	v_fma_f32 v61, -v60, v59, v58
	v_cmp_ge_f32_e64 s[0:1], 0, v61
	v_add_u32_e32 v61, 1, v59
	s_nop 0
	v_cndmask_b32_e64 v60, v59, v60, s[0:1]
	v_fma_f32 v59, -v61, v59, v58
	v_cmp_lt_f32_e64 s[0:1], 0, v59
	s_nop 1
	v_cndmask_b32_e64 v59, v60, v61, s[0:1]
	v_mul_f32_e32 v60, 0x37800000, v59
	v_cndmask_b32_e32 v59, v59, v60, vcc
	v_cmp_class_f32_e32 vcc, v58, v79
	s_nop 1
	v_cndmask_b32_e32 v83, v59, v58, vcc
	global_load_dwordx4 v[58:61], v[70:71], off offset:-1024
	global_load_dwordx4 v[62:65], v[70:71], off
	v_div_scale_f32 v85, s[0:1], v83, v83, 1.0
	v_rcp_f32_e32 v87, v85
	s_add_i32 s0, s4, 5
	s_cmp_gt_u32 s0, 12
	v_fma_f32 v89, -v85, v87, 1.0
	v_fmac_f32_e32 v87, v89, v87
	v_div_scale_f32 v89, vcc, 1.0, v83, 1.0
	v_mul_f32_e32 v98, v89, v87
	v_fma_f32 v99, -v85, v98, v89
	v_fmac_f32_e32 v98, v99, v87
	v_fma_f32 v85, -v85, v98, v89
	v_div_fmas_f32 v85, v85, v87, v98
	v_div_fixup_f32 v98, v85, v83, 1.0
	v_pk_mul_f32 v[90:91], v[90:91], v[98:99] op_sel_hi:[1,0]
	v_pk_mul_f32 v[72:73], v[72:73], v[98:99] op_sel_hi:[1,0]
	v_mov_b32_e32 v83, v84
	v_pk_fma_f32 v[90:91], v[6:7], v[90:91], v[14:15]
	v_pk_mul_f32 v[80:81], v[80:81], v[98:99] op_sel_hi:[1,0]
	v_pk_fma_f32 v[102:103], v[22:23], v[72:73], v[30:31]
	v_pk_mul_f32 v[72:73], v[82:83], v[98:99] op_sel_hi:[1,0]
	v_mov_b32_e32 v87, v88
	v_pk_fma_f32 v[100:101], v[24:25], v[80:81], v[32:33]
	v_pk_mul_f32 v[80:81], v[86:87], v[98:99] op_sel_hi:[1,0]
	v_pk_fma_f32 v[86:87], v[18:19], v[72:73], v[26:27]
	v_pk_mul_f32 v[94:95], v[94:95], v[98:99] op_sel_hi:[1,0]
	v_pk_fma_f32 v[94:95], v[8:9], v[94:95], v[16:17]
	v_pk_fma_f32 v[84:85], v[20:21], v[80:81], v[28:29]
	v_cvt_pk_bf16_f32 v80, v90, v91
	v_pk_mul_f32 v[92:93], v[92:93], v[98:99] op_sel_hi:[1,0]
	v_pk_fma_f32 v[92:93], v[2:3], v[92:93], v[10:11]
	v_cvt_pk_bf16_f32 v81, v94, v95
	v_pk_mul_f32 v[96:97], v[96:97], v[98:99] op_sel_hi:[1,0]
	v_pk_fma_f32 v[96:97], v[4:5], v[96:97], v[12:13]
	v_cvt_pk_bf16_f32 v82, v92, v93
	v_cvt_pk_bf16_f32 v83, v96, v97
	v_add_co_u32_e32 v72, vcc, s8, v70
	s_nop 1
	v_addc_co_u32_e32 v73, vcc, -1, v71, vcc
	global_store_dwordx4 v[72:73], v[80:83], off offset:-3072
	s_nop 1
	v_cvt_pk_bf16_f32 v80, v102, v103
	v_cvt_pk_bf16_f32 v81, v100, v101
	v_cvt_pk_bf16_f32 v82, v86, v87
	v_cvt_pk_bf16_f32 v83, v84, v85
	global_store_dwordx4 v[72:73], v[80:83], off offset:-2048
	s_cbranch_scc1 .LBB0_724
	v_add3_u32 v34, v66, s4, 8
	v_ashrrev_i32_e32 v35, 31, v34
	v_lshlrev_b64 v[34:35], 11, v[34:35]
	v_lshl_add_u64 v[38:39], v[68:69], 0, v[34:35]
	global_load_dwordx4 v[34:37], v[38:39], off
	s_nop 0
	global_load_dwordx4 v[38:41], v[38:39], off offset:1024
.LBB0_724:
	s_waitcnt vmcnt(7)
	v_lshlrev_b32_e32 v93, 16, v43
	v_lshlrev_b32_e32 v92, 16, v42
	v_and_b32_e32 v95, 0xffff0000, v43
	v_and_b32_e32 v94, 0xffff0000, v42
	v_pk_add_f32 v[96:97], v[92:93], v[94:95]
	v_and_b32_e32 v99, 0xffff0000, v45
	v_add_f32_e32 v85, v96, v97
	v_lshlrev_b32_e32 v97, 16, v45
	v_lshlrev_b32_e32 v96, 16, v44
	v_and_b32_e32 v98, 0xffff0000, v44
	v_pk_add_f32 v[100:101], v[96:97], v[98:99]
	s_waitcnt vmcnt(6)
	v_lshlrev_b32_e32 v80, 16, v46
	v_and_b32_e32 v81, 0xffff0000, v46
	v_lshlrev_b32_e32 v82, 16, v47
	v_and_b32_e32 v83, 0xffff0000, v47
	v_pk_add_f32 v[100:101], v[100:101], v[100:101] op_sel_hi:[0,1]
	v_lshlrev_b32_e32 v84, 16, v48
	v_and_b32_e32 v86, 0xffff0000, v48
	v_lshlrev_b32_e32 v88, 16, v49
	v_and_b32_e32 v90, 0xffff0000, v49
	v_add_f32_e32 v91, 0, v85
	v_add_f32_e32 v85, v80, v81
	v_add_f32_e32 v87, v82, v83
	v_mov_b32_e32 v89, v101
	v_pk_add_f32 v[102:103], v[84:85], v[86:87]
	v_pk_add_f32 v[100:101], v[88:89], v[90:91]
	s_nop 0
	v_pk_add_f32 v[100:101], v[102:103], v[100:101]
	s_nop 0
	v_add_f32_e32 v85, v100, v101
	s_waitcnt lgkmcnt(0)
	s_nop 1
	v_add_f32_dpp v85, v85, v85 quad_perm:[1,0,3,2] row_mask:0xf bank_mask:0xf
	s_nop 1
	v_add_f32_dpp v85, v85, v85 quad_perm:[2,3,0,1] row_mask:0xf bank_mask:0xf
	s_nop 1
	v_add_f32_dpp v85, v85, v85 row_half_mirror row_mask:0xf bank_mask:0xf
	s_nop 1
	v_add_f32_dpp v85, v85, v85 row_mirror row_mask:0xf bank_mask:0xf
	v_mov_b32_e32 v87, v85
	s_nop 1
	v_permlane16_swap_b32_e32 v85, v87
	v_add_f32_e32 v85, v85, v87
	v_mov_b32_e32 v87, v85
	s_nop 1
	v_permlane32_swap_b32_e32 v85, v87
	v_add_f32_e32 v85, v85, v87
	v_fmac_f32_e32 v94, 0xba800000, v85
	v_fmac_f32_e32 v95, 0xba800000, v85
	v_fmac_f32_e32 v93, 0xba800000, v85
	v_fmac_f32_e32 v92, 0xba800000, v85
	v_mov_b32_e32 v100, v93
	v_mov_b32_e32 v101, v95
	v_mov_b32_e32 v93, v94
	v_pk_mul_f32 v[102:103], v[100:101], v[100:101]
	v_pk_mul_f32 v[94:95], v[92:93], v[92:93]
	v_fmac_f32_e32 v98, 0xba800000, v85
	v_pk_mov_b32 v[104:105], v[94:95], v[102:103] op_sel:[1,0]
	v_mov_b32_e32 v95, v103
	v_fmac_f32_e32 v99, 0xba800000, v85
	v_fmac_f32_e32 v97, 0xba800000, v85
	v_pk_add_f32 v[94:95], v[104:105], v[94:95]
	v_fmac_f32_e32 v96, 0xba800000, v85
	v_mov_b32_e32 v102, v97
	v_mov_b32_e32 v103, v99
	v_mov_b32_e32 v97, v98
	v_pk_add_f32 v[94:95], v[94:95], v[94:95] op_sel_hi:[0,1]
	v_pk_mul_f32 v[104:105], v[102:103], v[102:103]
	v_pk_mul_f32 v[98:99], v[96:97], v[96:97]
	v_fmac_f32_e32 v80, 0xba800000, v85
	v_pk_mov_b32 v[106:107], v[98:99], v[104:105] op_sel:[1,0]
	v_mov_b32_e32 v99, v105
	v_fmac_f32_e32 v81, 0xba800000, v85
	v_fmac_f32_e32 v82, 0xba800000, v85
	v_mul_f32_e32 v94, v80, v80
	v_pk_add_f32 v[98:99], v[106:107], v[98:99]
	v_fmac_f32_e32 v83, 0xba800000, v85
	v_pk_fma_f32 v[104:105], v[80:81], v[80:81], v[94:95] op_sel_hi:[1,1,0]
	v_mul_f32_e32 v94, v82, v82
	v_pk_add_f32 v[98:99], v[98:99], v[98:99] op_sel_hi:[0,1]
	v_pk_fma_f32 v[106:107], v[82:83], v[82:83], v[94:95] op_sel_hi:[1,1,0]
	v_fmac_f32_e32 v90, 0xba800000, v85
	v_fmac_f32_e32 v88, 0xba800000, v85
	v_fmac_f32_e32 v86, 0xba800000, v85
	v_fmac_f32_e32 v84, 0xba800000, v85
	v_mul_f32_e32 v104, v84, v84
	v_mul_f32_e32 v106, v86, v86
	v_mul_f32_e32 v94, v88, v88
	v_mul_f32_e32 v98, v90, v90
	v_pk_add_f32 v[104:105], v[104:105], v[106:107]
	v_pk_add_f32 v[94:95], v[94:95], v[98:99]
	s_nop 0
	v_pk_add_f32 v[94:95], v[104:105], v[94:95]
	s_nop 0
	v_add_f32_e32 v85, v94, v95
	s_waitcnt lgkmcnt(0)
	s_nop 1
	v_add_f32_dpp v85, v85, v85 quad_perm:[1,0,3,2] row_mask:0xf bank_mask:0xf
	s_nop 1
	v_add_f32_dpp v85, v85, v85 quad_perm:[2,3,0,1] row_mask:0xf bank_mask:0xf
	s_nop 1
	v_add_f32_dpp v85, v85, v85 row_half_mirror row_mask:0xf bank_mask:0xf
	s_nop 1
	v_add_f32_dpp v85, v85, v85 row_mirror row_mask:0xf bank_mask:0xf
	v_mov_b32_e32 v87, v85
	s_nop 1
	v_permlane16_swap_b32_e32 v85, v87
	v_add_f32_e32 v85, v85, v87
	v_mov_b32_e32 v87, v85
	s_nop 1
	v_permlane32_swap_b32_e32 v85, v87
	v_add_f32_e32 v85, v85, v87
	v_fmamk_f32 v85, v85, 0x3a800000, v78
	v_mul_f32_e32 v87, 0x4f800000, v85
	v_cmp_gt_f32_e32 vcc, s6, v85
	s_nop 1
	v_cndmask_b32_e32 v85, v85, v87, vcc
	v_sqrt_f32_e32 v87, v85
	s_nop 0
	v_add_u32_e32 v89, -1, v87
	v_fma_f32 v91, -v89, v87, v85
	v_cmp_ge_f32_e64 s[0:1], 0, v91
	v_add_u32_e32 v91, 1, v87
	s_nop 0
	v_cndmask_b32_e64 v89, v87, v89, s[0:1]
	v_fma_f32 v87, -v91, v87, v85
	v_cmp_lt_f32_e64 s[0:1], 0, v87
	s_nop 1
	v_cndmask_b32_e64 v87, v89, v91, s[0:1]
	v_mul_f32_e32 v89, 0x37800000, v87
	v_cndmask_b32_e32 v87, v87, v89, vcc
	v_cmp_class_f32_e32 vcc, v85, v79
	s_nop 1
	v_cndmask_b32_e32 v85, v87, v85, vcc
	v_div_scale_f32 v87, s[0:1], v85, v85, 1.0
	v_rcp_f32_e32 v89, v87
	s_add_i32 s0, s4, 6
	s_cmp_gt_u32 s0, 12
	v_fma_f32 v91, -v87, v89, 1.0
	v_fmac_f32_e32 v89, v91, v89
	v_div_scale_f32 v91, vcc, 1.0, v85, 1.0
	v_mul_f32_e32 v94, v91, v89
	v_fma_f32 v95, -v87, v94, v91
	v_fmac_f32_e32 v94, v95, v89
	v_fma_f32 v87, -v87, v94, v91
	v_div_fmas_f32 v87, v87, v89, v94
	v_div_fixup_f32 v94, v87, v85, 1.0
	v_pk_mul_f32 v[92:93], v[92:93], v[94:95] op_sel_hi:[1,0]
	v_pk_mul_f32 v[80:81], v[80:81], v[94:95] op_sel_hi:[1,0]
	v_mov_b32_e32 v85, v86
	v_pk_fma_f32 v[92:93], v[6:7], v[92:93], v[14:15]
	v_pk_fma_f32 v[104:105], v[22:23], v[80:81], v[30:31]
	v_pk_mul_f32 v[80:81], v[84:85], v[94:95] op_sel_hi:[1,0]
	v_pk_mul_f32 v[98:99], v[100:101], v[94:95] op_sel_hi:[1,0]
	v_pk_fma_f32 v[86:87], v[18:19], v[80:81], v[26:27]
	v_pk_fma_f32 v[98:99], v[8:9], v[98:99], v[16:17]
	v_pk_mul_f32 v[82:83], v[82:83], v[94:95] op_sel_hi:[1,0]
	v_mov_b32_e32 v89, v90
	v_pk_mul_f32 v[100:101], v[102:103], v[94:95] op_sel_hi:[1,0]
	v_pk_fma_f32 v[102:103], v[24:25], v[82:83], v[32:33]
	v_pk_mul_f32 v[82:83], v[88:89], v[94:95] op_sel_hi:[1,0]
	v_cvt_pk_bf16_f32 v80, v92, v93
	v_bfe_u32 v81, v98, 16, 1
	v_pk_mul_f32 v[96:97], v[96:97], v[94:95] op_sel_hi:[1,0]
	v_pk_fma_f32 v[84:85], v[20:21], v[82:83], v[28:29]
	v_add3_u32 v81, v98, v81, s7
	v_bfe_u32 v82, v99, 16, 1
	v_pk_fma_f32 v[96:97], v[2:3], v[96:97], v[10:11]
	v_lshrrev_b32_e32 v81, 16, v81
	v_add3_u32 v82, v99, v82, s7
	v_and_or_b32 v81, v82, s5, v81
	v_pk_fma_f32 v[100:101], v[4:5], v[100:101], v[12:13]
	v_cvt_pk_bf16_f32 v82, v96, v97
	v_cvt_pk_bf16_f32 v83, v100, v101
	global_store_dwordx4 v[72:73], v[80:83], off offset:-1024
	s_nop 1
	v_cvt_pk_bf16_f32 v80, v104, v105
	v_cvt_pk_bf16_f32 v81, v102, v103
	v_cvt_pk_bf16_f32 v82, v86, v87
	v_cvt_pk_bf16_f32 v83, v84, v85
	global_store_dwordx4 v[70:71], v[80:83], off offset:-4096
	s_cbranch_scc1 .LBB0_726
	v_add3_u32 v42, v66, s4, 9
	v_ashrrev_i32_e32 v43, 31, v42
	v_lshlrev_b64 v[42:43], 11, v[42:43]
	v_lshl_add_u64 v[46:47], v[68:69], 0, v[42:43]
	global_load_dwordx4 v[42:45], v[46:47], off
	s_nop 0
	global_load_dwordx4 v[46:49], v[46:47], off offset:1024
.LBB0_726:
	s_waitcnt vmcnt(7)
	v_lshlrev_b32_e32 v91, 16, v51
	v_lshlrev_b32_e32 v90, 16, v50
	v_and_b32_e32 v93, 0xffff0000, v51
	v_and_b32_e32 v92, 0xffff0000, v50
	v_pk_add_f32 v[94:95], v[90:91], v[92:93]
	v_and_b32_e32 v97, 0xffff0000, v53
	v_add_f32_e32 v83, v94, v95
	v_lshlrev_b32_e32 v95, 16, v53
	v_lshlrev_b32_e32 v94, 16, v52
	v_and_b32_e32 v96, 0xffff0000, v52
	v_pk_add_f32 v[98:99], v[94:95], v[96:97]
	s_waitcnt vmcnt(6)
	v_lshlrev_b32_e32 v72, 16, v54
	v_and_b32_e32 v73, 0xffff0000, v54
	v_lshlrev_b32_e32 v80, 16, v55
	v_and_b32_e32 v81, 0xffff0000, v55
	v_pk_add_f32 v[98:99], v[98:99], v[98:99] op_sel_hi:[0,1]
	v_lshlrev_b32_e32 v82, 16, v56
	v_and_b32_e32 v84, 0xffff0000, v56
	v_lshlrev_b32_e32 v86, 16, v57
	v_and_b32_e32 v88, 0xffff0000, v57
	v_add_f32_e32 v89, 0, v83
	v_add_f32_e32 v83, v72, v73
	v_add_f32_e32 v85, v80, v81
	v_mov_b32_e32 v87, v99
	v_pk_add_f32 v[100:101], v[82:83], v[84:85]
	v_pk_add_f32 v[98:99], v[86:87], v[88:89]
	s_nop 0
	v_pk_add_f32 v[98:99], v[100:101], v[98:99]
	s_nop 0
	v_add_f32_e32 v83, v98, v99
	s_waitcnt lgkmcnt(0)
	s_nop 1
	v_add_f32_dpp v83, v83, v83 quad_perm:[1,0,3,2] row_mask:0xf bank_mask:0xf
	s_nop 1
	v_add_f32_dpp v83, v83, v83 quad_perm:[2,3,0,1] row_mask:0xf bank_mask:0xf
	s_nop 1
	v_add_f32_dpp v83, v83, v83 row_half_mirror row_mask:0xf bank_mask:0xf
	s_nop 1
	v_add_f32_dpp v83, v83, v83 row_mirror row_mask:0xf bank_mask:0xf
	v_mov_b32_e32 v85, v83
	s_nop 1
	v_permlane16_swap_b32_e32 v83, v85
	v_add_f32_e32 v83, v83, v85
	v_mov_b32_e32 v85, v83
	s_nop 1
	v_permlane32_swap_b32_e32 v83, v85
	v_add_f32_e32 v83, v83, v85
	v_fmac_f32_e32 v92, 0xba800000, v83
	v_fmac_f32_e32 v93, 0xba800000, v83
	v_fmac_f32_e32 v91, 0xba800000, v83
	v_fmac_f32_e32 v90, 0xba800000, v83
	v_mov_b32_e32 v98, v91
	v_mov_b32_e32 v99, v93
	v_mov_b32_e32 v91, v92
	v_pk_mul_f32 v[100:101], v[98:99], v[98:99]
	v_pk_mul_f32 v[92:93], v[90:91], v[90:91]
	v_fmac_f32_e32 v96, 0xba800000, v83
	v_pk_mov_b32 v[102:103], v[92:93], v[100:101] op_sel:[1,0]
	v_mov_b32_e32 v93, v101
	v_fmac_f32_e32 v97, 0xba800000, v83
	v_fmac_f32_e32 v95, 0xba800000, v83
	v_pk_add_f32 v[92:93], v[102:103], v[92:93]
	v_fmac_f32_e32 v94, 0xba800000, v83
	v_mov_b32_e32 v100, v95
	v_mov_b32_e32 v101, v97
	v_mov_b32_e32 v95, v96
	v_pk_add_f32 v[92:93], v[92:93], v[92:93] op_sel_hi:[0,1]
	v_pk_mul_f32 v[102:103], v[100:101], v[100:101]
	v_pk_mul_f32 v[96:97], v[94:95], v[94:95]
	v_fmac_f32_e32 v72, 0xba800000, v83
	v_pk_mov_b32 v[104:105], v[96:97], v[102:103] op_sel:[1,0]
	v_mov_b32_e32 v97, v103
	v_fmac_f32_e32 v73, 0xba800000, v83
	v_fmac_f32_e32 v80, 0xba800000, v83
	v_mul_f32_e32 v92, v72, v72
	v_pk_add_f32 v[96:97], v[104:105], v[96:97]
	v_fmac_f32_e32 v81, 0xba800000, v83
	v_pk_fma_f32 v[102:103], v[72:73], v[72:73], v[92:93] op_sel_hi:[1,1,0]
	v_mul_f32_e32 v92, v80, v80
	v_pk_add_f32 v[96:97], v[96:97], v[96:97] op_sel_hi:[0,1]
	v_pk_fma_f32 v[104:105], v[80:81], v[80:81], v[92:93] op_sel_hi:[1,1,0]
	v_fmac_f32_e32 v88, 0xba800000, v83
	v_fmac_f32_e32 v86, 0xba800000, v83
	v_fmac_f32_e32 v84, 0xba800000, v83
	v_fmac_f32_e32 v82, 0xba800000, v83
	v_mul_f32_e32 v102, v82, v82
	v_mul_f32_e32 v104, v84, v84
	v_mul_f32_e32 v92, v86, v86
	v_mul_f32_e32 v96, v88, v88
	v_pk_add_f32 v[102:103], v[102:103], v[104:105]
	v_pk_add_f32 v[92:93], v[92:93], v[96:97]
	s_nop 0
	v_pk_add_f32 v[92:93], v[102:103], v[92:93]
	s_nop 0
	v_add_f32_e32 v83, v92, v93
	s_waitcnt lgkmcnt(0)
	s_nop 1
	v_add_f32_dpp v83, v83, v83 quad_perm:[1,0,3,2] row_mask:0xf bank_mask:0xf
	s_nop 1
	v_add_f32_dpp v83, v83, v83 quad_perm:[2,3,0,1] row_mask:0xf bank_mask:0xf
	s_nop 1
	v_add_f32_dpp v83, v83, v83 row_half_mirror row_mask:0xf bank_mask:0xf
	s_nop 1
	v_add_f32_dpp v83, v83, v83 row_mirror row_mask:0xf bank_mask:0xf
	v_mov_b32_e32 v85, v83
	s_nop 1
	v_permlane16_swap_b32_e32 v83, v85
	v_add_f32_e32 v83, v83, v85
	v_mov_b32_e32 v85, v83
	s_nop 1
	v_permlane32_swap_b32_e32 v83, v85
	v_add_f32_e32 v83, v83, v85
	v_fmamk_f32 v83, v83, 0x3a800000, v78
	v_mul_f32_e32 v85, 0x4f800000, v83
	v_cmp_gt_f32_e32 vcc, s6, v83
	s_nop 1
	v_cndmask_b32_e32 v83, v83, v85, vcc
	v_sqrt_f32_e32 v85, v83
	s_nop 0
	v_add_u32_e32 v87, -1, v85
	v_fma_f32 v89, -v87, v85, v83
	v_cmp_ge_f32_e64 s[0:1], 0, v89
	v_add_u32_e32 v89, 1, v85
	s_nop 0
	v_cndmask_b32_e64 v87, v85, v87, s[0:1]
	v_fma_f32 v85, -v89, v85, v83
	v_cmp_lt_f32_e64 s[0:1], 0, v85
	s_nop 1
	v_cndmask_b32_e64 v85, v87, v89, s[0:1]
	v_mul_f32_e32 v87, 0x37800000, v85
	v_cndmask_b32_e32 v85, v85, v87, vcc
	v_cmp_class_f32_e32 vcc, v83, v79
	s_nop 1
	v_cndmask_b32_e32 v83, v85, v83, vcc
	v_div_scale_f32 v85, s[0:1], v83, v83, 1.0
	v_rcp_f32_e32 v87, v85
	s_add_i32 s0, s4, 7
	s_cmp_gt_u32 s0, 12
	v_fma_f32 v89, -v85, v87, 1.0
	v_fmac_f32_e32 v87, v89, v87
	v_div_scale_f32 v89, vcc, 1.0, v83, 1.0
	v_mul_f32_e32 v92, v89, v87
	v_fma_f32 v93, -v85, v92, v89
	v_fmac_f32_e32 v92, v93, v87
	v_fma_f32 v85, -v85, v92, v89
	v_div_fmas_f32 v85, v85, v87, v92
	v_div_fixup_f32 v92, v85, v83, 1.0
	v_pk_mul_f32 v[90:91], v[90:91], v[92:93] op_sel_hi:[1,0]
	v_pk_mul_f32 v[80:81], v[80:81], v[92:93] op_sel_hi:[1,0]
	v_mov_b32_e32 v83, v84
	v_pk_mul_f32 v[96:97], v[98:99], v[92:93] op_sel_hi:[1,0]
	v_pk_fma_f32 v[90:91], v[6:7], v[90:91], v[14:15]
	v_pk_mul_f32 v[98:99], v[100:101], v[92:93] op_sel_hi:[1,0]
	v_pk_fma_f32 v[100:101], v[24:25], v[80:81], v[32:33]
	v_pk_mul_f32 v[80:81], v[82:83], v[92:93] op_sel_hi:[1,0]
	v_mov_b32_e32 v87, v88
	v_pk_mul_f32 v[82:83], v[86:87], v[92:93] op_sel_hi:[1,0]
	v_pk_fma_f32 v[86:87], v[18:19], v[80:81], v[26:27]
	v_pk_fma_f32 v[96:97], v[8:9], v[96:97], v[16:17]
	v_cvt_pk_bf16_f32 v80, v90, v91
	v_bfe_u32 v81, v96, 16, 1
	v_pk_mul_f32 v[94:95], v[94:95], v[92:93] op_sel_hi:[1,0]
	v_pk_fma_f32 v[84:85], v[20:21], v[82:83], v[28:29]
	v_add3_u32 v81, v96, v81, s7
	v_bfe_u32 v82, v97, 16, 1
	v_pk_fma_f32 v[94:95], v[2:3], v[94:95], v[10:11]
	v_lshrrev_b32_e32 v81, 16, v81
	v_add3_u32 v82, v97, v82, s7
	v_and_or_b32 v81, v82, s5, v81
	v_pk_fma_f32 v[98:99], v[4:5], v[98:99], v[12:13]
	v_cvt_pk_bf16_f32 v82, v94, v95
	v_pk_mul_f32 v[72:73], v[72:73], v[92:93] op_sel_hi:[1,0]
	v_pk_fma_f32 v[72:73], v[22:23], v[72:73], v[30:31]
	v_cvt_pk_bf16_f32 v83, v98, v99
	global_store_dwordx4 v[70:71], v[80:83], off offset:-3072
	s_nop 1
	v_cvt_pk_bf16_f32 v80, v72, v73
	v_cvt_pk_bf16_f32 v81, v100, v101
	v_cvt_pk_bf16_f32 v82, v86, v87
	v_cvt_pk_bf16_f32 v83, v84, v85
	global_store_dwordx4 v[70:71], v[80:83], off offset:-2048
	s_cbranch_scc1 .LBB0_721
	v_add3_u32 v50, v66, s4, 10
	v_ashrrev_i32_e32 v51, 31, v50
	v_lshlrev_b64 v[50:51], 11, v[50:51]
	v_lshl_add_u64 v[54:55], v[68:69], 0, v[50:51]
	global_load_dwordx4 v[50:53], v[54:55], off
	s_nop 0
	global_load_dwordx4 v[54:57], v[54:55], off offset:1024
	s_branch .LBB0_721

.LBB0_767:
	v_cvt_pk_bf16_f32 v114, v130, v131
	v_cvt_pk_bf16_f32 v115, v132, v133
	s_lshl_b32 s4, s72, 8
	v_cvt_pk_bf16_f32 v116, v134, v135
	s_ashr_i32 s5, s4, 31
	v_lshl_add_u32 v166, s73, 8, v162
	v_lshl_add_u64 v[160:161], s[4:5], 1, v[154:155]
	v_mad_i64_i32 v[118:119], s[4:5], v166, s77, v[160:161]
	v_cvt_pk_bf16_f32 v117, v136, v137
	global_store_dwordx4 v[118:119], v[114:117], off
	v_bfe_u32 v120, v145, 16, 1
	v_add3_u32 v120, v145, v120, s79
	v_cvt_pk_bf16_f32 v114, v138, v139
	v_cvt_pk_bf16_f32 v115, v140, v141
	v_cvt_pk_bf16_f32 v116, v142, v143
	v_bfe_u32 v117, v144, 16, 1
	v_add3_u32 v117, v144, v117, s79
	v_lshrrev_b32_e32 v117, 16, v117
	v_and_or_b32 v117, v120, s80, v117
	global_store_dwordx4 v[118:119], v[114:117], off offset:256
	s_andn2_b64 vcc, exec, s[52:53]
	s_mov_b64 s[38:39], -1
	v_cndmask_b32_e64 v114, 0, 1, s[52:53]
	v_cmp_ne_u32_e64 s[4:5], 1, v114
	s_cbranch_vccnz .LBB0_771
	v_mov_b64_e32 v[116:117], v[112:113]
	v_mov_b64_e32 v[128:129], v[100:101]
	v_mov_b64_e32 v[124:125], v[104:105]
	v_mov_b64_e32 v[120:121], v[108:109]
	s_and_b64 vcc, exec, s[2:3]
	v_mov_b64_e32 v[114:115], v[110:111]
	v_mov_b64_e32 v[126:127], v[98:99]
	v_mov_b64_e32 v[122:123], v[102:103]
	v_mov_b64_e32 v[118:119], v[106:107]
	s_cbranch_vccnz .LBB0_770
	v_pk_mul_f32 v[116:117], v[112:113], s[20:21] op_sel_hi:[1,0]
	v_pk_mul_f32 v[114:115], v[110:111], s[20:21] op_sel_hi:[1,0]
	v_pk_mul_f32 v[120:121], v[108:109], s[20:21] op_sel_hi:[1,0]
	v_pk_mul_f32 v[118:119], v[106:107], s[20:21] op_sel_hi:[1,0]
	v_pk_mul_f32 v[124:125], v[104:105], s[20:21] op_sel_hi:[1,0]
	v_pk_mul_f32 v[122:123], v[102:103], s[20:21] op_sel_hi:[1,0]
	v_pk_mul_f32 v[128:129], v[100:101], s[20:21] op_sel_hi:[1,0]
	v_pk_mul_f32 v[126:127], v[98:99], s[20:21] op_sel_hi:[1,0]

.LBB0_773:
	v_or_b32_e32 v98, 16, v166
	v_mad_i64_i32 v[102:103], s[38:39], v98, s77, v[160:161]
	v_cvt_pk_bf16_f32 v98, v114, v115
	v_cvt_pk_bf16_f32 v99, v116, v117
	v_cvt_pk_bf16_f32 v100, v118, v119
	v_cvt_pk_bf16_f32 v101, v120, v121
	global_store_dwordx4 v[102:103], v[98:101], off
	v_bfe_u32 v104, v129, 16, 1
	v_add3_u32 v104, v129, v104, s79
	v_cvt_pk_bf16_f32 v98, v122, v123
	v_cvt_pk_bf16_f32 v99, v124, v125
	v_cvt_pk_bf16_f32 v100, v126, v127
	v_bfe_u32 v101, v128, 16, 1
	v_add3_u32 v101, v128, v101, s79
	v_lshrrev_b32_e32 v101, 16, v101
	v_and_or_b32 v101, v104, s80, v101
	s_and_b64 vcc, exec, s[4:5]
	s_mov_b64 s[38:39], -1
	global_store_dwordx4 v[102:103], v[98:101], off offset:256
	s_cbranch_vccnz .LBB0_777
	s_nop 0
	v_mov_b64_e32 v[100:101], v[96:97]
	v_mov_b64_e32 v[112:113], v[84:85]
	v_mov_b64_e32 v[108:109], v[88:89]
	v_mov_b64_e32 v[104:105], v[92:93]
	s_and_b64 vcc, exec, s[2:3]
	v_mov_b64_e32 v[98:99], v[94:95]
	v_mov_b64_e32 v[110:111], v[82:83]
	v_mov_b64_e32 v[106:107], v[86:87]
	v_mov_b64_e32 v[102:103], v[90:91]
	s_cbranch_vccnz .LBB0_776
	v_pk_mul_f32 v[100:101], v[96:97], s[20:21] op_sel_hi:[1,0]
	v_pk_mul_f32 v[98:99], v[94:95], s[20:21] op_sel_hi:[1,0]
	v_pk_mul_f32 v[104:105], v[92:93], s[20:21] op_sel_hi:[1,0]
	v_pk_mul_f32 v[102:103], v[90:91], s[20:21] op_sel_hi:[1,0]
	v_pk_mul_f32 v[108:109], v[88:89], s[20:21] op_sel_hi:[1,0]
	v_pk_mul_f32 v[106:107], v[86:87], s[20:21] op_sel_hi:[1,0]
	v_pk_mul_f32 v[112:113], v[84:85], s[20:21] op_sel_hi:[1,0]
	v_pk_mul_f32 v[110:111], v[82:83], s[20:21] op_sel_hi:[1,0]

.LBB0_779:
	v_or_b32_e32 v82, 32, v166
	v_mad_i64_i32 v[86:87], s[38:39], v82, s77, v[160:161]
	v_cvt_pk_bf16_f32 v82, v98, v99
	v_cvt_pk_bf16_f32 v83, v100, v101
	v_cvt_pk_bf16_f32 v84, v102, v103
	v_cvt_pk_bf16_f32 v85, v104, v105
	global_store_dwordx4 v[86:87], v[82:85], off
	v_bfe_u32 v88, v113, 16, 1
	v_add3_u32 v88, v113, v88, s79
	v_cvt_pk_bf16_f32 v82, v106, v107
	v_cvt_pk_bf16_f32 v83, v108, v109
	v_cvt_pk_bf16_f32 v84, v110, v111
	v_bfe_u32 v85, v112, 16, 1
	v_add3_u32 v85, v112, v85, s79
	v_lshrrev_b32_e32 v85, 16, v85
	v_and_or_b32 v85, v88, s80, v85
	s_and_b64 vcc, exec, s[4:5]
	s_mov_b64 s[38:39], -1
	global_store_dwordx4 v[86:87], v[82:85], off offset:256
	s_cbranch_vccnz .LBB0_783
	s_nop 0
	v_mov_b64_e32 v[84:85], v[80:81]
	v_mov_b64_e32 v[96:97], v[68:69]
	v_mov_b64_e32 v[92:93], v[72:73]
	v_mov_b64_e32 v[88:89], v[76:77]
	s_and_b64 vcc, exec, s[2:3]
	v_mov_b64_e32 v[82:83], v[78:79]
	v_mov_b64_e32 v[94:95], v[66:67]
	v_mov_b64_e32 v[90:91], v[70:71]
	v_mov_b64_e32 v[86:87], v[74:75]
	s_cbranch_vccnz .LBB0_782
	v_pk_mul_f32 v[84:85], v[80:81], s[20:21] op_sel_hi:[1,0]
	v_pk_mul_f32 v[82:83], v[78:79], s[20:21] op_sel_hi:[1,0]
	v_pk_mul_f32 v[88:89], v[76:77], s[20:21] op_sel_hi:[1,0]
	v_pk_mul_f32 v[86:87], v[74:75], s[20:21] op_sel_hi:[1,0]
	v_pk_mul_f32 v[92:93], v[72:73], s[20:21] op_sel_hi:[1,0]
	v_pk_mul_f32 v[90:91], v[70:71], s[20:21] op_sel_hi:[1,0]
	v_pk_mul_f32 v[96:97], v[68:69], s[20:21] op_sel_hi:[1,0]
	v_pk_mul_f32 v[94:95], v[66:67], s[20:21] op_sel_hi:[1,0]

.LBB0_785:
	v_or_b32_e32 v66, 48, v166
	v_mad_i64_i32 v[70:71], s[38:39], v66, s77, v[160:161]
	v_cvt_pk_bf16_f32 v66, v82, v83
	v_cvt_pk_bf16_f32 v67, v84, v85
	v_cvt_pk_bf16_f32 v68, v86, v87
	v_cvt_pk_bf16_f32 v69, v88, v89
	global_store_dwordx4 v[70:71], v[66:69], off
	v_bfe_u32 v72, v97, 16, 1
	v_add3_u32 v72, v97, v72, s79
	v_cvt_pk_bf16_f32 v66, v90, v91
	v_cvt_pk_bf16_f32 v67, v92, v93
	v_cvt_pk_bf16_f32 v68, v94, v95
	v_bfe_u32 v69, v96, 16, 1
	v_add3_u32 v69, v96, v69, s79
	v_lshrrev_b32_e32 v69, 16, v69
	v_and_or_b32 v69, v72, s80, v69
	s_and_b64 vcc, exec, s[4:5]
	s_mov_b64 s[38:39], -1
	global_store_dwordx4 v[70:71], v[66:69], off offset:256
	s_cbranch_vccnz .LBB0_789
	s_nop 0
	v_mov_b64_e32 v[68:69], v[64:65]
	v_mov_b64_e32 v[80:81], v[52:53]
	v_mov_b64_e32 v[76:77], v[56:57]
	v_mov_b64_e32 v[72:73], v[60:61]
	s_and_b64 vcc, exec, s[2:3]
	v_mov_b64_e32 v[66:67], v[62:63]
	v_mov_b64_e32 v[78:79], v[50:51]
	v_mov_b64_e32 v[74:75], v[54:55]
	v_mov_b64_e32 v[70:71], v[58:59]
	s_cbranch_vccnz .LBB0_788
	v_pk_mul_f32 v[68:69], v[64:65], s[20:21] op_sel_hi:[1,0]
	v_pk_mul_f32 v[66:67], v[62:63], s[20:21] op_sel_hi:[1,0]
	v_pk_mul_f32 v[72:73], v[60:61], s[20:21] op_sel_hi:[1,0]
	v_pk_mul_f32 v[70:71], v[58:59], s[20:21] op_sel_hi:[1,0]
	v_pk_mul_f32 v[76:77], v[56:57], s[20:21] op_sel_hi:[1,0]
	v_pk_mul_f32 v[74:75], v[54:55], s[20:21] op_sel_hi:[1,0]
	v_pk_mul_f32 v[80:81], v[52:53], s[20:21] op_sel_hi:[1,0]
	v_pk_mul_f32 v[78:79], v[50:51], s[20:21] op_sel_hi:[1,0]

.LBB0_791:
	v_add_u32_e32 v50, 0x80, v166
	v_mad_i64_i32 v[54:55], s[38:39], v50, s77, v[160:161]
	v_cvt_pk_bf16_f32 v50, v66, v67
	v_cvt_pk_bf16_f32 v51, v68, v69
	v_cvt_pk_bf16_f32 v52, v70, v71
	v_cvt_pk_bf16_f32 v53, v72, v73
	global_store_dwordx4 v[54:55], v[50:53], off
	v_bfe_u32 v56, v81, 16, 1
	v_add3_u32 v56, v81, v56, s79
	v_cvt_pk_bf16_f32 v50, v74, v75
	v_cvt_pk_bf16_f32 v51, v76, v77
	v_cvt_pk_bf16_f32 v52, v78, v79
	v_bfe_u32 v53, v80, 16, 1
	v_add3_u32 v53, v80, v53, s79
	v_lshrrev_b32_e32 v53, 16, v53
	v_and_or_b32 v53, v56, s80, v53
	s_and_b64 vcc, exec, s[4:5]
	s_mov_b64 s[38:39], -1
	global_store_dwordx4 v[54:55], v[50:53], off offset:256
	s_cbranch_vccnz .LBB0_795
	s_nop 0
	v_mov_b64_e32 v[52:53], v[48:49]
	v_mov_b64_e32 v[64:65], v[36:37]
	v_mov_b64_e32 v[60:61], v[40:41]
	v_mov_b64_e32 v[56:57], v[44:45]
	s_and_b64 vcc, exec, s[2:3]
	v_mov_b64_e32 v[50:51], v[46:47]
	v_mov_b64_e32 v[62:63], v[34:35]
	v_mov_b64_e32 v[58:59], v[38:39]
	v_mov_b64_e32 v[54:55], v[42:43]
	s_cbranch_vccnz .LBB0_794
	v_pk_mul_f32 v[52:53], v[48:49], s[20:21] op_sel_hi:[1,0]
	v_pk_mul_f32 v[50:51], v[46:47], s[20:21] op_sel_hi:[1,0]
	v_pk_mul_f32 v[56:57], v[44:45], s[20:21] op_sel_hi:[1,0]
	v_pk_mul_f32 v[54:55], v[42:43], s[20:21] op_sel_hi:[1,0]
	v_pk_mul_f32 v[60:61], v[40:41], s[20:21] op_sel_hi:[1,0]
	v_pk_mul_f32 v[58:59], v[38:39], s[20:21] op_sel_hi:[1,0]
	v_pk_mul_f32 v[64:65], v[36:37], s[20:21] op_sel_hi:[1,0]
	v_pk_mul_f32 v[62:63], v[34:35], s[20:21] op_sel_hi:[1,0]

.LBB0_797:
	v_add_u32_e32 v34, 0x90, v166
	v_mad_i64_i32 v[38:39], s[38:39], v34, s77, v[160:161]
	v_cvt_pk_bf16_f32 v34, v50, v51
	v_cvt_pk_bf16_f32 v35, v52, v53
	v_cvt_pk_bf16_f32 v36, v54, v55
	v_cvt_pk_bf16_f32 v37, v56, v57
	global_store_dwordx4 v[38:39], v[34:37], off
	v_bfe_u32 v40, v65, 16, 1
	v_add3_u32 v40, v65, v40, s79
	v_cvt_pk_bf16_f32 v34, v58, v59
	v_cvt_pk_bf16_f32 v35, v60, v61
	v_cvt_pk_bf16_f32 v36, v62, v63
	v_bfe_u32 v37, v64, 16, 1
	v_add3_u32 v37, v64, v37, s79
	v_lshrrev_b32_e32 v37, 16, v37
	v_and_or_b32 v37, v40, s80, v37
	s_and_b64 vcc, exec, s[4:5]
	s_mov_b64 s[38:39], -1
	global_store_dwordx4 v[38:39], v[34:37], off offset:256
	s_cbranch_vccnz .LBB0_801
	s_nop 0
	v_mov_b64_e32 v[36:37], v[32:33]
	v_mov_b64_e32 v[48:49], v[20:21]
	v_mov_b64_e32 v[44:45], v[24:25]
	v_mov_b64_e32 v[40:41], v[28:29]
	s_and_b64 vcc, exec, s[2:3]
	v_mov_b64_e32 v[34:35], v[30:31]
	v_mov_b64_e32 v[46:47], v[18:19]
	v_mov_b64_e32 v[42:43], v[22:23]
	v_mov_b64_e32 v[38:39], v[26:27]
	s_cbranch_vccnz .LBB0_800
	v_pk_mul_f32 v[36:37], v[32:33], s[20:21] op_sel_hi:[1,0]
	v_pk_mul_f32 v[34:35], v[30:31], s[20:21] op_sel_hi:[1,0]
	v_pk_mul_f32 v[40:41], v[28:29], s[20:21] op_sel_hi:[1,0]
	v_pk_mul_f32 v[38:39], v[26:27], s[20:21] op_sel_hi:[1,0]
	v_pk_mul_f32 v[44:45], v[24:25], s[20:21] op_sel_hi:[1,0]
	v_pk_mul_f32 v[42:43], v[22:23], s[20:21] op_sel_hi:[1,0]
	v_pk_mul_f32 v[48:49], v[20:21], s[20:21] op_sel_hi:[1,0]
	v_pk_mul_f32 v[46:47], v[18:19], s[20:21] op_sel_hi:[1,0]

.LBB0_803:
	v_add_u32_e32 v18, 0xa0, v166
	v_mad_i64_i32 v[22:23], s[38:39], v18, s77, v[160:161]
	v_cvt_pk_bf16_f32 v18, v34, v35
	v_cvt_pk_bf16_f32 v19, v36, v37
	v_cvt_pk_bf16_f32 v20, v38, v39
	v_cvt_pk_bf16_f32 v21, v40, v41
	global_store_dwordx4 v[22:23], v[18:21], off
	v_bfe_u32 v24, v49, 16, 1
	v_add3_u32 v24, v49, v24, s79
	v_cvt_pk_bf16_f32 v18, v42, v43
	v_cvt_pk_bf16_f32 v19, v44, v45
	v_cvt_pk_bf16_f32 v20, v46, v47
	v_bfe_u32 v21, v48, 16, 1
	v_add3_u32 v21, v48, v21, s79
	v_lshrrev_b32_e32 v21, 16, v21
	v_and_or_b32 v21, v24, s80, v21
	s_and_b64 vcc, exec, s[4:5]
	s_mov_b64 s[4:5], -1
	global_store_dwordx4 v[22:23], v[18:21], off offset:256
	s_cbranch_vccnz .LBB0_807
	s_nop 0
	v_mov_b64_e32 v[20:21], v[16:17]
	v_mov_b64_e32 v[32:33], v[4:5]
	v_mov_b64_e32 v[28:29], v[8:9]
	v_mov_b64_e32 v[24:25], v[12:13]
	s_and_b64 vcc, exec, s[2:3]
	v_mov_b64_e32 v[18:19], v[14:15]
	v_mov_b64_e32 v[30:31], v[2:3]
	v_mov_b64_e32 v[26:27], v[6:7]
	v_mov_b64_e32 v[22:23], v[10:11]
	s_cbranch_vccnz .LBB0_806
	v_pk_mul_f32 v[20:21], v[16:17], s[20:21] op_sel_hi:[1,0]
	v_pk_mul_f32 v[18:19], v[14:15], s[20:21] op_sel_hi:[1,0]
	v_pk_mul_f32 v[24:25], v[12:13], s[20:21] op_sel_hi:[1,0]
	v_pk_mul_f32 v[22:23], v[10:11], s[20:21] op_sel_hi:[1,0]
	v_pk_mul_f32 v[28:29], v[8:9], s[20:21] op_sel_hi:[1,0]
	v_pk_mul_f32 v[26:27], v[6:7], s[20:21] op_sel_hi:[1,0]
	v_pk_mul_f32 v[32:33], v[4:5], s[20:21] op_sel_hi:[1,0]
	v_pk_mul_f32 v[30:31], v[2:3], s[20:21] op_sel_hi:[1,0]

.LBB0_809:
	v_add_u32_e32 v2, 0xb0, v166
	v_mad_i64_i32 v[6:7], s[2:3], v2, s77, v[160:161]
	v_cvt_pk_bf16_f32 v2, v18, v19
	v_cvt_pk_bf16_f32 v3, v20, v21
	v_cvt_pk_bf16_f32 v4, v22, v23
	v_cvt_pk_bf16_f32 v5, v24, v25
	global_store_dwordx4 v[6:7], v[2:5], off
	v_bfe_u32 v8, v33, 16, 1
	v_add3_u32 v8, v33, v8, s79
	v_cvt_pk_bf16_f32 v2, v26, v27
	v_cvt_pk_bf16_f32 v3, v28, v29
	v_cvt_pk_bf16_f32 v4, v30, v31
	v_bfe_u32 v5, v32, 16, 1
	v_add3_u32 v5, v32, v5, s79
	v_lshrrev_b32_e32 v5, 16, v5
	v_and_or_b32 v5, v8, s80, v5
	s_mov_b64 s[2:3], -1
	s_and_b64 vcc, exec, s[44:45]
	global_store_dwordx4 v[6:7], v[2:5], off offset:256
	s_cbranch_vccz .LBB0_754
	s_and_b64 vcc, exec, s[6:7]
	s_cbranch_vccz .LBB0_753
	s_barrier
	s_branch .LBB0_753

.LBB0_955:
	s_cmp_lg_u32 0, -1
	s_cselect_b32 s0, 0, 0
	s_addk_i32 s0, 0x6000
	v_add3_u32 v8, v237, s0, v233
	s_add_i32 s0, s43, 0x4000
	v_add_f32_e32 v2, v243, v2
	s_and_b32 s0, s0, 0xffff
	v_add3_u32 v16, v8, v236, s0
	ds_read_b64_tr_b16 v[8:9],v16 offset:0
	ds_read_b64_tr_b16 v[10:11],v16 offset:512
	ds_read_b64_tr_b16 v[12:13],v16 offset:1024
	ds_read_b64_tr_b16 v[14:15],v16 offset:1536
	ds_read_b64_tr_b16 v[82:83],v16 offset:2048
	ds_read_b64_tr_b16 v[84:85],v16 offset:2560
	ds_read_b64_tr_b16 v[86:87],v16 offset:3072
	ds_read_b64_tr_b16 v[88:89],v16 offset:3584
	s_waitcnt lgkmcnt(0)
	s_nop 0
	v_mfma_f32_32x32x16_bf16 v[66:81], v[138:141], v[8:11], v[66:81]
	ds_read_b64_tr_b16 v[8:9],v16 offset:4096
	ds_read_b64_tr_b16 v[10:11],v16 offset:4608
	v_mfma_f32_32x32x16_bf16 v[66:81], v[134:137], v[12:15], v[66:81]
	ds_read_b64_tr_b16 v[12:13],v16 offset:5120
	ds_read_b64_tr_b16 v[14:15],v16 offset:5632
	v_mfma_f32_32x32x16_bf16 v[66:81], v[130:133], v[82:85], v[66:81]
	ds_read_b64_tr_b16 v[82:83],v16 offset:6144
	ds_read_b64_tr_b16 v[84:85],v16 offset:6656
	ds_read_b64_tr_b16 v[90:91],v16 offset:7168
	ds_read_b64_tr_b16 v[92:93],v16 offset:7680
	s_waitcnt lgkmcnt(0)
	v_mfma_f32_32x32x16_bf16 v[66:81], v[4:7], v[86:89], v[66:81]
	v_mfma_f32_32x32x16_bf16 v[50:65], v[138:141], v[8:11], v[50:65]
	v_add_u32_e32 v16, 0x2000, v16
	ds_read_b64_tr_b16 v[8:9],v16 offset:0
	ds_read_b64_tr_b16 v[10:11],v16 offset:512
	v_mfma_f32_32x32x16_bf16 v[50:65], v[134:137], v[12:15], v[50:65]
	ds_read_b64_tr_b16 v[12:13],v16 offset:1024
	ds_read_b64_tr_b16 v[14:15],v16 offset:1536
	v_mfma_f32_32x32x16_bf16 v[50:65], v[130:133], v[82:85], v[50:65]
	ds_read_b64_tr_b16 v[82:83],v16 offset:2048
	ds_read_b64_tr_b16 v[84:85],v16 offset:2560
	ds_read_b64_tr_b16 v[86:87],v16 offset:3072
	ds_read_b64_tr_b16 v[88:89],v16 offset:3584
	s_waitcnt lgkmcnt(0)
	v_mfma_f32_32x32x16_bf16 v[50:65], v[4:7], v[90:93], v[50:65]
	v_mfma_f32_32x32x16_bf16 v[34:49], v[138:141], v[8:11], v[34:49]
	ds_read_b64_tr_b16 v[8:9],v16 offset:4096
	ds_read_b64_tr_b16 v[10:11],v16 offset:4608
	v_mfma_f32_32x32x16_bf16 v[34:49], v[134:137], v[12:15], v[34:49]
	ds_read_b64_tr_b16 v[12:13],v16 offset:5120
	ds_read_b64_tr_b16 v[14:15],v16 offset:5632
	v_mfma_f32_32x32x16_bf16 v[34:49], v[130:133], v[82:85], v[34:49]
	ds_read_b64_tr_b16 v[82:83],v16 offset:6144
	ds_read_b64_tr_b16 v[84:85],v16 offset:6656
	ds_read_b64_tr_b16 v[90:91],v16 offset:7168
	ds_read_b64_tr_b16 v[92:93],v16 offset:7680
	s_waitcnt lgkmcnt(0)
	v_mfma_f32_32x32x16_bf16 v[34:49], v[4:7], v[86:89], v[34:49]
	v_mfma_f32_32x32x16_bf16 v[18:33], v[138:141], v[8:11], v[18:33]
	v_mov_b32_e32 v8, v2
	s_nop 1
	v_permlane32_swap_b32_e32 v2, v8
	v_cmp_gt_u32_e32 vcc, 32, v230
	v_mfma_f32_32x32x16_bf16 v[18:33], v[134:137], v[12:15], v[18:33]
	v_mfma_f32_32x32x16_bf16 v[18:33], v[130:133], v[82:85], v[18:33]
	v_mfma_f32_32x32x16_bf16 v[18:33], v[4:7], v[90:93], v[18:33]
	s_and_saveexec_b64 s[0:1], vcc
	v_add_f32_e32 v2, v2, v8
	ds_write_b32 v235, v2 offset:128
	s_or_b64 exec, exec, s[0:1]
	s_waitcnt lgkmcnt(0)
	ds_read_b128 v[4:7], v234 offset:128
	ds_read_b128 v[8:11], v234 offset:160
	s_lshl_b32 s0, s42, 8
	s_add_u32 s2, s6, s0
	s_addc_u32 s3, s7, 0
	s_waitcnt lgkmcnt(1)
	v_rcp_f32_e32 v14, v4
	v_rcp_f32_e32 v15, v5
	v_rcp_f32_e32 v16, v6
	v_rcp_f32_e32 v17, v7
	ds_read_b128 v[4:7], v234 offset:192
	s_lshl_b64 s[0:1], s[26:27], 11
	s_add_u32 s0, s2, s0
	s_addc_u32 s1, s3, s1
	s_lshl_b32 s2, s33, 12
	s_add_i32 s2, s2, 0
	v_lshlrev_b32_e32 v2, 1, v232
	s_add_i32 s2, s2, 0x16800
	v_and_b32_e32 v2, 0x70, v2
	s_waitcnt lgkmcnt(1)
	v_rcp_f32_e32 v82, v8
	v_rcp_f32_e32 v83, v9
	v_rcp_f32_e32 v84, v10
	v_rcp_f32_e32 v85, v11
	ds_read_b128 v[8:11], v234 offset:224
	s_waitcnt lgkmcnt(1)
	v_rcp_f32_e32 v86, v4
	v_lshlrev_b32_e32 v4, 1, v231
	v_add_u32_e32 v95, s2, v2
	v_lshl_add_u64 v[12:13], s[0:1], 0, v[2:3]
	v_lshlrev_b32_e32 v2, 9, v229
	v_add3_u32 v97, s2, v4, v2
	v_mul_f32_e32 v2, v66, v14
	v_cvt_pk_bf16_f32 v2, v2, s0
	ds_write_b16 v97, v2
	v_mul_f32_e32 v2, v50, v14
	v_cvt_pk_bf16_f32 v2, v2, s0
	ds_write_b16 v97, v2 offset:64
	v_mul_f32_e32 v2, v67, v15
	v_cvt_pk_bf16_f32 v2, v2, s0
	ds_write_b16 v97, v2 offset:128
	v_mul_f32_e32 v2, v51, v15
	v_cvt_pk_bf16_f32 v2, v2, s0
	ds_write_b16 v97, v2 offset:192
	v_mul_f32_e32 v2, v68, v16
	v_cvt_pk_bf16_f32 v2, v2, s0
	ds_write_b16 v97, v2 offset:256
	v_mul_f32_e32 v2, v52, v16
	v_cvt_pk_bf16_f32 v2, v2, s0
	ds_write_b16 v97, v2 offset:320
	v_mul_f32_e32 v2, v69, v17
	v_cvt_pk_bf16_f32 v2, v2, s0
	ds_write_b16 v97, v2 offset:384
	v_mul_f32_e32 v2, v53, v17
	v_cvt_pk_bf16_f32 v2, v2, s0
	ds_write_b16 v97, v2 offset:448
	v_mul_f32_e32 v2, v70, v82
	v_cvt_pk_bf16_f32 v2, v2, s0
	ds_write_b16 v97, v2 offset:1024
	v_mul_f32_e32 v2, v54, v82
	v_cvt_pk_bf16_f32 v2, v2, s0
	ds_write_b16 v97, v2 offset:1088
	v_mul_f32_e32 v2, v71, v83
	v_cvt_pk_bf16_f32 v2, v2, s0
	ds_write_b16 v97, v2 offset:1152
	v_mul_f32_e32 v2, v55, v83
	v_cvt_pk_bf16_f32 v2, v2, s0
	ds_write_b16 v97, v2 offset:1216
	v_mul_f32_e32 v2, v72, v84
	v_cvt_pk_bf16_f32 v2, v2, s0
	ds_write_b16 v97, v2 offset:1280
	v_mul_f32_e32 v2, v56, v84
	v_cvt_pk_bf16_f32 v2, v2, s0
	ds_write_b16 v97, v2 offset:1344
	v_mul_f32_e32 v2, v73, v85
	v_cvt_pk_bf16_f32 v2, v2, s0
	ds_write_b16 v97, v2 offset:1408
	v_mul_f32_e32 v2, v57, v85
	v_cvt_pk_bf16_f32 v2, v2, s0
	v_rcp_f32_e32 v87, v5
	ds_write_b16 v97, v2 offset:1472
	v_mul_f32_e32 v2, v74, v86
	v_cvt_pk_bf16_f32 v2, v2, s0
	ds_write_b16 v97, v2 offset:2048
	v_mul_f32_e32 v2, v58, v86
	v_cvt_pk_bf16_f32 v2, v2, s0
	v_rcp_f32_e32 v88, v6
	ds_write_b16 v97, v2 offset:2112
	v_mul_f32_e32 v2, v75, v87
	v_cvt_pk_bf16_f32 v2, v2, s0
	ds_write_b16 v97, v2 offset:2176
	v_mul_f32_e32 v2, v59, v87
	v_cvt_pk_bf16_f32 v2, v2, s0
	v_rcp_f32_e32 v89, v7
	ds_write_b16 v97, v2 offset:2240
	v_mul_f32_e32 v2, v76, v88
	v_cvt_pk_bf16_f32 v2, v2, s0
	ds_write_b16 v97, v2 offset:2304
	v_mul_f32_e32 v2, v60, v88
	v_cvt_pk_bf16_f32 v2, v2, s0
	s_waitcnt lgkmcnt(14)
	v_rcp_f32_e32 v90, v8
	ds_write_b16 v97, v2 offset:2368
	v_mul_f32_e32 v2, v77, v89
	v_cvt_pk_bf16_f32 v2, v2, s0
	ds_write_b16 v97, v2 offset:2432
	v_mul_f32_e32 v2, v61, v89
	v_cvt_pk_bf16_f32 v2, v2, s0
	v_rcp_f32_e32 v91, v9
	ds_write_b16 v97, v2 offset:2496
	v_mul_f32_e32 v2, v78, v90
	v_cvt_pk_bf16_f32 v2, v2, s0
	ds_write_b16 v97, v2 offset:3072
	v_mul_f32_e32 v2, v62, v90
	v_cvt_pk_bf16_f32 v2, v2, s0
	v_rcp_f32_e32 v92, v10
	ds_write_b16 v97, v2 offset:3136
	v_mul_f32_e32 v2, v79, v91
	v_cvt_pk_bf16_f32 v2, v2, s0
	ds_write_b16 v97, v2 offset:3200
	v_mul_f32_e32 v2, v63, v91
	v_cvt_pk_bf16_f32 v2, v2, s0
	v_rcp_f32_e32 v93, v11
	ds_write_b16 v97, v2 offset:3264
	v_mul_f32_e32 v2, v80, v92
	v_cvt_pk_bf16_f32 v2, v2, s0
	ds_write_b16 v97, v2 offset:3328
	v_mul_f32_e32 v2, v64, v92
	v_cvt_pk_bf16_f32 v2, v2, s0
	ds_write_b16 v97, v2 offset:3392
	v_mul_f32_e32 v2, v81, v93
	v_cvt_pk_bf16_f32 v2, v2, s0
	ds_write_b16 v97, v2 offset:3456
	v_mul_f32_e32 v2, v65, v93
	v_lshrrev_b32_e32 v94, 3, v230
	v_cvt_pk_bf16_f32 v2, v2, s0
	ds_write_b16 v97, v2 offset:3520
	v_or_b32_e32 v52, 8, v94
	v_lshl_add_u32 v96, v94, 7, v95
	s_waitcnt lgkmcnt(0)
	v_lshl_add_u32 v58, v52, 7, v95
	ds_read_b128 v[4:7], v96
	ds_read_b128 v[8:11], v58
	v_lshlrev_b32_e32 v2, 11, v94
	v_lshl_add_u64 v[50:51], v[12:13], 0, v[2:3]
	v_lshlrev_b32_e32 v2, 11, v52
	v_lshl_add_u64 v[52:53], v[12:13], 0, v[2:3]
	v_or_b32_e32 v2, 16, v94
	v_or_b32_e32 v56, 24, v94
	v_lshl_add_u32 v59, v2, 7, v95
	v_lshl_add_u32 v60, v56, 7, v95
	s_waitcnt lgkmcnt(1)
	global_store_dwordx4 v[50:51], v[4:7], off
	ds_read_b128 v[4:7], v59
	s_waitcnt lgkmcnt(1)
	global_store_dwordx4 v[52:53], v[8:11], off
	ds_read_b128 v[8:11], v60
	v_lshlrev_b32_e32 v2, 11, v2
	v_lshl_add_u64 v[54:55], v[12:13], 0, v[2:3]
	v_lshlrev_b32_e32 v2, 11, v56
	v_lshl_add_u64 v[56:57], v[12:13], 0, v[2:3]
	v_mul_f32_e32 v2, v34, v14
	s_waitcnt lgkmcnt(1)
	global_store_dwordx4 v[54:55], v[4:7], off
	s_waitcnt lgkmcnt(0)
	global_store_dwordx4 v[56:57], v[8:11], off
	v_cvt_pk_bf16_f32 v2, v2, s0
	s_waitcnt lgkmcnt(0)
	ds_write_b16 v97, v2
	v_mul_f32_e32 v2, v18, v14
	v_cvt_pk_bf16_f32 v2, v2, s0
	ds_write_b16 v97, v2 offset:64
	v_mul_f32_e32 v2, v35, v15
	v_cvt_pk_bf16_f32 v2, v2, s0
	ds_write_b16 v97, v2 offset:128
	v_mul_f32_e32 v2, v19, v15
	v_cvt_pk_bf16_f32 v2, v2, s0
	ds_write_b16 v97, v2 offset:192
	v_mul_f32_e32 v2, v36, v16
	v_cvt_pk_bf16_f32 v2, v2, s0
	ds_write_b16 v97, v2 offset:256
	v_mul_f32_e32 v2, v20, v16
	v_cvt_pk_bf16_f32 v2, v2, s0
	ds_write_b16 v97, v2 offset:320
	v_mul_f32_e32 v2, v37, v17
	v_cvt_pk_bf16_f32 v2, v2, s0
	ds_write_b16 v97, v2 offset:384
	v_mul_f32_e32 v2, v21, v17
	v_cvt_pk_bf16_f32 v2, v2, s0
	ds_write_b16 v97, v2 offset:448
	v_mul_f32_e32 v2, v38, v82
	v_cvt_pk_bf16_f32 v2, v2, s0
	ds_write_b16 v97, v2 offset:1024
	v_mul_f32_e32 v2, v22, v82
	v_cvt_pk_bf16_f32 v2, v2, s0
	ds_write_b16 v97, v2 offset:1088
	v_mul_f32_e32 v2, v39, v83
	v_cvt_pk_bf16_f32 v2, v2, s0
	ds_write_b16 v97, v2 offset:1152
	v_mul_f32_e32 v2, v23, v83
	v_cvt_pk_bf16_f32 v2, v2, s0
	ds_write_b16 v97, v2 offset:1216
	v_mul_f32_e32 v2, v40, v84
	v_cvt_pk_bf16_f32 v2, v2, s0
	ds_write_b16 v97, v2 offset:1280
	v_mul_f32_e32 v2, v24, v84
	v_cvt_pk_bf16_f32 v2, v2, s0
	ds_write_b16 v97, v2 offset:1344
	v_mul_f32_e32 v2, v41, v85
	v_cvt_pk_bf16_f32 v2, v2, s0
	ds_write_b16 v97, v2 offset:1408
	v_mul_f32_e32 v2, v25, v85
	v_cvt_pk_bf16_f32 v2, v2, s0
	ds_write_b16 v97, v2 offset:1472
	v_mul_f32_e32 v2, v42, v86
	v_cvt_pk_bf16_f32 v2, v2, s0
	ds_write_b16 v97, v2 offset:2048
	v_mul_f32_e32 v2, v26, v86
	v_cvt_pk_bf16_f32 v2, v2, s0
	ds_write_b16 v97, v2 offset:2112
	v_mul_f32_e32 v2, v43, v87
	v_cvt_pk_bf16_f32 v2, v2, s0
	ds_write_b16 v97, v2 offset:2176
	v_mul_f32_e32 v2, v27, v87
	v_cvt_pk_bf16_f32 v2, v2, s0
	ds_write_b16 v97, v2 offset:2240
	v_mul_f32_e32 v2, v44, v88
	v_cvt_pk_bf16_f32 v2, v2, s0
	ds_write_b16 v97, v2 offset:2304
	v_mul_f32_e32 v2, v28, v88
	v_cvt_pk_bf16_f32 v2, v2, s0
	ds_write_b16 v97, v2 offset:2368
	v_mul_f32_e32 v2, v45, v89
	v_cvt_pk_bf16_f32 v2, v2, s0
	ds_write_b16 v97, v2 offset:2432
	v_mul_f32_e32 v2, v29, v89
	v_cvt_pk_bf16_f32 v2, v2, s0
	ds_write_b16 v97, v2 offset:2496
	v_mul_f32_e32 v2, v46, v90
	v_cvt_pk_bf16_f32 v2, v2, s0
	ds_write_b16 v97, v2 offset:3072
	v_mul_f32_e32 v2, v30, v90
	v_cvt_pk_bf16_f32 v2, v2, s0
	ds_write_b16 v97, v2 offset:3136
	v_mul_f32_e32 v2, v47, v91
	v_cvt_pk_bf16_f32 v2, v2, s0
	ds_write_b16 v97, v2 offset:3200
	v_mul_f32_e32 v2, v31, v91
	v_cvt_pk_bf16_f32 v2, v2, s0
	ds_write_b16 v97, v2 offset:3264
	v_mul_f32_e32 v2, v48, v92
	v_cvt_pk_bf16_f32 v2, v2, s0
	ds_write_b16 v97, v2 offset:3328
	v_mul_f32_e32 v2, v32, v92
	v_cvt_pk_bf16_f32 v2, v2, s0
	ds_write_b16 v97, v2 offset:3392
	v_mul_f32_e32 v2, v49, v93
	v_cvt_pk_bf16_f32 v2, v2, s0
	ds_write_b16 v97, v2 offset:3456
	v_mul_f32_e32 v2, v33, v93
	v_cvt_pk_bf16_f32 v2, v2, s0
	ds_write_b16 v97, v2 offset:3520
	s_waitcnt lgkmcnt(0)
	ds_read_b128 v[4:7], v96
	ds_read_b128 v[8:11], v58
	ds_read_b128 v[12:15], v59
	ds_read_b128 v[16:19], v60
	s_waitcnt lgkmcnt(3)
	global_store_dwordx4 v[50:51], v[4:7], off offset:128
	s_waitcnt lgkmcnt(2)
	global_store_dwordx4 v[52:53], v[8:11], off offset:128
	s_waitcnt lgkmcnt(1)
	global_store_dwordx4 v[54:55], v[12:15], off offset:128
	s_waitcnt lgkmcnt(0)
	global_store_dwordx4 v[56:57], v[16:19], off offset:128
	s_waitcnt lgkmcnt(0)
	s_waitcnt lgkmcnt(0)
	s_barrier
	s_cmp_lt_u32 s21, 2
	s_cbranch_scc1 .LBB0_872
	v_mov_b32_e32 v6, v0
	s_lshl_b32 s0, s63, 8
	v_ashrrev_i32_e32 v4, 1, v6
	s_or_b32 s0, s8, s0
	s_mov_b32 s1, s9
	v_ashrrev_i32_e32 v5, 31, v4
	v_lshl_add_u64 v[12:13], s[0:1], 0, v[4:5]
	v_lshlrev_b32_e32 v2, 6, v6
	v_lshlrev_b64 v[4:5], 11, v[12:13]
	v_and_b32_e32 v7, 64, v2
	v_lshl_add_u64 v[4:5], s[6:7], 0, v[4:5]
	v_lshlrev_b32_e32 v2, 1, v7
	v_lshl_add_u64 v[4:5], v[4:5], 0, v[2:3]
	s_waitcnt vmcnt(0)
	s_barrier
	global_load_dwordx2 v[16:17], v[4:5], off sc1
	global_load_dwordx2 v[18:19], v[4:5], off offset:256 sc1
	global_load_dwordx2 v[24:25], v[4:5], off offset:8 sc1
	global_load_dwordx2 v[26:27], v[4:5], off offset:264 sc1
	global_load_dwordx2 v[30:31], v[4:5], off offset:16 sc1
	global_load_dwordx2 v[34:35], v[4:5], off offset:272 sc1
	global_load_dwordx2 v[42:43], v[4:5], off offset:24 sc1
	global_load_dwordx2 v[50:51], v[4:5], off offset:280 sc1
	v_lshlrev_b32_e32 v6, 2, v6
	v_bitop3_b32 v83, v6, 4, v228 bitop3:0x6c
	v_lshlrev_b32_e32 v82, 2, v7
	global_load_dwordx2 v[54:55], v[4:5], off offset:32 sc1
	global_load_dwordx2 v[60:61], v[4:5], off offset:288 sc1
	global_load_dwordx2 v[74:75], v[4:5], off offset:40 sc1
	global_load_dwordx2 v[84:85], v[4:5], off offset:296 sc1
	global_load_dwordx2 v[86:87], v[4:5], off offset:48 sc1
	global_load_dwordx2 v[88:89], v[4:5], off offset:304 sc1
	global_load_dwordx2 v[90:91], v[4:5], off offset:56 sc1
	global_load_dwordx2 v[28:29], v[4:5], off offset:312 sc1
	global_load_dwordx2 v[58:59], v[4:5], off offset:64 sc1
	global_load_dwordx2 v[36:37], v[4:5], off offset:320 sc1
	global_load_dwordx2 v[66:67], v[4:5], off offset:72 sc1
	global_load_dwordx2 v[44:45], v[4:5], off offset:328 sc1
	global_load_dwordx2 v[62:63], v[4:5], off offset:80 sc1
	global_load_dwordx2 v[52:53], v[4:5], off offset:336 sc1
	global_load_dwordx2 v[76:77], v[4:5], off offset:88 sc1
	global_load_dwordx2 v[32:33], v[4:5], off offset:344 sc1
	global_load_dwordx2 v[68:69], v[4:5], off offset:96 sc1
	global_load_dwordx2 v[38:39], v[4:5], off offset:352 sc1
	global_load_dwordx2 v[80:81], v[4:5], off offset:104 sc1
	global_load_dwordx2 v[20:21], v[4:5], off offset:360 sc1
	global_load_dwordx2 v[46:47], v[4:5], off offset:112 sc1
	global_load_dwordx2 v[22:23], v[4:5], off offset:368 sc1
	global_load_dwordx2 v[56:57], v[4:5], off offset:120 sc1
	global_load_dwordx2 v[48:49], v[4:5], off offset:376 sc1
	s_nop 0
	global_load_dwordx4 v[4:7], v82, s[58:59] offset:528
	global_load_dwordx4 v[8:11], v82, s[58:59] offset:512
	v_mov_b64_e32 v[14:15], s[16:17]
	v_mad_u64_u32 v[14:15], s[0:1], v12, s5, v[14:15]
	v_mad_i32_i24 v15, v13, s5, v15
	v_lshl_add_u64 v[12:13], v[14:15], 0, v[2:3]
	s_mov_b32 s0, 0xf800000
	s_waitcnt vmcnt(33)
	v_lshlrev_b32_e32 v41, 16, v17
	v_lshlrev_b32_e32 v40, 16, v16
	s_waitcnt vmcnt(32)
	v_lshlrev_b32_e32 v65, 16, v19
	v_lshlrev_b32_e32 v64, 16, v18
	v_and_b32_e32 v17, 0xffff0000, v17
	v_and_b32_e32 v16, 0xffff0000, v16
	v_and_b32_e32 v19, 0xffff0000, v19
	v_and_b32_e32 v18, 0xffff0000, v18
	s_waitcnt vmcnt(29)
	v_lshlrev_b32_e32 v95, 16, v31
	v_lshlrev_b32_e32 v94, 16, v30
	s_waitcnt vmcnt(28)
	v_lshlrev_b32_e32 v97, 16, v35
	v_lshlrev_b32_e32 v96, 16, v34
	v_and_b32_e32 v31, 0xffff0000, v31
	v_and_b32_e32 v30, 0xffff0000, v30
	v_and_b32_e32 v35, 0xffff0000, v35
	v_and_b32_e32 v34, 0xffff0000, v34
	v_pk_fma_f32 v[72:73], v[214:215], v[18:19], v[16:17] neg_lo:[1,0,0] neg_hi:[1,0,0]
	v_pk_fma_f32 v[18:19], v[214:215], v[96:97], v[94:95] neg_lo:[1,0,0] neg_hi:[1,0,0]
	v_pk_fma_f32 v[16:17], v[214:215], v[34:35], v[30:31] neg_lo:[1,0,0] neg_hi:[1,0,0]
	v_lshlrev_b32_e32 v71, 16, v25
	v_lshlrev_b32_e32 v70, 16, v24
	v_lshlrev_b32_e32 v93, 16, v27
	v_lshlrev_b32_e32 v92, 16, v26
	v_and_b32_e32 v25, 0xffff0000, v25
	v_and_b32_e32 v24, 0xffff0000, v24
	v_and_b32_e32 v27, 0xffff0000, v27
	v_and_b32_e32 v26, 0xffff0000, v26
	v_mov_b32_e32 v30, v18
	v_mov_b32_e32 v31, v16
	v_mul_f32_e32 v34, v16, v16
	v_pk_fma_f32 v[78:79], v[214:215], v[64:65], v[40:41] neg_lo:[1,0,0] neg_hi:[1,0,0]
	v_pk_fma_f32 v[64:65], v[214:215], v[26:27], v[24:25] neg_lo:[1,0,0] neg_hi:[1,0,0]
	v_pk_fma_f32 v[30:31], v[30:31], v[30:31], v[34:35] op_sel_hi:[1,1,0]
	v_mov_b32_e32 v34, v19
	v_mov_b32_e32 v35, v17
	v_mul_f32_e32 v40, v17, v17
	v_pk_fma_f32 v[70:71], v[214:215], v[92:93], v[70:71] neg_lo:[1,0,0] neg_hi:[1,0,0]
	v_pk_mul_f32 v[24:25], v[72:73], v[72:73]
	v_pk_mul_f32 v[26:27], v[64:65], v[64:65]
	v_pk_fma_f32 v[34:35], v[34:35], v[34:35], v[40:41] op_sel_hi:[1,1,0]
	s_waitcnt vmcnt(27)
	v_lshlrev_b32_e32 v41, 16, v43
	v_lshlrev_b32_e32 v40, 16, v42
	s_waitcnt vmcnt(26)
	v_lshlrev_b32_e32 v93, 16, v51
	v_lshlrev_b32_e32 v92, 16, v50
	v_and_b32_e32 v43, 0xffff0000, v43
	v_and_b32_e32 v42, 0xffff0000, v42
	v_and_b32_e32 v51, 0xffff0000, v51
	v_and_b32_e32 v50, 0xffff0000, v50
	v_pk_fma_f32 v[24:25], v[78:79], v[78:79], v[24:25]
	v_pk_fma_f32 v[26:27], v[70:71], v[70:71], v[26:27]
	v_pk_fma_f32 v[40:41], v[214:215], v[92:93], v[40:41] neg_lo:[1,0,0] neg_hi:[1,0,0]
	v_pk_fma_f32 v[50:51], v[214:215], v[50:51], v[42:43] neg_lo:[1,0,0] neg_hi:[1,0,0]
	v_pk_add_f32 v[24:25], v[24:25], v[24:25] op_sel:[0,1] op_sel_hi:[1,0]
	v_pk_add_f32 v[26:27], v[26:27], v[26:27] op_sel:[0,1] op_sel_hi:[1,0]
	v_pk_mul_f32 v[42:43], v[40:41], v[40:41]
	v_pk_mul_f32 v[92:93], v[50:51], v[50:51]
	v_mov_b32_e32 v25, v42
	v_mov_b32_e32 v27, v92
	v_mov_b32_e32 v31, v43
	v_mov_b32_e32 v35, v93
	v_pk_add_f32 v[24:25], v[24:25], v[26:27]
	v_pk_add_f32 v[26:27], v[30:31], v[34:35]
	s_waitcnt vmcnt(24)
	v_and_b32_e32 v31, 0xffff0000, v61
	v_pk_add_f32 v[24:25], v[24:25], v[26:27]
	v_lshlrev_b32_e32 v27, 16, v61
	v_pk_add_f32 v[92:93], v[24:25], v[24:25] op_sel:[0,1] op_sel_hi:[1,0]
	v_lshlrev_b32_e32 v25, 16, v55
	v_lshlrev_b32_e32 v24, 16, v54
	v_lshlrev_b32_e32 v26, 16, v60
	v_pk_fma_f32 v[26:27], v[214:215], v[26:27], v[24:25] neg_lo:[1,0,0] neg_hi:[1,0,0]
	v_and_b32_e32 v25, 0xffff0000, v55
	v_and_b32_e32 v24, 0xffff0000, v54
	v_and_b32_e32 v30, 0xffff0000, v60
	v_pk_fma_f32 v[34:35], v[214:215], v[30:31], v[24:25] neg_lo:[1,0,0] neg_hi:[1,0,0]
	s_waitcnt vmcnt(22)
	v_lshlrev_b32_e32 v31, 16, v85
	v_pk_mul_f32 v[24:25], v[34:35], v[34:35]
	v_lshlrev_b32_e32 v30, 16, v84
	v_pk_fma_f32 v[24:25], v[26:27], v[26:27], v[24:25]
	s_waitcnt vmcnt(0)
	v_mov_b32_e32 v15, v10
	v_pk_add_f32 v[60:61], v[24:25], v[24:25] op_sel:[0,1] op_sel_hi:[1,0]
	v_lshlrev_b32_e32 v25, 16, v75
	v_lshlrev_b32_e32 v24, 16, v74
	v_pk_fma_f32 v[42:43], v[214:215], v[30:31], v[24:25] neg_lo:[1,0,0] neg_hi:[1,0,0]
	v_and_b32_e32 v25, 0xffff0000, v75
	v_and_b32_e32 v24, 0xffff0000, v74
	v_and_b32_e32 v31, 0xffff0000, v85
	v_and_b32_e32 v30, 0xffff0000, v84
	v_pk_fma_f32 v[54:55], v[214:215], v[30:31], v[24:25] neg_lo:[1,0,0] neg_hi:[1,0,0]
	v_mov_b32_e32 v24, v42
	v_mov_b32_e32 v25, v54
	v_mul_f32_e32 v30, v54, v54
	v_pk_fma_f32 v[74:75], v[24:25], v[24:25], v[30:31] op_sel_hi:[1,1,0]
	v_mov_b32_e32 v24, v43
	v_mov_b32_e32 v25, v55
	v_mul_f32_e32 v30, v55, v55
	v_pk_fma_f32 v[84:85], v[24:25], v[24:25], v[30:31] op_sel_hi:[1,1,0]
	v_lshlrev_b32_e32 v25, 16, v87
	v_lshlrev_b32_e32 v24, 16, v86
	v_lshlrev_b32_e32 v31, 16, v89
	v_lshlrev_b32_e32 v30, 16, v88
	v_pk_fma_f32 v[24:25], v[214:215], v[30:31], v[24:25] neg_lo:[1,0,0] neg_hi:[1,0,0]
	v_and_b32_e32 v31, 0xffff0000, v87
	v_and_b32_e32 v30, 0xffff0000, v86
	v_and_b32_e32 v87, 0xffff0000, v89
	v_and_b32_e32 v86, 0xffff0000, v88
	v_pk_fma_f32 v[30:31], v[214:215], v[86:87], v[30:31] neg_lo:[1,0,0] neg_hi:[1,0,0]
	v_pk_mul_f32 v[86:87], v[24:25], v[24:25]
	v_pk_mul_f32 v[88:89], v[30:31], v[30:31]
	v_mov_b32_e32 v93, v86
	v_mov_b32_e32 v61, v88
	v_mov_b32_e32 v75, v87
	v_mov_b32_e32 v85, v89
	v_pk_add_f32 v[60:61], v[92:93], v[60:61]
	v_pk_add_f32 v[74:75], v[74:75], v[84:85]
	v_lshlrev_b32_e32 v89, 16, v37
	v_pk_add_f32 v[60:61], v[60:61], v[74:75]
	v_lshlrev_b32_e32 v75, 16, v29
	v_pk_add_f32 v[84:85], v[60:61], v[60:61] op_sel:[0,1] op_sel_hi:[1,0]
	v_lshlrev_b32_e32 v61, 16, v91
	v_lshlrev_b32_e32 v60, 16, v90
	v_lshlrev_b32_e32 v74, 16, v28
	v_pk_fma_f32 v[60:61], v[214:215], v[74:75], v[60:61] neg_lo:[1,0,0] neg_hi:[1,0,0]
	v_and_b32_e32 v75, 0xffff0000, v91
	v_and_b32_e32 v74, 0xffff0000, v90
	v_and_b32_e32 v29, 0xffff0000, v29
	v_and_b32_e32 v28, 0xffff0000, v28
	v_pk_fma_f32 v[74:75], v[214:215], v[28:29], v[74:75] neg_lo:[1,0,0] neg_hi:[1,0,0]
	v_lshlrev_b32_e32 v88, 16, v36
	v_pk_mul_f32 v[28:29], v[74:75], v[74:75]
	v_and_b32_e32 v37, 0xffff0000, v37
	v_pk_fma_f32 v[28:29], v[60:61], v[60:61], v[28:29]
	v_and_b32_e32 v36, 0xffff0000, v36
	v_pk_add_f32 v[86:87], v[28:29], v[28:29] op_sel:[0,1] op_sel_hi:[1,0]
	v_lshlrev_b32_e32 v29, 16, v59
	v_lshlrev_b32_e32 v28, 16, v58
	v_and_b32_e32 v59, 0xffff0000, v59
	v_and_b32_e32 v58, 0xffff0000, v58
	v_pk_fma_f32 v[28:29], v[214:215], v[88:89], v[28:29] neg_lo:[1,0,0] neg_hi:[1,0,0]
	v_pk_fma_f32 v[36:37], v[214:215], v[36:37], v[58:59] neg_lo:[1,0,0] neg_hi:[1,0,0]
	v_mov_b32_e32 v58, v28
	v_mov_b32_e32 v59, v36
	v_mul_f32_e32 v88, v36, v36
	v_pk_fma_f32 v[88:89], v[58:59], v[58:59], v[88:89] op_sel_hi:[1,1,0]
	v_mov_b32_e32 v58, v29
	v_mov_b32_e32 v59, v37
	v_mul_f32_e32 v90, v37, v37
	v_pk_fma_f32 v[90:91], v[58:59], v[58:59], v[90:91] op_sel_hi:[1,1,0]
	v_lshlrev_b32_e32 v59, 16, v67
	v_lshlrev_b32_e32 v58, 16, v66
	v_lshlrev_b32_e32 v93, 16, v45
	v_lshlrev_b32_e32 v92, 16, v44
	v_and_b32_e32 v67, 0xffff0000, v67
	v_and_b32_e32 v66, 0xffff0000, v66
	v_and_b32_e32 v45, 0xffff0000, v45
	v_and_b32_e32 v44, 0xffff0000, v44
	v_pk_fma_f32 v[58:59], v[214:215], v[92:93], v[58:59] neg_lo:[1,0,0] neg_hi:[1,0,0]
	v_pk_fma_f32 v[66:67], v[214:215], v[44:45], v[66:67] neg_lo:[1,0,0] neg_hi:[1,0,0]
	v_pk_mul_f32 v[44:45], v[58:59], v[58:59]
	v_pk_mul_f32 v[92:93], v[66:67], v[66:67]
	v_mov_b32_e32 v85, v44
	v_mov_b32_e32 v87, v92
	v_mov_b32_e32 v89, v45
	v_mov_b32_e32 v91, v93
	v_pk_add_f32 v[84:85], v[84:85], v[86:87]
	v_pk_add_f32 v[44:45], v[88:89], v[90:91]
	v_lshlrev_b32_e32 v87, 16, v53
	v_pk_add_f32 v[44:45], v[84:85], v[44:45]
	v_lshlrev_b32_e32 v86, 16, v52
	v_pk_add_f32 v[84:85], v[44:45], v[44:45] op_sel:[0,1] op_sel_hi:[1,0]
	v_lshlrev_b32_e32 v45, 16, v63
	v_lshlrev_b32_e32 v44, 16, v62
	v_and_b32_e32 v63, 0xffff0000, v63
	v_and_b32_e32 v62, 0xffff0000, v62
	v_and_b32_e32 v53, 0xffff0000, v53
	v_and_b32_e32 v52, 0xffff0000, v52
	v_pk_fma_f32 v[52:53], v[214:215], v[52:53], v[62:63] neg_lo:[1,0,0] neg_hi:[1,0,0]
	v_pk_fma_f32 v[44:45], v[214:215], v[86:87], v[44:45] neg_lo:[1,0,0] neg_hi:[1,0,0]
	v_pk_mul_f32 v[62:63], v[52:53], v[52:53]
	v_lshlrev_b32_e32 v89, 16, v33
	v_pk_fma_f32 v[62:63], v[44:45], v[44:45], v[62:63]
	v_lshlrev_b32_e32 v88, 16, v32
	v_pk_add_f32 v[86:87], v[62:63], v[62:63] op_sel:[0,1] op_sel_hi:[1,0]
	v_lshlrev_b32_e32 v63, 16, v77
	v_lshlrev_b32_e32 v62, 16, v76
	v_and_b32_e32 v77, 0xffff0000, v77
	v_and_b32_e32 v76, 0xffff0000, v76
	v_and_b32_e32 v33, 0xffff0000, v33
	v_and_b32_e32 v32, 0xffff0000, v32
	v_pk_fma_f32 v[62:63], v[214:215], v[88:89], v[62:63] neg_lo:[1,0,0] neg_hi:[1,0,0]
	v_pk_fma_f32 v[76:77], v[214:215], v[32:33], v[76:77] neg_lo:[1,0,0] neg_hi:[1,0,0]
	v_mov_b32_e32 v32, v62
	v_mov_b32_e32 v33, v76
	v_mul_f32_e32 v88, v76, v76
	v_pk_fma_f32 v[88:89], v[32:33], v[32:33], v[88:89] op_sel_hi:[1,1,0]
	v_mov_b32_e32 v32, v63
	v_mov_b32_e32 v33, v77
	v_mul_f32_e32 v90, v77, v77
	v_pk_fma_f32 v[90:91], v[32:33], v[32:33], v[90:91] op_sel_hi:[1,1,0]
	v_lshlrev_b32_e32 v33, 16, v69
	v_lshlrev_b32_e32 v32, 16, v68
	v_lshlrev_b32_e32 v93, 16, v39
	v_lshlrev_b32_e32 v92, 16, v38
	v_and_b32_e32 v69, 0xffff0000, v69
	v_and_b32_e32 v68, 0xffff0000, v68
	v_and_b32_e32 v39, 0xffff0000, v39
	v_and_b32_e32 v38, 0xffff0000, v38
	v_pk_fma_f32 v[32:33], v[214:215], v[92:93], v[32:33] neg_lo:[1,0,0] neg_hi:[1,0,0]
	v_pk_fma_f32 v[38:39], v[214:215], v[38:39], v[68:69] neg_lo:[1,0,0] neg_hi:[1,0,0]
	v_pk_mul_f32 v[68:69], v[32:33], v[32:33]
	v_pk_mul_f32 v[92:93], v[38:39], v[38:39]
	v_mov_b32_e32 v85, v68
	v_mov_b32_e32 v87, v92
	v_mov_b32_e32 v89, v69
	v_mov_b32_e32 v91, v93
	v_pk_add_f32 v[84:85], v[84:85], v[86:87]
	v_pk_add_f32 v[68:69], v[88:89], v[90:91]
	v_lshlrev_b32_e32 v87, 16, v21
	v_pk_add_f32 v[68:69], v[84:85], v[68:69]
	v_lshlrev_b32_e32 v86, 16, v20
	v_pk_add_f32 v[84:85], v[68:69], v[68:69] op_sel:[0,1] op_sel_hi:[1,0]
	v_lshlrev_b32_e32 v69, 16, v81
	v_lshlrev_b32_e32 v68, 16, v80
	v_and_b32_e32 v81, 0xffff0000, v81
	v_and_b32_e32 v80, 0xffff0000, v80
	v_and_b32_e32 v21, 0xffff0000, v21
	v_and_b32_e32 v20, 0xffff0000, v20
	v_pk_fma_f32 v[80:81], v[214:215], v[20:21], v[80:81] neg_lo:[1,0,0] neg_hi:[1,0,0]
	v_pk_fma_f32 v[68:69], v[214:215], v[86:87], v[68:69] neg_lo:[1,0,0] neg_hi:[1,0,0]
	v_pk_mul_f32 v[20:21], v[80:81], v[80:81]
	v_lshlrev_b32_e32 v89, 16, v23
	v_pk_fma_f32 v[20:21], v[68:69], v[68:69], v[20:21]
	v_lshlrev_b32_e32 v88, 16, v22
	v_pk_add_f32 v[86:87], v[20:21], v[20:21] op_sel:[0,1] op_sel_hi:[1,0]
	v_lshlrev_b32_e32 v21, 16, v47
	v_lshlrev_b32_e32 v20, 16, v46
	v_and_b32_e32 v47, 0xffff0000, v47
	v_and_b32_e32 v46, 0xffff0000, v46
	v_and_b32_e32 v23, 0xffff0000, v23
	v_and_b32_e32 v22, 0xffff0000, v22
	v_pk_fma_f32 v[20:21], v[214:215], v[88:89], v[20:21] neg_lo:[1,0,0] neg_hi:[1,0,0]
	v_pk_fma_f32 v[22:23], v[214:215], v[22:23], v[46:47] neg_lo:[1,0,0] neg_hi:[1,0,0]
	v_mov_b32_e32 v46, v20
	v_mov_b32_e32 v47, v22
	v_mul_f32_e32 v88, v22, v22
	v_pk_fma_f32 v[88:89], v[46:47], v[46:47], v[88:89] op_sel_hi:[1,1,0]
	v_mov_b32_e32 v46, v21
	v_mov_b32_e32 v47, v23
	v_mul_f32_e32 v90, v23, v23
	v_pk_fma_f32 v[90:91], v[46:47], v[46:47], v[90:91] op_sel_hi:[1,1,0]
	v_lshlrev_b32_e32 v47, 16, v57
	v_lshlrev_b32_e32 v46, 16, v56
	v_lshlrev_b32_e32 v93, 16, v49
	v_lshlrev_b32_e32 v92, 16, v48
	v_and_b32_e32 v57, 0xffff0000, v57
	v_and_b32_e32 v56, 0xffff0000, v56
	v_and_b32_e32 v49, 0xffff0000, v49
	v_and_b32_e32 v48, 0xffff0000, v48
	v_pk_fma_f32 v[46:47], v[214:215], v[92:93], v[46:47] neg_lo:[1,0,0] neg_hi:[1,0,0]
	v_pk_fma_f32 v[48:49], v[214:215], v[48:49], v[56:57] neg_lo:[1,0,0] neg_hi:[1,0,0]
	v_pk_mul_f32 v[56:57], v[46:47], v[46:47]
	v_pk_mul_f32 v[92:93], v[48:49], v[48:49]
	v_mov_b32_e32 v85, v56
	v_mov_b32_e32 v87, v92
	v_mov_b32_e32 v89, v57
	v_mov_b32_e32 v91, v93
	v_pk_add_f32 v[84:85], v[84:85], v[86:87]
	v_pk_add_f32 v[56:57], v[88:89], v[90:91]
	v_mov_b32_e32 v10, v9
	v_pk_add_f32 v[56:57], v[84:85], v[56:57]
	s_nop 0
	v_add_f32_e32 v56, v56, v57
	ds_bpermute_b32 v57, v83, v56
	s_waitcnt lgkmcnt(0)
	v_add_f32_e32 v2, v56, v57
	v_fmamk_f32 v2, v2, 0x3c000000, v1
	v_mul_f32_e32 v14, 0x4f800000, v2
	v_cmp_gt_f32_e32 vcc, s0, v2
	s_nop 1
	v_cndmask_b32_e32 v2, v2, v14, vcc
	v_sqrt_f32_e32 v56, v2
	v_mov_b32_e32 v14, v8
	v_add_u32_e32 v8, -1, v56
	v_fma_f32 v9, -v8, v56, v2
	v_cmp_ge_f32_e64 s[0:1], 0, v9
	v_add_u32_e32 v9, 1, v56
	s_nop 0
	v_cndmask_b32_e64 v8, v56, v8, s[0:1]
	v_fma_f32 v56, -v9, v56, v2
	v_cmp_lt_f32_e64 s[0:1], 0, v56
	s_nop 1
	v_cndmask_b32_e64 v8, v8, v9, s[0:1]
	v_mul_f32_e32 v9, 0x37800000, v8
	v_cndmask_b32_e32 v8, v8, v9, vcc
	v_cmp_class_f32_e32 vcc, v2, v226
	v_mov_b32_e32 v9, v6
	v_mov_b32_e32 v6, v5
	v_cndmask_b32_e32 v2, v8, v2, vcc
	v_div_scale_f32 v56, s[0:1], v2, v2, 1.0
	v_rcp_f32_e32 v57, v56
	v_mov_b32_e32 v8, v4
	v_fma_f32 v4, -v56, v57, 1.0
	v_fmac_f32_e32 v57, v4, v57
	v_div_scale_f32 v4, vcc, 1.0, v2, 1.0
	v_mul_f32_e32 v5, v4, v57
	v_fma_f32 v83, -v56, v5, v4
	v_fmac_f32_e32 v5, v83, v57
	v_fma_f32 v4, -v56, v5, v4
	v_div_fmas_f32 v4, v4, v57, v5
	v_div_fixup_f32 v2, v4, v2, 1.0
	v_mul_f32_e32 v2, 0x3f24fd5c, v2
	v_pk_mul_f32 v[4:5], v[78:79], v[2:3] op_sel_hi:[1,0]
	v_pk_mul_f32 v[16:17], v[16:17], v[2:3] op_sel_hi:[1,0]
	v_pk_mul_f32 v[4:5], v[14:15], v[4:5]
	v_pk_mul_f32 v[14:15], v[72:73], v[2:3] op_sel_hi:[1,0]
	s_nop 0
	v_pk_mul_f32 v[10:11], v[10:11], v[14:15]
	v_pk_mul_f32 v[14:15], v[70:71], v[2:3] op_sel_hi:[1,0]
	v_bfe_u32 v56, v11, 16, 1
	v_pk_mul_f32 v[8:9], v[8:9], v[14:15]
	v_pk_mul_f32 v[14:15], v[64:65], v[2:3] op_sel_hi:[1,0]
	v_bfe_u32 v57, v10, 16, 1
	v_pk_mul_f32 v[6:7], v[6:7], v[14:15]
	v_add3_u32 v10, v10, v57, s62
	v_bfe_u32 v14, v7, 16, 1
	v_bfe_u32 v15, v6, 16, 1
	v_add3_u32 v11, v11, v56, s62
	v_add3_u32 v6, v6, v15, s62
	v_add3_u32 v7, v7, v14, s62
	v_bfe_u32 v14, v4, 16, 1
	v_bfe_u32 v15, v5, 16, 1
	v_bfe_u32 v56, v8, 16, 1
	v_bfe_u32 v57, v9, 16, 1
	v_add3_u32 v9, v9, v57, s62
	v_add3_u32 v8, v8, v56, s62
	v_add3_u32 v5, v5, v15, s62
	v_add3_u32 v4, v4, v14, s62
	v_lshrrev_b32_e32 v4, 16, v4
	v_lshrrev_b32_e32 v5, 16, v5
	v_lshrrev_b32_e32 v8, 16, v8
	v_lshrrev_b32_e32 v9, 16, v9
	v_and_or_b32 v7, v7, s61, v9
	v_and_or_b32 v6, v6, s61, v8
	v_and_or_b32 v5, v11, s61, v5
	v_and_or_b32 v4, v10, s61, v4
	global_store_dwordx4 v[12:13], v[4:7], off offset:1024
	global_load_dwordx4 v[4:7], v82, s[58:59] offset:544
	s_nop 0
	global_load_dwordx4 v[8:11], v82, s[58:59] offset:560
	v_pk_mul_f32 v[14:15], v[18:19], v[2:3] op_sel_hi:[1,0]
	s_waitcnt vmcnt(1)
	v_mov_b32_e32 v19, v6
	v_mov_b32_e32 v6, v5
	v_mov_b32_e32 v18, v4
	v_pk_mul_f32 v[4:5], v[6:7], v[16:17]
	v_pk_mul_f32 v[6:7], v[40:41], v[2:3] op_sel_hi:[1,0]
	s_waitcnt vmcnt(0)
	v_mov_b32_e32 v16, v8
	v_mov_b32_e32 v17, v10
	v_pk_mul_f32 v[6:7], v[16:17], v[6:7]
	v_pk_mul_f32 v[16:17], v[50:51], v[2:3] op_sel_hi:[1,0]
	v_mov_b32_e32 v10, v9
	v_pk_mul_f32 v[8:9], v[10:11], v[16:17]
	v_pk_mul_f32 v[14:15], v[18:19], v[14:15]
	v_bfe_u32 v10, v9, 16, 1
	v_bfe_u32 v11, v8, 16, 1
	v_bfe_u32 v16, v5, 16, 1
	v_bfe_u32 v17, v4, 16, 1
	v_add3_u32 v4, v4, v17, s62
	v_add3_u32 v5, v5, v16, s62
	v_add3_u32 v8, v8, v11, s62
	v_add3_u32 v9, v9, v10, s62
	v_bfe_u32 v10, v14, 16, 1
	v_bfe_u32 v11, v15, 16, 1
	v_bfe_u32 v16, v6, 16, 1
	v_bfe_u32 v17, v7, 16, 1
	v_add3_u32 v7, v7, v17, s62
	v_add3_u32 v6, v6, v16, s62
	v_add3_u32 v11, v15, v11, s62
	v_add3_u32 v10, v14, v10, s62
	v_lshrrev_b32_e32 v10, 16, v10
	v_lshrrev_b32_e32 v11, 16, v11
	v_lshrrev_b32_e32 v6, 16, v6
	v_lshrrev_b32_e32 v7, 16, v7
	v_and_or_b32 v7, v9, s61, v7
	v_and_or_b32 v6, v8, s61, v6
	v_and_or_b32 v5, v5, s61, v11
	v_and_or_b32 v4, v4, s61, v10
	global_store_dwordx4 v[12:13], v[4:7], off offset:1040
	global_load_dwordx4 v[4:7], v82, s[58:59] offset:576
	s_nop 0
	global_load_dwordx4 v[8:11], v82, s[58:59] offset:592
	v_pk_mul_f32 v[14:15], v[26:27], v[2:3] op_sel_hi:[1,0]
	v_pk_mul_f32 v[18:19], v[62:63], v[2:3] op_sel_hi:[1,0]
	s_waitcnt vmcnt(1)
	v_mov_b32_e32 v16, v4
	v_mov_b32_e32 v17, v6
	v_pk_mul_f32 v[14:15], v[14:15], v[16:17]
	v_pk_mul_f32 v[16:17], v[34:35], v[2:3] op_sel_hi:[1,0]
	v_mov_b32_e32 v6, v5
	v_pk_mul_f32 v[4:5], v[16:17], v[6:7]
	v_pk_mul_f32 v[6:7], v[42:43], v[2:3] op_sel_hi:[1,0]
	s_waitcnt vmcnt(0)
	v_mov_b32_e32 v16, v8
	v_mov_b32_e32 v17, v10
	v_pk_mul_f32 v[6:7], v[6:7], v[16:17]
	v_pk_mul_f32 v[16:17], v[54:55], v[2:3] op_sel_hi:[1,0]
	v_mov_b32_e32 v10, v9
	v_pk_mul_f32 v[8:9], v[16:17], v[10:11]
	v_bfe_u32 v16, v5, 16, 1
	v_bfe_u32 v10, v9, 16, 1
	v_bfe_u32 v11, v8, 16, 1
	v_bfe_u32 v17, v4, 16, 1
	v_add3_u32 v4, v4, v17, s62
	v_add3_u32 v5, v5, v16, s62
	v_add3_u32 v8, v8, v11, s62
	v_add3_u32 v9, v9, v10, s62
	v_bfe_u32 v10, v14, 16, 1
	v_bfe_u32 v11, v15, 16, 1
	v_bfe_u32 v16, v6, 16, 1
	v_bfe_u32 v17, v7, 16, 1
	v_add3_u32 v7, v7, v17, s62
	v_add3_u32 v6, v6, v16, s62
	v_add3_u32 v11, v15, v11, s62
	v_add3_u32 v10, v14, v10, s62
	v_lshrrev_b32_e32 v10, 16, v10
	v_lshrrev_b32_e32 v11, 16, v11
	v_lshrrev_b32_e32 v6, 16, v6
	v_lshrrev_b32_e32 v7, 16, v7
	v_and_or_b32 v7, v9, s61, v7
	v_and_or_b32 v6, v8, s61, v6
	v_and_or_b32 v5, v5, s61, v11
	v_and_or_b32 v4, v4, s61, v10
	global_store_dwordx4 v[12:13], v[4:7], off offset:1056
	global_load_dwordx4 v[4:7], v82, s[58:59] offset:608
	s_nop 0
	global_load_dwordx4 v[8:11], v82, s[58:59] offset:624
	v_pk_mul_f32 v[14:15], v[24:25], v[2:3] op_sel_hi:[1,0]
	v_pk_mul_f32 v[24:25], v[76:77], v[2:3] op_sel_hi:[1,0]
	s_waitcnt vmcnt(1)
	v_mov_b32_e32 v16, v4
	v_mov_b32_e32 v17, v6
	v_pk_mul_f32 v[14:15], v[14:15], v[16:17]
	v_pk_mul_f32 v[16:17], v[30:31], v[2:3] op_sel_hi:[1,0]
	v_mov_b32_e32 v6, v5
	v_pk_mul_f32 v[4:5], v[16:17], v[6:7]
	v_pk_mul_f32 v[6:7], v[60:61], v[2:3] op_sel_hi:[1,0]
	s_waitcnt vmcnt(0)
	v_mov_b32_e32 v16, v8
	v_mov_b32_e32 v17, v10
	v_pk_mul_f32 v[6:7], v[6:7], v[16:17]
	v_pk_mul_f32 v[16:17], v[74:75], v[2:3] op_sel_hi:[1,0]
	v_mov_b32_e32 v10, v9
	v_pk_mul_f32 v[8:9], v[16:17], v[10:11]
	v_bfe_u32 v16, v5, 16, 1
	v_bfe_u32 v10, v9, 16, 1
	v_bfe_u32 v11, v8, 16, 1
	v_bfe_u32 v17, v4, 16, 1
	v_add3_u32 v4, v4, v17, s62
	v_add3_u32 v5, v5, v16, s62
	v_add3_u32 v8, v8, v11, s62
	v_add3_u32 v9, v9, v10, s62
	v_bfe_u32 v10, v14, 16, 1
	v_bfe_u32 v11, v15, 16, 1
	v_bfe_u32 v16, v6, 16, 1
	v_bfe_u32 v17, v7, 16, 1
	v_add3_u32 v7, v7, v17, s62
	v_add3_u32 v6, v6, v16, s62
	v_add3_u32 v11, v15, v11, s62
	v_add3_u32 v10, v14, v10, s62
	v_lshrrev_b32_e32 v10, 16, v10
	v_lshrrev_b32_e32 v11, 16, v11
	v_lshrrev_b32_e32 v6, 16, v6
	v_lshrrev_b32_e32 v7, 16, v7
	v_and_or_b32 v7, v9, s61, v7
	v_and_or_b32 v6, v8, s61, v6
	v_and_or_b32 v5, v5, s61, v11
	v_and_or_b32 v4, v4, s61, v10
	global_store_dwordx4 v[12:13], v[4:7], off offset:1072
	global_load_dwordx4 v[4:7], v82, s[58:59] offset:640
	s_nop 0
	global_load_dwordx4 v[8:11], v82, s[58:59] offset:656
	v_pk_mul_f32 v[14:15], v[28:29], v[2:3] op_sel_hi:[1,0]
	s_waitcnt vmcnt(1)
	v_mov_b32_e32 v16, v4
	v_mov_b32_e32 v17, v6
	v_pk_mul_f32 v[14:15], v[14:15], v[16:17]
	v_pk_mul_f32 v[16:17], v[36:37], v[2:3] op_sel_hi:[1,0]
	v_mov_b32_e32 v6, v5
	v_pk_mul_f32 v[4:5], v[16:17], v[6:7]
	v_pk_mul_f32 v[6:7], v[58:59], v[2:3] op_sel_hi:[1,0]
	s_waitcnt vmcnt(0)
	v_mov_b32_e32 v16, v8
	v_mov_b32_e32 v17, v10
	v_pk_mul_f32 v[6:7], v[6:7], v[16:17]
	v_pk_mul_f32 v[16:17], v[66:67], v[2:3] op_sel_hi:[1,0]
	v_mov_b32_e32 v10, v9
	v_pk_mul_f32 v[8:9], v[16:17], v[10:11]
	v_bfe_u32 v16, v5, 16, 1
	v_bfe_u32 v10, v9, 16, 1
	v_bfe_u32 v11, v8, 16, 1
	v_bfe_u32 v17, v4, 16, 1
	v_add3_u32 v4, v4, v17, s62
	v_add3_u32 v5, v5, v16, s62
	v_add3_u32 v8, v8, v11, s62
	v_add3_u32 v9, v9, v10, s62
	v_bfe_u32 v10, v14, 16, 1
	v_bfe_u32 v11, v15, 16, 1
	v_bfe_u32 v16, v6, 16, 1
	v_bfe_u32 v17, v7, 16, 1
	v_add3_u32 v7, v7, v17, s62
	v_add3_u32 v6, v6, v16, s62
	v_add3_u32 v11, v15, v11, s62
	v_add3_u32 v10, v14, v10, s62
	v_lshrrev_b32_e32 v10, 16, v10
	v_lshrrev_b32_e32 v11, 16, v11
	v_lshrrev_b32_e32 v6, 16, v6
	v_lshrrev_b32_e32 v7, 16, v7
	v_and_or_b32 v7, v9, s61, v7
	v_and_or_b32 v6, v8, s61, v6
	v_and_or_b32 v5, v5, s61, v11
	v_and_or_b32 v4, v4, s61, v10
	global_store_dwordx4 v[12:13], v[4:7], off offset:1088
	global_load_dwordx4 v[4:7], v82, s[58:59] offset:672
	s_nop 0
	global_load_dwordx4 v[8:11], v82, s[58:59] offset:688
	v_pk_mul_f32 v[16:17], v[52:53], v[2:3] op_sel_hi:[1,0]
	v_pk_mul_f32 v[14:15], v[44:45], v[2:3] op_sel_hi:[1,0]
	s_waitcnt vmcnt(1)
	v_mov_b32_e32 v27, v6
	v_mov_b32_e32 v6, v5
	s_waitcnt vmcnt(0)
	v_mov_b32_e32 v5, v10
	v_mov_b32_e32 v10, v9
	v_mov_b32_e32 v26, v4
	v_mov_b32_e32 v4, v8
	v_pk_mul_f32 v[6:7], v[16:17], v[6:7]
	v_pk_mul_f32 v[10:11], v[24:25], v[10:11]
	v_pk_mul_f32 v[8:9], v[14:15], v[26:27]
	v_pk_mul_f32 v[4:5], v[18:19], v[4:5]
	v_bfe_u32 v14, v11, 16, 1
	v_bfe_u32 v15, v10, 16, 1
	v_bfe_u32 v16, v7, 16, 1
	v_bfe_u32 v17, v6, 16, 1
	v_add3_u32 v17, v6, v17, s62
	v_add3_u32 v16, v7, v16, s62
	v_add3_u32 v6, v10, v15, s62
	v_add3_u32 v7, v11, v14, s62
	v_bfe_u32 v10, v8, 16, 1
	v_bfe_u32 v11, v9, 16, 1
	v_bfe_u32 v14, v4, 16, 1
	v_bfe_u32 v15, v5, 16, 1
	v_add3_u32 v5, v5, v15, s62
	v_add3_u32 v4, v4, v14, s62
	v_add3_u32 v9, v9, v11, s62
	v_add3_u32 v8, v8, v10, s62
	v_lshrrev_b32_e32 v8, 16, v8
	v_lshrrev_b32_e32 v9, 16, v9
	v_lshrrev_b32_e32 v4, 16, v4
	v_lshrrev_b32_e32 v5, 16, v5
	v_and_or_b32 v7, v7, s61, v5
	v_and_or_b32 v6, v6, s61, v4
	v_and_or_b32 v5, v16, s61, v9
	v_and_or_b32 v4, v17, s61, v8
	global_store_dwordx4 v[12:13], v[4:7], off offset:1104
	global_load_dwordx4 v[4:7], v82, s[58:59] offset:704
	s_nop 0
	global_load_dwordx4 v[8:11], v82, s[58:59] offset:720
	v_pk_mul_f32 v[14:15], v[32:33], v[2:3] op_sel_hi:[1,0]
	v_pk_mul_f32 v[18:19], v[68:69], v[2:3] op_sel_hi:[1,0]
	v_pk_mul_f32 v[16:17], v[38:39], v[2:3] op_sel_hi:[1,0]
	v_pk_mul_f32 v[24:25], v[80:81], v[2:3] op_sel_hi:[1,0]
	s_waitcnt vmcnt(1)
	v_mov_b32_e32 v26, v4
	v_mov_b32_e32 v27, v6
	v_mov_b32_e32 v6, v5
	s_waitcnt vmcnt(0)
	v_mov_b32_e32 v4, v8
	v_mov_b32_e32 v5, v10
	v_mov_b32_e32 v10, v9
	v_pk_mul_f32 v[8:9], v[14:15], v[26:27]
	v_pk_mul_f32 v[4:5], v[18:19], v[4:5]
	v_pk_mul_f32 v[6:7], v[16:17], v[6:7]
	v_pk_mul_f32 v[10:11], v[24:25], v[10:11]
	v_bfe_u32 v18, v8, 16, 1
	v_bfe_u32 v19, v9, 16, 1
	v_bfe_u32 v24, v4, 16, 1
	v_bfe_u32 v25, v5, 16, 1
	v_bfe_u32 v14, v11, 16, 1
	v_bfe_u32 v15, v10, 16, 1
	v_bfe_u32 v16, v7, 16, 1
	v_bfe_u32 v17, v6, 16, 1
	v_add3_u32 v5, v5, v25, s62
	v_add3_u32 v4, v4, v24, s62
	v_add3_u32 v9, v9, v19, s62
	v_add3_u32 v8, v8, v18, s62
	v_add3_u32 v17, v6, v17, s62
	v_add3_u32 v16, v7, v16, s62
	v_add3_u32 v6, v10, v15, s62
	v_add3_u32 v7, v11, v14, s62
	v_lshrrev_b32_e32 v8, 16, v8
	v_lshrrev_b32_e32 v9, 16, v9
	v_lshrrev_b32_e32 v4, 16, v4
	v_lshrrev_b32_e32 v5, 16, v5
	v_and_or_b32 v7, v7, s61, v5
	v_and_or_b32 v6, v6, s61, v4
	v_and_or_b32 v5, v16, s61, v9
	v_and_or_b32 v4, v17, s61, v8
	global_store_dwordx4 v[12:13], v[4:7], off offset:1120
	global_load_dwordx4 v[4:7], v82, s[58:59] offset:736
	s_nop 0
	global_load_dwordx4 v[8:11], v82, s[58:59] offset:752
	v_pk_mul_f32 v[14:15], v[20:21], v[2:3] op_sel_hi:[1,0]
	v_pk_mul_f32 v[16:17], v[22:23], v[2:3] op_sel_hi:[1,0]
	v_pk_mul_f32 v[18:19], v[46:47], v[2:3] op_sel_hi:[1,0]
	v_pk_mul_f32 v[20:21], v[48:49], v[2:3] op_sel_hi:[1,0]
	s_waitcnt vmcnt(1)
	v_mov_b32_e32 v22, v4
	v_mov_b32_e32 v23, v6
	v_mov_b32_e32 v6, v5
	s_waitcnt vmcnt(0)
	v_mov_b32_e32 v4, v8
	v_mov_b32_e32 v5, v10
	v_mov_b32_e32 v10, v9
	v_pk_mul_f32 v[8:9], v[14:15], v[22:23]
	v_pk_mul_f32 v[6:7], v[16:17], v[6:7]
	v_pk_mul_f32 v[4:5], v[18:19], v[4:5]
	v_pk_mul_f32 v[10:11], v[20:21], v[10:11]
	v_bfe_u32 v15, v7, 16, 1
	v_bfe_u32 v17, v8, 16, 1
	v_bfe_u32 v18, v9, 16, 1
	v_bfe_u32 v19, v4, 16, 1
	v_bfe_u32 v14, v10, 16, 1
	v_bfe_u32 v16, v6, 16, 1
	v_add3_u32 v15, v7, v15, s62
	v_add3_u32 v4, v4, v19, s62
	v_add3_u32 v7, v9, v18, s62
	v_add3_u32 v8, v8, v17, s62
	v_add3_u32 v16, v6, v16, s62
	v_add3_u32 v6, v10, v14, s62
	v_lshrrev_b32_e32 v8, 16, v8
	v_lshrrev_b32_e32 v9, 16, v7
	v_lshrrev_b32_e32 v4, 16, v4
	v_cvt_pk_bf16_f32 v7, v5, v11
	v_and_or_b32 v6, v6, s61, v4
	v_and_or_b32 v5, v15, s61, v9
	v_and_or_b32 v4, v16, s61, v8
	global_store_dwordx4 v[12:13], v[4:7], off offset:1136
	s_branch .LBB0_872

.LBB0_990:
	s_or_b64 exec, exec, s[12:13]
	v_min_i32_e32 v34, 2, v56
	v_cvt_f32_i32_e32 v34, v34
	v_lshlrev_b32_e32 v35, 2, v59
	v_add3_u32 v53, 0, v50, v35
	v_lshlrev_b32_e32 v51, 1, v59
	v_div_scale_f32 v46, s[12:13], v34, v34, 1.0
	v_rcp_f32_e32 v47, v46
	v_div_scale_f32 v35, vcc, 1.0, v34, 1.0
	s_movk_i32 s12, 0x90
	v_fma_f32 v48, -v46, v47, 1.0
	v_fmac_f32_e32 v47, v48, v47
	v_mul_f32_e32 v48, v35, v47
	v_fma_f32 v49, -v46, v48, v35
	v_fmac_f32_e32 v48, v49, v47
	v_fma_f32 v35, -v46, v48, v35
	v_div_fmas_f32 v35, v35, v47, v48
	ds_read_b128 v[46:49], v53 offset:3840
	v_div_fixup_f32 v34, v35, v34, 1.0
	v_mul_lo_u32 v35, v58, s12
	v_add3_u32 v51, 0, v35, v51
	s_movk_i32 s12, 0x7fff
	s_waitcnt lgkmcnt(0)
	v_xor_b32_e32 v49, 0x80000000, v49
	v_xor_b32_e32 v48, 0x80000000, v48
	v_pk_fma_f32 v[44:45], v[34:35], v[44:45], v[46:47] op_sel_hi:[0,1,1] neg_lo:[0,0,1] neg_hi:[0,0,1]
	v_pk_fma_f32 v[36:37], v[34:35], v[36:37], v[48:49] op_sel_hi:[0,1,1]
	s_mov_b32 s13, 0xffff0000
	v_cvt_pk_bf16_f32 v44, v44, v45
	v_cvt_pk_bf16_f32 v45, v36, v37
	ds_write_b64 v51, v[44:45] offset:40960
	v_mov_b32_e32 v45, 0
	v_mov_b32_e32 v44, v45
	v_mov_b32_e32 v37, v45
	v_mov_b32_e32 v36, v45
	s_and_saveexec_b64 s[12:13], s[2:3]
	s_cbranch_execz .LBB0_994
	v_lshlrev_b32_e32 v35, 6, v1
	v_add3_u32 v35, v50, v35, 0
	v_mov_b32_e32 v36, 0
	v_add_u32_e32 v35, 0xf10, v35
	s_mov_b64 s[14:15], 0
	v_mov_b32_e32 v46, v39
	v_mov_b32_e32 v37, v36
	v_mov_b32_e32 v44, v36
	v_mov_b32_e32 v45, v36

.LBB0_994:
	s_or_b64 exec, exec, s[12:13]
	ds_read_b128 v[46:49], v53 offset:3856
	v_mov_b32_e32 v35, v34
	s_movk_i32 s12, 0x7fff
	v_mov_b32_e32 v60, v34
	v_mov_b32_e32 v61, v34
	s_waitcnt lgkmcnt(0)
	v_pk_fma_f32 v[36:37], v[34:35], v[36:37], v[46:47] neg_lo:[0,0,1] neg_hi:[0,0,1]
	v_xor_b32_e32 v49, 0x80000000, v49
	v_xor_b32_e32 v48, 0x80000000, v48
	v_pk_fma_f32 v[44:45], v[60:61], v[44:45], v[48:49]
	s_mov_b32 s13, 0xffff0000
	v_cvt_pk_bf16_f32 v36, v36, v37
	v_cvt_pk_bf16_f32 v37, v44, v45
	v_mov_b32_e32 v45, 0
	ds_write_b64 v51, v[36:37] offset:40968
	v_mov_b32_e32 v44, v45
	v_mov_b32_e32 v37, v45
	v_mov_b32_e32 v36, v45
	s_and_saveexec_b64 s[12:13], s[2:3]
	s_cbranch_execz .LBB0_998
	v_lshlrev_b32_e32 v36, 6, v1
	v_add3_u32 v36, v50, v36, 0
	v_add_u32_e32 v46, 0xf20, v36
	v_mov_b32_e32 v36, 0
	s_mov_b64 s[14:15], 0
	v_mov_b32_e32 v47, v39
	v_mov_b32_e32 v37, v36
	v_mov_b32_e32 v44, v36
	v_mov_b32_e32 v45, v36

.LBB0_998:
	s_or_b64 exec, exec, s[12:13]
	ds_read_b128 v[46:49], v53 offset:3872
	s_movk_i32 s12, 0x7fff
	v_mov_b32_e32 v60, v34
	v_mov_b32_e32 v61, v34
	s_mov_b32 s13, 0xffff0000
	s_waitcnt lgkmcnt(0)
	v_pk_fma_f32 v[36:37], v[34:35], v[36:37], v[46:47] neg_lo:[0,0,1] neg_hi:[0,0,1]
	v_xor_b32_e32 v49, 0x80000000, v49
	v_xor_b32_e32 v48, 0x80000000, v48
	v_pk_fma_f32 v[44:45], v[60:61], v[44:45], v[48:49]
	v_cvt_pk_bf16_f32 v36, v36, v37
	v_cvt_pk_bf16_f32 v37, v44, v45
	v_mov_b32_e32 v45, 0
	ds_write_b64 v51, v[36:37] offset:40976
	v_mov_b32_e32 v44, v45
	v_mov_b32_e32 v37, v45
	v_mov_b32_e32 v36, v45
	s_and_saveexec_b64 s[12:13], s[2:3]
	s_cbranch_execz .LBB0_1002
	v_lshlrev_b32_e32 v36, 6, v1
	v_add3_u32 v36, v50, v36, 0
	v_add_u32_e32 v46, 0xf30, v36
	v_mov_b32_e32 v36, 0
	s_mov_b64 s[14:15], 0
	v_mov_b32_e32 v37, v36
	v_mov_b32_e32 v44, v36
	v_mov_b32_e32 v45, v36

.LBB0_1002:
	s_or_b64 exec, exec, s[12:13]
	ds_read_b128 v[46:49], v53 offset:3888
	v_mov_b32_e32 v60, v34
	v_mov_b32_e32 v61, v34
	s_movk_i32 s14, 0x7fff
	s_mov_b32 s15, 0xffff0000
	s_waitcnt lgkmcnt(0)
	v_pk_fma_f32 v[34:35], v[34:35], v[36:37], v[46:47] neg_lo:[0,0,1] neg_hi:[0,0,1]
	v_xor_b32_e32 v49, 0x80000000, v49
	v_xor_b32_e32 v48, 0x80000000, v48
	v_pk_fma_f32 v[44:45], v[60:61], v[44:45], v[48:49]
	v_or_b32_e32 v68, s29, v55
	s_movk_i32 s12, 0x90
	v_cvt_pk_bf16_f32 v34, v34, v35
	v_mul_lo_u32 v39, v68, s12
	v_add_u32_e32 v39, 0, v39
	v_cvt_pk_bf16_f32 v35, v44, v45
	v_add_u32_e32 v55, v39, v38
	ds_write_b64 v51, v[34:35] offset:40984
	s_waitcnt lgkmcnt(0)
	s_barrier
	ds_read_b128 v[34:37], v55 offset:40960
	ds_read_b128 v[44:47], v55 offset:41024
	s_waitcnt vmcnt(10) lgkmcnt(1)
	v_mfma_f32_16x16x32_bf16 v[60:63], v[26:29], v[34:37], 0
	v_lshlrev_b32_e32 v26, 4, v41
	v_ashrrev_i32_e32 v69, 31, v68
	s_waitcnt vmcnt(9)
	v_mfma_f32_16x16x32_bf16 v[30:33], v[30:33], v[34:37], 0
	s_movk_i32 s18, 0x1200
	v_mov_b64_e32 v[28:29], s[10:11]
	v_lshl_add_u64 v[38:39], s[0:1], 0, v[68:69]
	s_waitcnt lgkmcnt(0)
	v_mfma_f32_16x16x32_bf16 v[14:17], v[14:17], v[44:47], v[30:33]
	v_mad_u64_u32 v[28:29], s[12:13], v38, s18, v[28:29]
	v_mov_b32_e32 v41, 0
	v_mad_i32_i24 v29, v39, s18, v29
	v_lshl_add_u64 v[38:39], v[28:29], 0, v[40:41]
	s_waitcnt vmcnt(8)
	v_mfma_f32_16x16x32_bf16 v[10:13], v[10:13], v[44:47], v[60:63]
	s_waitcnt vmcnt(0)
	s_nop 0
	v_pk_mul_f32 v[16:17], v[16:17], v[102:103]
	v_pk_mul_f32 v[14:15], v[14:15], v[100:101]
	v_cvt_pk_bf16_f32 v14, v14, v15
	v_cvt_pk_bf16_f32 v15, v16, v17
	global_store_dwordx2 v[38:39], v[14:15], off offset:512
	v_mfma_f32_16x16x32_bf16 v[22:25], v[22:25], v[34:37], 0
	v_mov_b32_e32 v27, v41
	v_pk_mul_f32 v[12:13], v[12:13], v[106:107]
	v_pk_mul_f32 v[10:11], v[10:11], v[104:105]
	v_cvt_pk_bf16_f32 v10, v10, v11
	v_cvt_pk_bf16_f32 v11, v12, v13
	global_store_dwordx2 v[38:39], v[10:11], off offset:544
	v_mfma_f32_16x16x32_bf16 v[6:9], v[6:9], v[44:47], v[22:25]
	v_mfma_f32_16x16x32_bf16 v[18:21], v[18:21], v[34:37], 0
	v_mfma_f32_16x16x32_bf16 v[2:5], v[2:5], v[44:47], v[18:21]
	s_nop 5
	v_pk_mul_f32 v[8:9], v[8:9], v[110:111]
	v_pk_mul_f32 v[6:7], v[6:7], v[108:109]
	v_cvt_pk_bf16_f32 v6, v6, v7
	v_cvt_pk_bf16_f32 v7, v8, v9
	global_store_dwordx2 v[38:39], v[6:7], off offset:576
	v_pk_mul_f32 v[4:5], v[4:5], v[114:115]
	v_pk_mul_f32 v[2:3], v[2:3], v[112:113]
	v_cvt_pk_bf16_f32 v2, v2, v3
	v_cvt_pk_bf16_f32 v3, v4, v5
	global_store_dwordx2 v[38:39], v[2:3], off offset:608
	s_barrier
	v_lshlrev_b32_e32 v180, 16, v130
	v_and_b32_e32 v181, 0xffff0000, v130
	v_lshlrev_b32_e32 v182, 16, v131
	v_and_b32_e32 v183, 0xffff0000, v131
	v_lshlrev_b32_e32 v184, 16, v132
	v_and_b32_e32 v185, 0xffff0000, v132
	v_lshlrev_b32_e32 v186, 16, v133
	v_and_b32_e32 v187, 0xffff0000, v133
	v_lshlrev_b32_e32 v188, 16, v134
	v_and_b32_e32 v189, 0xffff0000, v134
	v_lshlrev_b32_e32 v190, 16, v135
	v_and_b32_e32 v191, 0xffff0000, v135
	v_lshlrev_b32_e32 v192, 16, v136
	v_and_b32_e32 v193, 0xffff0000, v136
	v_lshlrev_b32_e32 v194, 16, v137
	v_and_b32_e32 v195, 0xffff0000, v137
	v_lshlrev_b32_e32 v196, 16, v138
	v_and_b32_e32 v197, 0xffff0000, v138
	v_lshlrev_b32_e32 v198, 16, v139
	v_and_b32_e32 v199, 0xffff0000, v139
	v_lshlrev_b32_e32 v200, 16, v140
	v_and_b32_e32 v201, 0xffff0000, v140
	v_lshlrev_b32_e32 v202, 16, v141
	v_and_b32_e32 v203, 0xffff0000, v141
	ds_write_b128 v204, v[180:183]
	ds_write_b128 v204, v[184:187] offset:16
	ds_write_b128 v204, v[188:191] offset:16384
	ds_write_b128 v204, v[192:195] offset:16400
	s_mov_b64 s[98:99], exec
	v_cmp_gt_u32_e32 vcc, 0x78, v52
	s_and_b64 exec, s[98:99], vcc
	ds_write_b128 v204, v[196:199] offset:32768
	ds_write_b128 v204, v[200:203] offset:32784
	s_mov_b64 exec, s[98:99]
	v_add_co_u32_e32 v2, vcc, 0x2000, v42
	v_lshl_add_u64 v[40:41], s[64:65], 0, v[26:27]
	s_nop 0
	v_addc_co_u32_e32 v3, vcc, 0, v43, vcc
	v_add_co_u32_e32 v34, vcc, 0x3000, v42
	global_load_dwordx4 v[18:21], v[2:3], off
	global_load_dwordx4 v[14:17], v[2:3], off offset:64
	global_load_dwordx4 v[22:25], v[2:3], off offset:2048
	global_load_dwordx4 v[10:13], v[2:3], off offset:2112
	v_addc_co_u32_e32 v35, vcc, 0, v43, vcc
	global_load_dwordx4 v[26:29], v[34:35], off
	global_load_dwordx4 v[6:9], v[34:35], off offset:64
	global_load_dwordx4 v[30:33], v[34:35], off offset:2048
	global_load_dwordx4 v[2:5], v[34:35], off offset:2112
	global_load_dwordx4 v[100:103], v[40:41], off offset:1280
	global_load_dwordx4 v[104:107], v[40:41], off offset:1344
	global_load_dwordx4 v[108:111], v[40:41], off offset:1408
	global_load_dwordx4 v[112:115], v[40:41], off offset:1472
	v_max_i32_e32 v34, 0, v54
	v_add_u32_e32 v60, 1, v34
	v_mov_b32_e32 v45, 0
	v_min_u32_e32 v46, 4, v60
	v_mov_b32_e32 v44, v45
	v_mov_b32_e32 v37, v45
	v_mov_b32_e32 v36, v45
	s_waitcnt lgkmcnt(0)
	s_barrier
	s_and_saveexec_b64 s[12:13], s[2:3]
	s_cbranch_execz .LBB0_1011
	v_lshlrev_b32_e32 v34, 6, v1
	v_add3_u32 v34, v50, v34, 0
	v_mov_b32_e32 v36, 0
	v_add_u32_e32 v34, 0xf00, v34
	s_mov_b64 s[14:15], 0
	v_mov_b32_e32 v35, v46
	v_mov_b32_e32 v37, v36
	v_mov_b32_e32 v44, v36
	v_mov_b32_e32 v45, v36

.LBB0_1011:
	s_or_b64 exec, exec, s[12:13]
	v_min_i32_e32 v34, 4, v56
	v_cvt_f32_i32_e32 v34, v34
	ds_read_b128 v[62:65], v53 offset:3840
	v_div_scale_f32 v35, s[12:13], v34, v34, 1.0
	v_rcp_f32_e32 v47, v35
	v_div_scale_f32 v48, vcc, 1.0, v34, 1.0
	s_waitcnt lgkmcnt(0)
	v_xor_b32_e32 v49, 0x80000000, v65
	v_fma_f32 v61, -v35, v47, 1.0
	v_fmac_f32_e32 v47, v61, v47
	v_mul_f32_e32 v61, v48, v47
	v_fma_f32 v65, -v35, v61, v48
	v_fmac_f32_e32 v61, v65, v47
	v_fma_f32 v35, -v35, v61, v48
	v_div_fmas_f32 v35, v35, v47, v61
	v_div_fixup_f32 v34, v35, v34, 1.0
	v_xor_b32_e32 v48, 0x80000000, v64
	v_pk_fma_f32 v[36:37], v[34:35], v[36:37], v[62:63] op_sel_hi:[0,1,1] neg_lo:[0,0,1] neg_hi:[0,0,1]
	v_pk_fma_f32 v[44:45], v[34:35], v[44:45], v[48:49] op_sel_hi:[0,1,1]
	s_movk_i32 s12, 0x7fff
	s_mov_b32 s13, 0xffff0000
	v_cvt_pk_bf16_f32 v36, v36, v37
	v_cvt_pk_bf16_f32 v37, v44, v45
	v_mov_b32_e32 v45, 0
	ds_write_b64 v51, v[36:37] offset:40960
	v_mov_b32_e32 v44, v45
	v_mov_b32_e32 v37, v45
	v_mov_b32_e32 v36, v45
	s_and_saveexec_b64 s[12:13], s[2:3]
	s_cbranch_execz .LBB0_1015
	v_lshlrev_b32_e32 v35, 6, v1
	v_add3_u32 v35, v50, v35, 0
	v_mov_b32_e32 v36, 0
	v_add_u32_e32 v35, 0xf10, v35
	s_mov_b64 s[14:15], 0
	v_mov_b32_e32 v47, v46
	v_mov_b32_e32 v37, v36
	v_mov_b32_e32 v44, v36
	v_mov_b32_e32 v45, v36

.LBB0_1015:
	s_or_b64 exec, exec, s[12:13]
	ds_read_b128 v[62:65], v53 offset:3856
	v_mov_b32_e32 v35, v34
	s_movk_i32 s12, 0x7fff
	v_mov_b32_e32 v48, v34
	v_mov_b32_e32 v49, v34
	s_waitcnt lgkmcnt(0)
	v_pk_fma_f32 v[36:37], v[34:35], v[36:37], v[62:63] neg_lo:[0,0,1] neg_hi:[0,0,1]
	v_xor_b32_e32 v65, 0x80000000, v65
	v_xor_b32_e32 v64, 0x80000000, v64
	v_pk_fma_f32 v[44:45], v[48:49], v[44:45], v[64:65]
	s_mov_b32 s13, 0xffff0000
	v_cvt_pk_bf16_f32 v36, v36, v37
	v_cvt_pk_bf16_f32 v37, v44, v45
	v_mov_b32_e32 v45, 0
	ds_write_b64 v51, v[36:37] offset:40968
	v_mov_b32_e32 v44, v45
	v_mov_b32_e32 v37, v45
	v_mov_b32_e32 v36, v45
	s_and_saveexec_b64 s[12:13], s[2:3]
	s_cbranch_execz .LBB0_1019
	v_lshlrev_b32_e32 v36, 6, v1
	v_add3_u32 v36, v50, v36, 0
	v_add_u32_e32 v47, 0xf20, v36
	v_mov_b32_e32 v36, 0
	s_mov_b64 s[14:15], 0
	v_mov_b32_e32 v48, v46
	v_mov_b32_e32 v37, v36
	v_mov_b32_e32 v44, v36
	v_mov_b32_e32 v45, v36

.LBB0_1019:
	s_or_b64 exec, exec, s[12:13]
	ds_read_b128 v[62:65], v53 offset:3872
	s_movk_i32 s12, 0x7fff
	v_mov_b32_e32 v48, v34
	v_mov_b32_e32 v49, v34
	s_mov_b32 s13, 0xffff0000
	s_waitcnt lgkmcnt(0)
	v_pk_fma_f32 v[36:37], v[34:35], v[36:37], v[62:63] neg_lo:[0,0,1] neg_hi:[0,0,1]
	v_xor_b32_e32 v65, 0x80000000, v65
	v_xor_b32_e32 v64, 0x80000000, v64
	v_pk_fma_f32 v[44:45], v[48:49], v[44:45], v[64:65]
	v_cvt_pk_bf16_f32 v36, v36, v37
	v_cvt_pk_bf16_f32 v37, v44, v45
	v_mov_b32_e32 v45, 0
	ds_write_b64 v51, v[36:37] offset:40976
	v_mov_b32_e32 v44, v45
	v_mov_b32_e32 v37, v45
	v_mov_b32_e32 v36, v45
	s_and_saveexec_b64 s[12:13], s[2:3]
	s_cbranch_execz .LBB0_1023
	v_lshlrev_b32_e32 v36, 6, v1
	v_add3_u32 v36, v50, v36, 0
	v_add_u32_e32 v47, 0xf30, v36
	v_mov_b32_e32 v36, 0
	s_mov_b64 s[14:15], 0
	v_mov_b32_e32 v37, v36
	v_mov_b32_e32 v44, v36
	v_mov_b32_e32 v45, v36

.LBB0_1023:
	s_or_b64 exec, exec, s[12:13]
	ds_read_b128 v[46:49], v53 offset:3888
	v_mov_b32_e32 v62, v34
	v_mov_b32_e32 v63, v34
	s_movk_i32 s12, 0x7fff
	s_mov_b32 s13, 0xffff0000
	s_waitcnt lgkmcnt(0)
	v_xor_b32_e32 v49, 0x80000000, v49
	v_xor_b32_e32 v48, 0x80000000, v48
	v_pk_fma_f32 v[34:35], v[34:35], v[36:37], v[46:47] neg_lo:[0,0,1] neg_hi:[0,0,1]
	v_pk_fma_f32 v[36:37], v[62:63], v[44:45], v[48:49]
	v_cvt_pk_bf16_f32 v34, v34, v35
	v_cvt_pk_bf16_f32 v35, v36, v37
	ds_write_b64 v51, v[34:35] offset:40984
	s_waitcnt lgkmcnt(0)
	s_barrier
	ds_read_b128 v[34:37], v55 offset:40960
	ds_read_b128 v[44:47], v55 offset:41024
	s_waitcnt vmcnt(11) lgkmcnt(1)
	v_mfma_f32_16x16x32_bf16 v[18:21], v[18:21], v[34:37], 0
	s_waitcnt vmcnt(9)
	v_mfma_f32_16x16x32_bf16 v[22:25], v[22:25], v[34:37], 0
	s_waitcnt vmcnt(7)
	v_mfma_f32_16x16x32_bf16 v[26:29], v[26:29], v[34:37], 0
	s_waitcnt vmcnt(5)
	v_mfma_f32_16x16x32_bf16 v[30:33], v[30:33], v[34:37], 0
	s_waitcnt lgkmcnt(0)
	v_mfma_f32_16x16x32_bf16 v[14:17], v[14:17], v[44:47], v[18:21]
	v_mfma_f32_16x16x32_bf16 v[10:13], v[10:13], v[44:47], v[22:25]
	v_mfma_f32_16x16x32_bf16 v[6:9], v[6:9], v[44:47], v[26:29]
	s_waitcnt vmcnt(0)
	s_nop 4
	v_pk_mul_f32 v[16:17], v[16:17], v[102:103]
	v_pk_mul_f32 v[14:15], v[14:15], v[100:101]
	v_cvt_pk_bf16_f32 v14, v14, v15
	v_cvt_pk_bf16_f32 v15, v16, v17
	global_store_dwordx2 v[38:39], v[14:15], off offset:640
	v_mfma_f32_16x16x32_bf16 v[2:5], v[2:5], v[44:47], v[30:33]
	v_pk_mul_f32 v[12:13], v[12:13], v[106:107]
	v_pk_mul_f32 v[10:11], v[10:11], v[104:105]
	v_cvt_pk_bf16_f32 v10, v10, v11
	v_cvt_pk_bf16_f32 v11, v12, v13
	global_store_dwordx2 v[38:39], v[10:11], off offset:672
	v_pk_mul_f32 v[8:9], v[8:9], v[110:111]
	v_pk_mul_f32 v[6:7], v[6:7], v[108:109]
	v_cvt_pk_bf16_f32 v6, v6, v7
	v_cvt_pk_bf16_f32 v7, v8, v9
	global_store_dwordx2 v[38:39], v[6:7], off offset:704
	v_pk_mul_f32 v[4:5], v[4:5], v[114:115]
	v_pk_mul_f32 v[2:3], v[2:3], v[112:113]
	v_cvt_pk_bf16_f32 v2, v2, v3
	v_cvt_pk_bf16_f32 v3, v4, v5
	global_store_dwordx2 v[38:39], v[2:3], off offset:736
	s_barrier
	v_lshlrev_b32_e32 v180, 16, v142
	v_and_b32_e32 v181, 0xffff0000, v142
	v_lshlrev_b32_e32 v182, 16, v143
	v_and_b32_e32 v183, 0xffff0000, v143
	v_lshlrev_b32_e32 v184, 16, v144
	v_and_b32_e32 v185, 0xffff0000, v144
	v_lshlrev_b32_e32 v186, 16, v145
	v_and_b32_e32 v187, 0xffff0000, v145
	v_lshlrev_b32_e32 v188, 16, v146
	v_and_b32_e32 v189, 0xffff0000, v146
	v_lshlrev_b32_e32 v190, 16, v147
	v_and_b32_e32 v191, 0xffff0000, v147
	v_lshlrev_b32_e32 v192, 16, v148
	v_and_b32_e32 v193, 0xffff0000, v148
	v_lshlrev_b32_e32 v194, 16, v149
	v_and_b32_e32 v195, 0xffff0000, v149
	v_lshlrev_b32_e32 v196, 16, v150
	v_and_b32_e32 v197, 0xffff0000, v150
	v_lshlrev_b32_e32 v198, 16, v151
	v_and_b32_e32 v199, 0xffff0000, v151
	v_lshlrev_b32_e32 v200, 16, v152
	v_and_b32_e32 v201, 0xffff0000, v152
	v_lshlrev_b32_e32 v202, 16, v153
	v_and_b32_e32 v203, 0xffff0000, v153
	ds_write_b128 v204, v[180:183]
	ds_write_b128 v204, v[184:187] offset:16
	ds_write_b128 v204, v[188:191] offset:16384
	ds_write_b128 v204, v[192:195] offset:16400
	s_mov_b64 s[98:99], exec
	v_cmp_gt_u32_e32 vcc, 0x78, v52
	s_and_b64 exec, s[98:99], vcc
	ds_write_b128 v204, v[196:199] offset:32768
	ds_write_b128 v204, v[200:203] offset:32784
	s_mov_b64 exec, s[98:99]
	v_add_co_u32_e32 v2, vcc, 0x4000, v42
	s_nop 1
	v_addc_co_u32_e32 v3, vcc, 0, v43, vcc
	v_add_co_u32_e32 v34, vcc, 0x5000, v42
	global_load_dwordx4 v[18:21], v[2:3], off
	global_load_dwordx4 v[14:17], v[2:3], off offset:64
	global_load_dwordx4 v[22:25], v[2:3], off offset:2048
	global_load_dwordx4 v[10:13], v[2:3], off offset:2112
	v_addc_co_u32_e32 v35, vcc, 0, v43, vcc
	global_load_dwordx4 v[26:29], v[34:35], off
	global_load_dwordx4 v[6:9], v[34:35], off offset:64
	global_load_dwordx4 v[30:33], v[34:35], off offset:2048
	global_load_dwordx4 v[2:5], v[34:35], off offset:2112
	global_load_dwordx4 v[100:103], v[40:41], off offset:1536
	global_load_dwordx4 v[104:107], v[40:41], off offset:1600
	global_load_dwordx4 v[108:111], v[40:41], off offset:1664
	global_load_dwordx4 v[112:115], v[40:41], off offset:1728
	s_waitcnt lgkmcnt(0)
	s_barrier
	s_and_saveexec_b64 s[12:13], s[8:9]
	s_xor_b64 s[12:13], exec, s[12:13]
	ds_read_b128 v[34:37], v53 offset:3840
	s_or_saveexec_b64 s[12:13], s[12:13]
	v_lshl_add_u32 v59, v59, 2, 0
	v_add_u32_e32 v44, 15, v58
	v_mov_b32_e32 v46, 0
	v_lshl_add_u32 v58, v44, 8, v59
	v_mov_b32_e32 v47, 0
	v_mov_b32_e32 v48, 0
	v_mov_b32_e32 v49, 0
	s_xor_b64 exec, exec, s[12:13]
	s_cbranch_execz .LBB0_1046
	s_waitcnt lgkmcnt(0)
	ds_read_b128 v[34:37], v58
	s_waitcnt lgkmcnt(0)
	v_pk_add_f32 v[48:49], v[36:37], 0 op_sel_hi:[1,0]
	v_pk_add_f32 v[46:47], v[34:35], 0 op_sel_hi:[1,0]
	s_and_saveexec_b64 s[14:15], s[6:7]
	s_cbranch_execz .LBB0_1045
	v_add_u32_e32 v44, v59, v50
	ds_read_b128 v[62:65], v44 offset:3584
	v_cmp_ne_u32_e32 vcc, 2, v60
	s_waitcnt lgkmcnt(0)
	v_pk_add_f32 v[48:49], v[48:49], v[64:65]
	v_pk_add_f32 v[46:47], v[46:47], v[62:63]
	s_and_saveexec_b64 s[16:17], vcc
	s_cbranch_execz .LBB0_1044
	ds_read_b128 v[62:65], v44 offset:3328
	v_cmp_ne_u32_e32 vcc, 3, v60
	s_waitcnt lgkmcnt(0)
	v_pk_add_f32 v[48:49], v[48:49], v[64:65]
	v_pk_add_f32 v[46:47], v[46:47], v[62:63]
	s_and_saveexec_b64 s[18:19], vcc
	s_cbranch_execz .LBB0_1043
	ds_read_b128 v[62:65], v44 offset:3072
	v_cmp_ne_u32_e32 vcc, 4, v60
	s_waitcnt lgkmcnt(0)
	v_pk_add_f32 v[48:49], v[48:49], v[64:65]
	v_pk_add_f32 v[46:47], v[46:47], v[62:63]
	s_and_saveexec_b64 s[20:21], vcc
	s_cbranch_execz .LBB0_1042
	ds_read_b128 v[62:65], v44 offset:2816
	v_cmp_ne_u32_e32 vcc, 5, v60
	s_waitcnt lgkmcnt(0)
	v_pk_add_f32 v[48:49], v[48:49], v[64:65]
	v_pk_add_f32 v[46:47], v[46:47], v[62:63]
	s_and_saveexec_b64 s[22:23], vcc
	s_cbranch_execz .LBB0_1041
	ds_read_b128 v[62:65], v44 offset:2560
	v_cmp_ne_u32_e32 vcc, 6, v60
	s_waitcnt lgkmcnt(0)
	v_pk_add_f32 v[48:49], v[48:49], v[64:65]
	v_pk_add_f32 v[46:47], v[46:47], v[62:63]
	s_and_saveexec_b64 s[24:25], vcc
	s_cbranch_execz .LBB0_1040
	ds_read_b128 v[62:65], v44 offset:2304
	v_cmp_ne_u32_e32 vcc, 7, v60
	s_waitcnt lgkmcnt(0)
	v_pk_add_f32 v[48:49], v[48:49], v[64:65]
	v_pk_add_f32 v[46:47], v[46:47], v[62:63]
	s_and_saveexec_b64 s[26:27], vcc
	s_cbranch_execz .LBB0_1039
	ds_read_b128 v[62:65], v44 offset:2048
	s_waitcnt lgkmcnt(0)
	v_pk_add_f32 v[48:49], v[48:49], v[64:65]
	v_pk_add_f32 v[46:47], v[46:47], v[62:63]

.LBB0_1046:
	s_or_b64 exec, exec, s[12:13]
	v_min_i32_e32 v44, 8, v56
	v_cvt_f32_i32_e32 v44, v44
	s_waitcnt lgkmcnt(0)
	v_xor_b32_e32 v37, 0x80000000, v37
	v_xor_b32_e32 v36, 0x80000000, v36
	v_div_scale_f32 v45, s[12:13], v44, v44, 1.0
	v_rcp_f32_e32 v61, v45
	v_div_scale_f32 v62, vcc, 1.0, v44, 1.0
	s_movk_i32 s12, 0x7fff
	v_fma_f32 v63, -v45, v61, 1.0
	v_fmac_f32_e32 v61, v63, v61
	v_mul_f32_e32 v63, v62, v61
	v_fma_f32 v64, -v45, v63, v62
	v_fmac_f32_e32 v63, v64, v61
	v_fma_f32 v45, -v45, v63, v62
	v_div_fmas_f32 v45, v45, v61, v63
	v_div_fixup_f32 v44, v45, v44, 1.0
	v_pk_fma_f32 v[34:35], v[44:45], v[46:47], v[34:35] op_sel_hi:[0,1,1] neg_lo:[0,0,1] neg_hi:[0,0,1]
	v_pk_fma_f32 v[36:37], v[44:45], v[48:49], v[36:37] op_sel_hi:[0,1,1]
	s_mov_b32 s13, 0xffff0000
	v_cvt_pk_bf16_f32 v34, v34, v35
	v_cvt_pk_bf16_f32 v35, v36, v37
	ds_write_b64 v51, v[34:35] offset:40960
	s_and_saveexec_b64 s[12:13], s[8:9]
	s_xor_b64 s[12:13], exec, s[12:13]
	ds_read_b128 v[34:37], v53 offset:3856
	s_or_saveexec_b64 s[12:13], s[12:13]
	v_mov_b32_e32 v45, v44
	v_mov_b32_e32 v46, 0
	v_mov_b32_e32 v47, 0
	v_mov_b32_e32 v48, 0
	v_mov_b32_e32 v49, 0
	s_xor_b64 exec, exec, s[12:13]
	s_cbranch_execz .LBB0_1064
	s_waitcnt lgkmcnt(0)
	ds_read_b128 v[34:37], v58 offset:16
	s_waitcnt lgkmcnt(0)
	v_pk_add_f32 v[48:49], v[36:37], 0 op_sel_hi:[1,0]
	v_pk_add_f32 v[46:47], v[34:35], 0 op_sel_hi:[1,0]
	s_and_saveexec_b64 s[14:15], s[6:7]
	s_cbranch_execz .LBB0_1063
	v_add_u32_e32 v61, v59, v50
	ds_read_b128 v[62:65], v61 offset:3600
	v_cmp_ne_u32_e32 vcc, 2, v60
	s_waitcnt lgkmcnt(0)
	v_pk_add_f32 v[48:49], v[48:49], v[64:65]
	v_pk_add_f32 v[46:47], v[46:47], v[62:63]
	s_and_saveexec_b64 s[16:17], vcc
	s_cbranch_execz .LBB0_1062
	ds_read_b128 v[62:65], v61 offset:3344
	v_cmp_ne_u32_e32 vcc, 3, v60
	s_waitcnt lgkmcnt(0)
	v_pk_add_f32 v[48:49], v[48:49], v[64:65]
	v_pk_add_f32 v[46:47], v[46:47], v[62:63]
	s_and_saveexec_b64 s[18:19], vcc
	s_cbranch_execz .LBB0_1061
	ds_read_b128 v[62:65], v61 offset:3088
	v_cmp_ne_u32_e32 vcc, 4, v60
	s_waitcnt lgkmcnt(0)
	v_pk_add_f32 v[48:49], v[48:49], v[64:65]
	v_pk_add_f32 v[46:47], v[46:47], v[62:63]
	s_and_saveexec_b64 s[20:21], vcc
	s_cbranch_execz .LBB0_1060
	ds_read_b128 v[62:65], v61 offset:2832
	v_cmp_ne_u32_e32 vcc, 5, v60
	s_waitcnt lgkmcnt(0)
	v_pk_add_f32 v[48:49], v[48:49], v[64:65]
	v_pk_add_f32 v[46:47], v[46:47], v[62:63]
	s_and_saveexec_b64 s[22:23], vcc
	s_cbranch_execz .LBB0_1059
	ds_read_b128 v[62:65], v61 offset:2576
	v_cmp_ne_u32_e32 vcc, 6, v60
	s_waitcnt lgkmcnt(0)
	v_pk_add_f32 v[48:49], v[48:49], v[64:65]
	v_pk_add_f32 v[46:47], v[46:47], v[62:63]
	s_and_saveexec_b64 s[24:25], vcc
	s_cbranch_execz .LBB0_1058
	ds_read_b128 v[62:65], v61 offset:2320
	v_cmp_ne_u32_e32 vcc, 7, v60
	s_waitcnt lgkmcnt(0)
	v_pk_add_f32 v[48:49], v[48:49], v[64:65]
	v_pk_add_f32 v[46:47], v[46:47], v[62:63]
	s_and_saveexec_b64 s[26:27], vcc
	s_cbranch_execz .LBB0_1057
	ds_read_b128 v[62:65], v61 offset:2064
	s_waitcnt lgkmcnt(0)
	v_pk_add_f32 v[48:49], v[48:49], v[64:65]
	v_pk_add_f32 v[46:47], v[46:47], v[62:63]

.LBB0_1064:
	s_or_b64 exec, exec, s[12:13]
	s_waitcnt lgkmcnt(0)
	v_pk_fma_f32 v[34:35], v[44:45], v[46:47], v[34:35] neg_lo:[0,0,1] neg_hi:[0,0,1]
	s_movk_i32 s12, 0x7fff
	v_xor_b32_e32 v37, 0x80000000, v37
	v_xor_b32_e32 v36, 0x80000000, v36
	v_mov_b32_e32 v62, v44
	v_mov_b32_e32 v63, v44
	v_pk_fma_f32 v[36:37], v[62:63], v[48:49], v[36:37]
	s_mov_b32 s13, 0xffff0000
	v_cvt_pk_bf16_f32 v34, v34, v35
	v_cvt_pk_bf16_f32 v35, v36, v37
	ds_write_b64 v51, v[34:35] offset:40968
	s_and_saveexec_b64 s[12:13], s[8:9]
	s_xor_b64 s[12:13], exec, s[12:13]
	ds_read_b128 v[34:37], v53 offset:3872
	s_or_saveexec_b64 s[12:13], s[12:13]
	v_mov_b32_e32 v46, 0
	v_mov_b32_e32 v47, 0
	v_mov_b32_e32 v48, 0
	v_mov_b32_e32 v49, 0
	s_xor_b64 exec, exec, s[12:13]
	s_cbranch_execz .LBB0_1082
	s_waitcnt lgkmcnt(0)
	ds_read_b128 v[34:37], v58 offset:32
	s_waitcnt lgkmcnt(0)
	v_pk_add_f32 v[48:49], v[36:37], 0 op_sel_hi:[1,0]
	v_pk_add_f32 v[46:47], v[34:35], 0 op_sel_hi:[1,0]
	s_and_saveexec_b64 s[14:15], s[6:7]
	s_cbranch_execz .LBB0_1081
	v_add_u32_e32 v61, v59, v50
	ds_read_b128 v[62:65], v61 offset:3616
	v_cmp_ne_u32_e32 vcc, 2, v60
	s_waitcnt lgkmcnt(0)
	v_pk_add_f32 v[48:49], v[48:49], v[64:65]
	v_pk_add_f32 v[46:47], v[46:47], v[62:63]
	s_and_saveexec_b64 s[16:17], vcc
	s_cbranch_execz .LBB0_1080
	ds_read_b128 v[62:65], v61 offset:3360
	v_cmp_ne_u32_e32 vcc, 3, v60
	s_waitcnt lgkmcnt(0)
	v_pk_add_f32 v[48:49], v[48:49], v[64:65]
	v_pk_add_f32 v[46:47], v[46:47], v[62:63]
	s_and_saveexec_b64 s[18:19], vcc
	s_cbranch_execz .LBB0_1079
	ds_read_b128 v[62:65], v61 offset:3104
	v_cmp_ne_u32_e32 vcc, 4, v60
	s_waitcnt lgkmcnt(0)
	v_pk_add_f32 v[48:49], v[48:49], v[64:65]
	v_pk_add_f32 v[46:47], v[46:47], v[62:63]
	s_and_saveexec_b64 s[20:21], vcc
	s_cbranch_execz .LBB0_1078
	ds_read_b128 v[62:65], v61 offset:2848
	v_cmp_ne_u32_e32 vcc, 5, v60
	s_waitcnt lgkmcnt(0)
	v_pk_add_f32 v[48:49], v[48:49], v[64:65]
	v_pk_add_f32 v[46:47], v[46:47], v[62:63]
	s_and_saveexec_b64 s[22:23], vcc
	s_cbranch_execz .LBB0_1077
	ds_read_b128 v[62:65], v61 offset:2592
	v_cmp_ne_u32_e32 vcc, 6, v60
	s_waitcnt lgkmcnt(0)
	v_pk_add_f32 v[48:49], v[48:49], v[64:65]
	v_pk_add_f32 v[46:47], v[46:47], v[62:63]
	s_and_saveexec_b64 s[24:25], vcc
	s_cbranch_execz .LBB0_1076
	ds_read_b128 v[62:65], v61 offset:2336
	v_cmp_ne_u32_e32 vcc, 7, v60
	s_waitcnt lgkmcnt(0)
	v_pk_add_f32 v[48:49], v[48:49], v[64:65]
	v_pk_add_f32 v[46:47], v[46:47], v[62:63]
	s_and_saveexec_b64 s[26:27], vcc
	s_cbranch_execz .LBB0_1075
	ds_read_b128 v[62:65], v61 offset:2080
	s_waitcnt lgkmcnt(0)
	v_pk_add_f32 v[48:49], v[48:49], v[64:65]
	v_pk_add_f32 v[46:47], v[46:47], v[62:63]

.LBB0_1082:
	s_or_b64 exec, exec, s[12:13]
	s_waitcnt lgkmcnt(0)
	v_pk_fma_f32 v[34:35], v[44:45], v[46:47], v[34:35] neg_lo:[0,0,1] neg_hi:[0,0,1]
	s_movk_i32 s12, 0x7fff
	v_xor_b32_e32 v37, 0x80000000, v37
	v_xor_b32_e32 v36, 0x80000000, v36
	v_mov_b32_e32 v62, v44
	v_mov_b32_e32 v63, v44
	v_pk_fma_f32 v[36:37], v[62:63], v[48:49], v[36:37]
	s_mov_b32 s13, 0xffff0000
	v_cvt_pk_bf16_f32 v34, v34, v35
	v_cvt_pk_bf16_f32 v35, v36, v37
	ds_write_b64 v51, v[34:35] offset:40976
	s_and_saveexec_b64 s[12:13], s[8:9]
	s_xor_b64 s[8:9], exec, s[12:13]
	ds_read_b128 v[34:37], v53 offset:3888
	s_or_saveexec_b64 s[8:9], s[8:9]
	v_mov_b32_e32 v46, 0
	v_mov_b32_e32 v47, 0
	v_mov_b32_e32 v48, 0
	v_mov_b32_e32 v49, 0
	s_xor_b64 exec, exec, s[8:9]
	s_cbranch_execz .LBB0_1100
	s_waitcnt lgkmcnt(0)
	ds_read_b128 v[34:37], v58 offset:48
	s_waitcnt lgkmcnt(0)
	v_pk_add_f32 v[48:49], v[36:37], 0 op_sel_hi:[1,0]
	v_pk_add_f32 v[46:47], v[34:35], 0 op_sel_hi:[1,0]
	s_and_saveexec_b64 s[12:13], s[6:7]
	s_cbranch_execz .LBB0_1099
	v_add_u32_e32 v58, v59, v50
	ds_read_b128 v[62:65], v58 offset:3632
	v_cmp_ne_u32_e32 vcc, 2, v60
	s_waitcnt lgkmcnt(0)
	v_pk_add_f32 v[48:49], v[48:49], v[64:65]
	v_pk_add_f32 v[46:47], v[46:47], v[62:63]
	s_and_saveexec_b64 s[6:7], vcc
	s_cbranch_execz .LBB0_1098
	ds_read_b128 v[62:65], v58 offset:3376
	v_cmp_ne_u32_e32 vcc, 3, v60
	s_waitcnt lgkmcnt(0)
	v_pk_add_f32 v[48:49], v[48:49], v[64:65]
	v_pk_add_f32 v[46:47], v[46:47], v[62:63]
	s_and_saveexec_b64 s[14:15], vcc
	s_cbranch_execz .LBB0_1097
	ds_read_b128 v[62:65], v58 offset:3120
	v_cmp_ne_u32_e32 vcc, 4, v60
	s_waitcnt lgkmcnt(0)
	v_pk_add_f32 v[48:49], v[48:49], v[64:65]
	v_pk_add_f32 v[46:47], v[46:47], v[62:63]
	s_and_saveexec_b64 s[16:17], vcc
	s_cbranch_execz .LBB0_1096
	ds_read_b128 v[62:65], v58 offset:2864
	v_cmp_ne_u32_e32 vcc, 5, v60
	s_waitcnt lgkmcnt(0)
	v_pk_add_f32 v[48:49], v[48:49], v[64:65]
	v_pk_add_f32 v[46:47], v[46:47], v[62:63]
	s_and_saveexec_b64 s[18:19], vcc
	s_cbranch_execz .LBB0_1095
	ds_read_b128 v[62:65], v58 offset:2608
	v_cmp_ne_u32_e32 vcc, 6, v60
	s_waitcnt lgkmcnt(0)
	v_pk_add_f32 v[48:49], v[48:49], v[64:65]
	v_pk_add_f32 v[46:47], v[46:47], v[62:63]
	s_and_saveexec_b64 s[20:21], vcc
	s_cbranch_execz .LBB0_1094
	ds_read_b128 v[62:65], v58 offset:2352
	v_cmp_ne_u32_e32 vcc, 7, v60
	s_waitcnt lgkmcnt(0)
	v_pk_add_f32 v[48:49], v[48:49], v[64:65]
	v_pk_add_f32 v[46:47], v[46:47], v[62:63]
	s_and_saveexec_b64 s[22:23], vcc
	s_cbranch_execz .LBB0_1093
	ds_read_b128 v[62:65], v58 offset:2096
	s_waitcnt lgkmcnt(0)
	v_pk_add_f32 v[48:49], v[48:49], v[64:65]
	v_pk_add_f32 v[46:47], v[46:47], v[62:63]

.LBB0_1100:
	s_or_b64 exec, exec, s[8:9]
	s_waitcnt lgkmcnt(0)
	v_pk_fma_f32 v[34:35], v[44:45], v[46:47], v[34:35] neg_lo:[0,0,1] neg_hi:[0,0,1]
	v_mov_b32_e32 v58, v44
	v_mov_b32_e32 v59, v44
	s_movk_i32 s6, 0x7fff
	v_xor_b32_e32 v37, 0x80000000, v37
	v_xor_b32_e32 v36, 0x80000000, v36
	v_pk_fma_f32 v[36:37], v[58:59], v[48:49], v[36:37]
	s_mov_b32 s7, 0xffff0000
	v_cvt_pk_bf16_f32 v34, v34, v35
	v_cvt_pk_bf16_f32 v35, v36, v37
	ds_write_b64 v51, v[34:35] offset:40984
	s_waitcnt lgkmcnt(0)
	s_barrier
	ds_read_b128 v[34:37], v55 offset:40960
	ds_read_b128 v[44:47], v55 offset:41024
	s_waitcnt vmcnt(11) lgkmcnt(1)
	v_mfma_f32_16x16x32_bf16 v[18:21], v[18:21], v[34:37], 0
	s_waitcnt vmcnt(9)
	v_mfma_f32_16x16x32_bf16 v[22:25], v[22:25], v[34:37], 0
	s_waitcnt vmcnt(7)
	v_mfma_f32_16x16x32_bf16 v[26:29], v[26:29], v[34:37], 0
	s_waitcnt vmcnt(5)
	v_mfma_f32_16x16x32_bf16 v[30:33], v[30:33], v[34:37], 0
	s_waitcnt lgkmcnt(0)
	v_mfma_f32_16x16x32_bf16 v[14:17], v[14:17], v[44:47], v[18:21]
	v_mfma_f32_16x16x32_bf16 v[10:13], v[10:13], v[44:47], v[22:25]
	v_mfma_f32_16x16x32_bf16 v[6:9], v[6:9], v[44:47], v[26:29]
	s_waitcnt vmcnt(0)
	s_nop 4
	v_pk_mul_f32 v[16:17], v[16:17], v[102:103]
	v_pk_mul_f32 v[14:15], v[14:15], v[100:101]
	v_cvt_pk_bf16_f32 v14, v14, v15
	v_cvt_pk_bf16_f32 v15, v16, v17
	global_store_dwordx2 v[38:39], v[14:15], off offset:768
	v_mfma_f32_16x16x32_bf16 v[2:5], v[2:5], v[44:47], v[30:33]
	v_pk_mul_f32 v[12:13], v[12:13], v[106:107]
	v_pk_mul_f32 v[10:11], v[10:11], v[104:105]
	v_cvt_pk_bf16_f32 v10, v10, v11
	v_cvt_pk_bf16_f32 v11, v12, v13
	global_store_dwordx2 v[38:39], v[10:11], off offset:800
	v_pk_mul_f32 v[8:9], v[8:9], v[110:111]
	v_pk_mul_f32 v[6:7], v[6:7], v[108:109]
	v_cvt_pk_bf16_f32 v6, v6, v7
	v_cvt_pk_bf16_f32 v7, v8, v9
	global_store_dwordx2 v[38:39], v[6:7], off offset:832
	v_pk_mul_f32 v[4:5], v[4:5], v[114:115]
	v_pk_mul_f32 v[2:3], v[2:3], v[112:113]
	v_cvt_pk_bf16_f32 v2, v2, v3
	v_cvt_pk_bf16_f32 v3, v4, v5
	global_store_dwordx2 v[38:39], v[2:3], off offset:864
	s_barrier
	v_lshlrev_b32_e32 v180, 16, v154
	v_and_b32_e32 v181, 0xffff0000, v154
	v_lshlrev_b32_e32 v182, 16, v155
	v_and_b32_e32 v183, 0xffff0000, v155
	v_lshlrev_b32_e32 v184, 16, v156
	v_and_b32_e32 v185, 0xffff0000, v156
	v_lshlrev_b32_e32 v186, 16, v157
	v_and_b32_e32 v187, 0xffff0000, v157
	v_lshlrev_b32_e32 v188, 16, v158
	v_and_b32_e32 v189, 0xffff0000, v158
	v_lshlrev_b32_e32 v190, 16, v159
	v_and_b32_e32 v191, 0xffff0000, v159
	v_lshlrev_b32_e32 v192, 16, v160
	v_and_b32_e32 v193, 0xffff0000, v160
	v_lshlrev_b32_e32 v194, 16, v161
	v_and_b32_e32 v195, 0xffff0000, v161
	v_lshlrev_b32_e32 v196, 16, v162
	v_and_b32_e32 v197, 0xffff0000, v162
	v_lshlrev_b32_e32 v198, 16, v163
	v_and_b32_e32 v199, 0xffff0000, v163
	v_lshlrev_b32_e32 v200, 16, v164
	v_and_b32_e32 v201, 0xffff0000, v164
	v_lshlrev_b32_e32 v202, 16, v165
	v_and_b32_e32 v203, 0xffff0000, v165
	ds_write_b128 v204, v[180:183]
	ds_write_b128 v204, v[184:187] offset:16
	ds_write_b128 v204, v[188:191] offset:16384
	ds_write_b128 v204, v[192:195] offset:16400
	s_mov_b64 s[98:99], exec
	v_cmp_gt_u32_e32 vcc, 0x78, v52
	s_and_b64 exec, s[98:99], vcc
	ds_write_b128 v204, v[196:199] offset:32768
	ds_write_b128 v204, v[200:203] offset:32784
	s_mov_b64 exec, s[98:99]
	v_add_co_u32_e32 v2, vcc, 0x6000, v42
	v_min_u32_e32 v44, 16, v60
	s_nop 0
	v_addc_co_u32_e32 v3, vcc, 0, v43, vcc
	v_add_co_u32_e32 v34, vcc, 0x7000, v42
	global_load_dwordx4 v[18:21], v[2:3], off
	global_load_dwordx4 v[14:17], v[2:3], off offset:64
	global_load_dwordx4 v[22:25], v[2:3], off offset:2048
	global_load_dwordx4 v[10:13], v[2:3], off offset:2112
	v_addc_co_u32_e32 v35, vcc, 0, v43, vcc
	global_load_dwordx4 v[26:29], v[34:35], off
	global_load_dwordx4 v[6:9], v[34:35], off offset:64
	global_load_dwordx4 v[30:33], v[34:35], off offset:2048
	global_load_dwordx4 v[2:5], v[34:35], off offset:2112
	global_load_dwordx4 v[100:103], v[40:41], off offset:1792
	global_load_dwordx4 v[104:107], v[40:41], off offset:1856
	global_load_dwordx4 v[108:111], v[40:41], off offset:1920
	global_load_dwordx4 v[112:115], v[40:41], off offset:1984
	v_mov_b32_e32 v43, 0
	v_mov_b32_e32 v42, 0
	v_mov_b32_e32 v37, 0
	v_mov_b32_e32 v36, 0
	s_waitcnt lgkmcnt(0)
	s_barrier
	s_and_saveexec_b64 s[0:1], s[2:3]
	s_cbranch_execz .LBB0_1115
	v_mov_b32_e32 v36, 0
	v_cmp_lt_i32_e32 vcc, 6, v54
	s_mov_b32 s8, 0
	v_mov_b32_e32 v37, v36
	v_mov_b32_e32 v42, v36
	v_mov_b32_e32 v43, v36
	v_mov_b32_e32 v34, v36
	s_and_saveexec_b64 s[4:5], vcc
	s_cbranch_execz .LBB0_1110
	v_lshlrev_b32_e32 v35, 6, v1
	v_add3_u32 v35, v50, v35, 0
	v_mov_b32_e32 v36, 0
	v_and_b32_e32 v34, 24, v44
	v_add_u32_e32 v35, 0x800, v35
	s_mov_b64 s[6:7], 0
	v_mov_b32_e32 v37, v36
	v_mov_b32_e32 v42, v36
	v_mov_b32_e32 v43, v36

.LBB0_1145:
	s_or_b64 exec, exec, s[0:1]
	ds_read_b128 v[44:47], v53 offset:3888
	v_mov_b32_e32 v48, v34
	v_mov_b32_e32 v49, v34
	s_movk_i32 s0, 0x7fff
	s_mov_b32 s1, 0xffff0000
	s_waitcnt lgkmcnt(0)
	v_pk_fma_f32 v[34:35], v[34:35], v[36:37], v[44:45] neg_lo:[0,0,1] neg_hi:[0,0,1]
	v_xor_b32_e32 v47, 0x80000000, v47
	v_xor_b32_e32 v46, 0x80000000, v46
	v_pk_fma_f32 v[36:37], v[48:49], v[42:43], v[46:47]
	v_cvt_pk_bf16_f32 v34, v34, v35
	v_cvt_pk_bf16_f32 v35, v36, v37
	ds_write_b64 v51, v[34:35] offset:40984
	s_waitcnt lgkmcnt(0)
	s_barrier
	ds_read_b128 v[34:37], v55 offset:40960
	ds_read_b128 v[42:45], v55 offset:41024
	s_waitcnt vmcnt(11) lgkmcnt(1)
	v_mfma_f32_16x16x32_bf16 v[18:21], v[18:21], v[34:37], 0
	s_mov_b32 s3, 0
	s_waitcnt vmcnt(9)
	v_mfma_f32_16x16x32_bf16 v[22:25], v[22:25], v[34:37], 0
	s_waitcnt vmcnt(7)
	v_mfma_f32_16x16x32_bf16 v[26:29], v[26:29], v[34:37], 0
	s_waitcnt vmcnt(5)
	v_mfma_f32_16x16x32_bf16 v[30:33], v[30:33], v[34:37], 0
	s_waitcnt lgkmcnt(0)
	v_mfma_f32_16x16x32_bf16 v[14:17], v[14:17], v[42:45], v[18:21]
	v_mfma_f32_16x16x32_bf16 v[10:13], v[10:13], v[42:45], v[22:25]
	v_mfma_f32_16x16x32_bf16 v[6:9], v[6:9], v[42:45], v[26:29]
	s_waitcnt vmcnt(0)
	s_nop 4
	v_pk_mul_f32 v[16:17], v[16:17], v[102:103]
	v_pk_mul_f32 v[14:15], v[14:15], v[100:101]
	v_bfe_u32 v19, v16, 16, 1
	v_bfe_u32 v1, v14, 16, 1
	v_bfe_u32 v18, v15, 16, 1
	v_bfe_u32 v20, v17, 16, 1
	v_add3_u32 v1, v14, v1, s0
	v_add3_u32 v14, v15, v18, s0
	v_add3_u32 v15, v16, v19, s0
	v_add3_u32 v16, v17, v20, s0
	v_lshrrev_b32_e32 v1, 16, v1
	v_lshrrev_b32_e32 v15, 16, v15
	v_and_or_b32 v14, v14, s1, v1
	v_and_or_b32 v15, v16, s1, v15
	global_store_dwordx2 v[38:39], v[14:15], off offset:896
	v_mfma_f32_16x16x32_bf16 v[2:5], v[2:5], v[42:45], v[30:33]
	v_pk_mul_f32 v[12:13], v[12:13], v[106:107]
	v_pk_mul_f32 v[10:11], v[10:11], v[104:105]
	v_bfe_u32 v15, v12, 16, 1
	v_bfe_u32 v1, v10, 16, 1
	v_bfe_u32 v14, v11, 16, 1
	v_bfe_u32 v16, v13, 16, 1
	v_add3_u32 v1, v10, v1, s0
	v_add3_u32 v10, v11, v14, s0
	v_add3_u32 v11, v12, v15, s0
	v_add3_u32 v12, v13, v16, s0
	v_lshrrev_b32_e32 v1, 16, v1
	v_lshrrev_b32_e32 v11, 16, v11
	v_and_or_b32 v10, v10, s1, v1
	v_and_or_b32 v11, v12, s1, v11
	global_store_dwordx2 v[38:39], v[10:11], off offset:928
	v_pk_mul_f32 v[8:9], v[8:9], v[110:111]
	v_pk_mul_f32 v[6:7], v[6:7], v[108:109]
	v_bfe_u32 v11, v8, 16, 1
	v_bfe_u32 v1, v6, 16, 1
	v_bfe_u32 v10, v7, 16, 1
	v_bfe_u32 v12, v9, 16, 1
	v_add3_u32 v1, v6, v1, s0
	v_add3_u32 v6, v7, v10, s0
	v_add3_u32 v7, v8, v11, s0
	v_add3_u32 v8, v9, v12, s0
	v_lshrrev_b32_e32 v1, 16, v1
	v_lshrrev_b32_e32 v7, 16, v7
	v_and_or_b32 v6, v6, s1, v1
	v_and_or_b32 v7, v8, s1, v7
	global_store_dwordx2 v[38:39], v[6:7], off offset:960
	v_pk_mul_f32 v[4:5], v[4:5], v[114:115]
	v_pk_mul_f32 v[2:3], v[2:3], v[112:113]
	v_bfe_u32 v7, v4, 16, 1
	v_bfe_u32 v1, v2, 16, 1
	v_bfe_u32 v6, v3, 16, 1
	v_bfe_u32 v8, v5, 16, 1
	v_add3_u32 v1, v2, v1, s0
	v_add3_u32 v2, v3, v6, s0
	v_add3_u32 v3, v4, v7, s0
	v_add3_u32 v4, v5, v8, s0
	v_lshrrev_b32_e32 v1, 16, v1
	v_lshrrev_b32_e32 v3, 16, v3
	v_and_or_b32 v2, v2, s1, v1
	v_and_or_b32 v3, v4, s1, v3
	global_store_dwordx2 v[38:39], v[2:3], off offset:992
	s_barrier
	s_waitcnt vmcnt(0)
	s_barrier
	s_mov_b64 s[0:1], exec
	v_readlane_b32 s4, v254, 2
	v_readlane_b32 s5, v254, 3
	s_and_b64 s[4:5], s[0:1], s[4:5]
	s_mov_b64 exec, s[4:5]
	s_cbranch_execz .LBB0_1197
	s_mov_b32 s2, 0
	s_lshl_b64 s[2:3], s[2:3], 2
	v_readlane_b32 s4, v254, 0
	v_readlane_b32 s5, v254, 1
	s_add_u32 s2, s4, s2
	s_addc_u32 s3, s5, s3
	s_add_i32 s4, 0, 0x20160
	v_mov_b32_e32 v1, s4
	s_waitcnt vmcnt(0) expcnt(0) lgkmcnt(0)
	ds_read_b32 v3, v1
	s_add_i32 s4, 0, 0x20164
	v_mov_b32_e32 v1, s4
	ds_read_b32 v1, v1
	s_waitcnt lgkmcnt(1)
	v_cmp_ne_u32_e32 vcc, 0, v3
	s_cbranch_vccnz .LBB0_1161
	v_readlane_b32 s8, v254, 20
	v_readlane_b32 s9, v254, 21
	s_load_dword s6, s[8:9], 0x14
	s_load_dwordx2 s[4:5], s[8:9], 0x4
	s_mov_b32 s19, 1
	v_mov_b32_e32 v17, 0
	s_waitcnt lgkmcnt(0)
	s_lshr_b32 s8, s6, 16
	s_and_b32 s6, s6, 0xffff
	s_cmp_lg_u32 s6, 0
	s_cselect_b64 s[6:7], -1, 0
	s_cmp_lg_u64 s[6:7], 0
	s_addc_u32 s4, s4, 0
	v_readlane_b32 s6, v254, 22
	s_cmp_lg_u32 s8, 0
	s_mul_i32 s18, s4, s6
	s_cselect_b64 s[6:7], -1, 0
	s_cmp_lg_u64 s[6:7], 0
	s_addc_u32 s4, s5, 0
	s_mul_i32 s18, s18, s4
	s_add_u32 s4, s2, 0x1000
	s_addc_u32 s5, s3, 0
	s_add_u32 s6, s2, 0x1100
	s_addc_u32 s7, s3, 0
	s_add_u32 s8, s2, 0x1200
	s_addc_u32 s9, s3, 0
	s_add_u32 s10, s2, 0x1300
	s_addc_u32 s11, s3, 0
	s_branch .LBB0_1149

.LBB0_1208:
	v_lshl_add_u32 v146, s29, 8, v152
	s_lshl_b32 s18, s43, 8
	s_ashr_i32 s19, s18, 31
	v_ashrrev_i32_e32 v147, 31, v146
	v_lshl_add_u64 v[144:145], s[18:19], 1, v[138:139]
	v_lshlrev_b64 v[148:149], 11, v[146:147]
	v_lshl_add_u64 v[150:151], v[144:145], 0, v[148:149]
	global_load_dwordx4 v[156:159], v[150:151], off
	global_load_dwordx4 v[160:163], v[150:151], off offset:256
	v_or_b32_e32 v148, 16, v146
	v_ashrrev_i32_e32 v149, 31, v148
	v_lshlrev_b64 v[148:149], 11, v[148:149]
	v_lshl_add_u64 v[148:149], v[144:145], 0, v[148:149]
	global_load_dwordx4 v[164:167], v[148:149], off
	global_load_dwordx4 v[168:171], v[148:149], off offset:256
	v_or_b32_e32 v172, 32, v146
	s_and_b64 vcc, exec, s[2:3]
	s_mov_b64 s[2:3], -1
	s_waitcnt vmcnt(0)
	v_lshlrev_b32_e32 v174, 16, v156
	v_and_b32_e32 v175, 0xffff0000, v156
	v_lshlrev_b32_e32 v156, 16, v157
	v_and_b32_e32 v157, 0xffff0000, v157
	v_lshlrev_b32_e32 v176, 16, v158
	v_and_b32_e32 v177, 0xffff0000, v158
	v_lshlrev_b32_e32 v158, 16, v159
	v_and_b32_e32 v159, 0xffff0000, v159
	v_lshlrev_b32_e32 v178, 16, v160
	v_and_b32_e32 v179, 0xffff0000, v160
	v_lshlrev_b32_e32 v160, 16, v161
	v_and_b32_e32 v161, 0xffff0000, v161
	v_lshlrev_b32_e32 v180, 16, v162
	v_and_b32_e32 v181, 0xffff0000, v162
	v_lshlrev_b32_e32 v162, 16, v163
	v_and_b32_e32 v163, 0xffff0000, v163
	v_pk_fma_f32 v[128:129], v[156:157], s[12:13], v[128:129] op_sel_hi:[1,0,1]
	v_pk_fma_f32 v[126:127], v[174:175], s[12:13], v[126:127] op_sel_hi:[1,0,1]
	v_pk_fma_f32 v[124:125], v[158:159], s[12:13], v[124:125] op_sel_hi:[1,0,1]
	v_pk_fma_f32 v[122:123], v[176:177], s[12:13], v[122:123] op_sel_hi:[1,0,1]
	v_pk_fma_f32 v[120:121], v[160:161], s[12:13], v[120:121] op_sel_hi:[1,0,1]
	v_pk_fma_f32 v[118:119], v[178:179], s[12:13], v[118:119] op_sel_hi:[1,0,1]
	v_pk_fma_f32 v[116:117], v[162:163], s[12:13], v[116:117] op_sel_hi:[1,0,1]
	v_pk_fma_f32 v[114:115], v[180:181], s[12:13], v[114:115] op_sel_hi:[1,0,1]
	v_bfe_u32 v147, v126, 16, 1
	v_bfe_u32 v158, v128, 16, 1
	v_bfe_u32 v157, v127, 16, 1
	v_bfe_u32 v159, v129, 16, 1
	v_bfe_u32 v173, v118, 16, 1
	v_bfe_u32 v175, v120, 16, 1
	v_bfe_u32 v177, v114, 16, 1
	v_bfe_u32 v178, v115, 16, 1
	v_bfe_u32 v179, v116, 16, 1
	v_bfe_u32 v180, v117, 16, 1
	v_add3_u32 v126, v126, v147, s39
	v_add3_u32 v128, v128, v158, s39
	v_bfe_u32 v174, v119, 16, 1
	v_bfe_u32 v176, v121, 16, 1
	v_add3_u32 v127, v127, v157, s39
	v_add3_u32 v129, v129, v159, s39
	v_add3_u32 v118, v118, v173, s39
	v_add3_u32 v120, v120, v175, s39
	v_add3_u32 v114, v114, v177, s39
	v_add3_u32 v147, v115, v178, s39
	v_add3_u32 v115, v116, v179, s39
	v_add3_u32 v157, v117, v180, s39
	v_lshrrev_b32_e32 v116, 16, v126
	v_lshrrev_b32_e32 v117, 16, v128
	v_add3_u32 v119, v119, v174, s39
	v_add3_u32 v121, v121, v176, s39
	v_lshrrev_b32_e32 v118, 16, v118
	v_lshrrev_b32_e32 v120, 16, v120
	v_lshrrev_b32_e32 v126, 16, v114
	v_lshrrev_b32_e32 v128, 16, v115
	v_and_or_b32 v114, v127, s38, v116
	v_and_or_b32 v115, v129, s38, v117
	v_cvt_pk_bf16_f32 v116, v122, v123
	v_cvt_pk_bf16_f32 v117, v124, v125
	v_ashrrev_i32_e32 v173, 31, v172
	v_and_or_b32 v118, v119, s38, v118
	v_and_or_b32 v119, v121, s38, v120
	v_and_or_b32 v120, v147, s38, v126
	v_and_or_b32 v121, v157, s38, v128
	global_store_dwordx4 v[150:151], v[114:117], off
	global_store_dwordx4 v[150:151], v[118:121], off offset:256
	v_lshlrev_b32_e32 v156, 16, v164
	v_lshlrev_b64 v[114:115], 11, v[172:173]
	v_lshl_add_u64 v[114:115], v[144:145], 0, v[114:115]
	global_load_dwordx4 v[116:119], v[114:115], off
	global_load_dwordx4 v[120:123], v[114:115], off offset:256
	v_and_b32_e32 v157, 0xffff0000, v164
	v_lshlrev_b32_e32 v124, 16, v165
	v_and_b32_e32 v125, 0xffff0000, v165
	v_lshlrev_b32_e32 v126, 16, v166
	v_and_b32_e32 v127, 0xffff0000, v166
	v_lshlrev_b32_e32 v128, 16, v167
	v_and_b32_e32 v129, 0xffff0000, v167
	v_pk_fma_f32 v[110:111], v[156:157], s[12:13], v[110:111] op_sel_hi:[1,0,1]
	v_pk_fma_f32 v[112:113], v[124:125], s[12:13], v[112:113] op_sel_hi:[1,0,1]
	v_pk_fma_f32 v[124:125], v[128:129], s[12:13], v[108:109] op_sel_hi:[1,0,1]
	v_pk_fma_f32 v[108:109], v[126:127], s[12:13], v[106:107] op_sel_hi:[1,0,1]
	v_cvt_pk_bf16_f32 v106, v110, v111
	v_cvt_pk_bf16_f32 v107, v112, v113
	v_cvt_pk_bf16_f32 v108, v108, v109
	v_lshlrev_b32_e32 v150, 16, v168
	v_and_b32_e32 v151, 0xffff0000, v168
	v_lshlrev_b32_e32 v162, 16, v171
	v_and_b32_e32 v163, 0xffff0000, v171
	v_cvt_pk_bf16_f32 v109, v124, v125
	v_pk_fma_f32 v[102:103], v[150:151], s[12:13], v[102:103] op_sel_hi:[1,0,1]
	global_store_dwordx4 v[148:149], v[106:109], off
	v_lshlrev_b32_e32 v158, 16, v169
	v_and_b32_e32 v159, 0xffff0000, v169
	v_pk_fma_f32 v[108:109], v[162:163], s[12:13], v[100:101] op_sel_hi:[1,0,1]
	v_pk_fma_f32 v[104:105], v[158:159], s[12:13], v[104:105] op_sel_hi:[1,0,1]
	v_cvt_pk_bf16_f32 v100, v102, v103
	v_lshlrev_b32_e32 v160, 16, v170
	v_and_b32_e32 v161, 0xffff0000, v170
	v_pk_fma_f32 v[98:99], v[160:161], s[12:13], v[98:99] op_sel_hi:[1,0,1]
	v_cvt_pk_bf16_f32 v101, v104, v105
	v_cvt_pk_bf16_f32 v102, v98, v99
	v_bfe_u32 v98, v108, 16, 1
	v_add3_u32 v98, v108, v98, s39
	v_lshrrev_b32_e32 v103, 16, v98
	v_or_b32_e32 v98, 48, v146
	v_ashrrev_i32_e32 v99, 31, v98
	v_lshlrev_b64 v[98:99], 11, v[98:99]
	v_lshl_add_u64 v[98:99], v[144:145], 0, v[98:99]
	global_load_dwordx4 v[104:107], v[98:99], off
	v_bfe_u32 v108, v109, 16, 1
	v_add3_u32 v108, v109, v108, s39
	v_and_or_b32 v103, v108, s38, v103
	global_store_dwordx4 v[148:149], v[100:103], off offset:256
	global_load_dwordx4 v[100:103], v[98:99], off offset:256
	s_waitcnt vmcnt(5)
	v_lshlrev_b32_e32 v108, 16, v116
	v_and_b32_e32 v109, 0xffff0000, v116
	v_lshlrev_b32_e32 v110, 16, v117
	v_and_b32_e32 v111, 0xffff0000, v117
	v_lshlrev_b32_e32 v112, 16, v118
	v_and_b32_e32 v113, 0xffff0000, v118
	v_lshlrev_b32_e32 v116, 16, v119
	v_and_b32_e32 v117, 0xffff0000, v119
	v_pk_fma_f32 v[94:95], v[108:109], s[12:13], v[94:95] op_sel_hi:[1,0,1]
	v_pk_fma_f32 v[108:109], v[116:117], s[12:13], v[92:93] op_sel_hi:[1,0,1]
	v_pk_fma_f32 v[92:93], v[112:113], s[12:13], v[90:91] op_sel_hi:[1,0,1]
	v_pk_fma_f32 v[96:97], v[110:111], s[12:13], v[96:97] op_sel_hi:[1,0,1]
	v_cvt_pk_bf16_f32 v90, v94, v95
	v_cvt_pk_bf16_f32 v91, v96, v97
	v_cvt_pk_bf16_f32 v92, v92, v93
	s_waitcnt vmcnt(4)
	v_lshlrev_b32_e32 v118, 16, v120
	v_and_b32_e32 v119, 0xffff0000, v120
	v_lshlrev_b32_e32 v124, 16, v122
	v_and_b32_e32 v125, 0xffff0000, v122
	v_lshlrev_b32_e32 v122, 16, v123
	v_and_b32_e32 v123, 0xffff0000, v123
	v_cvt_pk_bf16_f32 v93, v108, v109
	v_pk_fma_f32 v[86:87], v[118:119], s[12:13], v[86:87] op_sel_hi:[1,0,1]
	global_store_dwordx4 v[114:115], v[90:93], off
	v_lshlrev_b32_e32 v120, 16, v121
	v_and_b32_e32 v121, 0xffff0000, v121
	v_pk_fma_f32 v[90:91], v[122:123], s[12:13], v[84:85] op_sel_hi:[1,0,1]
	v_pk_fma_f32 v[84:85], v[124:125], s[12:13], v[82:83] op_sel_hi:[1,0,1]
	v_pk_fma_f32 v[88:89], v[120:121], s[12:13], v[88:89] op_sel_hi:[1,0,1]
	v_cvt_pk_bf16_f32 v82, v86, v87
	v_cvt_pk_bf16_f32 v83, v88, v89
	v_cvt_pk_bf16_f32 v84, v84, v85
	v_cvt_pk_bf16_f32 v85, v90, v91
	global_store_dwordx4 v[114:115], v[82:85], off offset:256
	s_waitcnt vmcnt(4)
	v_lshlrev_b32_e32 v92, 16, v104
	v_and_b32_e32 v93, 0xffff0000, v104
	v_add_u32_e32 v82, 0x80, v146
	v_ashrrev_i32_e32 v83, 31, v82
	v_lshlrev_b64 v[82:83], 11, v[82:83]
	v_lshl_add_u64 v[82:83], v[144:145], 0, v[82:83]
	global_load_dwordx4 v[84:87], v[82:83], off
	global_load_dwordx4 v[88:91], v[82:83], off offset:256
	v_lshlrev_b32_e32 v94, 16, v105
	v_and_b32_e32 v95, 0xffff0000, v105
	v_lshlrev_b32_e32 v96, 16, v106
	v_and_b32_e32 v97, 0xffff0000, v106
	v_lshlrev_b32_e32 v104, 16, v107
	v_and_b32_e32 v105, 0xffff0000, v107
	v_pk_fma_f32 v[78:79], v[92:93], s[12:13], v[78:79] op_sel_hi:[1,0,1]
	v_pk_fma_f32 v[92:93], v[104:105], s[12:13], v[76:77] op_sel_hi:[1,0,1]
	v_pk_fma_f32 v[76:77], v[96:97], s[12:13], v[74:75] op_sel_hi:[1,0,1]
	v_pk_fma_f32 v[80:81], v[94:95], s[12:13], v[80:81] op_sel_hi:[1,0,1]
	v_cvt_pk_bf16_f32 v74, v78, v79
	v_cvt_pk_bf16_f32 v75, v80, v81
	v_cvt_pk_bf16_f32 v76, v76, v77
	s_waitcnt vmcnt(4)
	v_lshlrev_b32_e32 v106, 16, v100
	v_and_b32_e32 v107, 0xffff0000, v100
	v_lshlrev_b32_e32 v108, 16, v102
	v_and_b32_e32 v109, 0xffff0000, v102
	v_lshlrev_b32_e32 v102, 16, v103
	v_and_b32_e32 v103, 0xffff0000, v103
	v_cvt_pk_bf16_f32 v77, v92, v93
	v_pk_fma_f32 v[70:71], v[106:107], s[12:13], v[70:71] op_sel_hi:[1,0,1]
	global_store_dwordx4 v[98:99], v[74:77], off
	v_lshlrev_b32_e32 v100, 16, v101
	v_and_b32_e32 v101, 0xffff0000, v101
	v_pk_fma_f32 v[76:77], v[102:103], s[12:13], v[68:69] op_sel_hi:[1,0,1]
	v_pk_fma_f32 v[72:73], v[100:101], s[12:13], v[72:73] op_sel_hi:[1,0,1]
	v_cvt_pk_bf16_f32 v68, v70, v71
	v_pk_fma_f32 v[66:67], v[108:109], s[12:13], v[66:67] op_sel_hi:[1,0,1]
	v_cvt_pk_bf16_f32 v69, v72, v73
	v_cvt_pk_bf16_f32 v70, v66, v67
	v_bfe_u32 v66, v76, 16, 1
	v_add3_u32 v66, v76, v66, s39
	v_lshrrev_b32_e32 v71, 16, v66
	v_add_u32_e32 v66, 0x90, v146
	v_ashrrev_i32_e32 v67, 31, v66
	v_lshlrev_b64 v[66:67], 11, v[66:67]
	v_lshl_add_u64 v[66:67], v[144:145], 0, v[66:67]
	global_load_dwordx4 v[72:75], v[66:67], off
	v_bfe_u32 v76, v77, 16, 1
	v_add3_u32 v76, v77, v76, s39
	v_and_or_b32 v71, v76, s38, v71
	global_store_dwordx4 v[98:99], v[68:71], off offset:256
	global_load_dwordx4 v[68:71], v[66:67], off offset:256
	s_waitcnt vmcnt(5)
	v_lshlrev_b32_e32 v76, 16, v84
	v_and_b32_e32 v77, 0xffff0000, v84
	v_lshlrev_b32_e32 v78, 16, v85
	v_and_b32_e32 v79, 0xffff0000, v85
	v_lshlrev_b32_e32 v80, 16, v86
	v_and_b32_e32 v81, 0xffff0000, v86
	v_lshlrev_b32_e32 v84, 16, v87
	v_and_b32_e32 v85, 0xffff0000, v87
	v_pk_fma_f32 v[62:63], v[76:77], s[12:13], v[62:63] op_sel_hi:[1,0,1]
	v_pk_fma_f32 v[76:77], v[84:85], s[12:13], v[60:61] op_sel_hi:[1,0,1]
	v_pk_fma_f32 v[60:61], v[80:81], s[12:13], v[58:59] op_sel_hi:[1,0,1]
	v_pk_fma_f32 v[64:65], v[78:79], s[12:13], v[64:65] op_sel_hi:[1,0,1]
	v_cvt_pk_bf16_f32 v58, v62, v63
	v_cvt_pk_bf16_f32 v59, v64, v65
	v_cvt_pk_bf16_f32 v60, v60, v61
	s_waitcnt vmcnt(4)
	v_lshlrev_b32_e32 v86, 16, v88
	v_and_b32_e32 v87, 0xffff0000, v88
	v_lshlrev_b32_e32 v92, 16, v90
	v_and_b32_e32 v93, 0xffff0000, v90
	v_lshlrev_b32_e32 v90, 16, v91
	v_and_b32_e32 v91, 0xffff0000, v91
	v_cvt_pk_bf16_f32 v61, v76, v77
	v_pk_fma_f32 v[54:55], v[86:87], s[12:13], v[54:55] op_sel_hi:[1,0,1]
	global_store_dwordx4 v[82:83], v[58:61], off
	v_lshlrev_b32_e32 v88, 16, v89
	v_and_b32_e32 v89, 0xffff0000, v89
	v_pk_fma_f32 v[58:59], v[90:91], s[12:13], v[52:53] op_sel_hi:[1,0,1]
	v_pk_fma_f32 v[52:53], v[92:93], s[12:13], v[50:51] op_sel_hi:[1,0,1]
	v_pk_fma_f32 v[56:57], v[88:89], s[12:13], v[56:57] op_sel_hi:[1,0,1]
	v_cvt_pk_bf16_f32 v50, v54, v55
	v_cvt_pk_bf16_f32 v51, v56, v57
	v_cvt_pk_bf16_f32 v52, v52, v53
	v_cvt_pk_bf16_f32 v53, v58, v59
	global_store_dwordx4 v[82:83], v[50:53], off offset:256
	s_waitcnt vmcnt(4)
	v_lshlrev_b32_e32 v60, 16, v72
	v_and_b32_e32 v61, 0xffff0000, v72
	v_add_u32_e32 v50, 0xa0, v146
	v_ashrrev_i32_e32 v51, 31, v50
	v_lshlrev_b64 v[50:51], 11, v[50:51]
	v_lshl_add_u64 v[50:51], v[144:145], 0, v[50:51]
	global_load_dwordx4 v[52:55], v[50:51], off
	global_load_dwordx4 v[56:59], v[50:51], off offset:256
	v_lshlrev_b32_e32 v62, 16, v73
	v_and_b32_e32 v63, 0xffff0000, v73
	v_lshlrev_b32_e32 v64, 16, v74
	v_and_b32_e32 v65, 0xffff0000, v74
	v_lshlrev_b32_e32 v72, 16, v75
	v_and_b32_e32 v73, 0xffff0000, v75
	v_pk_fma_f32 v[46:47], v[60:61], s[12:13], v[46:47] op_sel_hi:[1,0,1]
	v_pk_fma_f32 v[60:61], v[72:73], s[12:13], v[44:45] op_sel_hi:[1,0,1]
	v_pk_fma_f32 v[44:45], v[64:65], s[12:13], v[42:43] op_sel_hi:[1,0,1]
	v_pk_fma_f32 v[48:49], v[62:63], s[12:13], v[48:49] op_sel_hi:[1,0,1]
	v_cvt_pk_bf16_f32 v42, v46, v47
	v_cvt_pk_bf16_f32 v43, v48, v49
	v_cvt_pk_bf16_f32 v44, v44, v45
	s_waitcnt vmcnt(4)
	v_lshlrev_b32_e32 v74, 16, v68
	v_and_b32_e32 v75, 0xffff0000, v68
	v_lshlrev_b32_e32 v76, 16, v70
	v_and_b32_e32 v77, 0xffff0000, v70
	v_lshlrev_b32_e32 v70, 16, v71
	v_and_b32_e32 v71, 0xffff0000, v71
	v_cvt_pk_bf16_f32 v45, v60, v61
	v_pk_fma_f32 v[38:39], v[74:75], s[12:13], v[38:39] op_sel_hi:[1,0,1]
	global_store_dwordx4 v[66:67], v[42:45], off
	v_lshlrev_b32_e32 v68, 16, v69
	v_and_b32_e32 v69, 0xffff0000, v69
	v_pk_fma_f32 v[42:43], v[70:71], s[12:13], v[36:37] op_sel_hi:[1,0,1]
	v_pk_fma_f32 v[36:37], v[76:77], s[12:13], v[34:35] op_sel_hi:[1,0,1]
	v_pk_fma_f32 v[40:41], v[68:69], s[12:13], v[40:41] op_sel_hi:[1,0,1]
	v_cvt_pk_bf16_f32 v34, v38, v39
	v_cvt_pk_bf16_f32 v35, v40, v41
	v_bfe_u32 v38, v36, 16, 1
	v_add3_u32 v36, v36, v38, s39
	v_bfe_u32 v38, v37, 16, 1
	v_add3_u32 v37, v37, v38, s39
	v_add_u32_e32 v38, 0xb0, v146
	v_ashrrev_i32_e32 v39, 31, v38
	v_lshlrev_b64 v[38:39], 11, v[38:39]
	v_lshl_add_u64 v[44:45], v[144:145], 0, v[38:39]
	global_load_dwordx4 v[38:41], v[44:45], off
	v_lshrrev_b32_e32 v36, 16, v36
	v_and_or_b32 v36, v37, s38, v36
	v_cvt_pk_bf16_f32 v37, v42, v43
	global_store_dwordx4 v[66:67], v[34:37], off offset:256
	global_load_dwordx4 v[34:37], v[44:45], off offset:256
	s_waitcnt vmcnt(5)
	v_lshlrev_b32_e32 v42, 16, v52
	v_and_b32_e32 v43, 0xffff0000, v52
	v_lshlrev_b32_e32 v46, 16, v53
	v_and_b32_e32 v47, 0xffff0000, v53
	v_lshlrev_b32_e32 v48, 16, v54
	v_and_b32_e32 v49, 0xffff0000, v54
	v_lshlrev_b32_e32 v52, 16, v55
	v_and_b32_e32 v53, 0xffff0000, v55
	v_pk_fma_f32 v[30:31], v[42:43], s[12:13], v[30:31] op_sel_hi:[1,0,1]
	v_pk_fma_f32 v[42:43], v[52:53], s[12:13], v[28:29] op_sel_hi:[1,0,1]
	v_pk_fma_f32 v[28:29], v[48:49], s[12:13], v[26:27] op_sel_hi:[1,0,1]
	v_pk_fma_f32 v[32:33], v[46:47], s[12:13], v[32:33] op_sel_hi:[1,0,1]
	v_cvt_pk_bf16_f32 v26, v30, v31
	v_cvt_pk_bf16_f32 v27, v32, v33
	v_cvt_pk_bf16_f32 v28, v28, v29
	s_waitcnt vmcnt(4)
	v_lshlrev_b32_e32 v54, 16, v56
	v_and_b32_e32 v55, 0xffff0000, v56
	v_lshlrev_b32_e32 v60, 16, v58
	v_and_b32_e32 v61, 0xffff0000, v58
	v_lshlrev_b32_e32 v58, 16, v59
	v_and_b32_e32 v59, 0xffff0000, v59
	v_cvt_pk_bf16_f32 v29, v42, v43
	v_pk_fma_f32 v[22:23], v[54:55], s[12:13], v[22:23] op_sel_hi:[1,0,1]
	global_store_dwordx4 v[50:51], v[26:29], off
	v_lshlrev_b32_e32 v56, 16, v57
	v_and_b32_e32 v57, 0xffff0000, v57
	v_pk_fma_f32 v[26:27], v[58:59], s[12:13], v[20:21] op_sel_hi:[1,0,1]
	v_pk_fma_f32 v[20:21], v[60:61], s[12:13], v[18:19] op_sel_hi:[1,0,1]
	v_pk_fma_f32 v[24:25], v[56:57], s[12:13], v[24:25] op_sel_hi:[1,0,1]
	v_cvt_pk_bf16_f32 v18, v22, v23
	v_cvt_pk_bf16_f32 v19, v24, v25
	v_cvt_pk_bf16_f32 v20, v20, v21
	v_cvt_pk_bf16_f32 v21, v26, v27
	global_store_dwordx4 v[50:51], v[18:21], off offset:256
	s_waitcnt vmcnt(4)
	v_lshlrev_b32_e32 v22, 16, v40
	v_and_b32_e32 v23, 0xffff0000, v40
	v_lshlrev_b32_e32 v18, 16, v38
	v_and_b32_e32 v19, 0xffff0000, v38
	v_lshlrev_b32_e32 v24, 16, v41
	v_and_b32_e32 v25, 0xffff0000, v41
	v_pk_fma_f32 v[14:15], v[18:19], s[12:13], v[14:15] op_sel_hi:[1,0,1]
	v_pk_fma_f32 v[18:19], v[24:25], s[12:13], v[12:13] op_sel_hi:[1,0,1]
	v_pk_fma_f32 v[12:13], v[22:23], s[12:13], v[10:11] op_sel_hi:[1,0,1]
	v_lshlrev_b32_e32 v20, 16, v39
	v_and_b32_e32 v21, 0xffff0000, v39
	v_pk_fma_f32 v[16:17], v[20:21], s[12:13], v[16:17] op_sel_hi:[1,0,1]
	v_cvt_pk_bf16_f32 v10, v14, v15
	v_cvt_pk_bf16_f32 v11, v16, v17
	v_cvt_pk_bf16_f32 v12, v12, v13
	s_waitcnt vmcnt(2)
	v_lshlrev_b32_e32 v26, 16, v34
	v_and_b32_e32 v27, 0xffff0000, v34
	v_lshlrev_b32_e32 v30, 16, v36
	v_and_b32_e32 v31, 0xffff0000, v36
	v_lshlrev_b32_e32 v32, 16, v37
	v_and_b32_e32 v33, 0xffff0000, v37
	v_cvt_pk_bf16_f32 v13, v18, v19
	v_pk_fma_f32 v[6:7], v[26:27], s[12:13], v[6:7] op_sel_hi:[1,0,1]
	global_store_dwordx4 v[44:45], v[10:13], off
	v_lshlrev_b32_e32 v28, 16, v35
	v_and_b32_e32 v29, 0xffff0000, v35
	v_pk_fma_f32 v[10:11], v[32:33], s[12:13], v[4:5] op_sel_hi:[1,0,1]
	v_pk_fma_f32 v[4:5], v[30:31], s[12:13], v[2:3] op_sel_hi:[1,0,1]
	v_pk_fma_f32 v[8:9], v[28:29], s[12:13], v[8:9] op_sel_hi:[1,0,1]
	v_cvt_pk_bf16_f32 v2, v6, v7
	v_cvt_pk_bf16_f32 v3, v8, v9
	v_cvt_pk_bf16_f32 v4, v4, v5
	v_cvt_pk_bf16_f32 v5, v10, v11
	global_store_dwordx4 v[44:45], v[2:5], off offset:256
	s_cbranch_vccnz .LBB0_1201
	s_andn2_b64 vcc, exec, s[4:5]
	s_cbranch_vccnz .LBB0_1200
	s_barrier
	s_branch .LBB0_1200

.LBB0_1233:
	s_waitcnt vmcnt(5)
	v_lshlrev_b32_e32 v217, 16, v163
	s_waitcnt lgkmcnt(2)
	v_lshlrev_b32_e32 v216, 16, v162
	v_and_b32_e32 v187, 0xffff0000, v163
	v_and_b32_e32 v186, 0xffff0000, v162
	v_pk_add_f32 v[188:189], v[216:217], v[186:187]
	v_lshlrev_b32_e32 v235, 16, v165
	v_add_f32_e32 v188, v188, v189
	v_add_f32_e32 v233, 0, v188
	v_lshlrev_b32_e32 v234, 16, v164
	v_and_b32_e32 v189, 0xffff0000, v165
	v_and_b32_e32 v188, 0xffff0000, v164
	v_pk_add_f32 v[190:191], v[234:235], v[188:189]
	s_waitcnt vmcnt(4)
	v_lshlrev_b32_e32 v194, 16, v166
	v_and_b32_e32 v195, 0xffff0000, v166
	v_lshlrev_b32_e32 v196, 16, v167
	v_and_b32_e32 v197, 0xffff0000, v167
	v_pk_add_f32 v[190:191], v[190:191], v[190:191] op_sel_hi:[0,1]
	v_lshlrev_b32_e32 v212, 16, v168
	v_and_b32_e32 v214, 0xffff0000, v168
	s_waitcnt lgkmcnt(1)
	v_lshlrev_b32_e32 v218, 16, v169
	s_waitcnt lgkmcnt(0)
	v_and_b32_e32 v232, 0xffff0000, v169
	v_add_f32_e32 v213, v194, v195
	v_add_f32_e32 v215, v196, v197
	v_mov_b32_e32 v219, v191
	v_pk_add_f32 v[192:193], v[212:213], v[214:215]
	v_pk_add_f32 v[190:191], v[218:219], v[232:233]
	s_nop 0
	v_pk_add_f32 v[190:191], v[192:193], v[190:191]
	s_nop 0
	v_add_f32_e32 v190, v190, v191
	s_waitcnt lgkmcnt(0)
	s_nop 1
	v_add_f32_dpp v190, v190, v190 quad_perm:[1,0,3,2] row_mask:0xf bank_mask:0xf
	s_nop 1
	v_add_f32_dpp v190, v190, v190 quad_perm:[2,3,0,1] row_mask:0xf bank_mask:0xf
	s_nop 1
	v_add_f32_dpp v190, v190, v190 row_half_mirror row_mask:0xf bank_mask:0xf
	s_nop 1
	v_add_f32_dpp v190, v190, v190 row_mirror row_mask:0xf bank_mask:0xf
	v_mov_b32_e32 v191, v190
	s_nop 1
	v_permlane16_swap_b32_e32 v190, v191
	v_add_f32_e32 v190, v190, v191
	v_mov_b32_e32 v191, v190
	s_nop 1
	v_permlane32_swap_b32_e32 v190, v191
	v_add_f32_e32 v210, v190, v191
	v_fmac_f32_e32 v186, 0xba800000, v210
	v_fmac_f32_e32 v187, 0xba800000, v210
	v_fmac_f32_e32 v217, 0xba800000, v210
	v_fmac_f32_e32 v216, 0xba800000, v210
	v_mov_b32_e32 v236, v217
	v_mov_b32_e32 v237, v187
	v_mov_b32_e32 v217, v186
	v_pk_mul_f32 v[190:191], v[236:237], v[236:237]
	v_pk_mul_f32 v[186:187], v[216:217], v[216:217]
	v_fmac_f32_e32 v188, 0xba800000, v210
	v_pk_mov_b32 v[192:193], v[186:187], v[190:191] op_sel:[1,0]
	v_mov_b32_e32 v187, v191
	v_fmac_f32_e32 v189, 0xba800000, v210
	v_fmac_f32_e32 v235, 0xba800000, v210
	v_pk_add_f32 v[186:187], v[192:193], v[186:187]
	v_fmac_f32_e32 v234, 0xba800000, v210
	v_mov_b32_e32 v238, v235
	v_mov_b32_e32 v239, v189
	v_mov_b32_e32 v235, v188
	v_pk_add_f32 v[186:187], v[186:187], v[186:187] op_sel_hi:[0,1]
	v_pk_mul_f32 v[190:191], v[238:239], v[238:239]
	v_pk_mul_f32 v[188:189], v[234:235], v[234:235]
	v_fmac_f32_e32 v194, 0xba800000, v210
	v_pk_mov_b32 v[192:193], v[188:189], v[190:191] op_sel:[1,0]
	v_mov_b32_e32 v189, v191
	v_fmac_f32_e32 v195, 0xba800000, v210
	v_fmac_f32_e32 v196, 0xba800000, v210
	v_mul_f32_e32 v186, v194, v194
	v_pk_add_f32 v[188:189], v[192:193], v[188:189]
	v_fmac_f32_e32 v197, 0xba800000, v210
	v_pk_fma_f32 v[190:191], v[194:195], v[194:195], v[186:187] op_sel_hi:[1,1,0]
	v_mul_f32_e32 v186, v196, v196
	v_pk_add_f32 v[188:189], v[188:189], v[188:189] op_sel_hi:[0,1]
	v_pk_fma_f32 v[192:193], v[196:197], v[196:197], v[186:187] op_sel_hi:[1,1,0]
	v_fmac_f32_e32 v232, 0xba800000, v210
	v_fmac_f32_e32 v218, 0xba800000, v210
	v_fmac_f32_e32 v214, 0xba800000, v210
	v_fmac_f32_e32 v212, 0xba800000, v210
	v_mul_f32_e32 v190, v212, v212
	v_mul_f32_e32 v192, v214, v214
	v_mul_f32_e32 v186, v218, v218
	v_mul_f32_e32 v188, v232, v232
	v_pk_add_f32 v[190:191], v[190:191], v[192:193]
	v_pk_add_f32 v[186:187], v[186:187], v[188:189]
	v_lshl_add_u64 v[210:211], s[94:95], 0, v[208:209]
	v_pk_add_f32 v[186:187], v[190:191], v[186:187]
	v_add_co_u32_e32 v190, vcc, 0xca01000, v210
	v_add_f32_e32 v186, v186, v187
	s_waitcnt lgkmcnt(0)
	v_addc_co_u32_e32 v191, vcc, 0, v211, vcc
	s_nop 1
	v_add_f32_dpp v186, v186, v186 quad_perm:[1,0,3,2] row_mask:0xf bank_mask:0xf
	s_nop 1
	v_add_f32_dpp v186, v186, v186 quad_perm:[2,3,0,1] row_mask:0xf bank_mask:0xf
	s_nop 1
	v_add_f32_dpp v186, v186, v186 row_half_mirror row_mask:0xf bank_mask:0xf
	s_nop 1
	v_add_f32_dpp v186, v186, v186 row_mirror row_mask:0xf bank_mask:0xf
	v_mov_b32_e32 v187, v186
	s_nop 1
	v_permlane16_swap_b32_e32 v186, v187
	v_add_f32_e32 v186, v186, v187
	v_mov_b32_e32 v187, v186
	s_nop 1
	v_permlane32_swap_b32_e32 v186, v187
	v_add_f32_e32 v186, v186, v187
	v_fmamk_f32 v186, v186, 0x3a800000, v228
	v_mul_f32_e32 v187, 0x4f800000, v186
	v_cmp_gt_f32_e64 s[0:1], s30, v186
	s_nop 1
	v_cndmask_b32_e64 v186, v186, v187, s[0:1]
	v_sqrt_f32_e32 v187, v186
	s_nop 0
	v_add_u32_e32 v188, -1, v187
	v_fma_f32 v189, -v188, v187, v186
	v_cmp_ge_f32_e64 s[4:5], 0, v189
	v_add_u32_e32 v189, 1, v187
	s_nop 0
	v_cndmask_b32_e64 v188, v187, v188, s[4:5]
	v_fma_f32 v187, -v189, v187, v186
	v_cmp_lt_f32_e64 s[4:5], 0, v187
	s_nop 1
	v_cndmask_b32_e64 v187, v188, v189, s[4:5]
	v_mul_f32_e32 v188, 0x37800000, v187
	v_cndmask_b32_e64 v187, v187, v188, s[0:1]
	v_cmp_class_f32_e64 s[0:1], v186, v229
	s_nop 1
	v_cndmask_b32_e64 v213, v187, v186, s[0:1]
	v_div_scale_f32 v215, s[0:1], v213, v213, 1.0
	v_rcp_f32_e32 v219, v215
	global_load_dwordx4 v[186:189], v[190:191], off offset:2048
	s_nop 0
	global_load_dwordx4 v[190:193], v[190:191], off offset:3072
	v_fma_f32 v233, -v215, v219, 1.0
	v_fmac_f32_e32 v219, v233, v219
	v_div_scale_f32 v233, vcc, 1.0, v213, 1.0
	v_mul_f32_e32 v240, v233, v219
	v_fma_f32 v241, -v215, v240, v233
	v_fmac_f32_e32 v240, v241, v219
	v_fma_f32 v215, -v215, v240, v233
	v_div_fmas_f32 v215, v215, v219, v240
	v_div_fixup_f32 v240, v215, v213, 1.0
	v_pk_mul_f32 v[216:217], v[216:217], v[240:241] op_sel_hi:[1,0]
	v_pk_mul_f32 v[194:195], v[194:195], v[240:241] op_sel_hi:[1,0]
	v_mov_b32_e32 v213, v214
	v_pk_fma_f32 v[242:243], v[2:3], v[216:217], v[6:7]
	v_pk_mul_f32 v[216:217], v[234:235], v[240:241] op_sel_hi:[1,0]
	v_pk_mul_f32 v[196:197], v[196:197], v[240:241] op_sel_hi:[1,0]
	v_pk_fma_f32 v[244:245], v[18:19], v[194:195], v[30:31]
	v_pk_mul_f32 v[194:195], v[212:213], v[240:241] op_sel_hi:[1,0]
	v_mov_b32_e32 v219, v232
	v_pk_mul_f32 v[234:235], v[238:239], v[240:241] op_sel_hi:[1,0]
	v_pk_fma_f32 v[238:239], v[14:15], v[216:217], v[26:27]
	v_pk_fma_f32 v[216:217], v[20:21], v[196:197], v[32:33]
	v_pk_mul_f32 v[196:197], v[218:219], v[240:241] op_sel_hi:[1,0]
	v_pk_fma_f32 v[218:219], v[10:11], v[194:195], v[22:23]
	v_pk_mul_f32 v[236:237], v[236:237], v[240:241] op_sel_hi:[1,0]
	v_pk_fma_f32 v[236:237], v[4:5], v[236:237], v[8:9]
	v_cvt_pk_bf16_f32 v194, v242, v243
	v_bfe_u32 v195, v236, 16, 1
	v_pk_fma_f32 v[214:215], v[12:13], v[196:197], v[24:25]
	v_add3_u32 v195, v236, v195, s31
	v_bfe_u32 v196, v237, 16, 1
	v_lshrrev_b32_e32 v195, 16, v195
	v_add3_u32 v196, v237, v196, s31
	v_and_or_b32 v195, v196, s29, v195
	v_fma_f32 v240, v36, v242, 0
	v_fma_f32 v241, v37, v242, 0
	v_fma_f32 v246, v38, v242, 0
	v_fma_f32 v247, v39, v242, 0
	v_fma_f32 v248, v40, v242, 0
	v_fma_f32 v249, v41, v242, 0
	v_pk_fma_f32 v[232:233], v[34:35], v[242:243], 0 op_sel_hi:[1,0,0]
	v_pk_fma_f32 v[234:235], v[16:17], v[234:235], v[28:29]
	v_fmac_f32_e32 v240, v44, v243
	v_fmac_f32_e32 v241, v45, v243
	v_fmac_f32_e32 v246, v46, v243
	v_fmac_f32_e32 v247, v47, v243
	v_fmac_f32_e32 v248, v48, v243
	v_fmac_f32_e32 v249, v49, v243
	v_pk_fma_f32 v[232:233], v[42:43], v[242:243], v[232:233] op_sel:[0,1,0]
	v_cvt_pk_bf16_f32 v196, v238, v239
	v_fmac_f32_e32 v240, v52, v236
	v_fmac_f32_e32 v241, v53, v236
	v_fmac_f32_e32 v246, v54, v236
	v_fmac_f32_e32 v247, v55, v236
	v_fmac_f32_e32 v248, v56, v236
	v_fmac_f32_e32 v249, v57, v236
	v_pk_fma_f32 v[232:233], v[50:51], v[236:237], v[232:233] op_sel_hi:[1,0,1]
	v_fmac_f32_e32 v240, v60, v237
	v_fmac_f32_e32 v241, v61, v237
	v_fmac_f32_e32 v246, v62, v237
	v_fmac_f32_e32 v247, v63, v237
	v_fmac_f32_e32 v248, v64, v237
	v_fmac_f32_e32 v249, v65, v237
	v_pk_fma_f32 v[232:233], v[58:59], v[236:237], v[232:233] op_sel:[0,1,0]
	v_fmac_f32_e32 v240, v68, v238
	v_fmac_f32_e32 v241, v69, v238
	v_fmac_f32_e32 v246, v70, v238
	v_fmac_f32_e32 v247, v71, v238
	v_fmac_f32_e32 v248, v72, v238
	v_fmac_f32_e32 v249, v73, v238
	v_pk_fma_f32 v[232:233], v[66:67], v[238:239], v[232:233] op_sel_hi:[1,0,1]
	v_cvt_pk_bf16_f32 v197, v234, v235
	v_add_co_u32_e32 v212, vcc, s33, v210
	v_fmac_f32_e32 v240, v76, v239
	v_fmac_f32_e32 v241, v77, v239
	v_fmac_f32_e32 v246, v78, v239
	v_fmac_f32_e32 v247, v79, v239
	v_fmac_f32_e32 v248, v80, v239
	v_fmac_f32_e32 v249, v81, v239
	v_pk_fma_f32 v[232:233], v[74:75], v[238:239], v[232:233] op_sel:[0,1,0]
	v_addc_co_u32_e32 v213, vcc, 0, v211, vcc
	v_fmac_f32_e32 v240, v84, v234
	v_fmac_f32_e32 v241, v85, v234
	v_fmac_f32_e32 v246, v86, v234
	v_fmac_f32_e32 v247, v87, v234
	v_fmac_f32_e32 v248, v88, v234
	v_fmac_f32_e32 v249, v89, v234
	v_pk_fma_f32 v[232:233], v[82:83], v[234:235], v[232:233] op_sel_hi:[1,0,1]
	global_store_dwordx4 v[212:213], v[194:197], off
	v_fmac_f32_e32 v240, v92, v235
	v_fmac_f32_e32 v241, v93, v235
	v_fmac_f32_e32 v246, v94, v235
	v_fmac_f32_e32 v247, v95, v235
	v_fmac_f32_e32 v248, v96, v235
	v_fmac_f32_e32 v249, v97, v235
	v_pk_fma_f32 v[232:233], v[90:91], v[234:235], v[232:233] op_sel:[0,1,0]
	v_fmac_f32_e32 v240, v108, v244
	v_fmac_f32_e32 v241, v109, v244
	v_fmac_f32_e32 v246, v98, v244
	v_fmac_f32_e32 v247, v99, v244
	v_fmac_f32_e32 v248, v100, v244
	v_fmac_f32_e32 v249, v101, v244
	v_pk_fma_f32 v[232:233], v[106:107], v[244:245], v[232:233] op_sel_hi:[1,0,1]
	v_pk_fma_f32 v[232:233], v[102:103], v[244:245], v[232:233] op_sel:[0,1,0]
	v_fmac_f32_e32 v240, v104, v245
	v_fmac_f32_e32 v241, v105, v245
	v_fmac_f32_e32 v246, v110, v245
	v_fmac_f32_e32 v247, v111, v245
	v_fmac_f32_e32 v248, v112, v245
	v_fmac_f32_e32 v249, v113, v245
	v_cvt_pk_bf16_f32 v194, v244, v245
	v_bfe_u32 v195, v216, 16, 1
	v_bfe_u32 v196, v217, 16, 1
	v_fmac_f32_e32 v240, v124, v216
	v_fmac_f32_e32 v241, v125, v216
	v_fmac_f32_e32 v246, v138, v216
	v_fmac_f32_e32 v247, v139, v216
	v_fmac_f32_e32 v248, v140, v216
	v_fmac_f32_e32 v249, v141, v216
	v_pk_fma_f32 v[232:233], v[122:123], v[216:217], v[232:233] op_sel_hi:[1,0,1]
	v_add3_u32 v195, v216, v195, s31
	v_add3_u32 v196, v217, v196, s31
	v_fmac_f32_e32 v240, v116, v217
	v_fmac_f32_e32 v241, v117, v217
	v_fmac_f32_e32 v246, v118, v217
	v_fmac_f32_e32 v247, v119, v217
	v_fmac_f32_e32 v248, v120, v217
	v_fmac_f32_e32 v249, v121, v217
	v_pk_fma_f32 v[216:217], v[114:115], v[216:217], v[232:233] op_sel:[0,1,0]
	v_lshrrev_b32_e32 v195, 16, v195
	v_pk_fma_f32 v[216:217], v[126:127], v[218:219], v[216:217] op_sel_hi:[1,0,1]
	v_and_or_b32 v195, v196, s29, v195
	v_pk_fma_f32 v[216:217], v[134:135], v[218:219], v[216:217] op_sel:[0,1,0]
	v_bfe_u32 v196, v218, 16, 1
	v_pk_fma_f32 v[216:217], v[142:143], v[214:215], v[216:217] op_sel_hi:[1,0,1]
	v_bfe_u32 v197, v219, 16, 1
	v_pk_fma_f32 v[216:217], v[154:155], v[214:215], v[216:217] op_sel:[0,1,0]
	ds_bpermute_b32 v232, v220, v216
	ds_bpermute_b32 v233, v220, v217
	v_fmac_f32_e32 v240, v128, v218
	v_fmac_f32_e32 v241, v129, v218
	v_fmac_f32_e32 v246, v130, v218
	v_fmac_f32_e32 v247, v131, v218
	v_fmac_f32_e32 v248, v132, v218
	v_fmac_f32_e32 v249, v133, v218
	s_waitcnt lgkmcnt(0)
	v_pk_add_f32 v[216:217], v[216:217], v[232:233]
	v_add3_u32 v196, v218, v196, s31
	v_add3_u32 v197, v219, v197, s31
	v_fmac_f32_e32 v240, v136, v219
	v_fmac_f32_e32 v241, v137, v219
	v_fmac_f32_e32 v246, v146, v219
	v_fmac_f32_e32 v247, v147, v219
	v_fmac_f32_e32 v248, v148, v219
	v_fmac_f32_e32 v249, v149, v219
	ds_bpermute_b32 v218, v221, v216
	ds_bpermute_b32 v219, v221, v217
	v_lshrrev_b32_e32 v196, 16, v196
	v_fmac_f32_e32 v240, v144, v214
	v_and_or_b32 v196, v197, s29, v196
	v_bfe_u32 v197, v214, 16, 1
	s_waitcnt lgkmcnt(0)
	v_pk_add_f32 v[216:217], v[216:217], v[218:219]
	v_fmac_f32_e32 v240, v156, v215
	v_add3_u32 v197, v214, v197, s31
	v_fmac_f32_e32 v241, v145, v214
	v_fmac_f32_e32 v246, v150, v214
	v_fmac_f32_e32 v247, v151, v214
	v_fmac_f32_e32 v248, v152, v214
	v_fmac_f32_e32 v249, v153, v214
	ds_bpermute_b32 v218, v222, v216
	ds_bpermute_b32 v219, v222, v217
	ds_bpermute_b32 v214, v220, v240
	v_fmac_f32_e32 v241, v157, v215
	v_fmac_f32_e32 v246, v158, v215
	ds_bpermute_b32 v233, v220, v241
	s_waitcnt lgkmcnt(2)
	v_pk_add_f32 v[216:217], v[216:217], v[218:219]
	s_waitcnt lgkmcnt(1)
	v_add_f32_e32 v214, v240, v214
	ds_bpermute_b32 v218, v223, v216
	ds_bpermute_b32 v219, v223, v217
	ds_bpermute_b32 v232, v221, v214
	ds_bpermute_b32 v234, v220, v246
	v_fmac_f32_e32 v247, v159, v215
	v_fmac_f32_e32 v248, v160, v215
	s_waitcnt lgkmcnt(2)
	v_pk_add_f32 v[216:217], v[216:217], v[218:219]
	s_waitcnt lgkmcnt(1)
	v_add_f32_e32 v214, v214, v232
	ds_bpermute_b32 v218, v224, v216
	ds_bpermute_b32 v219, v224, v217
	ds_bpermute_b32 v232, v222, v214
	v_fmac_f32_e32 v249, v161, v215
	ds_bpermute_b32 v238, v220, v247
	ds_bpermute_b32 v239, v220, v249
	s_waitcnt lgkmcnt(3)
	v_pk_add_f32 v[216:217], v[216:217], v[218:219]
	v_add_f32_e32 v218, v241, v233
	s_waitcnt lgkmcnt(2)
	v_add_f32_e32 v214, v214, v232
	v_add_f32_e32 v232, v246, v234
	ds_bpermute_b32 v219, v221, v218
	ds_bpermute_b32 v233, v221, v232
	ds_bpermute_b32 v234, v223, v214
	s_waitcnt lgkmcnt(4)
	v_add_f32_e32 v238, v247, v238
	s_waitcnt lgkmcnt(3)
	v_add_f32_e32 v239, v249, v239
	s_waitcnt lgkmcnt(2)
	v_add_f32_e32 v219, v218, v219
	s_waitcnt lgkmcnt(1)
	v_add_f32_e32 v232, v232, v233
	ds_bpermute_b32 v235, v222, v219
	ds_bpermute_b32 v233, v222, v232
	s_waitcnt lgkmcnt(2)
	v_add_f32_e32 v214, v214, v234
	ds_bpermute_b32 v236, v224, v214
	ds_bpermute_b32 v240, v221, v238
	s_waitcnt lgkmcnt(3)
	v_add_f32_e32 v234, v219, v235
	s_waitcnt lgkmcnt(2)
	v_add_f32_e32 v232, v232, v233
	ds_bpermute_b32 v235, v223, v234
	ds_bpermute_b32 v233, v223, v232
	s_waitcnt lgkmcnt(3)
	v_add_f32_e32 v214, v214, v236
	ds_bpermute_b32 v242, v221, v239
	s_waitcnt lgkmcnt(3)
	v_add_f32_e32 v238, v238, v240
	s_waitcnt lgkmcnt(2)
	v_add_f32_e32 v234, v234, v235
	s_waitcnt lgkmcnt(1)
	v_add_f32_e32 v236, v232, v233
	ds_bpermute_b32 v235, v224, v234
	ds_bpermute_b32 v237, v224, v236
	s_waitcnt lgkmcnt(2)
	v_add_f32_e32 v239, v239, v242
	ds_bpermute_b32 v240, v222, v238
	ds_bpermute_b32 v242, v222, v239
	s_waitcnt lgkmcnt(3)
	v_add_f32_e32 v233, v234, v235
	s_waitcnt lgkmcnt(2)
	v_add_f32_e32 v235, v236, v237
	ds_bpermute_b32 v237, v220, v248
	s_waitcnt lgkmcnt(2)
	v_add_f32_e32 v238, v238, v240
	s_waitcnt lgkmcnt(1)
	v_add_f32_e32 v239, v239, v242
	ds_bpermute_b32 v240, v223, v238
	ds_bpermute_b32 v242, v223, v239
	s_waitcnt lgkmcnt(2)
	v_add_f32_e32 v237, v248, v237
	ds_bpermute_b32 v241, v221, v237
	ds_bpermute_b32 v218, v225, v216
	s_waitcnt lgkmcnt(3)
	v_add_f32_e32 v238, v238, v240
	s_waitcnt lgkmcnt(2)
	v_add_f32_e32 v242, v239, v242
	ds_bpermute_b32 v240, v224, v238
	s_waitcnt lgkmcnt(2)
	v_add_f32_e32 v237, v237, v241
	ds_bpermute_b32 v241, v222, v237
	ds_bpermute_b32 v244, v224, v242
	ds_bpermute_b32 v219, v225, v217
	ds_bpermute_b32 v232, v225, v214
	ds_bpermute_b32 v234, v225, v233
	s_waitcnt lgkmcnt(4)
	v_add_f32_e32 v237, v237, v241
	ds_bpermute_b32 v241, v223, v237
	ds_bpermute_b32 v236, v225, v235
	v_lshrrev_b32_e32 v197, 16, v197
	s_waitcnt lgkmcnt(1)
	v_add_f32_e32 v241, v237, v241
	ds_bpermute_b32 v243, v224, v241
	v_add_f32_e32 v237, v238, v240
	ds_bpermute_b32 v238, v225, v237
	s_waitcnt lgkmcnt(1)
	v_add_f32_e32 v239, v241, v243
	v_add_f32_e32 v241, v242, v244
	ds_bpermute_b32 v240, v225, v239
	ds_bpermute_b32 v242, v225, v241
	v_bfe_u32 v243, v215, 16, 1
	v_add3_u32 v215, v215, v243, s31
	v_and_or_b32 v197, v215, s29, v197
	global_store_dwordx4 v[212:213], v[194:197], off offset:1024
	s_and_saveexec_b64 s[24:25], s[2:3]
	s_cbranch_execz .LBB0_1235
	v_pk_add_f32 v[196:197], v[216:217], v[218:219]
	v_add_f32_e32 v214, v214, v232
	v_cmp_gt_f32_e32 vcc, v197, v196
	v_add_f32_e32 v233, v233, v234
	v_add_f32_e32 v235, v235, v236
	v_cndmask_b32_e32 v194, v196, v197, vcc
	v_cmp_gt_f32_e64 s[0:1], v214, v194
	s_waitcnt lgkmcnt(2)
	v_add_f32_e32 v237, v237, v238
	s_waitcnt lgkmcnt(1)
	v_add_f32_e32 v215, v239, v240
	v_cndmask_b32_e64 v194, v194, v214, s[0:1]
	v_cmp_gt_f32_e64 s[4:5], v233, v194
	s_waitcnt lgkmcnt(0)
	v_add_f32_e32 v195, v241, v242
	v_cmp_nlg_f32_e64 s[14:15], s34, v196
	v_cndmask_b32_e64 v194, v194, v233, s[4:5]
	v_cmp_gt_f32_e64 s[6:7], v235, v194
	s_nop 1
	v_cndmask_b32_e64 v194, v194, v235, s[6:7]
	v_cmp_gt_f32_e64 s[8:9], v237, v194
	s_nop 1
	v_cndmask_b32_e64 v194, v194, v237, s[8:9]
	v_cmp_gt_f32_e64 s[10:11], v215, v194
	s_nop 1
	v_cndmask_b32_e64 v216, v194, v215, s[10:11]
	v_cndmask_b32_e64 v194, 0, 1, vcc
	v_cndmask_b32_e64 v194, v194, 2, s[0:1]
	v_cndmask_b32_e64 v194, v194, 3, s[4:5]
	v_cndmask_b32_e64 v194, v194, 4, s[6:7]
	v_cndmask_b32_e64 v194, v194, 5, s[8:9]
	v_cndmask_b32_e64 v194, v194, 6, s[10:11]
	v_cmp_ngt_f32_e32 vcc, v195, v216
	s_and_b64 s[16:17], s[10:11], vcc
	s_nop 0
	v_cndmask_b32_e32 v194, 7, v194, vcc
	v_cmp_eq_u32_e64 s[12:13], 0, v194
	s_or_b64 s[12:13], s[12:13], s[14:15]
	v_cmp_ne_u32_e64 s[10:11], 1, v194
	v_cndmask_b32_e64 v196, v196, v231, s[12:13]
	v_cmp_gt_f32_e64 s[14:15], v197, v196
	s_and_b64 s[10:11], s[10:11], s[14:15]
	v_cndmask_b32_e64 v196, v196, v197, s[10:11]
	v_cmp_ne_u32_e64 s[8:9], 2, v194
	v_cmp_gt_f32_e64 s[14:15], v214, v196
	s_and_b64 s[8:9], s[8:9], s[14:15]
	v_cndmask_b32_e64 v196, v196, v214, s[8:9]
	v_cmp_ne_u32_e64 s[6:7], 3, v194
	v_cmp_gt_f32_e64 s[14:15], v233, v196
	s_and_b64 s[6:7], s[6:7], s[14:15]
	v_cndmask_b32_e64 v196, v196, v233, s[6:7]
	v_cmp_ne_u32_e64 s[4:5], 4, v194
	v_cmp_gt_f32_e64 s[14:15], v235, v196
	s_and_b64 s[4:5], s[4:5], s[14:15]
	v_cndmask_b32_e64 v196, v196, v235, s[4:5]
	v_cmp_ne_u32_e64 s[0:1], 5, v194
	v_cmp_gt_f32_e64 s[14:15], v237, v196
	s_and_b64 s[0:1], s[0:1], s[14:15]
	v_cndmask_b32_e64 v196, v196, v237, s[0:1]
	v_cmp_ngt_f32_e64 s[14:15], v215, v196
	s_or_b64 s[14:15], s[16:17], s[14:15]
	v_cndmask_b32_e64 v197, 0, -1, s[12:13]
	v_cndmask_b32_e64 v196, v215, v196, s[14:15]
	v_cmp_gt_f32_e64 s[16:17], v195, v196
	s_and_b64 s[16:17], vcc, s[16:17]
	v_cndmask_b32_e64 v197, v197, 1, s[10:11]
	v_cndmask_b32_e64 v196, v196, v195, s[16:17]
	v_cndmask_b32_e32 v195, v195, v216, vcc
	v_sub_f32_e32 v195, v196, v195
	v_mul_f32_e32 v195, 0x3fb8aa3b, v195
	v_exp_f32_e32 v215, v195
	v_cndmask_b32_e64 v195, v197, 2, s[8:9]
	v_cndmask_b32_e64 v195, v195, 3, s[6:7]
	v_cndmask_b32_e64 v195, v195, 4, s[4:5]
	v_add_f32_e32 v214, 1.0, v215
	v_div_scale_f32 v196, s[4:5], v214, v214, 1.0
	v_rcp_f32_e32 v216, v196
	v_cndmask_b32_e64 v195, v195, 5, s[0:1]
	v_cndmask_b32_e64 v195, 6, v195, s[14:15]
	v_cndmask_b32_e64 v195, v195, 7, s[16:17]
	v_fma_f32 v197, -v196, v216, 1.0
	v_fmac_f32_e32 v216, v197, v216
	v_div_scale_f32 v197, vcc, 1.0, v214, 1.0
	v_mul_f32_e32 v217, v197, v216
	v_fma_f32 v218, -v196, v217, v197
	v_fmac_f32_e32 v217, v218, v216
	v_fma_f32 v218, -v196, v217, v197
	v_lshl_add_u32 v196, v194, 2, 0
	ds_add_rtn_u32 v196, v196, v230
	v_lshl_add_u32 v197, v195, 2, 0
	ds_add_rtn_u32 v197, v197, v230
	v_div_fmas_f32 v216, v218, v216, v217
	v_div_fixup_f32 v214, v216, v214, 1.0
	v_mul_f32_e32 v215, v215, v214
	s_waitcnt lgkmcnt(0)
	ds_write_b128 v226, v[194:197]
	v_lshl_add_u64 v[194:195], s[94:95], 0, v[206:207]
	v_add_co_u32_e32 v194, vcc, 0x280000, v194
	s_nop 1
	v_addc_co_u32_e32 v195, vcc, 0, v195, vcc
	global_store_dwordx2 v[194:195], v[214:215], off

.LBB0_1237:
	s_waitcnt vmcnt(7)
	v_lshlrev_b32_e32 v217, 16, v171
	v_lshlrev_b32_e32 v216, 16, v170
	v_and_b32_e32 v237, 0xffff0000, v171
	v_and_b32_e32 v236, 0xffff0000, v170
	s_waitcnt lgkmcnt(2)
	v_pk_add_f32 v[238:239], v[216:217], v[236:237]
	v_and_b32_e32 v241, 0xffff0000, v173
	v_add_f32_e32 v215, v238, v239
	v_lshlrev_b32_e32 v239, 16, v173
	v_lshlrev_b32_e32 v238, 16, v172
	s_waitcnt lgkmcnt(1)
	v_and_b32_e32 v240, 0xffff0000, v172
	s_waitcnt lgkmcnt(0)
	v_pk_add_f32 v[242:243], v[238:239], v[240:241]
	s_waitcnt vmcnt(6)
	v_lshlrev_b32_e32 v194, 16, v174
	v_and_b32_e32 v195, 0xffff0000, v174
	v_lshlrev_b32_e32 v196, 16, v175
	v_and_b32_e32 v197, 0xffff0000, v175
	v_pk_add_f32 v[242:243], v[242:243], v[242:243] op_sel_hi:[0,1]
	v_lshlrev_b32_e32 v214, 16, v176
	v_and_b32_e32 v218, 0xffff0000, v176
	v_lshlrev_b32_e32 v232, 16, v177
	v_and_b32_e32 v234, 0xffff0000, v177
	v_add_f32_e32 v235, 0, v215
	v_add_f32_e32 v215, v194, v195
	v_add_f32_e32 v219, v196, v197
	v_mov_b32_e32 v233, v243
	v_pk_add_f32 v[244:245], v[214:215], v[218:219]
	v_pk_add_f32 v[242:243], v[232:233], v[234:235]
	s_nop 0
	v_pk_add_f32 v[242:243], v[244:245], v[242:243]
	s_nop 0
	v_add_f32_e32 v215, v242, v243
	s_waitcnt lgkmcnt(0)
	s_nop 1
	v_add_f32_dpp v215, v215, v215 quad_perm:[1,0,3,2] row_mask:0xf bank_mask:0xf
	s_nop 1
	v_add_f32_dpp v215, v215, v215 quad_perm:[2,3,0,1] row_mask:0xf bank_mask:0xf
	s_nop 1
	v_add_f32_dpp v215, v215, v215 row_half_mirror row_mask:0xf bank_mask:0xf
	s_nop 1
	v_add_f32_dpp v215, v215, v215 row_mirror row_mask:0xf bank_mask:0xf
	v_mov_b32_e32 v219, v215
	s_nop 1
	v_permlane16_swap_b32_e32 v215, v219
	v_add_f32_e32 v215, v215, v219
	v_mov_b32_e32 v219, v215
	s_nop 1
	v_permlane32_swap_b32_e32 v215, v219
	v_add_f32_e32 v215, v215, v219
	v_fmac_f32_e32 v236, 0xba800000, v215
	v_fmac_f32_e32 v237, 0xba800000, v215
	v_fmac_f32_e32 v217, 0xba800000, v215
	v_fmac_f32_e32 v216, 0xba800000, v215
	v_mov_b32_e32 v242, v217
	v_mov_b32_e32 v243, v237
	v_mov_b32_e32 v217, v236
	v_pk_mul_f32 v[244:245], v[242:243], v[242:243]
	v_pk_mul_f32 v[236:237], v[216:217], v[216:217]
	v_fmac_f32_e32 v240, 0xba800000, v215
	v_pk_mov_b32 v[246:247], v[236:237], v[244:245] op_sel:[1,0]
	v_mov_b32_e32 v237, v245
	v_fmac_f32_e32 v241, 0xba800000, v215
	v_fmac_f32_e32 v239, 0xba800000, v215
	v_pk_add_f32 v[236:237], v[246:247], v[236:237]
	v_fmac_f32_e32 v238, 0xba800000, v215
	v_mov_b32_e32 v244, v239
	v_mov_b32_e32 v245, v241
	v_mov_b32_e32 v239, v240
	v_pk_add_f32 v[236:237], v[236:237], v[236:237] op_sel_hi:[0,1]
	v_pk_mul_f32 v[246:247], v[244:245], v[244:245]
	v_pk_mul_f32 v[240:241], v[238:239], v[238:239]
	v_fmac_f32_e32 v194, 0xba800000, v215
	v_pk_mov_b32 v[248:249], v[240:241], v[246:247] op_sel:[1,0]
	v_mov_b32_e32 v241, v247
	v_fmac_f32_e32 v195, 0xba800000, v215
	v_fmac_f32_e32 v196, 0xba800000, v215
	v_mul_f32_e32 v236, v194, v194
	v_pk_add_f32 v[240:241], v[248:249], v[240:241]
	v_fmac_f32_e32 v197, 0xba800000, v215
	v_pk_fma_f32 v[246:247], v[194:195], v[194:195], v[236:237] op_sel_hi:[1,1,0]
	v_mul_f32_e32 v236, v196, v196
	v_pk_add_f32 v[240:241], v[240:241], v[240:241] op_sel_hi:[0,1]
	v_pk_fma_f32 v[248:249], v[196:197], v[196:197], v[236:237] op_sel_hi:[1,1,0]
	v_fmac_f32_e32 v234, 0xba800000, v215
	v_fmac_f32_e32 v232, 0xba800000, v215
	v_fmac_f32_e32 v218, 0xba800000, v215
	v_fmac_f32_e32 v214, 0xba800000, v215
	v_mul_f32_e32 v246, v214, v214
	v_mul_f32_e32 v248, v218, v218
	v_mul_f32_e32 v236, v232, v232
	v_mul_f32_e32 v240, v234, v234
	v_pk_add_f32 v[246:247], v[246:247], v[248:249]
	v_pk_add_f32 v[236:237], v[236:237], v[240:241]
	s_nop 0
	v_pk_add_f32 v[236:237], v[246:247], v[236:237]
	s_nop 0
	v_add_f32_e32 v215, v236, v237
	s_waitcnt lgkmcnt(0)
	s_nop 1
	v_add_f32_dpp v215, v215, v215 quad_perm:[1,0,3,2] row_mask:0xf bank_mask:0xf
	s_nop 1
	v_add_f32_dpp v215, v215, v215 quad_perm:[2,3,0,1] row_mask:0xf bank_mask:0xf
	s_nop 1
	v_add_f32_dpp v215, v215, v215 row_half_mirror row_mask:0xf bank_mask:0xf
	s_nop 1
	v_add_f32_dpp v215, v215, v215 row_mirror row_mask:0xf bank_mask:0xf
	v_mov_b32_e32 v219, v215
	s_nop 1
	v_permlane16_swap_b32_e32 v215, v219
	v_add_f32_e32 v215, v215, v219
	v_mov_b32_e32 v219, v215
	s_nop 1
	v_permlane32_swap_b32_e32 v215, v219
	v_add_f32_e32 v215, v215, v219
	v_fmamk_f32 v215, v215, 0x3a800000, v228
	v_mul_f32_e32 v219, 0x4f800000, v215
	v_cmp_gt_f32_e32 vcc, s30, v215
	s_nop 1
	v_cndmask_b32_e32 v215, v215, v219, vcc
	v_sqrt_f32_e32 v219, v215
	s_nop 0
	v_add_u32_e32 v233, -1, v219
	v_fma_f32 v235, -v233, v219, v215
	v_cmp_ge_f32_e64 s[0:1], 0, v235
	v_add_u32_e32 v235, 1, v219
	s_nop 0
	v_cndmask_b32_e64 v233, v219, v233, s[0:1]
	v_fma_f32 v219, -v235, v219, v215
	v_cmp_lt_f32_e64 s[0:1], 0, v219
	s_nop 1
	v_cndmask_b32_e64 v219, v233, v235, s[0:1]
	v_mul_f32_e32 v233, 0x37800000, v219
	v_cndmask_b32_e32 v219, v219, v233, vcc
	v_cmp_class_f32_e32 vcc, v215, v229
	s_nop 1
	v_cndmask_b32_e32 v215, v219, v215, vcc
	v_div_scale_f32 v219, s[0:1], v215, v215, 1.0
	v_rcp_f32_e32 v233, v219
	s_nop 0
	v_fma_f32 v235, -v219, v233, 1.0
	v_fmac_f32_e32 v233, v235, v233
	v_div_scale_f32 v235, vcc, 1.0, v215, 1.0
	v_mul_f32_e32 v236, v235, v233
	v_fma_f32 v237, -v219, v236, v235
	v_fmac_f32_e32 v236, v237, v233
	v_fma_f32 v219, -v219, v236, v235
	v_div_fmas_f32 v219, v219, v233, v236
	v_div_fixup_f32 v236, v219, v215, 1.0
	v_pk_mul_f32 v[216:217], v[216:217], v[236:237] op_sel_hi:[1,0]
	v_pk_mul_f32 v[194:195], v[194:195], v[236:237] op_sel_hi:[1,0]
	v_mov_b32_e32 v215, v218
	v_pk_mul_f32 v[240:241], v[242:243], v[236:237] op_sel_hi:[1,0]
	v_pk_fma_f32 v[242:243], v[2:3], v[216:217], v[6:7]
	v_pk_fma_f32 v[246:247], v[18:19], v[194:195], v[30:31]
	v_pk_mul_f32 v[194:195], v[214:215], v[236:237] op_sel_hi:[1,0]
	v_pk_fma_f32 v[240:241], v[4:5], v[240:241], v[8:9]
	v_pk_fma_f32 v[218:219], v[10:11], v[194:195], v[22:23]
	v_pk_mul_f32 v[216:217], v[238:239], v[236:237] op_sel_hi:[1,0]
	v_pk_mul_f32 v[196:197], v[196:197], v[236:237] op_sel_hi:[1,0]
	v_mov_b32_e32 v233, v234
	v_pk_mul_f32 v[238:239], v[244:245], v[236:237] op_sel_hi:[1,0]
	v_pk_fma_f32 v[244:245], v[14:15], v[216:217], v[26:27]
	v_pk_fma_f32 v[216:217], v[20:21], v[196:197], v[32:33]
	v_pk_mul_f32 v[196:197], v[232:233], v[236:237] op_sel_hi:[1,0]
	v_cvt_pk_bf16_f32 v194, v242, v243
	v_bfe_u32 v195, v240, 16, 1
	v_pk_fma_f32 v[214:215], v[12:13], v[196:197], v[24:25]
	v_add3_u32 v195, v240, v195, s31
	v_bfe_u32 v196, v241, 16, 1
	v_lshrrev_b32_e32 v195, 16, v195
	v_add3_u32 v196, v241, v196, s31
	v_and_or_b32 v195, v196, s29, v195
	v_pk_fma_f32 v[238:239], v[16:17], v[238:239], v[28:29]
	v_cvt_pk_bf16_f32 v196, v244, v245
	v_cvt_pk_bf16_f32 v197, v238, v239
	v_fma_f32 v234, v36, v242, 0
	v_fma_f32 v235, v37, v242, 0
	v_fma_f32 v236, v38, v242, 0
	v_fma_f32 v237, v39, v242, 0
	v_fma_f32 v248, v40, v242, 0
	v_fma_f32 v249, v41, v242, 0
	v_pk_fma_f32 v[232:233], v[34:35], v[242:243], 0 op_sel_hi:[1,0,0]
	v_fmac_f32_e32 v234, v44, v243
	v_fmac_f32_e32 v235, v45, v243
	v_fmac_f32_e32 v236, v46, v243
	v_fmac_f32_e32 v237, v47, v243
	v_fmac_f32_e32 v248, v48, v243
	v_fmac_f32_e32 v249, v49, v243
	v_pk_fma_f32 v[232:233], v[42:43], v[242:243], v[232:233] op_sel:[0,1,0]
	v_fmac_f32_e32 v234, v52, v240
	v_fmac_f32_e32 v235, v53, v240
	v_fmac_f32_e32 v236, v54, v240
	v_fmac_f32_e32 v237, v55, v240
	v_fmac_f32_e32 v248, v56, v240
	v_fmac_f32_e32 v249, v57, v240
	v_pk_fma_f32 v[232:233], v[50:51], v[240:241], v[232:233] op_sel_hi:[1,0,1]
	v_fmac_f32_e32 v234, v60, v241
	v_fmac_f32_e32 v235, v61, v241
	v_fmac_f32_e32 v236, v62, v241
	v_fmac_f32_e32 v237, v63, v241
	v_fmac_f32_e32 v248, v64, v241
	v_fmac_f32_e32 v249, v65, v241
	v_pk_fma_f32 v[232:233], v[58:59], v[240:241], v[232:233] op_sel:[0,1,0]
	v_fmac_f32_e32 v234, v68, v244
	v_fmac_f32_e32 v235, v69, v244
	v_fmac_f32_e32 v236, v70, v244
	v_fmac_f32_e32 v237, v71, v244
	v_fmac_f32_e32 v248, v72, v244
	v_fmac_f32_e32 v249, v73, v244
	v_pk_fma_f32 v[232:233], v[66:67], v[244:245], v[232:233] op_sel_hi:[1,0,1]
	v_fmac_f32_e32 v234, v76, v245
	v_fmac_f32_e32 v235, v77, v245
	v_fmac_f32_e32 v236, v78, v245
	v_fmac_f32_e32 v237, v79, v245
	v_fmac_f32_e32 v248, v80, v245
	v_fmac_f32_e32 v249, v81, v245
	v_pk_fma_f32 v[232:233], v[74:75], v[244:245], v[232:233] op_sel:[0,1,0]
	v_fmac_f32_e32 v234, v84, v238
	v_fmac_f32_e32 v235, v85, v238
	v_fmac_f32_e32 v236, v86, v238
	v_fmac_f32_e32 v237, v87, v238
	v_fmac_f32_e32 v248, v88, v238
	v_fmac_f32_e32 v249, v89, v238
	v_pk_fma_f32 v[232:233], v[82:83], v[238:239], v[232:233] op_sel_hi:[1,0,1]
	global_store_dwordx4 v[212:213], v[194:197], off offset:2048
	v_fmac_f32_e32 v234, v92, v239
	v_fmac_f32_e32 v235, v93, v239
	v_fmac_f32_e32 v236, v94, v239
	v_fmac_f32_e32 v237, v95, v239
	v_fmac_f32_e32 v248, v96, v239
	v_fmac_f32_e32 v249, v97, v239
	v_pk_fma_f32 v[232:233], v[90:91], v[238:239], v[232:233] op_sel:[0,1,0]
	v_fmac_f32_e32 v234, v108, v246
	v_fmac_f32_e32 v235, v109, v246
	v_fmac_f32_e32 v236, v98, v246
	v_fmac_f32_e32 v237, v99, v246
	v_fmac_f32_e32 v248, v100, v246
	v_fmac_f32_e32 v249, v101, v246
	v_pk_fma_f32 v[232:233], v[106:107], v[246:247], v[232:233] op_sel_hi:[1,0,1]
	v_pk_fma_f32 v[232:233], v[102:103], v[246:247], v[232:233] op_sel:[0,1,0]
	v_fmac_f32_e32 v234, v104, v247
	v_fmac_f32_e32 v235, v105, v247
	v_fmac_f32_e32 v236, v110, v247
	v_fmac_f32_e32 v237, v111, v247
	v_fmac_f32_e32 v248, v112, v247
	v_fmac_f32_e32 v249, v113, v247
	v_cvt_pk_bf16_f32 v194, v246, v247
	v_bfe_u32 v195, v216, 16, 1
	v_bfe_u32 v196, v217, 16, 1
	v_fmac_f32_e32 v234, v124, v216
	v_fmac_f32_e32 v235, v125, v216
	v_fmac_f32_e32 v236, v138, v216
	v_fmac_f32_e32 v237, v139, v216
	v_fmac_f32_e32 v248, v140, v216
	v_fmac_f32_e32 v249, v141, v216
	v_pk_fma_f32 v[232:233], v[122:123], v[216:217], v[232:233] op_sel_hi:[1,0,1]
	v_add3_u32 v195, v216, v195, s31
	v_add3_u32 v196, v217, v196, s31
	v_fmac_f32_e32 v234, v116, v217
	v_fmac_f32_e32 v235, v117, v217
	v_fmac_f32_e32 v236, v118, v217
	v_fmac_f32_e32 v237, v119, v217
	v_fmac_f32_e32 v248, v120, v217
	v_fmac_f32_e32 v249, v121, v217
	v_pk_fma_f32 v[216:217], v[114:115], v[216:217], v[232:233] op_sel:[0,1,0]
	v_lshrrev_b32_e32 v195, 16, v195
	v_pk_fma_f32 v[216:217], v[126:127], v[218:219], v[216:217] op_sel_hi:[1,0,1]
	v_and_or_b32 v195, v196, s29, v195
	v_pk_fma_f32 v[216:217], v[134:135], v[218:219], v[216:217] op_sel:[0,1,0]
	v_bfe_u32 v196, v218, 16, 1
	v_pk_fma_f32 v[216:217], v[142:143], v[214:215], v[216:217] op_sel_hi:[1,0,1]
	v_bfe_u32 v197, v219, 16, 1
	v_pk_fma_f32 v[216:217], v[154:155], v[214:215], v[216:217] op_sel:[0,1,0]
	ds_bpermute_b32 v232, v220, v216
	ds_bpermute_b32 v233, v220, v217
	v_fmac_f32_e32 v234, v128, v218
	v_fmac_f32_e32 v235, v129, v218
	v_fmac_f32_e32 v236, v130, v218
	v_fmac_f32_e32 v237, v131, v218
	v_fmac_f32_e32 v248, v132, v218
	v_fmac_f32_e32 v249, v133, v218
	s_waitcnt lgkmcnt(0)
	v_pk_add_f32 v[216:217], v[216:217], v[232:233]
	v_add3_u32 v196, v218, v196, s31
	v_add3_u32 v197, v219, v197, s31
	v_fmac_f32_e32 v234, v136, v219
	v_fmac_f32_e32 v235, v137, v219
	v_fmac_f32_e32 v236, v146, v219
	v_fmac_f32_e32 v237, v147, v219
	v_fmac_f32_e32 v248, v148, v219
	v_fmac_f32_e32 v249, v149, v219
	ds_bpermute_b32 v218, v221, v216
	ds_bpermute_b32 v219, v221, v217
	v_lshrrev_b32_e32 v196, 16, v196
	v_fmac_f32_e32 v234, v144, v214
	v_and_or_b32 v196, v197, s29, v196
	v_bfe_u32 v197, v214, 16, 1
	s_waitcnt lgkmcnt(0)
	v_pk_add_f32 v[216:217], v[216:217], v[218:219]
	v_fmac_f32_e32 v234, v156, v215
	v_add3_u32 v197, v214, v197, s31
	v_fmac_f32_e32 v235, v145, v214
	v_fmac_f32_e32 v236, v150, v214
	v_fmac_f32_e32 v237, v151, v214
	v_fmac_f32_e32 v248, v152, v214
	v_fmac_f32_e32 v249, v153, v214
	ds_bpermute_b32 v218, v222, v216
	ds_bpermute_b32 v219, v222, v217
	ds_bpermute_b32 v214, v220, v234
	v_fmac_f32_e32 v235, v157, v215
	v_fmac_f32_e32 v236, v158, v215
	ds_bpermute_b32 v233, v220, v235
	s_waitcnt lgkmcnt(2)
	v_pk_add_f32 v[216:217], v[216:217], v[218:219]
	s_waitcnt lgkmcnt(1)
	v_add_f32_e32 v214, v234, v214
	ds_bpermute_b32 v218, v223, v216
	ds_bpermute_b32 v219, v223, v217
	ds_bpermute_b32 v232, v221, v214
	ds_bpermute_b32 v234, v220, v236
	v_fmac_f32_e32 v237, v159, v215
	v_fmac_f32_e32 v248, v160, v215
	s_waitcnt lgkmcnt(2)
	v_pk_add_f32 v[216:217], v[216:217], v[218:219]
	s_waitcnt lgkmcnt(1)
	v_add_f32_e32 v214, v214, v232
	ds_bpermute_b32 v218, v224, v216
	ds_bpermute_b32 v219, v224, v217
	ds_bpermute_b32 v232, v222, v214
	v_fmac_f32_e32 v249, v161, v215
	ds_bpermute_b32 v239, v220, v237
	ds_bpermute_b32 v240, v220, v249
	s_waitcnt lgkmcnt(3)
	v_pk_add_f32 v[216:217], v[216:217], v[218:219]
	v_add_f32_e32 v218, v235, v233
	s_waitcnt lgkmcnt(2)
	v_add_f32_e32 v214, v214, v232
	v_add_f32_e32 v232, v236, v234
	ds_bpermute_b32 v219, v221, v218
	ds_bpermute_b32 v233, v221, v232
	ds_bpermute_b32 v234, v223, v214
	s_waitcnt lgkmcnt(4)
	v_add_f32_e32 v237, v237, v239
	s_waitcnt lgkmcnt(3)
	v_add_f32_e32 v240, v249, v240
	s_waitcnt lgkmcnt(2)
	v_add_f32_e32 v219, v218, v219
	s_waitcnt lgkmcnt(1)
	v_add_f32_e32 v232, v232, v233
	ds_bpermute_b32 v235, v222, v219
	ds_bpermute_b32 v233, v222, v232
	s_waitcnt lgkmcnt(2)
	v_add_f32_e32 v214, v214, v234
	ds_bpermute_b32 v236, v224, v214
	ds_bpermute_b32 v239, v221, v237
	s_waitcnt lgkmcnt(3)
	v_add_f32_e32 v234, v219, v235
	s_waitcnt lgkmcnt(2)
	v_add_f32_e32 v232, v232, v233
	ds_bpermute_b32 v235, v223, v234
	ds_bpermute_b32 v233, v223, v232
	s_waitcnt lgkmcnt(3)
	v_add_f32_e32 v214, v214, v236
	ds_bpermute_b32 v242, v221, v240
	s_waitcnt lgkmcnt(3)
	v_add_f32_e32 v237, v237, v239
	s_waitcnt lgkmcnt(2)
	v_add_f32_e32 v234, v234, v235
	s_waitcnt lgkmcnt(1)
	v_add_f32_e32 v236, v232, v233
	ds_bpermute_b32 v235, v224, v234
	ds_bpermute_b32 v238, v224, v236
	s_waitcnt lgkmcnt(2)
	v_add_f32_e32 v240, v240, v242
	ds_bpermute_b32 v239, v222, v237
	ds_bpermute_b32 v242, v222, v240
	s_waitcnt lgkmcnt(3)
	v_add_f32_e32 v233, v234, v235
	s_waitcnt lgkmcnt(2)
	v_add_f32_e32 v235, v236, v238
	ds_bpermute_b32 v238, v220, v248
	s_waitcnt lgkmcnt(2)
	v_add_f32_e32 v237, v237, v239
	s_waitcnt lgkmcnt(1)
	v_add_f32_e32 v240, v240, v242
	ds_bpermute_b32 v239, v223, v237
	ds_bpermute_b32 v242, v223, v240
	s_waitcnt lgkmcnt(2)
	v_add_f32_e32 v238, v248, v238
	ds_bpermute_b32 v241, v221, v238
	ds_bpermute_b32 v218, v225, v216
	s_waitcnt lgkmcnt(3)
	v_add_f32_e32 v237, v237, v239
	s_waitcnt lgkmcnt(2)
	v_add_f32_e32 v242, v240, v242
	ds_bpermute_b32 v239, v224, v237
	s_waitcnt lgkmcnt(2)
	v_add_f32_e32 v238, v238, v241
	ds_bpermute_b32 v241, v222, v238
	ds_bpermute_b32 v244, v224, v242
	ds_bpermute_b32 v219, v225, v217
	s_waitcnt lgkmcnt(3)
	v_add_f32_e32 v237, v237, v239
	ds_bpermute_b32 v232, v225, v214
	s_waitcnt lgkmcnt(3)
	v_add_f32_e32 v238, v238, v241
	ds_bpermute_b32 v241, v223, v238
	ds_bpermute_b32 v234, v225, v233
	ds_bpermute_b32 v236, v225, v235
	v_lshrrev_b32_e32 v197, 16, v197
	s_waitcnt lgkmcnt(2)
	v_add_f32_e32 v241, v238, v241
	ds_bpermute_b32 v243, v224, v241
	ds_bpermute_b32 v238, v225, v237
	s_waitcnt lgkmcnt(1)
	v_add_f32_e32 v239, v241, v243
	v_add_f32_e32 v241, v242, v244
	ds_bpermute_b32 v240, v225, v239
	ds_bpermute_b32 v242, v225, v241
	v_bfe_u32 v243, v215, 16, 1
	v_add3_u32 v215, v215, v243, s31
	v_and_or_b32 v197, v215, s29, v197
	global_store_dwordx4 v[212:213], v[194:197], off offset:3072
	s_and_saveexec_b64 s[24:25], s[2:3]
	s_cbranch_execz .LBB0_1239
	v_pk_add_f32 v[196:197], v[216:217], v[218:219]
	v_add_f32_e32 v214, v214, v232
	v_cmp_gt_f32_e32 vcc, v197, v196
	v_add_f32_e32 v233, v233, v234
	v_add_f32_e32 v215, v235, v236
	v_cndmask_b32_e32 v194, v196, v197, vcc
	v_cmp_gt_f32_e64 s[0:1], v214, v194
	s_waitcnt lgkmcnt(2)
	v_add_f32_e32 v213, v237, v238
	s_waitcnt lgkmcnt(1)
	v_add_f32_e32 v212, v239, v240
	v_cndmask_b32_e64 v194, v194, v214, s[0:1]
	v_cmp_gt_f32_e64 s[4:5], v233, v194
	s_waitcnt lgkmcnt(0)
	v_add_f32_e32 v195, v241, v242
	v_cmp_nlg_f32_e64 s[14:15], s34, v196
	v_cndmask_b32_e64 v194, v194, v233, s[4:5]
	v_cmp_gt_f32_e64 s[6:7], v215, v194
	s_nop 1
	v_cndmask_b32_e64 v194, v194, v215, s[6:7]
	v_cmp_gt_f32_e64 s[8:9], v213, v194
	s_nop 1
	v_cndmask_b32_e64 v194, v194, v213, s[8:9]
	v_cmp_gt_f32_e64 s[10:11], v212, v194
	s_nop 1
	v_cndmask_b32_e64 v216, v194, v212, s[10:11]
	v_cndmask_b32_e64 v194, 0, 1, vcc
	v_cndmask_b32_e64 v194, v194, 2, s[0:1]
	v_cndmask_b32_e64 v194, v194, 3, s[4:5]
	v_cndmask_b32_e64 v194, v194, 4, s[6:7]
	v_cndmask_b32_e64 v194, v194, 5, s[8:9]
	v_cndmask_b32_e64 v194, v194, 6, s[10:11]
	v_cmp_ngt_f32_e32 vcc, v195, v216
	s_and_b64 s[16:17], s[10:11], vcc
	s_nop 0
	v_cndmask_b32_e32 v194, 7, v194, vcc
	v_cmp_eq_u32_e64 s[12:13], 0, v194
	s_or_b64 s[12:13], s[12:13], s[14:15]
	v_cmp_ne_u32_e64 s[10:11], 1, v194
	v_cndmask_b32_e64 v196, v196, v231, s[12:13]
	v_cmp_gt_f32_e64 s[14:15], v197, v196
	s_and_b64 s[10:11], s[10:11], s[14:15]
	v_cndmask_b32_e64 v196, v196, v197, s[10:11]
	v_cmp_ne_u32_e64 s[8:9], 2, v194
	v_cmp_gt_f32_e64 s[14:15], v214, v196
	s_and_b64 s[8:9], s[8:9], s[14:15]
	v_cndmask_b32_e64 v196, v196, v214, s[8:9]
	v_cmp_ne_u32_e64 s[6:7], 3, v194
	v_cmp_gt_f32_e64 s[14:15], v233, v196
	s_and_b64 s[6:7], s[6:7], s[14:15]
	v_cndmask_b32_e64 v196, v196, v233, s[6:7]
	v_cmp_ne_u32_e64 s[4:5], 4, v194
	v_cmp_gt_f32_e64 s[14:15], v215, v196
	s_and_b64 s[4:5], s[4:5], s[14:15]
	v_cndmask_b32_e64 v196, v196, v215, s[4:5]
	v_cmp_ne_u32_e64 s[0:1], 5, v194
	v_cmp_gt_f32_e64 s[14:15], v213, v196
	s_and_b64 s[0:1], s[0:1], s[14:15]
	v_cndmask_b32_e64 v196, v196, v213, s[0:1]
	v_cmp_ngt_f32_e64 s[14:15], v212, v196
	s_or_b64 s[14:15], s[16:17], s[14:15]
	v_cndmask_b32_e64 v197, 0, -1, s[12:13]
	v_cndmask_b32_e64 v196, v212, v196, s[14:15]
	v_cmp_gt_f32_e64 s[16:17], v195, v196
	s_and_b64 s[16:17], vcc, s[16:17]
	v_cndmask_b32_e64 v197, v197, 1, s[10:11]
	v_cndmask_b32_e64 v196, v196, v195, s[16:17]
	v_cndmask_b32_e32 v195, v195, v216, vcc
	v_sub_f32_e32 v195, v196, v195
	v_mul_f32_e32 v195, 0x3fb8aa3b, v195
	v_exp_f32_e32 v213, v195
	v_cndmask_b32_e64 v195, v197, 2, s[8:9]
	v_cndmask_b32_e64 v195, v195, 3, s[6:7]
	v_cndmask_b32_e64 v195, v195, 4, s[4:5]
	v_add_f32_e32 v212, 1.0, v213
	v_div_scale_f32 v196, s[4:5], v212, v212, 1.0
	v_rcp_f32_e32 v214, v196
	v_cndmask_b32_e64 v195, v195, 5, s[0:1]
	v_cndmask_b32_e64 v195, 6, v195, s[14:15]
	v_cndmask_b32_e64 v195, v195, 7, s[16:17]
	v_fma_f32 v197, -v196, v214, 1.0
	v_fmac_f32_e32 v214, v197, v214
	v_div_scale_f32 v197, vcc, 1.0, v212, 1.0
	v_mul_f32_e32 v215, v197, v214
	v_fma_f32 v216, -v196, v215, v197
	v_fmac_f32_e32 v215, v216, v214
	v_fma_f32 v216, -v196, v215, v197
	v_lshl_add_u32 v196, v194, 2, 0
	ds_add_rtn_u32 v196, v196, v230
	v_lshl_add_u32 v197, v195, 2, 0
	ds_add_rtn_u32 v197, v197, v230
	v_div_fmas_f32 v214, v216, v214, v215
	v_div_fixup_f32 v212, v214, v212, 1.0
	v_mul_f32_e32 v213, v213, v212
	s_waitcnt lgkmcnt(0)
	ds_write_b128 v226, v[194:197] offset:16
	v_add_u32_e32 v194, 2, v227
	v_ashrrev_i32_e32 v195, 31, v194
	v_lshl_add_u64 v[194:195], v[194:195], 2, s[36:37]
	global_store_dwordx2 v[194:195], v[212:213], off

.LBB0_1241:
	s_waitcnt vmcnt(7)
	v_lshlrev_b32_e32 v217, 16, v179
	v_lshlrev_b32_e32 v216, 16, v178
	v_and_b32_e32 v235, 0xffff0000, v179
	v_and_b32_e32 v234, 0xffff0000, v178
	v_pk_add_f32 v[236:237], v[216:217], v[234:235]
	v_and_b32_e32 v239, 0xffff0000, v181
	v_add_f32_e32 v213, v236, v237
	v_lshlrev_b32_e32 v237, 16, v181
	v_lshlrev_b32_e32 v236, 16, v180
	s_waitcnt lgkmcnt(2)
	v_and_b32_e32 v238, 0xffff0000, v180
	s_waitcnt lgkmcnt(1)
	v_pk_add_f32 v[240:241], v[236:237], v[238:239]
	s_waitcnt vmcnt(6)
	v_lshlrev_b32_e32 v194, 16, v182
	v_and_b32_e32 v195, 0xffff0000, v182
	v_lshlrev_b32_e32 v196, 16, v183
	v_and_b32_e32 v197, 0xffff0000, v183
	v_pk_add_f32 v[240:241], v[240:241], v[240:241] op_sel_hi:[0,1]
	v_lshlrev_b32_e32 v212, 16, v184
	v_and_b32_e32 v214, 0xffff0000, v184
	v_lshlrev_b32_e32 v218, 16, v185
	v_and_b32_e32 v232, 0xffff0000, v185
	v_add_f32_e32 v233, 0, v213
	v_add_f32_e32 v213, v194, v195
	v_add_f32_e32 v215, v196, v197
	v_mov_b32_e32 v219, v241
	s_waitcnt lgkmcnt(0)
	v_pk_add_f32 v[242:243], v[212:213], v[214:215]
	v_pk_add_f32 v[240:241], v[218:219], v[232:233]
	s_nop 0
	v_pk_add_f32 v[240:241], v[242:243], v[240:241]
	s_nop 0
	v_add_f32_e32 v213, v240, v241
	s_waitcnt lgkmcnt(0)
	s_nop 1
	v_add_f32_dpp v213, v213, v213 quad_perm:[1,0,3,2] row_mask:0xf bank_mask:0xf
	s_nop 1
	v_add_f32_dpp v213, v213, v213 quad_perm:[2,3,0,1] row_mask:0xf bank_mask:0xf
	s_nop 1
	v_add_f32_dpp v213, v213, v213 row_half_mirror row_mask:0xf bank_mask:0xf
	s_nop 1
	v_add_f32_dpp v213, v213, v213 row_mirror row_mask:0xf bank_mask:0xf
	v_mov_b32_e32 v215, v213
	s_nop 1
	v_permlane16_swap_b32_e32 v213, v215
	v_add_f32_e32 v213, v213, v215
	v_mov_b32_e32 v215, v213
	s_nop 1
	v_permlane32_swap_b32_e32 v213, v215
	v_add_f32_e32 v213, v213, v215
	v_fmac_f32_e32 v234, 0xba800000, v213
	v_fmac_f32_e32 v235, 0xba800000, v213
	v_fmac_f32_e32 v217, 0xba800000, v213
	v_fmac_f32_e32 v216, 0xba800000, v213
	v_mov_b32_e32 v240, v217
	v_mov_b32_e32 v241, v235
	v_mov_b32_e32 v217, v234
	v_pk_mul_f32 v[242:243], v[240:241], v[240:241]
	v_pk_mul_f32 v[234:235], v[216:217], v[216:217]
	v_fmac_f32_e32 v238, 0xba800000, v213
	v_pk_mov_b32 v[244:245], v[234:235], v[242:243] op_sel:[1,0]
	v_mov_b32_e32 v235, v243
	v_fmac_f32_e32 v239, 0xba800000, v213
	v_fmac_f32_e32 v237, 0xba800000, v213
	v_pk_add_f32 v[234:235], v[244:245], v[234:235]
	v_fmac_f32_e32 v236, 0xba800000, v213
	v_mov_b32_e32 v242, v237
	v_mov_b32_e32 v243, v239
	v_mov_b32_e32 v237, v238
	v_pk_add_f32 v[234:235], v[234:235], v[234:235] op_sel_hi:[0,1]
	v_pk_mul_f32 v[244:245], v[242:243], v[242:243]
	v_pk_mul_f32 v[238:239], v[236:237], v[236:237]
	v_fmac_f32_e32 v194, 0xba800000, v213
	v_pk_mov_b32 v[246:247], v[238:239], v[244:245] op_sel:[1,0]
	v_mov_b32_e32 v239, v245
	v_fmac_f32_e32 v195, 0xba800000, v213
	v_fmac_f32_e32 v196, 0xba800000, v213
	v_mul_f32_e32 v234, v194, v194
	v_pk_add_f32 v[238:239], v[246:247], v[238:239]
	v_fmac_f32_e32 v197, 0xba800000, v213
	v_pk_fma_f32 v[244:245], v[194:195], v[194:195], v[234:235] op_sel_hi:[1,1,0]
	v_mul_f32_e32 v234, v196, v196
	v_pk_add_f32 v[238:239], v[238:239], v[238:239] op_sel_hi:[0,1]
	v_pk_fma_f32 v[246:247], v[196:197], v[196:197], v[234:235] op_sel_hi:[1,1,0]
	v_fmac_f32_e32 v232, 0xba800000, v213
	v_fmac_f32_e32 v218, 0xba800000, v213
	v_fmac_f32_e32 v214, 0xba800000, v213
	v_fmac_f32_e32 v212, 0xba800000, v213
	v_mul_f32_e32 v244, v212, v212
	v_mul_f32_e32 v246, v214, v214
	v_mul_f32_e32 v234, v218, v218
	v_mul_f32_e32 v238, v232, v232
	v_pk_add_f32 v[244:245], v[244:245], v[246:247]
	v_pk_add_f32 v[234:235], v[234:235], v[238:239]
	s_nop 0
	v_pk_add_f32 v[234:235], v[244:245], v[234:235]
	s_nop 0
	v_add_f32_e32 v213, v234, v235
	s_waitcnt lgkmcnt(0)
	s_nop 1
	v_add_f32_dpp v213, v213, v213 quad_perm:[1,0,3,2] row_mask:0xf bank_mask:0xf
	s_nop 1
	v_add_f32_dpp v213, v213, v213 quad_perm:[2,3,0,1] row_mask:0xf bank_mask:0xf
	s_nop 1
	v_add_f32_dpp v213, v213, v213 row_half_mirror row_mask:0xf bank_mask:0xf
	s_nop 1
	v_add_f32_dpp v213, v213, v213 row_mirror row_mask:0xf bank_mask:0xf
	v_mov_b32_e32 v215, v213
	s_nop 1
	v_permlane16_swap_b32_e32 v213, v215
	v_add_f32_e32 v213, v213, v215
	v_mov_b32_e32 v215, v213
	s_nop 1
	v_permlane32_swap_b32_e32 v213, v215
	v_add_f32_e32 v213, v213, v215
	v_fmamk_f32 v213, v213, 0x3a800000, v228
	v_mul_f32_e32 v215, 0x4f800000, v213
	v_cmp_gt_f32_e32 vcc, s30, v213
	s_nop 1
	v_cndmask_b32_e32 v213, v213, v215, vcc
	v_sqrt_f32_e32 v215, v213
	s_nop 0
	v_add_u32_e32 v219, -1, v215
	v_fma_f32 v233, -v219, v215, v213
	v_cmp_ge_f32_e64 s[0:1], 0, v233
	v_add_u32_e32 v233, 1, v215
	s_nop 0
	v_cndmask_b32_e64 v219, v215, v219, s[0:1]
	v_fma_f32 v215, -v233, v215, v213
	v_cmp_lt_f32_e64 s[0:1], 0, v215
	s_nop 1
	v_cndmask_b32_e64 v215, v219, v233, s[0:1]
	v_mul_f32_e32 v219, 0x37800000, v215
	v_cndmask_b32_e32 v215, v215, v219, vcc
	v_cmp_class_f32_e32 vcc, v213, v229
	s_nop 1
	v_cndmask_b32_e32 v213, v215, v213, vcc
	v_div_scale_f32 v215, s[0:1], v213, v213, 1.0
	v_rcp_f32_e32 v219, v215
	s_nop 0
	v_fma_f32 v233, -v215, v219, 1.0
	v_fmac_f32_e32 v219, v233, v219
	v_div_scale_f32 v233, vcc, 1.0, v213, 1.0
	v_mul_f32_e32 v234, v233, v219
	v_fma_f32 v235, -v215, v234, v233
	v_fmac_f32_e32 v234, v235, v219
	v_fma_f32 v215, -v215, v234, v233
	v_div_fmas_f32 v215, v215, v219, v234
	v_div_fixup_f32 v234, v215, v213, 1.0
	v_pk_mul_f32 v[216:217], v[216:217], v[234:235] op_sel_hi:[1,0]
	v_pk_mul_f32 v[194:195], v[194:195], v[234:235] op_sel_hi:[1,0]
	v_mov_b32_e32 v213, v214
	v_pk_mul_f32 v[238:239], v[240:241], v[234:235] op_sel_hi:[1,0]
	v_pk_fma_f32 v[240:241], v[2:3], v[216:217], v[6:7]
	v_pk_mul_f32 v[216:217], v[236:237], v[234:235] op_sel_hi:[1,0]
	v_pk_mul_f32 v[196:197], v[196:197], v[234:235] op_sel_hi:[1,0]
	v_pk_fma_f32 v[244:245], v[18:19], v[194:195], v[30:31]
	v_pk_mul_f32 v[194:195], v[212:213], v[234:235] op_sel_hi:[1,0]
	v_mov_b32_e32 v219, v232
	v_pk_mul_f32 v[236:237], v[242:243], v[234:235] op_sel_hi:[1,0]
	v_pk_fma_f32 v[242:243], v[14:15], v[216:217], v[26:27]
	v_pk_fma_f32 v[216:217], v[20:21], v[196:197], v[32:33]
	v_pk_mul_f32 v[196:197], v[218:219], v[234:235] op_sel_hi:[1,0]
	v_pk_fma_f32 v[218:219], v[10:11], v[194:195], v[22:23]
	v_pk_fma_f32 v[238:239], v[4:5], v[238:239], v[8:9]
	v_cvt_pk_bf16_f32 v194, v240, v241
	v_bfe_u32 v195, v238, 16, 1
	v_pk_fma_f32 v[212:213], v[12:13], v[196:197], v[24:25]
	v_add3_u32 v195, v238, v195, s31
	v_bfe_u32 v196, v239, 16, 1
	v_lshrrev_b32_e32 v195, 16, v195
	v_add3_u32 v196, v239, v196, s31
	v_and_or_b32 v195, v196, s29, v195
	v_fma_f32 v234, v36, v240, 0
	v_fma_f32 v235, v37, v240, 0
	v_fma_f32 v246, v38, v240, 0
	v_fma_f32 v247, v39, v240, 0
	v_fma_f32 v248, v40, v240, 0
	v_fma_f32 v249, v41, v240, 0
	v_pk_fma_f32 v[232:233], v[34:35], v[240:241], 0 op_sel_hi:[1,0,0]
	v_pk_fma_f32 v[236:237], v[16:17], v[236:237], v[28:29]
	v_fmac_f32_e32 v234, v44, v241
	v_fmac_f32_e32 v235, v45, v241
	v_fmac_f32_e32 v246, v46, v241
	v_fmac_f32_e32 v247, v47, v241
	v_fmac_f32_e32 v248, v48, v241
	v_fmac_f32_e32 v249, v49, v241
	v_pk_fma_f32 v[232:233], v[42:43], v[240:241], v[232:233] op_sel:[0,1,0]
	v_cvt_pk_bf16_f32 v196, v242, v243
	v_fmac_f32_e32 v234, v52, v238
	v_fmac_f32_e32 v235, v53, v238
	v_fmac_f32_e32 v246, v54, v238
	v_fmac_f32_e32 v247, v55, v238
	v_fmac_f32_e32 v248, v56, v238
	v_fmac_f32_e32 v249, v57, v238
	v_pk_fma_f32 v[232:233], v[50:51], v[238:239], v[232:233] op_sel_hi:[1,0,1]
	v_fmac_f32_e32 v234, v60, v239
	v_fmac_f32_e32 v235, v61, v239
	v_fmac_f32_e32 v246, v62, v239
	v_fmac_f32_e32 v247, v63, v239
	v_fmac_f32_e32 v248, v64, v239
	v_fmac_f32_e32 v249, v65, v239
	v_pk_fma_f32 v[232:233], v[58:59], v[238:239], v[232:233] op_sel:[0,1,0]
	v_fmac_f32_e32 v234, v68, v242
	v_fmac_f32_e32 v235, v69, v242
	v_fmac_f32_e32 v246, v70, v242
	v_fmac_f32_e32 v247, v71, v242
	v_fmac_f32_e32 v248, v72, v242
	v_fmac_f32_e32 v249, v73, v242
	v_pk_fma_f32 v[232:233], v[66:67], v[242:243], v[232:233] op_sel_hi:[1,0,1]
	v_cvt_pk_bf16_f32 v197, v236, v237
	v_add_co_u32_e32 v214, vcc, s28, v210
	v_fmac_f32_e32 v234, v76, v243
	v_fmac_f32_e32 v235, v77, v243
	v_fmac_f32_e32 v246, v78, v243
	v_fmac_f32_e32 v247, v79, v243
	v_fmac_f32_e32 v248, v80, v243
	v_fmac_f32_e32 v249, v81, v243
	v_pk_fma_f32 v[232:233], v[74:75], v[242:243], v[232:233] op_sel:[0,1,0]
	v_addc_co_u32_e32 v215, vcc, 0, v211, vcc
	v_fmac_f32_e32 v234, v84, v236
	v_fmac_f32_e32 v235, v85, v236
	v_fmac_f32_e32 v246, v86, v236
	v_fmac_f32_e32 v247, v87, v236
	v_fmac_f32_e32 v248, v88, v236
	v_fmac_f32_e32 v249, v89, v236
	v_pk_fma_f32 v[232:233], v[82:83], v[236:237], v[232:233] op_sel_hi:[1,0,1]
	global_store_dwordx4 v[214:215], v[194:197], off
	v_fmac_f32_e32 v234, v92, v237
	v_fmac_f32_e32 v235, v93, v237
	v_fmac_f32_e32 v246, v94, v237
	v_fmac_f32_e32 v247, v95, v237
	v_fmac_f32_e32 v248, v96, v237
	v_fmac_f32_e32 v249, v97, v237
	v_pk_fma_f32 v[232:233], v[90:91], v[236:237], v[232:233] op_sel:[0,1,0]
	v_fmac_f32_e32 v234, v108, v244
	v_fmac_f32_e32 v235, v109, v244
	v_fmac_f32_e32 v246, v98, v244
	v_fmac_f32_e32 v247, v99, v244
	v_fmac_f32_e32 v248, v100, v244
	v_fmac_f32_e32 v249, v101, v244
	v_pk_fma_f32 v[232:233], v[106:107], v[244:245], v[232:233] op_sel_hi:[1,0,1]
	v_pk_fma_f32 v[232:233], v[102:103], v[244:245], v[232:233] op_sel:[0,1,0]
	v_fmac_f32_e32 v234, v104, v245
	v_fmac_f32_e32 v235, v105, v245
	v_fmac_f32_e32 v246, v110, v245
	v_fmac_f32_e32 v247, v111, v245
	v_fmac_f32_e32 v248, v112, v245
	v_fmac_f32_e32 v249, v113, v245
	v_cvt_pk_bf16_f32 v194, v244, v245
	v_bfe_u32 v195, v216, 16, 1
	v_bfe_u32 v196, v217, 16, 1
	v_fmac_f32_e32 v234, v124, v216
	v_fmac_f32_e32 v235, v125, v216
	v_fmac_f32_e32 v246, v138, v216
	v_fmac_f32_e32 v247, v139, v216
	v_fmac_f32_e32 v248, v140, v216
	v_fmac_f32_e32 v249, v141, v216
	v_pk_fma_f32 v[232:233], v[122:123], v[216:217], v[232:233] op_sel_hi:[1,0,1]
	v_add3_u32 v195, v216, v195, s31
	v_add3_u32 v196, v217, v196, s31
	v_fmac_f32_e32 v234, v116, v217
	v_fmac_f32_e32 v235, v117, v217
	v_fmac_f32_e32 v246, v118, v217
	v_fmac_f32_e32 v247, v119, v217
	v_fmac_f32_e32 v248, v120, v217
	v_fmac_f32_e32 v249, v121, v217
	v_pk_fma_f32 v[216:217], v[114:115], v[216:217], v[232:233] op_sel:[0,1,0]
	v_lshrrev_b32_e32 v195, 16, v195
	v_pk_fma_f32 v[216:217], v[126:127], v[218:219], v[216:217] op_sel_hi:[1,0,1]
	v_and_or_b32 v195, v196, s29, v195
	v_pk_fma_f32 v[216:217], v[134:135], v[218:219], v[216:217] op_sel:[0,1,0]
	v_bfe_u32 v196, v218, 16, 1
	v_pk_fma_f32 v[216:217], v[142:143], v[212:213], v[216:217] op_sel_hi:[1,0,1]
	v_bfe_u32 v197, v219, 16, 1
	v_pk_fma_f32 v[216:217], v[154:155], v[212:213], v[216:217] op_sel:[0,1,0]
	ds_bpermute_b32 v232, v220, v216
	ds_bpermute_b32 v233, v220, v217
	v_fmac_f32_e32 v234, v128, v218
	v_fmac_f32_e32 v235, v129, v218
	v_fmac_f32_e32 v246, v130, v218
	v_fmac_f32_e32 v247, v131, v218
	v_fmac_f32_e32 v248, v132, v218
	v_fmac_f32_e32 v249, v133, v218
	s_waitcnt lgkmcnt(0)
	v_pk_add_f32 v[216:217], v[216:217], v[232:233]
	v_add3_u32 v196, v218, v196, s31
	v_add3_u32 v197, v219, v197, s31
	v_fmac_f32_e32 v234, v136, v219
	v_fmac_f32_e32 v235, v137, v219
	v_fmac_f32_e32 v246, v146, v219
	v_fmac_f32_e32 v247, v147, v219
	v_fmac_f32_e32 v248, v148, v219
	v_fmac_f32_e32 v249, v149, v219
	ds_bpermute_b32 v218, v221, v216
	ds_bpermute_b32 v219, v221, v217
	v_lshrrev_b32_e32 v196, 16, v196
	v_fmac_f32_e32 v234, v144, v212
	v_and_or_b32 v196, v197, s29, v196
	v_bfe_u32 v197, v212, 16, 1
	s_waitcnt lgkmcnt(0)
	v_pk_add_f32 v[216:217], v[216:217], v[218:219]
	v_fmac_f32_e32 v234, v156, v213
	v_add3_u32 v197, v212, v197, s31
	v_fmac_f32_e32 v235, v145, v212
	v_fmac_f32_e32 v246, v150, v212
	v_fmac_f32_e32 v247, v151, v212
	v_fmac_f32_e32 v248, v152, v212
	v_fmac_f32_e32 v249, v153, v212
	ds_bpermute_b32 v218, v222, v216
	ds_bpermute_b32 v219, v222, v217
	ds_bpermute_b32 v212, v220, v234
	v_fmac_f32_e32 v235, v157, v213
	v_fmac_f32_e32 v246, v158, v213
	ds_bpermute_b32 v233, v220, v235
	s_waitcnt lgkmcnt(2)
	v_pk_add_f32 v[216:217], v[216:217], v[218:219]
	s_waitcnt lgkmcnt(1)
	v_add_f32_e32 v212, v234, v212
	ds_bpermute_b32 v218, v223, v216
	ds_bpermute_b32 v219, v223, v217
	ds_bpermute_b32 v232, v221, v212
	ds_bpermute_b32 v234, v220, v246
	v_fmac_f32_e32 v247, v159, v213
	v_fmac_f32_e32 v248, v160, v213
	s_waitcnt lgkmcnt(2)
	v_pk_add_f32 v[216:217], v[216:217], v[218:219]
	s_waitcnt lgkmcnt(1)
	v_add_f32_e32 v212, v212, v232
	ds_bpermute_b32 v218, v224, v216
	ds_bpermute_b32 v219, v224, v217
	ds_bpermute_b32 v232, v222, v212
	v_fmac_f32_e32 v249, v161, v213
	ds_bpermute_b32 v238, v220, v247
	ds_bpermute_b32 v239, v220, v249
	s_waitcnt lgkmcnt(3)
	v_pk_add_f32 v[216:217], v[216:217], v[218:219]
	v_add_f32_e32 v218, v235, v233
	s_waitcnt lgkmcnt(2)
	v_add_f32_e32 v212, v212, v232
	v_add_f32_e32 v232, v246, v234
	ds_bpermute_b32 v219, v221, v218
	ds_bpermute_b32 v233, v221, v232
	ds_bpermute_b32 v234, v223, v212
	s_waitcnt lgkmcnt(4)
	v_add_f32_e32 v238, v247, v238
	s_waitcnt lgkmcnt(3)
	v_add_f32_e32 v239, v249, v239
	s_waitcnt lgkmcnt(2)
	v_add_f32_e32 v219, v218, v219
	s_waitcnt lgkmcnt(1)
	v_add_f32_e32 v232, v232, v233
	ds_bpermute_b32 v235, v222, v219
	ds_bpermute_b32 v233, v222, v232
	s_waitcnt lgkmcnt(2)
	v_add_f32_e32 v212, v212, v234
	ds_bpermute_b32 v236, v224, v212
	ds_bpermute_b32 v240, v221, v238
	s_waitcnt lgkmcnt(3)
	v_add_f32_e32 v234, v219, v235
	s_waitcnt lgkmcnt(2)
	v_add_f32_e32 v232, v232, v233
	ds_bpermute_b32 v235, v223, v234
	ds_bpermute_b32 v233, v223, v232
	s_waitcnt lgkmcnt(3)
	v_add_f32_e32 v212, v212, v236
	ds_bpermute_b32 v242, v221, v239
	s_waitcnt lgkmcnt(3)
	v_add_f32_e32 v238, v238, v240
	s_waitcnt lgkmcnt(2)
	v_add_f32_e32 v234, v234, v235
	s_waitcnt lgkmcnt(1)
	v_add_f32_e32 v236, v232, v233
	ds_bpermute_b32 v235, v224, v234
	ds_bpermute_b32 v237, v224, v236
	s_waitcnt lgkmcnt(2)
	v_add_f32_e32 v239, v239, v242
	ds_bpermute_b32 v240, v222, v238
	ds_bpermute_b32 v242, v222, v239
	s_waitcnt lgkmcnt(3)
	v_add_f32_e32 v233, v234, v235
	s_waitcnt lgkmcnt(2)
	v_add_f32_e32 v235, v236, v237
	ds_bpermute_b32 v237, v220, v248
	s_waitcnt lgkmcnt(2)
	v_add_f32_e32 v238, v238, v240
	s_waitcnt lgkmcnt(1)
	v_add_f32_e32 v239, v239, v242
	ds_bpermute_b32 v240, v223, v238
	ds_bpermute_b32 v242, v223, v239
	s_waitcnt lgkmcnt(2)
	v_add_f32_e32 v237, v248, v237
	ds_bpermute_b32 v241, v221, v237
	ds_bpermute_b32 v218, v225, v216
	s_waitcnt lgkmcnt(3)
	v_add_f32_e32 v238, v238, v240
	s_waitcnt lgkmcnt(2)
	v_add_f32_e32 v242, v239, v242
	ds_bpermute_b32 v240, v224, v238
	s_waitcnt lgkmcnt(2)
	v_add_f32_e32 v237, v237, v241
	ds_bpermute_b32 v241, v222, v237
	ds_bpermute_b32 v244, v224, v242
	ds_bpermute_b32 v219, v225, v217
	ds_bpermute_b32 v232, v225, v212
	ds_bpermute_b32 v234, v225, v233
	s_waitcnt lgkmcnt(4)
	v_add_f32_e32 v237, v237, v241
	ds_bpermute_b32 v241, v223, v237
	ds_bpermute_b32 v236, v225, v235
	v_lshrrev_b32_e32 v197, 16, v197
	s_waitcnt lgkmcnt(1)
	v_add_f32_e32 v241, v237, v241
	ds_bpermute_b32 v243, v224, v241
	v_add_f32_e32 v237, v238, v240
	ds_bpermute_b32 v238, v225, v237
	s_waitcnt lgkmcnt(1)
	v_add_f32_e32 v239, v241, v243
	v_add_f32_e32 v241, v242, v244
	ds_bpermute_b32 v240, v225, v239
	ds_bpermute_b32 v242, v225, v241
	v_bfe_u32 v243, v213, 16, 1
	v_add3_u32 v213, v213, v243, s31
	v_and_or_b32 v197, v213, s29, v197
	global_store_dwordx4 v[214:215], v[194:197], off offset:1024
	s_and_saveexec_b64 s[24:25], s[2:3]
	s_cbranch_execz .LBB0_1243
	v_pk_add_f32 v[196:197], v[216:217], v[218:219]
	v_add_f32_e32 v212, v212, v232
	v_cmp_gt_f32_e32 vcc, v197, v196
	v_add_f32_e32 v233, v233, v234
	v_add_f32_e32 v215, v235, v236
	v_cndmask_b32_e32 v194, v196, v197, vcc
	v_cmp_gt_f32_e64 s[0:1], v212, v194
	s_waitcnt lgkmcnt(2)
	v_add_f32_e32 v214, v237, v238
	s_waitcnt lgkmcnt(1)
	v_add_f32_e32 v213, v239, v240
	v_cndmask_b32_e64 v194, v194, v212, s[0:1]
	v_cmp_gt_f32_e64 s[4:5], v233, v194
	s_waitcnt lgkmcnt(0)
	v_add_f32_e32 v195, v241, v242
	v_cmp_nlg_f32_e64 s[14:15], s34, v196
	v_cndmask_b32_e64 v194, v194, v233, s[4:5]
	v_cmp_gt_f32_e64 s[6:7], v215, v194
	s_nop 1
	v_cndmask_b32_e64 v194, v194, v215, s[6:7]
	v_cmp_gt_f32_e64 s[8:9], v214, v194
	s_nop 1
	v_cndmask_b32_e64 v194, v194, v214, s[8:9]
	v_cmp_gt_f32_e64 s[10:11], v213, v194
	s_nop 1
	v_cndmask_b32_e64 v216, v194, v213, s[10:11]
	v_cndmask_b32_e64 v194, 0, 1, vcc
	v_cndmask_b32_e64 v194, v194, 2, s[0:1]
	v_cndmask_b32_e64 v194, v194, 3, s[4:5]
	v_cndmask_b32_e64 v194, v194, 4, s[6:7]
	v_cndmask_b32_e64 v194, v194, 5, s[8:9]
	v_cndmask_b32_e64 v194, v194, 6, s[10:11]
	v_cmp_ngt_f32_e32 vcc, v195, v216
	s_and_b64 s[16:17], s[10:11], vcc
	s_nop 0
	v_cndmask_b32_e32 v194, 7, v194, vcc
	v_cmp_eq_u32_e64 s[12:13], 0, v194
	s_or_b64 s[12:13], s[12:13], s[14:15]
	v_cmp_ne_u32_e64 s[10:11], 1, v194
	v_cndmask_b32_e64 v196, v196, v231, s[12:13]
	v_cmp_gt_f32_e64 s[14:15], v197, v196
	s_and_b64 s[10:11], s[10:11], s[14:15]
	v_cndmask_b32_e64 v196, v196, v197, s[10:11]
	v_cmp_ne_u32_e64 s[8:9], 2, v194
	v_cmp_gt_f32_e64 s[14:15], v212, v196
	s_and_b64 s[8:9], s[8:9], s[14:15]
	v_cndmask_b32_e64 v196, v196, v212, s[8:9]
	v_cmp_ne_u32_e64 s[6:7], 3, v194
	v_cmp_gt_f32_e64 s[14:15], v233, v196
	s_and_b64 s[6:7], s[6:7], s[14:15]
	v_cndmask_b32_e64 v196, v196, v233, s[6:7]
	v_cmp_ne_u32_e64 s[4:5], 4, v194
	v_cmp_gt_f32_e64 s[14:15], v215, v196
	s_and_b64 s[4:5], s[4:5], s[14:15]
	v_cndmask_b32_e64 v196, v196, v215, s[4:5]
	v_cmp_ne_u32_e64 s[0:1], 5, v194
	v_cmp_gt_f32_e64 s[14:15], v214, v196
	s_and_b64 s[0:1], s[0:1], s[14:15]
	v_cndmask_b32_e64 v196, v196, v214, s[0:1]
	v_cmp_ngt_f32_e64 s[14:15], v213, v196
	s_or_b64 s[14:15], s[16:17], s[14:15]
	v_cndmask_b32_e64 v197, 0, -1, s[12:13]
	v_cndmask_b32_e64 v196, v213, v196, s[14:15]
	v_cmp_gt_f32_e64 s[16:17], v195, v196
	s_and_b64 s[16:17], vcc, s[16:17]
	v_cndmask_b32_e64 v197, v197, 1, s[10:11]
	v_cndmask_b32_e64 v196, v196, v195, s[16:17]
	v_cndmask_b32_e32 v195, v195, v216, vcc
	v_sub_f32_e32 v195, v196, v195
	v_mul_f32_e32 v195, 0x3fb8aa3b, v195
	v_exp_f32_e32 v213, v195
	v_cndmask_b32_e64 v195, v197, 2, s[8:9]
	v_cndmask_b32_e64 v195, v195, 3, s[6:7]
	v_cndmask_b32_e64 v195, v195, 4, s[4:5]
	v_add_f32_e32 v212, 1.0, v213
	v_div_scale_f32 v196, s[4:5], v212, v212, 1.0
	v_rcp_f32_e32 v214, v196
	v_cndmask_b32_e64 v195, v195, 5, s[0:1]
	v_cndmask_b32_e64 v195, 6, v195, s[14:15]
	v_cndmask_b32_e64 v195, v195, 7, s[16:17]
	v_fma_f32 v197, -v196, v214, 1.0
	v_fmac_f32_e32 v214, v197, v214
	v_div_scale_f32 v197, vcc, 1.0, v212, 1.0
	v_mul_f32_e32 v215, v197, v214
	v_fma_f32 v216, -v196, v215, v197
	v_fmac_f32_e32 v215, v216, v214
	v_fma_f32 v216, -v196, v215, v197
	v_lshl_add_u32 v196, v194, 2, 0
	ds_add_rtn_u32 v196, v196, v230
	v_lshl_add_u32 v197, v195, 2, 0
	ds_add_rtn_u32 v197, v197, v230
	v_div_fmas_f32 v214, v216, v214, v215
	v_div_fixup_f32 v212, v214, v212, 1.0
	v_mul_f32_e32 v213, v213, v212
	s_waitcnt lgkmcnt(0)
	ds_write_b128 v226, v[194:197] offset:32
	v_add_u32_e32 v194, 4, v227
	v_ashrrev_i32_e32 v195, 31, v194
	v_lshl_add_u64 v[194:195], v[194:195], 2, s[36:37]
	global_store_dwordx2 v[194:195], v[212:213], off

.LBB0_1245:
	s_waitcnt vmcnt(7)
	v_lshlrev_b32_e32 v219, 16, v187
	v_lshlrev_b32_e32 v218, 16, v186
	v_and_b32_e32 v187, 0xffff0000, v187
	v_and_b32_e32 v186, 0xffff0000, v186
	s_waitcnt vmcnt(6)
	v_lshlrev_b32_e32 v194, 16, v190
	v_and_b32_e32 v195, 0xffff0000, v190
	v_lshlrev_b32_e32 v196, 16, v191
	v_and_b32_e32 v197, 0xffff0000, v191
	v_pk_add_f32 v[190:191], v[218:219], v[186:187]
	v_lshlrev_b32_e32 v233, 16, v189
	v_add_f32_e32 v190, v190, v191
	v_lshlrev_b32_e32 v232, 16, v188
	v_and_b32_e32 v189, 0xffff0000, v189
	v_and_b32_e32 v188, 0xffff0000, v188
	v_add_f32_e32 v217, 0, v190
	v_pk_add_f32 v[190:191], v[232:233], v[188:189]
	v_lshlrev_b32_e32 v212, 16, v192
	v_pk_add_f32 v[190:191], v[190:191], v[190:191] op_sel_hi:[0,1]
	v_and_b32_e32 v192, 0xffff0000, v192
	v_lshlrev_b32_e32 v214, 16, v193
	v_and_b32_e32 v216, 0xffff0000, v193
	v_add_f32_e32 v213, v194, v195
	v_add_f32_e32 v193, v196, v197
	v_mov_b32_e32 v215, v191
	v_pk_add_f32 v[234:235], v[212:213], v[192:193]
	v_pk_add_f32 v[190:191], v[214:215], v[216:217]
	s_nop 0
	v_pk_add_f32 v[190:191], v[234:235], v[190:191]
	s_nop 0
	v_add_f32_e32 v190, v190, v191
	s_waitcnt lgkmcnt(0)
	s_nop 1
	v_add_f32_dpp v190, v190, v190 quad_perm:[1,0,3,2] row_mask:0xf bank_mask:0xf
	s_nop 1
	v_add_f32_dpp v190, v190, v190 quad_perm:[2,3,0,1] row_mask:0xf bank_mask:0xf
	s_nop 1
	v_add_f32_dpp v190, v190, v190 row_half_mirror row_mask:0xf bank_mask:0xf
	s_nop 1
	v_add_f32_dpp v190, v190, v190 row_mirror row_mask:0xf bank_mask:0xf
	v_mov_b32_e32 v191, v190
	s_nop 1
	v_permlane16_swap_b32_e32 v190, v191
	v_add_f32_e32 v190, v190, v191
	v_mov_b32_e32 v191, v190
	s_nop 1
	v_permlane32_swap_b32_e32 v190, v191
	v_add_f32_e32 v193, v190, v191
	v_fmac_f32_e32 v186, 0xba800000, v193
	v_fmac_f32_e32 v187, 0xba800000, v193
	v_fmac_f32_e32 v219, 0xba800000, v193
	v_fmac_f32_e32 v218, 0xba800000, v193
	v_mov_b32_e32 v234, v219
	v_mov_b32_e32 v235, v187
	v_mov_b32_e32 v219, v186
	v_pk_mul_f32 v[190:191], v[234:235], v[234:235]
	v_pk_mul_f32 v[186:187], v[218:219], v[218:219]
	v_fmac_f32_e32 v188, 0xba800000, v193
	v_pk_mov_b32 v[236:237], v[186:187], v[190:191] op_sel:[1,0]
	v_mov_b32_e32 v187, v191
	v_fmac_f32_e32 v189, 0xba800000, v193
	v_fmac_f32_e32 v233, 0xba800000, v193
	v_pk_add_f32 v[186:187], v[236:237], v[186:187]
	v_fmac_f32_e32 v232, 0xba800000, v193
	v_mov_b32_e32 v236, v233
	v_mov_b32_e32 v237, v189
	v_mov_b32_e32 v233, v188
	v_pk_add_f32 v[186:187], v[186:187], v[186:187] op_sel_hi:[0,1]
	v_pk_mul_f32 v[190:191], v[236:237], v[236:237]
	v_pk_mul_f32 v[188:189], v[232:233], v[232:233]
	v_fmac_f32_e32 v194, 0xba800000, v193
	v_pk_mov_b32 v[238:239], v[188:189], v[190:191] op_sel:[1,0]
	v_mov_b32_e32 v189, v191
	v_fmac_f32_e32 v195, 0xba800000, v193
	v_fmac_f32_e32 v196, 0xba800000, v193
	v_mul_f32_e32 v186, v194, v194
	v_pk_add_f32 v[188:189], v[238:239], v[188:189]
	v_fmac_f32_e32 v197, 0xba800000, v193
	v_pk_fma_f32 v[190:191], v[194:195], v[194:195], v[186:187] op_sel_hi:[1,1,0]
	v_mul_f32_e32 v186, v196, v196
	v_pk_add_f32 v[188:189], v[188:189], v[188:189] op_sel_hi:[0,1]
	v_pk_fma_f32 v[238:239], v[196:197], v[196:197], v[186:187] op_sel_hi:[1,1,0]
	v_fmac_f32_e32 v216, 0xba800000, v193
	v_fmac_f32_e32 v214, 0xba800000, v193
	v_fmac_f32_e32 v192, 0xba800000, v193
	v_fmac_f32_e32 v212, 0xba800000, v193
	v_mul_f32_e32 v190, v212, v212
	v_mul_f32_e32 v238, v192, v192
	v_mul_f32_e32 v186, v214, v214
	v_mul_f32_e32 v188, v216, v216
	v_pk_add_f32 v[190:191], v[190:191], v[238:239]
	v_pk_add_f32 v[186:187], v[186:187], v[188:189]
	v_lshl_add_u64 v[238:239], v[210:211], 0, s[18:19]
	v_pk_add_f32 v[186:187], v[190:191], v[186:187]
	v_lshl_add_u64 v[190:191], v[210:211], 0, s[20:21]
	v_add_f32_e32 v186, v186, v187
	ds_bpermute_b32 v187, v220, v186
	v_mov_b32_e32 v213, v192
	v_mov_b32_e32 v215, v216
	s_waitcnt lgkmcnt(0)
	v_add_f32_e32 v186, v186, v187
	ds_bpermute_b32 v187, v221, v186
	s_waitcnt lgkmcnt(0)
	v_add_f32_e32 v186, v186, v187
	ds_bpermute_b32 v187, v222, v186
	s_waitcnt lgkmcnt(0)
	v_add_f32_e32 v186, v186, v187
	ds_bpermute_b32 v187, v223, v186
	s_waitcnt lgkmcnt(0)
	v_add_f32_e32 v186, v186, v187
	ds_bpermute_b32 v187, v224, v186
	s_waitcnt lgkmcnt(0)
	v_add_f32_e32 v186, v186, v187
	ds_bpermute_b32 v187, v225, v186
	s_waitcnt lgkmcnt(0)
	v_add_f32_e32 v186, v186, v187
	v_fmamk_f32 v186, v186, 0x3a800000, v228
	v_mul_f32_e32 v187, 0x4f800000, v186
	v_cmp_gt_f32_e32 vcc, s30, v186
	s_nop 1
	v_cndmask_b32_e32 v186, v186, v187, vcc
	v_sqrt_f32_e32 v187, v186
	s_nop 0
	v_add_u32_e32 v188, -1, v187
	v_fma_f32 v189, -v188, v187, v186
	v_cmp_ge_f32_e64 s[0:1], 0, v189
	v_add_u32_e32 v189, 1, v187
	s_nop 0
	v_cndmask_b32_e64 v188, v187, v188, s[0:1]
	v_fma_f32 v187, -v189, v187, v186
	v_cmp_lt_f32_e64 s[0:1], 0, v187
	s_nop 1
	v_cndmask_b32_e64 v187, v188, v189, s[0:1]
	v_mul_f32_e32 v188, 0x37800000, v187
	v_cndmask_b32_e32 v187, v187, v188, vcc
	v_cmp_class_f32_e32 vcc, v186, v229
	s_nop 1
	v_cndmask_b32_e32 v186, v187, v186, vcc
	v_div_scale_f32 v187, s[0:1], v186, v186, 1.0
	v_rcp_f32_e32 v188, v187
	s_nop 0
	v_fma_f32 v189, -v187, v188, 1.0
	v_fmac_f32_e32 v188, v189, v188
	v_div_scale_f32 v189, vcc, 1.0, v186, 1.0
	v_mul_f32_e32 v193, v189, v188
	v_fma_f32 v210, -v187, v193, v189
	v_fmac_f32_e32 v193, v210, v188
	v_fma_f32 v187, -v187, v193, v189
	v_div_fmas_f32 v187, v187, v188, v193
	v_div_fixup_f32 v186, v187, v186, 1.0
	v_pk_mul_f32 v[188:189], v[218:219], v[186:187] op_sel_hi:[1,0]
	v_pk_mul_f32 v[210:211], v[234:235], v[186:187] op_sel_hi:[1,0]
	v_pk_fma_f32 v[218:219], v[2:3], v[188:189], v[6:7]
	v_pk_mul_f32 v[188:189], v[232:233], v[186:187] op_sel_hi:[1,0]
	v_pk_mul_f32 v[232:233], v[236:237], v[186:187] op_sel_hi:[1,0]
	v_pk_fma_f32 v[234:235], v[14:15], v[188:189], v[26:27]
	v_pk_mul_f32 v[188:189], v[194:195], v[186:187] op_sel_hi:[1,0]
	v_pk_mul_f32 v[194:195], v[196:197], v[186:187] op_sel_hi:[1,0]
	v_pk_fma_f32 v[236:237], v[18:19], v[188:189], v[30:31]
	v_pk_mul_f32 v[188:189], v[212:213], v[186:187] op_sel_hi:[1,0]
	v_pk_mul_f32 v[186:187], v[214:215], v[186:187] op_sel_hi:[1,0]
	v_pk_fma_f32 v[210:211], v[4:5], v[210:211], v[8:9]
	v_pk_fma_f32 v[192:193], v[12:13], v[186:187], v[24:25]
	v_cvt_pk_bf16_f32 v186, v218, v219
	v_bfe_u32 v187, v210, 16, 1
	v_pk_fma_f32 v[196:197], v[10:11], v[188:189], v[22:23]
	v_add3_u32 v187, v210, v187, s31
	v_bfe_u32 v188, v211, 16, 1
	v_lshrrev_b32_e32 v187, 16, v187
	v_add3_u32 v188, v211, v188, s31
	v_and_or_b32 v187, v188, s29, v187
	v_pk_fma_f32 v[232:233], v[16:17], v[232:233], v[28:29]
	v_cvt_pk_bf16_f32 v188, v234, v235
	v_cvt_pk_bf16_f32 v189, v232, v233
	global_store_dwordx4 v[238:239], v[186:189], off
	v_fma_f32 v214, v36, v218, 0
	v_fma_f32 v215, v37, v218, 0
	v_fma_f32 v216, v38, v218, 0
	v_fma_f32 v217, v39, v218, 0
	v_fma_f32 v238, v40, v218, 0
	v_fma_f32 v239, v41, v218, 0
	v_pk_fma_f32 v[212:213], v[34:35], v[218:219], 0 op_sel_hi:[1,0,0]
	v_fmac_f32_e32 v214, v44, v219
	v_fmac_f32_e32 v215, v45, v219
	v_fmac_f32_e32 v216, v46, v219
	v_fmac_f32_e32 v217, v47, v219
	v_fmac_f32_e32 v238, v48, v219
	v_fmac_f32_e32 v239, v49, v219
	v_pk_fma_f32 v[212:213], v[42:43], v[218:219], v[212:213] op_sel:[0,1,0]
	v_fmac_f32_e32 v214, v52, v210
	v_fmac_f32_e32 v215, v53, v210
	v_fmac_f32_e32 v216, v54, v210
	v_fmac_f32_e32 v217, v55, v210
	v_fmac_f32_e32 v238, v56, v210
	v_fmac_f32_e32 v239, v57, v210
	v_pk_fma_f32 v[212:213], v[50:51], v[210:211], v[212:213] op_sel_hi:[1,0,1]
	v_fmac_f32_e32 v214, v60, v211
	v_fmac_f32_e32 v215, v61, v211
	v_fmac_f32_e32 v216, v62, v211
	v_fmac_f32_e32 v217, v63, v211
	v_fmac_f32_e32 v238, v64, v211
	v_fmac_f32_e32 v239, v65, v211
	v_pk_fma_f32 v[210:211], v[58:59], v[210:211], v[212:213] op_sel:[0,1,0]
	v_fmac_f32_e32 v214, v68, v234
	v_fmac_f32_e32 v215, v69, v234
	v_fmac_f32_e32 v216, v70, v234
	v_fmac_f32_e32 v217, v71, v234
	v_fmac_f32_e32 v238, v72, v234
	v_fmac_f32_e32 v239, v73, v234
	v_pk_fma_f32 v[210:211], v[66:67], v[234:235], v[210:211] op_sel_hi:[1,0,1]
	v_fmac_f32_e32 v214, v76, v235
	v_fmac_f32_e32 v215, v77, v235
	v_fmac_f32_e32 v216, v78, v235
	v_fmac_f32_e32 v217, v79, v235
	v_fmac_f32_e32 v238, v80, v235
	v_fmac_f32_e32 v239, v81, v235
	v_pk_fma_f32 v[210:211], v[74:75], v[234:235], v[210:211] op_sel:[0,1,0]
	v_fmac_f32_e32 v214, v84, v232
	v_fmac_f32_e32 v215, v85, v232
	v_fmac_f32_e32 v216, v86, v232
	v_fmac_f32_e32 v217, v87, v232
	v_fmac_f32_e32 v238, v88, v232
	v_fmac_f32_e32 v239, v89, v232
	v_pk_fma_f32 v[210:211], v[82:83], v[232:233], v[210:211] op_sel_hi:[1,0,1]
	v_fmac_f32_e32 v214, v92, v233
	v_fmac_f32_e32 v215, v93, v233
	v_fmac_f32_e32 v216, v94, v233
	v_fmac_f32_e32 v217, v95, v233
	v_fmac_f32_e32 v238, v96, v233
	v_fmac_f32_e32 v239, v97, v233
	v_pk_fma_f32 v[210:211], v[90:91], v[232:233], v[210:211] op_sel:[0,1,0]
	v_fmac_f32_e32 v214, v108, v236
	v_fmac_f32_e32 v215, v109, v236
	v_fmac_f32_e32 v216, v98, v236
	v_fmac_f32_e32 v217, v99, v236
	v_fmac_f32_e32 v238, v100, v236
	v_fmac_f32_e32 v239, v101, v236
	v_pk_fma_f32 v[210:211], v[106:107], v[236:237], v[210:211] op_sel_hi:[1,0,1]
	v_pk_fma_f32 v[194:195], v[20:21], v[194:195], v[32:33]
	v_pk_fma_f32 v[210:211], v[102:103], v[236:237], v[210:211] op_sel:[0,1,0]
	v_fmac_f32_e32 v214, v104, v237
	v_fmac_f32_e32 v215, v105, v237
	v_fmac_f32_e32 v216, v110, v237
	v_fmac_f32_e32 v217, v111, v237
	v_fmac_f32_e32 v238, v112, v237
	v_fmac_f32_e32 v239, v113, v237
	v_cvt_pk_bf16_f32 v186, v236, v237
	v_bfe_u32 v187, v194, 16, 1
	v_bfe_u32 v188, v195, 16, 1
	v_fmac_f32_e32 v214, v124, v194
	v_fmac_f32_e32 v215, v125, v194
	v_fmac_f32_e32 v216, v138, v194
	v_fmac_f32_e32 v217, v139, v194
	v_fmac_f32_e32 v238, v140, v194
	v_fmac_f32_e32 v239, v141, v194
	v_pk_fma_f32 v[210:211], v[122:123], v[194:195], v[210:211] op_sel_hi:[1,0,1]
	v_add3_u32 v187, v194, v187, s31
	v_add3_u32 v188, v195, v188, s31
	v_fmac_f32_e32 v214, v116, v195
	v_fmac_f32_e32 v215, v117, v195
	v_fmac_f32_e32 v216, v118, v195
	v_fmac_f32_e32 v217, v119, v195
	v_fmac_f32_e32 v238, v120, v195
	v_fmac_f32_e32 v239, v121, v195
	v_pk_fma_f32 v[194:195], v[114:115], v[194:195], v[210:211] op_sel:[0,1,0]
	v_lshrrev_b32_e32 v187, 16, v187
	v_pk_fma_f32 v[194:195], v[126:127], v[196:197], v[194:195] op_sel_hi:[1,0,1]
	v_and_or_b32 v187, v188, s29, v187
	v_pk_fma_f32 v[194:195], v[134:135], v[196:197], v[194:195] op_sel:[0,1,0]
	v_bfe_u32 v188, v196, 16, 1
	v_pk_fma_f32 v[194:195], v[142:143], v[192:193], v[194:195] op_sel_hi:[1,0,1]
	v_bfe_u32 v189, v197, 16, 1
	v_pk_fma_f32 v[194:195], v[154:155], v[192:193], v[194:195] op_sel:[0,1,0]
	ds_bpermute_b32 v210, v220, v194
	ds_bpermute_b32 v211, v220, v195
	v_fmac_f32_e32 v214, v128, v196
	v_fmac_f32_e32 v215, v129, v196
	v_fmac_f32_e32 v216, v130, v196
	v_fmac_f32_e32 v217, v131, v196
	v_fmac_f32_e32 v238, v132, v196
	v_fmac_f32_e32 v239, v133, v196
	s_waitcnt lgkmcnt(0)
	v_pk_add_f32 v[194:195], v[194:195], v[210:211]
	v_add3_u32 v188, v196, v188, s31
	v_add3_u32 v189, v197, v189, s31
	v_fmac_f32_e32 v214, v136, v197
	v_fmac_f32_e32 v215, v137, v197
	v_fmac_f32_e32 v216, v146, v197
	v_fmac_f32_e32 v217, v147, v197
	v_fmac_f32_e32 v238, v148, v197
	v_fmac_f32_e32 v239, v149, v197
	ds_bpermute_b32 v196, v221, v194
	ds_bpermute_b32 v197, v221, v195
	v_lshrrev_b32_e32 v188, 16, v188
	v_fmac_f32_e32 v214, v144, v192
	v_and_or_b32 v188, v189, s29, v188
	v_bfe_u32 v189, v192, 16, 1
	s_waitcnt lgkmcnt(0)
	v_pk_add_f32 v[194:195], v[194:195], v[196:197]
	v_fmac_f32_e32 v214, v156, v193
	v_add3_u32 v189, v192, v189, s31
	v_fmac_f32_e32 v215, v145, v192
	v_fmac_f32_e32 v216, v150, v192
	v_fmac_f32_e32 v217, v151, v192
	v_fmac_f32_e32 v238, v152, v192
	v_fmac_f32_e32 v239, v153, v192
	ds_bpermute_b32 v196, v222, v194
	ds_bpermute_b32 v197, v222, v195
	ds_bpermute_b32 v192, v220, v214
	v_fmac_f32_e32 v215, v157, v193
	v_fmac_f32_e32 v216, v158, v193
	ds_bpermute_b32 v211, v220, v215
	s_waitcnt lgkmcnt(2)
	v_pk_add_f32 v[194:195], v[194:195], v[196:197]
	s_waitcnt lgkmcnt(1)
	v_add_f32_e32 v192, v214, v192
	ds_bpermute_b32 v196, v223, v194
	ds_bpermute_b32 v197, v223, v195
	ds_bpermute_b32 v210, v221, v192
	ds_bpermute_b32 v212, v220, v216
	v_fmac_f32_e32 v217, v159, v193
	v_fmac_f32_e32 v238, v160, v193
	s_waitcnt lgkmcnt(2)
	v_pk_add_f32 v[194:195], v[194:195], v[196:197]
	s_waitcnt lgkmcnt(1)
	v_add_f32_e32 v192, v192, v210
	ds_bpermute_b32 v196, v224, v194
	ds_bpermute_b32 v197, v224, v195
	ds_bpermute_b32 v210, v222, v192
	v_fmac_f32_e32 v239, v161, v193
	ds_bpermute_b32 v218, v220, v239
	v_lshrrev_b32_e32 v189, 16, v189
	s_waitcnt lgkmcnt(2)
	v_pk_add_f32 v[194:195], v[194:195], v[196:197]
	v_add_f32_e32 v196, v215, v211
	s_waitcnt lgkmcnt(1)
	v_add_f32_e32 v192, v192, v210
	v_add_f32_e32 v210, v216, v212
	ds_bpermute_b32 v197, v221, v196
	ds_bpermute_b32 v211, v221, v210
	ds_bpermute_b32 v212, v223, v192
	ds_bpermute_b32 v216, v220, v217
	s_waitcnt lgkmcnt(4)
	v_add_f32_e32 v218, v239, v218
	s_waitcnt lgkmcnt(3)
	v_add_f32_e32 v197, v196, v197
	s_waitcnt lgkmcnt(2)
	v_add_f32_e32 v210, v210, v211
	ds_bpermute_b32 v213, v222, v197
	ds_bpermute_b32 v211, v222, v210
	s_waitcnt lgkmcnt(3)
	v_add_f32_e32 v192, v192, v212
	ds_bpermute_b32 v214, v224, v192
	s_waitcnt lgkmcnt(3)
	v_add_f32_e32 v216, v217, v216
	s_waitcnt lgkmcnt(2)
	v_add_f32_e32 v212, v197, v213
	s_waitcnt lgkmcnt(1)
	v_add_f32_e32 v210, v210, v211
	ds_bpermute_b32 v213, v223, v212
	ds_bpermute_b32 v211, v223, v210
	s_waitcnt lgkmcnt(2)
	v_add_f32_e32 v192, v192, v214
	ds_bpermute_b32 v217, v221, v216
	ds_bpermute_b32 v232, v221, v218
	s_waitcnt lgkmcnt(3)
	v_add_f32_e32 v212, v212, v213
	s_waitcnt lgkmcnt(2)
	v_add_f32_e32 v214, v210, v211
	ds_bpermute_b32 v213, v224, v212
	ds_bpermute_b32 v215, v224, v214
	s_waitcnt lgkmcnt(3)
	v_add_f32_e32 v216, v216, v217
	s_waitcnt lgkmcnt(2)
	v_add_f32_e32 v218, v218, v232
	ds_bpermute_b32 v217, v222, v216
	s_waitcnt lgkmcnt(2)
	v_add_f32_e32 v211, v212, v213
	s_waitcnt lgkmcnt(1)
	v_add_f32_e32 v213, v214, v215
	ds_bpermute_b32 v215, v220, v238
	ds_bpermute_b32 v232, v222, v218
	s_waitcnt lgkmcnt(2)
	v_add_f32_e32 v216, v216, v217
	ds_bpermute_b32 v217, v223, v216
	ds_bpermute_b32 v196, v225, v194
	s_waitcnt lgkmcnt(3)
	v_add_f32_e32 v215, v238, v215
	ds_bpermute_b32 v219, v221, v215
	s_waitcnt lgkmcnt(3)
	v_add_f32_e32 v218, v218, v232
	ds_bpermute_b32 v232, v223, v218
	s_waitcnt lgkmcnt(3)
	v_add_f32_e32 v216, v216, v217
	ds_bpermute_b32 v217, v224, v216
	s_waitcnt lgkmcnt(2)
	v_add_f32_e32 v215, v215, v219
	ds_bpermute_b32 v219, v222, v215
	s_waitcnt lgkmcnt(2)
	v_add_f32_e32 v232, v218, v232
	ds_bpermute_b32 v234, v224, v232
	ds_bpermute_b32 v197, v225, v195
	ds_bpermute_b32 v210, v225, v192
	s_waitcnt lgkmcnt(3)
	v_add_f32_e32 v215, v215, v219
	ds_bpermute_b32 v219, v223, v215
	ds_bpermute_b32 v212, v225, v211
	ds_bpermute_b32 v214, v225, v213
	s_waitcnt lgkmcnt(2)
	v_add_f32_e32 v219, v215, v219
	ds_bpermute_b32 v233, v224, v219
	v_add_f32_e32 v215, v216, v217
	ds_bpermute_b32 v216, v225, v215
	s_waitcnt lgkmcnt(1)
	v_add_f32_e32 v217, v219, v233
	v_add_f32_e32 v219, v232, v234
	ds_bpermute_b32 v218, v225, v217
	ds_bpermute_b32 v232, v225, v219
	v_bfe_u32 v233, v193, 16, 1
	v_add3_u32 v193, v193, v233, s31
	v_and_or_b32 v189, v193, s29, v189
	global_store_dwordx4 v[190:191], v[186:189], off
	s_and_saveexec_b64 s[24:25], s[2:3]
	s_cbranch_execz .LBB0_1232
	v_pk_add_f32 v[188:189], v[194:195], v[196:197]
	v_add_f32_e32 v192, v192, v210
	v_cmp_gt_f32_e32 vcc, v189, v188
	v_add_f32_e32 v211, v211, v212
	v_add_f32_e32 v193, v213, v214
	v_cndmask_b32_e32 v186, v188, v189, vcc
	v_cmp_gt_f32_e64 s[0:1], v192, v186
	s_waitcnt lgkmcnt(2)
	v_add_f32_e32 v191, v215, v216
	s_waitcnt lgkmcnt(1)
	v_add_f32_e32 v190, v217, v218
	v_cndmask_b32_e64 v186, v186, v192, s[0:1]
	v_cmp_gt_f32_e64 s[4:5], v211, v186
	s_waitcnt lgkmcnt(0)
	v_add_f32_e32 v187, v219, v232
	v_cmp_nlg_f32_e64 s[14:15], s34, v188
	v_cndmask_b32_e64 v186, v186, v211, s[4:5]
	v_cmp_gt_f32_e64 s[6:7], v193, v186
	s_nop 1
	v_cndmask_b32_e64 v186, v186, v193, s[6:7]
	v_cmp_gt_f32_e64 s[8:9], v191, v186
	s_nop 1
	v_cndmask_b32_e64 v186, v186, v191, s[8:9]
	v_cmp_gt_f32_e64 s[10:11], v190, v186
	s_nop 1
	v_cndmask_b32_e64 v194, v186, v190, s[10:11]
	v_cndmask_b32_e64 v186, 0, 1, vcc
	v_cndmask_b32_e64 v186, v186, 2, s[0:1]
	v_cndmask_b32_e64 v186, v186, 3, s[4:5]
	v_cndmask_b32_e64 v186, v186, 4, s[6:7]
	v_cndmask_b32_e64 v186, v186, 5, s[8:9]
	v_cndmask_b32_e64 v186, v186, 6, s[10:11]
	v_cmp_ngt_f32_e32 vcc, v187, v194
	s_and_b64 s[16:17], s[10:11], vcc
	s_nop 0
	v_cndmask_b32_e32 v186, 7, v186, vcc
	v_cmp_eq_u32_e64 s[12:13], 0, v186
	s_or_b64 s[12:13], s[12:13], s[14:15]
	v_cmp_ne_u32_e64 s[10:11], 1, v186
	v_cndmask_b32_e64 v188, v188, v231, s[12:13]
	v_cmp_gt_f32_e64 s[14:15], v189, v188
	s_and_b64 s[10:11], s[10:11], s[14:15]
	v_cndmask_b32_e64 v188, v188, v189, s[10:11]
	v_cmp_ne_u32_e64 s[8:9], 2, v186
	v_cmp_gt_f32_e64 s[14:15], v192, v188
	s_and_b64 s[8:9], s[8:9], s[14:15]
	v_cndmask_b32_e64 v188, v188, v192, s[8:9]
	v_cmp_ne_u32_e64 s[6:7], 3, v186
	v_cmp_gt_f32_e64 s[14:15], v211, v188
	s_and_b64 s[6:7], s[6:7], s[14:15]
	v_cndmask_b32_e64 v188, v188, v211, s[6:7]
	v_cmp_ne_u32_e64 s[4:5], 4, v186
	v_cmp_gt_f32_e64 s[14:15], v193, v188
	s_and_b64 s[4:5], s[4:5], s[14:15]
	v_cndmask_b32_e64 v188, v188, v193, s[4:5]
	v_cmp_ne_u32_e64 s[0:1], 5, v186
	v_cmp_gt_f32_e64 s[14:15], v191, v188
	s_and_b64 s[0:1], s[0:1], s[14:15]
	v_cndmask_b32_e64 v188, v188, v191, s[0:1]
	v_cmp_ngt_f32_e64 s[14:15], v190, v188
	s_or_b64 s[14:15], s[16:17], s[14:15]
	v_cndmask_b32_e64 v189, 0, -1, s[12:13]
	v_cndmask_b32_e64 v188, v190, v188, s[14:15]
	v_cmp_gt_f32_e64 s[16:17], v187, v188
	s_and_b64 s[16:17], vcc, s[16:17]
	v_cndmask_b32_e64 v189, v189, 1, s[10:11]
	v_cndmask_b32_e64 v188, v188, v187, s[16:17]
	v_cndmask_b32_e32 v187, v187, v194, vcc
	v_sub_f32_e32 v187, v188, v187
	v_mul_f32_e32 v187, 0x3fb8aa3b, v187
	v_exp_f32_e32 v191, v187
	v_cndmask_b32_e64 v187, v189, 2, s[8:9]
	v_cndmask_b32_e64 v187, v187, 3, s[6:7]
	v_cndmask_b32_e64 v187, v187, 4, s[4:5]
	v_add_f32_e32 v190, 1.0, v191
	v_div_scale_f32 v188, s[4:5], v190, v190, 1.0
	v_rcp_f32_e32 v192, v188
	v_cndmask_b32_e64 v187, v187, 5, s[0:1]
	v_cndmask_b32_e64 v187, 6, v187, s[14:15]
	v_cndmask_b32_e64 v187, v187, 7, s[16:17]
	v_fma_f32 v189, -v188, v192, 1.0
	v_fmac_f32_e32 v192, v189, v192
	v_div_scale_f32 v189, vcc, 1.0, v190, 1.0
	v_mul_f32_e32 v193, v189, v192
	v_fma_f32 v194, -v188, v193, v189
	v_fmac_f32_e32 v193, v194, v192
	v_fma_f32 v194, -v188, v193, v189
	v_lshl_add_u32 v188, v186, 2, 0
	ds_add_rtn_u32 v188, v188, v230
	v_lshl_add_u32 v189, v187, 2, 0
	ds_add_rtn_u32 v189, v189, v230
	v_div_fmas_f32 v192, v194, v192, v193
	v_div_fixup_f32 v190, v192, v190, 1.0
	v_mul_f32_e32 v191, v191, v190
	s_waitcnt lgkmcnt(0)
	ds_write_b128 v226, v[186:189] offset:48
	v_add_u32_e32 v186, 6, v227
	v_ashrrev_i32_e32 v187, 31, v186
	v_lshl_add_u64 v[186:187], v[186:187], 2, s[36:37]
	global_store_dwordx2 v[186:187], v[190:191], off
	s_branch .LBB0_1232

.LBB0_1342:
	v_mov_b32_e32 v133, v0
	s_lshl_b32 s38, s61, 8
	s_add_i32 s38, s38, s45
	v_and_or_b32 v132, v133, 15, s38
	v_lshrrev_b32_e32 v133, 1, v133
	v_and_or_b32 v133, v133, 24, s47
	v_lshlrev_b32_e32 v194, 1, v133
	v_ashrrev_i32_e32 v133, 31, v132
	v_lshlrev_b64 v[140:141], 11, v[132:133]
	v_bfe_u32 v133, v126, 16, 1
	v_add3_u32 v126, v126, v133, s27
	v_bfe_u32 v133, v127, 16, 1
	v_lshrrev_b32_e32 v126, 16, v126
	v_add3_u32 v127, v127, v133, s27
	v_and_or_b32 v126, v127, s28, v126
	v_cvt_pk_bf16_f32 v127, v128, v129
	v_cvt_pk_bf16_f32 v128, v122, v123
	v_bfe_u32 v122, v124, 16, 1
	v_add3_u32 v122, v124, v122, s27
	v_bfe_u32 v123, v125, 16, 1
	v_lshrrev_b32_e32 v122, 16, v122
	v_add3_u32 v123, v125, v123, s27
	v_and_or_b32 v129, v123, s28, v122
	v_bfe_u32 v122, v118, 16, 1
	v_add3_u32 v118, v118, v122, s27
	v_bfe_u32 v122, v119, 16, 1
	v_lshrrev_b32_e32 v118, 16, v118
	v_add3_u32 v119, v119, v122, s27
	v_and_or_b32 v118, v119, s28, v118
	v_cvt_pk_bf16_f32 v119, v120, v121
	s_lshl_b32 s38, s64, 8
	s_ashr_i32 s39, s38, 31
	v_cvt_pk_bf16_f32 v120, v110, v111
	s_lshl_b64 s[38:39], s[38:39], 1
	s_add_u32 s38, s77, s38
	s_addc_u32 s39, s6, s39
	v_cvt_pk_bf16_f32 v121, v112, v113
	v_or_b32_e32 v110, 16, v132
	v_lshl_add_u64 v[134:135], s[38:39], 0, v[194:195]
	v_ashrrev_i32_e32 v111, 31, v110
	v_lshl_add_u64 v[140:141], v[134:135], 0, v[140:141]
	v_lshlrev_b64 v[110:111], 11, v[110:111]
	global_store_dwordx4 v[140:141], v[118:121], off offset:256
	v_bfe_u32 v112, v117, 16, 1
	v_add3_u32 v112, v117, v112, s27
	v_lshl_add_u64 v[118:119], v[134:135], 0, v[110:111]
	v_cvt_pk_bf16_f32 v110, v114, v115
	v_bfe_u32 v111, v116, 16, 1
	v_add3_u32 v111, v116, v111, s27
	v_lshrrev_b32_e32 v111, 16, v111
	v_and_or_b32 v111, v112, s28, v111
	v_cvt_pk_bf16_f32 v112, v106, v107
	v_bfe_u32 v106, v108, 16, 1
	v_add3_u32 v106, v108, v106, s27
	v_bfe_u32 v107, v109, 16, 1
	v_lshrrev_b32_e32 v106, 16, v106
	v_add3_u32 v107, v109, v107, s27
	v_and_or_b32 v113, v107, s28, v106
	v_bfe_u32 v106, v102, 16, 1
	v_add3_u32 v102, v102, v106, s27
	v_bfe_u32 v106, v103, 16, 1
	v_lshrrev_b32_e32 v102, 16, v102
	v_add3_u32 v103, v103, v106, s27
	v_and_or_b32 v102, v103, s28, v102
	v_cvt_pk_bf16_f32 v103, v104, v105
	v_cvt_pk_bf16_f32 v104, v94, v95
	v_cvt_pk_bf16_f32 v105, v96, v97
	v_or_b32_e32 v94, 32, v132
	v_ashrrev_i32_e32 v95, 31, v94
	v_lshlrev_b64 v[94:95], 11, v[94:95]
	global_store_dwordx4 v[118:119], v[102:105], off offset:256
	v_bfe_u32 v96, v101, 16, 1
	v_add3_u32 v96, v101, v96, s27
	v_lshl_add_u64 v[102:103], v[134:135], 0, v[94:95]
	v_cvt_pk_bf16_f32 v94, v98, v99
	v_bfe_u32 v95, v100, 16, 1
	v_add3_u32 v95, v100, v95, s27
	v_lshrrev_b32_e32 v95, 16, v95
	v_and_or_b32 v95, v96, s28, v95
	v_cvt_pk_bf16_f32 v96, v90, v91
	v_bfe_u32 v90, v92, 16, 1
	v_add3_u32 v90, v92, v90, s27
	v_bfe_u32 v91, v93, 16, 1
	v_lshrrev_b32_e32 v90, 16, v90
	v_add3_u32 v91, v93, v91, s27
	v_and_or_b32 v97, v91, s28, v90
	v_bfe_u32 v90, v86, 16, 1
	v_add3_u32 v86, v86, v90, s27
	v_bfe_u32 v90, v87, 16, 1
	v_lshrrev_b32_e32 v86, 16, v86
	v_add3_u32 v87, v87, v90, s27
	v_and_or_b32 v86, v87, s28, v86
	v_cvt_pk_bf16_f32 v87, v88, v89
	v_cvt_pk_bf16_f32 v88, v78, v79
	v_cvt_pk_bf16_f32 v89, v80, v81
	v_or_b32_e32 v78, 48, v132
	v_ashrrev_i32_e32 v79, 31, v78
	v_lshlrev_b64 v[78:79], 11, v[78:79]
	global_store_dwordx4 v[102:103], v[86:89], off offset:256
	v_bfe_u32 v80, v85, 16, 1
	v_add3_u32 v80, v85, v80, s27
	v_lshl_add_u64 v[86:87], v[134:135], 0, v[78:79]
	v_cvt_pk_bf16_f32 v78, v82, v83
	v_bfe_u32 v79, v84, 16, 1
	v_add3_u32 v79, v84, v79, s27
	v_lshrrev_b32_e32 v79, 16, v79
	v_and_or_b32 v79, v80, s28, v79
	v_cvt_pk_bf16_f32 v80, v74, v75
	v_bfe_u32 v74, v76, 16, 1
	v_add3_u32 v74, v76, v74, s27
	v_bfe_u32 v75, v77, 16, 1
	v_lshrrev_b32_e32 v74, 16, v74
	v_add3_u32 v75, v77, v75, s27
	v_and_or_b32 v81, v75, s28, v74
	v_bfe_u32 v74, v70, 16, 1
	v_add3_u32 v70, v70, v74, s27
	v_bfe_u32 v74, v71, 16, 1
	v_lshrrev_b32_e32 v70, 16, v70
	v_add3_u32 v71, v71, v74, s27
	v_and_or_b32 v70, v71, s28, v70
	v_cvt_pk_bf16_f32 v71, v72, v73
	v_cvt_pk_bf16_f32 v72, v66, v67
	v_bfe_u32 v66, v68, 16, 1
	v_add3_u32 v66, v68, v66, s27
	v_bfe_u32 v68, v62, 16, 1
	v_add3_u32 v62, v62, v68, s27
	v_bfe_u32 v68, v63, 16, 1
	v_lshrrev_b32_e32 v62, 16, v62
	v_add3_u32 v63, v63, v68, s27
	v_and_or_b32 v62, v63, s28, v62
	v_cvt_pk_bf16_f32 v63, v64, v65
	v_cvt_pk_bf16_f32 v64, v58, v59
	v_bfe_u32 v58, v60, 16, 1
	v_add3_u32 v58, v60, v58, s27
	v_bfe_u32 v59, v61, 16, 1
	v_lshrrev_b32_e32 v58, 16, v58
	v_add3_u32 v59, v61, v59, s27
	v_and_or_b32 v65, v59, s28, v58
	v_bfe_u32 v58, v54, 16, 1
	v_add3_u32 v54, v54, v58, s27
	v_bfe_u32 v58, v55, 16, 1
	v_lshrrev_b32_e32 v54, 16, v54
	v_add3_u32 v55, v55, v58, s27
	v_and_or_b32 v54, v55, s28, v54
	v_cvt_pk_bf16_f32 v55, v56, v57
	v_bfe_u32 v67, v69, 16, 1
	v_cvt_pk_bf16_f32 v56, v46, v47
	v_lshrrev_b32_e32 v66, 16, v66
	v_add3_u32 v67, v69, v67, s27
	v_and_or_b32 v73, v67, s28, v66
	v_add_u32_e32 v66, 0x80, v132
	v_ashrrev_i32_e32 v67, 31, v66
	v_cvt_pk_bf16_f32 v57, v48, v49
	v_add_u32_e32 v46, 0x90, v132
	v_lshlrev_b64 v[66:67], 11, v[66:67]
	v_ashrrev_i32_e32 v47, 31, v46
	v_lshl_add_u64 v[66:67], v[134:135], 0, v[66:67]
	v_lshlrev_b64 v[46:47], 11, v[46:47]
	global_store_dwordx4 v[66:67], v[54:57], off offset:256
	v_bfe_u32 v48, v53, 16, 1
	v_add3_u32 v48, v53, v48, s27
	v_lshl_add_u64 v[54:55], v[134:135], 0, v[46:47]
	v_cvt_pk_bf16_f32 v46, v50, v51
	v_bfe_u32 v47, v52, 16, 1
	v_add3_u32 v47, v52, v47, s27
	v_lshrrev_b32_e32 v47, 16, v47
	v_and_or_b32 v47, v48, s28, v47
	v_cvt_pk_bf16_f32 v48, v42, v43
	v_bfe_u32 v42, v44, 16, 1
	v_add3_u32 v42, v44, v42, s27
	v_bfe_u32 v43, v45, 16, 1
	v_lshrrev_b32_e32 v42, 16, v42
	v_add3_u32 v43, v45, v43, s27
	v_and_or_b32 v49, v43, s28, v42
	v_bfe_u32 v42, v38, 16, 1
	v_add3_u32 v38, v38, v42, s27
	v_bfe_u32 v42, v39, 16, 1
	v_lshrrev_b32_e32 v38, 16, v38
	v_add3_u32 v39, v39, v42, s27
	v_and_or_b32 v38, v39, s28, v38
	v_cvt_pk_bf16_f32 v39, v40, v41
	v_cvt_pk_bf16_f32 v40, v30, v31
	v_cvt_pk_bf16_f32 v41, v32, v33
	v_add_u32_e32 v30, 0xa0, v132
	v_ashrrev_i32_e32 v31, 31, v30
	v_lshlrev_b64 v[30:31], 11, v[30:31]
	global_store_dwordx4 v[54:55], v[38:41], off offset:256
	v_bfe_u32 v32, v37, 16, 1
	v_add3_u32 v32, v37, v32, s27
	v_lshl_add_u64 v[38:39], v[134:135], 0, v[30:31]
	v_cvt_pk_bf16_f32 v30, v34, v35
	v_bfe_u32 v31, v36, 16, 1
	v_add3_u32 v31, v36, v31, s27
	v_lshrrev_b32_e32 v31, 16, v31
	v_and_or_b32 v31, v32, s28, v31
	v_cvt_pk_bf16_f32 v32, v26, v27
	v_bfe_u32 v26, v28, 16, 1
	v_add3_u32 v26, v28, v26, s27
	v_bfe_u32 v27, v29, 16, 1
	v_lshrrev_b32_e32 v26, 16, v26
	v_add3_u32 v27, v29, v27, s27
	v_and_or_b32 v33, v27, s28, v26
	v_bfe_u32 v26, v22, 16, 1
	v_add3_u32 v22, v22, v26, s27
	v_bfe_u32 v26, v23, 16, 1
	v_lshrrev_b32_e32 v22, 16, v22
	v_add3_u32 v23, v23, v26, s27
	v_and_or_b32 v22, v23, s28, v22
	v_cvt_pk_bf16_f32 v23, v24, v25
	v_cvt_pk_bf16_f32 v24, v14, v15
	v_cvt_pk_bf16_f32 v25, v16, v17
	v_add_u32_e32 v14, 0xb0, v132
	v_ashrrev_i32_e32 v15, 31, v14
	v_lshlrev_b64 v[14:15], 11, v[14:15]
	global_store_dwordx4 v[38:39], v[22:25], off offset:256
	v_bfe_u32 v16, v21, 16, 1
	v_add3_u32 v16, v21, v16, s27
	v_lshl_add_u64 v[22:23], v[134:135], 0, v[14:15]
	v_cvt_pk_bf16_f32 v14, v18, v19
	v_bfe_u32 v15, v20, 16, 1
	v_add3_u32 v15, v20, v15, s27
	v_lshrrev_b32_e32 v15, 16, v15
	v_and_or_b32 v15, v16, s28, v15
	v_cvt_pk_bf16_f32 v16, v10, v11
	v_bfe_u32 v10, v12, 16, 1
	v_add3_u32 v10, v12, v10, s27
	v_bfe_u32 v11, v13, 16, 1
	v_lshrrev_b32_e32 v10, 16, v10
	v_add3_u32 v11, v13, v11, s27
	v_and_or_b32 v17, v11, s28, v10
	v_bfe_u32 v10, v6, 16, 1
	v_add3_u32 v6, v6, v10, s27
	v_bfe_u32 v10, v7, 16, 1
	v_lshrrev_b32_e32 v6, 16, v6
	v_add3_u32 v7, v7, v10, s27
	v_and_or_b32 v6, v7, s28, v6
	v_cvt_pk_bf16_f32 v7, v8, v9
	v_cvt_pk_bf16_f32 v8, v2, v3
	v_cvt_pk_bf16_f32 v9, v4, v5
	s_and_b64 vcc, exec, s[36:37]
	s_mov_b64 s[36:37], -1
	global_store_dwordx4 v[140:141], v[126:129], off
	global_store_dwordx4 v[118:119], v[110:113], off
	global_store_dwordx4 v[102:103], v[94:97], off
	global_store_dwordx4 v[86:87], v[78:81], off
	global_store_dwordx4 v[86:87], v[70:73], off offset:256
	global_store_dwordx4 v[66:67], v[62:65], off
	global_store_dwordx4 v[54:55], v[46:49], off
	global_store_dwordx4 v[38:39], v[30:33], off
	global_store_dwordx4 v[22:23], v[14:17], off
	global_store_dwordx4 v[22:23], v[6:9], off offset:256
	s_cbranch_vccnz .LBB0_1321
	s_andn2_b64 vcc, exec, s[82:83]
	s_cbranch_vccnz .LBB0_1320
	s_barrier
	s_branch .LBB0_1320
